# baseline (speedup 1.0000x reference)
.LBB0_9:
	s_or_b64 exec, exec, s[22:23]
	v_ashrrev_i32_e32 v5, 31, v4
	s_waitcnt lgkmcnt(0)
	v_lshl_add_u64 v[4:5], v[4:5], 4, s[20:21]
	global_store_dwordx4 v[4:5], v[0:3], off sc0 sc1

.LBB0_11:
	s_andn2_saveexec_b64 s[20:21], s[8:9]
	s_cbranch_execz .LBB0_13
	s_load_dwordx4 s[8:11], s[0:1], 0x48
	v_subrev_u32_e32 v0, s17, v0
	v_ashrrev_i32_e32 v4, 2, v0
	v_ashrrev_i32_e32 v5, 31, v4
	v_and_b32_e32 v10, 3, v0
	v_lshlrev_b64 v[0:1], 6, v[4:5]
	s_waitcnt lgkmcnt(0)
	v_lshl_add_u64 v[0:1], s[8:9], 0, v[0:1]
	v_lshlrev_b32_e32 v6, 4, v10
	v_mov_b32_e32 v7, 0
	v_lshl_add_u64 v[0:1], v[0:1], 0, v[6:7]
	global_load_dwordx4 v[0:3], v[0:1], off
	v_lshrrev_b32_e32 v5, 23, v5
	v_add_u32_e32 v5, v4, v5
	v_ashrrev_i32_e32 v8, 9, v5
	v_mul_i32_i24_e32 v5, 0x200, v8
	v_ashrrev_i32_e32 v9, 31, v8
	v_sub_u32_e32 v4, v4, v5
	v_lshlrev_b32_e32 v6, 9, v10
	v_lshlrev_b64 v[8:9], 15, v[8:9]
	v_ashrrev_i32_e32 v5, 31, v4
	s_mov_b32 s8, 0xbfb8aa3b
	v_lshl_add_u64 v[8:9], s[10:11], 0, v[8:9]
	v_lshl_add_u64 v[4:5], v[4:5], 0, v[6:7]
	v_lshl_add_u64 v[4:5], v[4:5], 4, v[8:9]
	s_waitcnt vmcnt(0)
	v_mul_f32_e32 v0, 0x3fb8aa3b, v0
	v_mul_f32_e32 v1, 0x3fb8aa3b, v1
	v_mul_f32_e32 v2, 0x3fb8aa3b, v2
	v_mul_f32_e32 v3, 0x3fb8aa3b, v3
	v_exp_f32_e32 v0, v0
	v_exp_f32_e32 v1, v1
	v_exp_f32_e32 v2, v2
	v_exp_f32_e32 v3, v3
	v_pk_mul_f32 v[0:1], v[0:1], s[8:9] op_sel_hi:[1,0]
	v_pk_mul_f32 v[2:3], v[2:3], s[8:9] op_sel_hi:[1,0]
	global_store_dwordx4 v[4:5], v[0:3], off sc0 sc1

.LBB0_20:
	v_ashrrev_i32_e32 v6, 5, v1
	v_sub_u32_e32 v7, 0, v6
	v_max_i32_e32 v7, v6, v7
	v_cvt_f32_u32_e32 v8, v7
	v_sub_u32_e32 v12, 0, v7
	v_ashrrev_i32_e32 v9, 6, v0
	v_sub_u32_e32 v11, 0, v9
	v_rcp_iflag_f32_e32 v8, v8
	v_max_i32_e32 v11, v9, v11
	v_xor_b32_e32 v10, v9, v6
	v_ashrrev_i32_e32 v10, 31, v10
	v_mul_f32_e32 v8, 0x4f7ffffe, v8
	v_cvt_u32_f32_e32 v8, v8
	v_mul_lo_u32 v12, v12, v8
	v_mul_hi_u32 v12, v8, v12
	v_add_u32_e32 v8, v8, v12
	v_mul_hi_u32 v8, v11, v8
	v_mul_lo_u32 v12, v8, v7
	v_sub_u32_e32 v11, v11, v12
	v_add_u32_e32 v13, 1, v8
	v_cmp_ge_u32_e32 vcc, v11, v7
	v_sub_u32_e32 v12, v11, v7
	s_nop 0
	v_cndmask_b32_e32 v8, v8, v13, vcc
	v_cndmask_b32_e32 v11, v11, v12, vcc
	v_add_u32_e32 v12, 1, v8
	v_cmp_ge_u32_e32 vcc, v11, v7
	s_nop 1
	v_cndmask_b32_e32 v7, v8, v12, vcc
	v_xor_b32_e32 v7, v7, v10
	v_sub_u32_e32 v7, v7, v10
	v_mul_lo_u32 v6, v7, v6
	v_sub_u32_e32 v8, v9, v6
	v_and_b32_e32 v6, 15, v0
	v_lshl_or_b32 v6, v7, 4, v6
	v_mad_i64_i32 v[6:7], s[0:1], v6, v1, 0
	v_lshl_add_u64 v[4:5], v[6:7], 2, v[4:5]
	v_lshlrev_b32_e32 v6, 5, v8
	v_ashrrev_i32_e32 v7, 31, v6
	v_lshlrev_b32_e32 v1, 1, v0
	v_lshl_add_u64 v[4:5], v[6:7], 2, v[4:5]
	v_and_b32_e32 v6, 0x60, v1
	v_mov_b32_e32 v7, 0
	v_lshl_add_u64 v[12:13], v[4:5], 0, v[6:7]
	global_load_dwordx4 v[4:7], v[12:13], off
	global_load_dwordx4 v[8:11], v[12:13], off offset:16
	v_ashrrev_i32_e32 v1, 31, v0
	v_lshl_add_u64 v[0:1], v[0:1], 4, v[2:3]
	s_waitcnt vmcnt(1)
	v_cvt_f16_f32_e32 v4, v4
	v_cvt_pk_f16_f32 v12, v5, v6
	s_waitcnt vmcnt(0)
	v_cvt_pk_f16_f32 v6, v7, v8
	v_cvt_f16_f32_e32 v8, v11
	v_cvt_pk_f16_f32 v7, v9, v10
	v_alignbit_b32 v5, v6, v12, 16
	v_alignbit_b32 v6, v7, v6, 16
	v_pack_b32_f16 v4, v4, v12
	v_alignbit_b32 v7, v8, v7, 16
	global_store_dwordx4 v[0:1], v[4:7], off sc0 sc1
	s_endpgm

_Z10k_ka_firstPKfPKiPfS0_S0_PKDF16_PDF16_:
	s_load_dwordx8 s[4:11], s[0:1], 0x0
	s_lshl_b32 s3, s2, 5
	s_and_b32 s3, s3, 0xe0
	s_lshr_b32 s12, s2, 3
	s_or_b32 s14, s3, s12
	v_or_b32_e32 v1, 0x200, v0
	s_lshl_b32 s51, s14, 5
	v_mov_b32_e32 v75, 0
	v_lshrrev_b32_e32 v26, 6, v0
	v_lshrrev_b32_e32 v27, 6, v1
	v_or_b32_e32 v1, 0x600, v0
	v_or_b32_e32 v2, s51, v26
	v_mov_b32_e32 v3, v75
	v_lshrrev_b32_e32 v28, 6, v1
	s_waitcnt lgkmcnt(0)
	v_lshl_add_u64 v[2:3], v[2:3], 2, s[6:7]
	v_or_b32_e32 v4, s51, v27
	v_mov_b32_e32 v5, v75
	v_or_b32_e32 v6, s51, v28
	v_mov_b32_e32 v7, v75
	v_lshl_add_u64 v[4:5], v[4:5], 2, s[6:7]
	v_lshl_add_u64 v[6:7], v[6:7], 2, s[6:7]
	global_load_dword v8, v[2:3], off
	global_load_dword v10, v[4:5], off
	global_load_dword v12, v[6:7], off
	global_load_dword v14, v[2:3], off offset:64
	v_and_b32_e32 v29, 63, v0
	v_lshlrev_b32_e32 v74, 4, v29
	v_lshl_add_u64 v[2:3], s[4:5], 0, v[74:75]
	s_movk_i32 s16, 0x410
	s_bfe_u32 s40, s2, 0x30003
	s_mov_b32 s3, 0
	s_lshl_b32 s2, s40, 10
	s_movk_i32 s48, 0x2000
	s_movk_i32 s49, 0x4000
	s_movk_i32 s33, 0x6000
	s_movk_i32 s18, 0x210
	s_mov_b32 s21, s3
	s_mov_b32 s27, s3
	v_mov_b32_e32 v80, 0x3727c5ac
	s_mov_b32 s39, 0x800000
	s_mov_b32 s23, s3
	s_mov_b32 s25, s3
	s_mov_b64 s[36:37], 0x40000
	s_mov_b32 s29, s3
	s_mov_b32 s31, s3
	s_mov_b32 s35, 0x14000
	s_mov_b32 s34, 0x3b800000
	v_and_b32_e32 v86, 15, v0
	s_mov_b32 s17, s3
	s_mov_b32 s15, s3
	s_lshl_b32 s52, s40, 5
	v_lshl_add_u64 v[102:103], s[8:9], 0, v[74:75]
	s_xor_b32 s44, s2, 0x1000
	s_mov_b32 s45, s3
	s_mov_b32 s43, s3
	s_mov_b32 s47, s3
	s_movk_i32 s50, 0x1c0
	s_waitcnt vmcnt(3)
	v_ashrrev_i32_e32 v9, 31, v8
	s_waitcnt vmcnt(2)
	v_ashrrev_i32_e32 v11, 31, v10
	s_waitcnt vmcnt(1)
	v_ashrrev_i32_e32 v13, 31, v12
	s_waitcnt vmcnt(0)
	v_ashrrev_i32_e32 v15, 31, v14
	v_lshlrev_b64 v[4:5], 10, v[8:9]
	v_lshlrev_b64 v[6:7], 10, v[10:11]
	v_lshlrev_b64 v[8:9], 10, v[14:15]
	v_lshlrev_b64 v[10:11], 10, v[12:13]
	v_lshl_add_u64 v[18:19], v[2:3], 0, v[4:5]
	v_lshl_add_u64 v[20:21], v[2:3], 0, v[6:7]
	v_lshl_add_u64 v[22:23], v[2:3], 0, v[8:9]
	v_lshl_add_u64 v[24:25], v[2:3], 0, v[10:11]
	global_load_dwordx4 v[2:5], v[18:19], off
	global_load_dwordx4 v[6:9], v[20:21], off
	global_load_dwordx4 v[10:13], v[22:23], off
	global_load_dwordx4 v[14:17], v[24:25], off
	s_load_dwordx4 s[4:7], s[0:1], 0x20
	s_load_dwordx2 s[12:13], s[0:1], 0x30
	v_lshrrev_b32_e32 v21, 1, v0
	v_and_b32_e32 v81, 24, v21
	v_mad_u32_u24 v21, v26, s16, v74
	v_mad_u32_u24 v23, v27, s16, v74
	v_mad_u32_u24 v24, v28, s16, v74
	v_lshrrev_b32_e32 v20, 4, v0
	v_mov_b32_e32 v18, 0x14000
	v_and_b32_e32 v1, 28, v20
	v_mov_b32_e32 v19, v75
	v_lshl_or_b32 v22, v29, 3, v18
	v_lshlrev_b32_e32 v18, 13, v1
	s_waitcnt lgkmcnt(0)
	v_lshl_add_u64 v[18:19], s[6:7], 0, v[18:19]
	v_lshl_add_u64 v[78:79], v[18:19], 0, v[74:75]
	v_mad_u32_u24 v54, v1, s16, v74
	v_lshl_add_u64 v[30:31], v[78:79], 0, s[2:3]
	v_or_b32_e32 v20, 3, v20
	v_mad_u32_u24 v87, v1, s18, v22
	v_mad_u32_u24 v100, v20, s16, v74
	v_mad_u32_u24 v101, v20, s18, v22
	s_lshl_b32 s1, s40, 6
	s_add_i32 s38, s1, 64
	s_and_b32 s18, s38, 0x1c0
	s_add_i32 s0, s1, 0x80
	s_lshl_b32 s20, s18, 4
	s_and_b32 s26, s0, 0x1c0
	v_lshl_add_u64 v[46:47], v[78:79], 0, s[20:21]
	s_lshl_b32 s26, s26, 4
	v_lshl_add_u64 v[52:53], v[78:79], 0, s[26:27]
	s_lshl_b32 s19, s38, 4
	s_or_b32 s22, s19, 0x2000
	s_or_b32 s24, s19, 0x6000
	v_lshl_add_u64 v[48:49], v[78:79], 0, s[22:23]
	v_lshl_add_u64 v[50:51], v[78:79], 0, s[24:25]
	s_lshl_b32 s30, s0, 4
	s_or_b32 s28, s30, 0x2000
	s_or_b32 s30, s30, 0x6000
	v_lshl_add_u64 v[76:77], v[78:79], 0, s[36:37]
	v_lshl_add_u64 v[88:89], v[78:79], 0, s[28:29]
	v_lshl_add_u64 v[90:91], v[78:79], 0, s[30:31]
	s_add_i32 s16, s1, 0xc0
	s_and_b32 s0, s14, 0x7ffffff
	s_and_b32 s14, s16, 0x1c0
	s_lshl_b32 s41, s16, 4
	s_lshl_b32 s16, s14, 4
	v_lshl_add_u64 v[82:83], v[78:79], 0, s[16:17]
	s_or_b32 s14, s41, 0x2000
	s_or_b32 s18, s41, 0x6000
	v_lshl_add_u64 v[84:85], v[78:79], 0, s[14:15]
	s_mov_b32 s41, s3
	s_mov_b32 s37, s3
	v_lshl_add_u64 v[120:121], v[78:79], 0, s[44:45]
	v_lshl_add_u64 v[148:149], v[76:77], 0, s[2:3]
	v_lshl_add_u64 v[150:151], v[76:77], 0, s[20:21]
	v_lshl_add_u64 v[152:153], v[76:77], 0, s[22:23]
	v_lshl_add_u64 v[154:155], v[76:77], 0, s[24:25]
	v_lshl_add_u64 v[156:157], v[76:77], 0, s[26:27]
	s_waitcnt vmcnt(3)
	ds_write_b128 v21, v[2:5] offset:37376
	s_waitcnt vmcnt(2)
	ds_write_b128 v23, v[6:9] offset:37376
	s_waitcnt vmcnt(1)
	ds_write_b128 v21, v[10:13] offset:54016
	s_waitcnt vmcnt(0)
	ds_write_b128 v24, v[14:17] offset:37376
	s_waitcnt lgkmcnt(0)
	s_barrier
	global_load_dwordx4 v[66:69], v74, s[10:11]
	global_load_dwordx4 v[70:73], v74, s[4:5]
	v_add_co_u32_e32 v6, vcc, s48, v30
	ds_read_b128 v[2:5], v54 offset:37376
	s_nop 0
	v_addc_co_u32_e32 v7, vcc, 0, v31, vcc
	v_add_co_u32_e32 v8, vcc, s49, v30
	v_lshl_add_u64 v[158:159], v[76:77], 0, s[28:29]
	s_nop 0
	v_addc_co_u32_e32 v9, vcc, 0, v31, vcc
	v_add_co_u32_e32 v10, vcc, s33, v30
	v_lshl_add_u64 v[160:161], v[76:77], 0, s[30:31]
	s_nop 0
	v_addc_co_u32_e32 v11, vcc, 0, v31, vcc
	global_load_dwordx4 v[26:29], v[30:31], off
	global_load_dwordx4 v[22:25], v[6:7], off
	global_load_dwordx4 v[18:21], v[8:9], off
	global_load_dwordx4 v[14:17], v[10:11], off
	s_waitcnt lgkmcnt(0)
	v_add_f32_e32 v6, v2, v3
	v_add_f32_e32 v6, v6, v4
	v_add_f32_e32 v6, v6, v5
	v_add_co_u32_e32 v12, vcc, s49, v46
	s_nop 0
	v_add_f32_dpp v6, v6, v6 quad_perm:[1,0,3,2] row_mask:0xf bank_mask:0xf bound_ctrl:1
	v_addc_co_u32_e32 v13, vcc, 0, v47, vcc
	s_nop 0
	v_add_f32_dpp v6, v6, v6 quad_perm:[2,3,0,1] row_mask:0xf bank_mask:0xf bound_ctrl:1
	v_add_co_u32_e32 v92, vcc, s49, v52
	s_nop 0
	v_add_f32_dpp v6, v6, v6 row_half_mirror row_mask:0xf bank_mask:0xf bound_ctrl:1
	v_addc_co_u32_e32 v93, vcc, 0, v53, vcc
	s_nop 0
	v_add_f32_dpp v6, v6, v6 row_mirror row_mask:0xf bank_mask:0xf bound_ctrl:1
	s_nop 0
	v_readlane_b32 s6, v6, 16
	v_readlane_b32 s7, v6, 48
	v_readlane_b32 s4, v6, 0
	v_readlane_b32 s5, v6, 32
	v_mov_b32_e32 v6, s6
	v_mov_b32_e32 v7, s7
	v_pk_add_f32 v[6:7], s[4:5], v[6:7]
	s_nop 0
	v_add_f32_e32 v6, v6, v7
	v_mul_f32_e32 v6, 0x3b800000, v6
	v_pk_add_f32 v[8:9], v[2:3], v[6:7] op_sel_hi:[1,0] neg_lo:[0,1] neg_hi:[0,1]
	v_pk_add_f32 v[6:7], v[4:5], v[6:7] op_sel_hi:[1,0] neg_lo:[0,1] neg_hi:[0,1]
	v_pk_mul_f32 v[10:11], v[8:9], v[8:9]
	v_pk_mul_f32 v[30:31], v[6:7], v[6:7]
	v_add_f32_e32 v10, v10, v11
	v_add_f32_e32 v10, v30, v10
	v_add_f32_e32 v10, v31, v10
	global_load_dwordx4 v[42:45], v[46:47], off
	global_load_dwordx4 v[38:41], v[48:49], off
	global_load_dwordx4 v[34:37], v[12:13], off
	global_load_dwordx4 v[30:33], v[50:51], off
	v_add_f32_dpp v10, v10, v10 quad_perm:[1,0,3,2] row_mask:0xf bank_mask:0xf bound_ctrl:1
	s_nop 1
	v_add_f32_dpp v10, v10, v10 quad_perm:[2,3,0,1] row_mask:0xf bank_mask:0xf bound_ctrl:1
	s_nop 1
	v_add_f32_dpp v10, v10, v10 row_half_mirror row_mask:0xf bank_mask:0xf bound_ctrl:1
	s_nop 1
	v_add_f32_dpp v10, v10, v10 row_mirror row_mask:0xf bank_mask:0xf bound_ctrl:1
	s_nop 0
	v_readlane_b32 s6, v10, 16
	v_readlane_b32 s7, v10, 48
	v_readlane_b32 s4, v10, 0
	v_readlane_b32 s5, v10, 32
	v_mov_b32_e32 v10, s6
	v_mov_b32_e32 v11, s7
	v_pk_add_f32 v[10:11], s[4:5], v[10:11]
	s_nop 0
	v_add_f32_e32 v10, v10, v11
	v_fmamk_f32 v10, v10, 0x3b800000, v80
	v_mul_f32_e32 v11, 0x4b800000, v10
	v_cmp_gt_f32_e32 vcc, s39, v10
	s_nop 1
	v_cndmask_b32_e32 v10, v10, v11, vcc
	v_rsq_f32_e32 v10, v10
	s_nop 0
	v_mul_f32_e32 v11, 0x45800000, v10
	v_cndmask_b32_e32 v10, v10, v11, vcc
	v_pk_mul_f32 v[8:9], v[8:9], v[10:11] op_sel_hi:[1,0]
	v_pk_mul_f32 v[6:7], v[6:7], v[10:11] op_sel_hi:[1,0]
	s_waitcnt vmcnt(8)
	v_pk_fma_f32 v[8:9], v[66:67], v[8:9], v[70:71]
	v_pk_fma_f32 v[6:7], v[68:69], v[6:7], v[72:73]
	v_cvt_pk_f16_f32 v8, v8, v9
	v_cvt_pk_f16_f32 v9, v6, v7
	ds_write_b64 v87, v[8:9]
	ds_read_b128 v[6:9], v54 offset:38416
	ds_read_b128 v[10:13], v54 offset:39456
	global_load_dwordx4 v[62:65], v[52:53], off
	global_load_dwordx4 v[58:61], v[88:89], off
	global_load_dwordx4 v[54:57], v[92:93], off
	global_load_dwordx4 v[46:49], v[90:91], off
	s_waitcnt lgkmcnt(1)
	v_add_f32_e32 v50, v6, v7
	s_waitcnt lgkmcnt(0)
	v_add_f32_e32 v51, v10, v11
	v_add_f32_e32 v50, v50, v8
	v_add_f32_e32 v51, v51, v12
	v_add_f32_e32 v50, v50, v9
	v_add_f32_e32 v51, v51, v13
	s_nop 0
	v_add_f32_dpp v50, v50, v50 quad_perm:[1,0,3,2] row_mask:0xf bank_mask:0xf bound_ctrl:1
	v_add_f32_dpp v51, v51, v51 quad_perm:[1,0,3,2] row_mask:0xf bank_mask:0xf bound_ctrl:1
	s_nop 0
	v_add_f32_dpp v50, v50, v50 quad_perm:[2,3,0,1] row_mask:0xf bank_mask:0xf bound_ctrl:1
	v_add_f32_dpp v51, v51, v51 quad_perm:[2,3,0,1] row_mask:0xf bank_mask:0xf bound_ctrl:1
	s_nop 0
	v_add_f32_dpp v50, v50, v50 row_half_mirror row_mask:0xf bank_mask:0xf bound_ctrl:1
	v_add_f32_dpp v51, v51, v51 row_half_mirror row_mask:0xf bank_mask:0xf bound_ctrl:1
	s_nop 0
	v_add_f32_dpp v50, v50, v50 row_mirror row_mask:0xf bank_mask:0xf bound_ctrl:1
	v_add_f32_dpp v51, v51, v51 row_mirror row_mask:0xf bank_mask:0xf bound_ctrl:1
	v_readlane_b32 s10, v50, 16
	v_readlane_b32 s11, v50, 48
	v_readlane_b32 s19, v51, 16
	v_readlane_b32 s36, v51, 48
	v_readlane_b32 s4, v50, 0
	v_readlane_b32 s5, v50, 32
	v_readlane_b32 s6, v51, 0
	v_readlane_b32 s7, v51, 32
	v_mov_b32_e32 v50, s10
	v_mov_b32_e32 v51, s11
	v_mov_b32_e32 v52, s19
	v_mov_b32_e32 v53, s36
	v_pk_add_f32 v[50:51], s[4:5], v[50:51]
	v_pk_add_f32 v[52:53], s[6:7], v[52:53]
	v_add_f32_e32 v50, v50, v51
	v_add_f32_e32 v51, v52, v53
	v_mul_f32_e32 v50, 0x3b800000, v50
	v_mul_f32_e32 v52, 0x3b800000, v51
	v_pk_add_f32 v[88:89], v[6:7], v[50:51] op_sel_hi:[1,0] neg_lo:[0,1] neg_hi:[0,1]
	v_pk_add_f32 v[90:91], v[10:11], v[52:53] op_sel_hi:[1,0] neg_lo:[0,1] neg_hi:[0,1]
	v_pk_add_f32 v[50:51], v[8:9], v[50:51] op_sel_hi:[1,0] neg_lo:[0,1] neg_hi:[0,1]
	v_pk_add_f32 v[52:53], v[12:13], v[52:53] op_sel_hi:[1,0] neg_lo:[0,1] neg_hi:[0,1]
	v_pk_mul_f32 v[92:93], v[88:89], v[88:89]
	v_pk_mul_f32 v[96:97], v[90:91], v[90:91]
	v_pk_mul_f32 v[94:95], v[50:51], v[50:51]
	v_pk_mul_f32 v[98:99], v[52:53], v[52:53]
	v_add_f32_e32 v92, v92, v93
	v_add_f32_e32 v93, v96, v97
	v_add_f32_e32 v92, v94, v92
	v_add_f32_e32 v93, v98, v93
	v_add_f32_e32 v92, v95, v92
	v_add_f32_e32 v93, v99, v93
	s_nop 0
	v_add_f32_dpp v92, v92, v92 quad_perm:[1,0,3,2] row_mask:0xf bank_mask:0xf bound_ctrl:1
	v_add_f32_dpp v93, v93, v93 quad_perm:[1,0,3,2] row_mask:0xf bank_mask:0xf bound_ctrl:1
	s_nop 0
	v_add_f32_dpp v92, v92, v92 quad_perm:[2,3,0,1] row_mask:0xf bank_mask:0xf bound_ctrl:1
	v_add_f32_dpp v93, v93, v93 quad_perm:[2,3,0,1] row_mask:0xf bank_mask:0xf bound_ctrl:1
	s_nop 0
	v_add_f32_dpp v92, v92, v92 row_half_mirror row_mask:0xf bank_mask:0xf bound_ctrl:1
	v_add_f32_dpp v93, v93, v93 row_half_mirror row_mask:0xf bank_mask:0xf bound_ctrl:1
	s_nop 0
	v_add_f32_dpp v92, v92, v92 row_mirror row_mask:0xf bank_mask:0xf bound_ctrl:1
	v_add_f32_dpp v93, v93, v93 row_mirror row_mask:0xf bank_mask:0xf bound_ctrl:1
	v_readlane_b32 s10, v92, 16
	v_readlane_b32 s11, v92, 48
	v_readlane_b32 s19, v93, 16
	v_readlane_b32 s36, v93, 48
	v_readlane_b32 s4, v92, 0
	v_readlane_b32 s5, v92, 32
	v_readlane_b32 s6, v93, 0
	v_readlane_b32 s7, v93, 32
	v_mov_b32_e32 v92, s10
	v_mov_b32_e32 v93, s11
	v_mov_b32_e32 v94, s19
	v_mov_b32_e32 v95, s36
	v_pk_add_f32 v[92:93], s[4:5], v[92:93]
	v_pk_add_f32 v[94:95], s[6:7], v[94:95]
	v_mov_b32_e32 v97, v92
	v_mov_b32_e32 v96, v94
	v_mov_b32_e32 v92, v95
	v_pk_add_f32 v[92:93], v[96:97], v[92:93]
	s_mov_b32 s19, s3
	v_pk_fma_f32 v[92:93], v[92:93], s[34:35], v[80:81] op_sel_hi:[1,0,0]
	s_mov_b32 s11, s3
	v_mul_f32_e32 v94, 0x4b800000, v93
	v_cmp_gt_f32_e32 vcc, s39, v93
	s_nop 1
	v_cndmask_b32_e32 v93, v93, v94, vcc
	v_rsq_f32_e32 v93, v93
	v_lshl_add_u64 v[94:95], v[78:79], 0, s[18:19]
	v_mul_f32_e32 v96, 0x45800000, v93
	v_cndmask_b32_e32 v96, v93, v96, vcc
	v_pk_mul_f32 v[88:89], v[88:89], v[96:97] op_sel_hi:[1,0]
	v_cmp_gt_f32_e32 vcc, s39, v92
	v_pk_fma_f32 v[88:89], v[66:67], v[88:89], v[70:71]
	v_pk_mul_f32 v[50:51], v[50:51], v[96:97] op_sel_hi:[1,0]
	v_cvt_pk_f16_f32 v88, v88, v89
	v_mul_f32_e32 v89, 0x4b800000, v92
	v_cndmask_b32_e32 v89, v92, v89, vcc
	v_rsq_f32_e32 v92, v89
	v_pk_fma_f32 v[50:51], v[68:69], v[50:51], v[72:73]
	s_nop 0
	v_cvt_pk_f16_f32 v89, v50, v51
	v_mul_f32_e32 v50, 0x45800000, v92
	v_cndmask_b32_e32 v50, v92, v50, vcc
	v_pk_mul_f32 v[90:91], v[90:91], v[50:51] op_sel_hi:[1,0]
	v_pk_mul_f32 v[50:51], v[52:53], v[50:51] op_sel_hi:[1,0]
	v_pk_fma_f32 v[90:91], v[66:67], v[90:91], v[70:71]
	v_pk_fma_f32 v[50:51], v[68:69], v[50:51], v[72:73]
	v_cvt_pk_f16_f32 v90, v90, v91
	v_cvt_pk_f16_f32 v91, v50, v51
	ds_write2_b64 v87, v[88:89], v[90:91] offset0:66 offset1:132
	ds_read_b128 v[50:53], v100 offset:37376
	v_lshlrev_b32_e32 v87, 1, v81
	v_mul_u32_u24_e32 v88, 0x210, v86
	v_add3_u32 v87, v88, v87, s35
	v_or_b32_e32 v100, s51, v1
	s_waitcnt lgkmcnt(0)
	v_add_f32_e32 v88, v50, v51
	v_add_f32_e32 v88, v88, v52
	v_add_f32_e32 v88, v88, v53
	v_or_b32_e32 v74, 1, v100
	v_add_u32_e32 v168, s1, v87
	v_add_f32_dpp v88, v88, v88 quad_perm:[1,0,3,2] row_mask:0xf bank_mask:0xf bound_ctrl:1
	s_mov_b32 s35, s3
	s_nop 0
	v_add_f32_dpp v88, v88, v88 quad_perm:[2,3,0,1] row_mask:0xf bank_mask:0xf bound_ctrl:1
	s_nop 1
	v_add_f32_dpp v88, v88, v88 row_half_mirror row_mask:0xf bank_mask:0xf bound_ctrl:1
	s_nop 1
	v_add_f32_dpp v88, v88, v88 row_mirror row_mask:0xf bank_mask:0xf bound_ctrl:1
	s_nop 0
	v_readlane_b32 s6, v88, 16
	v_readlane_b32 s7, v88, 48
	v_readlane_b32 s4, v88, 0
	v_readlane_b32 s5, v88, 32
	v_mov_b32_e32 v88, s6
	v_mov_b32_e32 v89, s7
	v_pk_add_f32 v[88:89], s[4:5], v[88:89]
	s_nop 0
	v_add_f32_e32 v88, v88, v89
	v_mul_f32_e32 v88, 0x3b800000, v88
	v_pk_add_f32 v[90:91], v[50:51], v[88:89] op_sel_hi:[1,0] neg_lo:[0,1] neg_hi:[0,1]
	v_pk_add_f32 v[88:89], v[52:53], v[88:89] op_sel_hi:[1,0] neg_lo:[0,1] neg_hi:[0,1]
	v_pk_mul_f32 v[92:93], v[90:91], v[90:91]
	v_pk_mul_f32 v[96:97], v[88:89], v[88:89]
	v_add_f32_e32 v92, v92, v93
	v_add_f32_e32 v92, v96, v92
	v_add_f32_e32 v92, v97, v92
	s_nop 1
	v_add_f32_dpp v92, v92, v92 quad_perm:[1,0,3,2] row_mask:0xf bank_mask:0xf bound_ctrl:1
	s_nop 1
	v_add_f32_dpp v92, v92, v92 quad_perm:[2,3,0,1] row_mask:0xf bank_mask:0xf bound_ctrl:1
	s_nop 1
	v_add_f32_dpp v92, v92, v92 row_half_mirror row_mask:0xf bank_mask:0xf bound_ctrl:1
	s_nop 1
	v_add_f32_dpp v92, v92, v92 row_mirror row_mask:0xf bank_mask:0xf bound_ctrl:1
	s_nop 0
	v_readlane_b32 s6, v92, 16
	v_readlane_b32 s7, v92, 48
	v_readlane_b32 s4, v92, 0
	v_readlane_b32 s5, v92, 32
	v_mov_b32_e32 v92, s6
	v_mov_b32_e32 v93, s7
	v_pk_add_f32 v[92:93], s[4:5], v[92:93]
	s_add_i32 s4, s52, 32
	v_add_f32_e32 v92, v92, v93
	v_fmac_f32_e32 v80, 0x3b800000, v92
	v_mul_f32_e32 v92, 0x4b800000, v80
	v_cmp_gt_f32_e32 vcc, s39, v80
	s_and_b32 s4, s4, 0xe0
	s_mov_b32 s39, s3
	v_cndmask_b32_e32 v80, v80, v92, vcc
	v_rsq_f32_e32 v80, v80
	s_mov_b32 s7, s3
	v_mul_f32_e32 v92, 0x45800000, v80
	v_cndmask_b32_e32 v80, v80, v92, vcc
	v_pk_mul_f32 v[90:91], v[90:91], v[80:81] op_sel_hi:[1,0]
	v_add_co_u32_e32 v92, vcc, s49, v82
	v_pk_fma_f32 v[66:67], v[66:67], v[90:91], v[70:71]
	v_pk_mul_f32 v[70:71], v[88:89], v[80:81] op_sel_hi:[1,0]
	v_cvt_pk_f16_f32 v66, v66, v67
	v_pk_fma_f32 v[68:69], v[68:69], v[70:71], v[72:73]
	v_addc_co_u32_e32 v93, vcc, 0, v83, vcc
	v_cvt_pk_f16_f32 v67, v68, v69
	ds_write_b64 v101, v[66:67]
	s_waitcnt lgkmcnt(0)
	s_barrier
	global_load_dwordx4 v[66:69], v[82:83], off
	global_load_dwordx4 v[70:73], v[84:85], off
	s_nop 0
	global_load_dwordx4 v[82:85], v[92:93], off
	global_load_dwordx4 v[88:91], v[94:95], off
	v_lshl_add_u32 v80, s4, 1, v87
	s_add_i32 s4, s1, 0x140
	s_and_b32 s5, s4, 0x1c0
	s_lshl_b32 s4, s4, 4
	s_or_b32 s46, s4, 0x2000
	s_or_b32 s40, s4, 0x6000
	s_sub_i32 s4, s38, s52
	s_and_b32 s4, s4, 0xe0
	v_lshl_add_u32 v169, s4, 1, v87
	s_add_i32 s4, s1, 0x180
	s_lshl_b32 s42, s5, 4
	s_and_b32 s5, s4, 0x1c0
	s_lshl_b32 s4, s4, 4
	s_or_b32 s38, s4, 0x2000
	s_or_b32 s34, s4, 0x6000
	s_add_i32 s4, s52, 0x60
	v_mov_b32_e32 v101, v75
	s_and_b32 s4, s4, 0xe0
	v_lshlrev_b64 v[92:93], 10, v[100:101]
	v_lshl_add_u32 v170, s4, 1, v87
	s_add_i32 s4, s1, 0x1c0
	s_xor_b32 s1, s1, 0x100
	v_lshl_add_u64 v[162:163], v[102:103], 0, v[92:93]
	v_lshlrev_b64 v[92:93], 10, v[74:75]
	v_add_u32_e32 v171, s1, v87
	s_add_i32 s1, s52, 0xa0
	v_lshl_add_u64 v[164:165], v[102:103], 0, v[92:93]
	ds_read_b128 v[92:95], v168
	ds_read_b128 v[96:99], v168 offset:8448
	s_and_b32 s1, s1, 0xe0
	v_lshl_add_u32 v172, s1, 1, v87
	s_add_i32 s1, s52, 0xc0
	v_or_b32_e32 v74, 2, v100
	s_lshl_b32 s36, s5, 4
	s_and_b32 s5, s4, 0x1c0
	s_lshl_b32 s4, s4, 4
	s_and_b32 s1, s1, 0xe0
	s_addk_i32 s52, 0xe0
	v_lshlrev_b64 v[104:105], 10, v[74:75]
	v_or_b32_e32 v74, 3, v100
	s_lshl_b32 s6, s5, 4
	s_or_b32 s10, s4, 0x2000
	s_or_b32 s4, s4, 0x6000
	s_mov_b32 s5, s3
	v_lshl_add_u32 v173, s1, 1, v87
	s_and_b32 s1, s52, 0xe0
	v_lshlrev_b64 v[74:75], 10, v[74:75]
	v_lshl_add_u64 v[132:133], v[78:79], 0, s[42:43]
	v_lshl_add_u64 v[134:135], v[78:79], 0, s[46:47]
	v_lshl_add_u64 v[136:137], v[78:79], 0, s[40:41]
	v_lshl_add_u64 v[138:139], v[78:79], 0, s[36:37]
	v_lshl_add_u64 v[140:141], v[78:79], 0, s[38:39]
	v_lshl_add_u64 v[142:143], v[78:79], 0, s[34:35]
	v_lshl_add_u64 v[144:145], v[78:79], 0, s[6:7]
	v_lshl_add_u64 v[146:147], v[78:79], 0, s[10:11]
	v_lshl_add_u64 v[78:79], v[78:79], 0, s[4:5]
	v_lshl_add_u32 v87, s1, 1, v87
	v_lshl_add_u64 v[166:167], v[102:103], 0, v[104:105]
	v_lshl_add_u64 v[74:75], v[102:103], 0, v[74:75]
	s_setprio 1
	s_waitcnt vmcnt(15) lgkmcnt(1)
	v_mfma_f32_16x16x32_f16 v[100:103], v[92:95], v[26:29], 0
	s_waitcnt lgkmcnt(0)
	v_mfma_f32_16x16x32_f16 v[26:29], v[96:99], v[26:29], 0
	s_waitcnt vmcnt(14)
	v_mfma_f32_16x16x32_f16 v[104:107], v[92:95], v[22:25], 0
	v_mfma_f32_16x16x32_f16 v[22:25], v[96:99], v[22:25], 0
	s_waitcnt vmcnt(13)
	v_mfma_f32_16x16x32_f16 v[108:111], v[92:95], v[18:21], 0
	v_mfma_f32_16x16x32_f16 v[18:21], v[96:99], v[18:21], 0
	s_waitcnt vmcnt(12)
	v_mfma_f32_16x16x32_f16 v[92:95], v[92:95], v[14:17], 0
	v_mfma_f32_16x16x32_f16 v[14:17], v[96:99], v[14:17], 0
	s_setprio 0
	v_add_co_u32_e32 v112, vcc, s48, v120
	global_load_dwordx4 v[96:99], v[120:121], off
	s_nop 0
	v_addc_co_u32_e32 v113, vcc, 0, v121, vcc
	v_add_co_u32_e32 v116, vcc, s49, v120
	s_nop 1
	v_addc_co_u32_e32 v117, vcc, 0, v121, vcc
	v_add_co_u32_e32 v120, vcc, s33, v120
	global_load_dwordx4 v[112:115], v[112:113], off
	s_nop 0
	global_load_dwordx4 v[116:119], v[116:117], off
	v_addc_co_u32_e32 v121, vcc, 0, v121, vcc
	global_load_dwordx4 v[120:123], v[120:121], off
	ds_read_b128 v[124:127], v80
	ds_read_b128 v[128:131], v80 offset:8448
	s_setprio 1
	s_waitcnt vmcnt(15) lgkmcnt(1)
	v_mfma_f32_16x16x32_f16 v[100:103], v[124:127], v[42:45], v[100:103]
	s_waitcnt lgkmcnt(0)
	v_mfma_f32_16x16x32_f16 v[26:29], v[128:131], v[42:45], v[26:29]
	s_waitcnt vmcnt(14)
	v_mfma_f32_16x16x32_f16 v[42:45], v[124:127], v[38:41], v[104:107]
	v_mfma_f32_16x16x32_f16 v[22:25], v[128:131], v[38:41], v[22:25]
	s_waitcnt vmcnt(13)
	v_mfma_f32_16x16x32_f16 v[38:41], v[124:127], v[34:37], v[108:111]
	v_mfma_f32_16x16x32_f16 v[18:21], v[128:131], v[34:37], v[18:21]
	s_waitcnt vmcnt(12)
	v_mfma_f32_16x16x32_f16 v[34:37], v[124:127], v[30:33], v[92:95]
	v_mfma_f32_16x16x32_f16 v[14:17], v[128:131], v[30:33], v[14:17]
	s_setprio 0
	v_add_co_u32_e32 v104, vcc, s49, v132
	global_load_dwordx4 v[30:33], v[132:133], off
	global_load_dwordx4 v[92:95], v[134:135], off
	v_addc_co_u32_e32 v105, vcc, 0, v133, vcc
	global_load_dwordx4 v[104:107], v[104:105], off
	s_nop 0
	global_load_dwordx4 v[108:111], v[136:137], off
	ds_read_b128 v[124:127], v169
	ds_read_b128 v[128:131], v169 offset:8448
	s_setprio 1
	s_waitcnt vmcnt(15) lgkmcnt(1)
	v_mfma_f32_16x16x32_f16 v[100:103], v[124:127], v[62:65], v[100:103]
	s_waitcnt lgkmcnt(0)
	v_mfma_f32_16x16x32_f16 v[26:29], v[128:131], v[62:65], v[26:29]
	s_waitcnt vmcnt(14)
	v_mfma_f32_16x16x32_f16 v[42:45], v[124:127], v[58:61], v[42:45]
	v_mfma_f32_16x16x32_f16 v[22:25], v[128:131], v[58:61], v[22:25]
	s_waitcnt vmcnt(13)
	v_mfma_f32_16x16x32_f16 v[38:41], v[124:127], v[54:57], v[38:41]
	v_mfma_f32_16x16x32_f16 v[18:21], v[128:131], v[54:57], v[18:21]
	s_waitcnt vmcnt(12)
	v_mfma_f32_16x16x32_f16 v[34:37], v[124:127], v[46:49], v[34:37]
	v_mfma_f32_16x16x32_f16 v[14:17], v[128:131], v[46:49], v[14:17]
	s_setprio 0
	v_add_co_u32_e32 v58, vcc, s49, v138
	global_load_dwordx4 v[46:49], v[138:139], off
	global_load_dwordx4 v[54:57], v[140:141], off
	v_addc_co_u32_e32 v59, vcc, 0, v139, vcc
	global_load_dwordx4 v[58:61], v[58:59], off
	s_nop 0
	global_load_dwordx4 v[62:65], v[142:143], off
	ds_read_b128 v[124:127], v170
	ds_read_b128 v[128:131], v170 offset:8448
	s_setprio 1
	s_waitcnt vmcnt(15) lgkmcnt(1)
	v_mfma_f32_16x16x32_f16 v[100:103], v[124:127], v[66:69], v[100:103]
	s_waitcnt lgkmcnt(0)
	v_mfma_f32_16x16x32_f16 v[26:29], v[128:131], v[66:69], v[26:29]
	s_waitcnt vmcnt(14)
	v_mfma_f32_16x16x32_f16 v[42:45], v[124:127], v[70:73], v[42:45]
	v_mfma_f32_16x16x32_f16 v[22:25], v[128:131], v[70:73], v[22:25]
	s_waitcnt vmcnt(13)
	v_mfma_f32_16x16x32_f16 v[38:41], v[124:127], v[82:85], v[38:41]
	v_mfma_f32_16x16x32_f16 v[18:21], v[128:131], v[82:85], v[18:21]
	s_waitcnt vmcnt(12)
	v_mfma_f32_16x16x32_f16 v[34:37], v[124:127], v[88:91], v[34:37]
	v_mfma_f32_16x16x32_f16 v[14:17], v[128:131], v[88:91], v[14:17]
	s_setprio 0
	v_add_co_u32_e32 v82, vcc, s49, v144
	global_load_dwordx4 v[66:69], v[144:145], off
	global_load_dwordx4 v[70:73], v[146:147], off
	v_addc_co_u32_e32 v83, vcc, 0, v145, vcc
	global_load_dwordx4 v[82:85], v[82:83], off
	s_nop 0
	global_load_dwordx4 v[88:91], v[78:79], off
	ds_read_b128 v[124:127], v171
	ds_read_b128 v[128:131], v171 offset:8448
	s_setprio 1
	s_waitcnt vmcnt(15) lgkmcnt(1)
	v_mfma_f32_16x16x32_f16 v[100:103], v[124:127], v[96:99], v[100:103]
	s_waitcnt lgkmcnt(0)
	v_mfma_f32_16x16x32_f16 v[26:29], v[128:131], v[96:99], v[26:29]
	s_waitcnt vmcnt(14)
	v_mfma_f32_16x16x32_f16 v[42:45], v[124:127], v[112:115], v[42:45]
	v_mfma_f32_16x16x32_f16 v[22:25], v[128:131], v[112:115], v[22:25]
	s_waitcnt vmcnt(13)
	v_mfma_f32_16x16x32_f16 v[38:41], v[124:127], v[116:119], v[38:41]
	v_mfma_f32_16x16x32_f16 v[18:21], v[128:131], v[116:119], v[18:21]
	s_waitcnt vmcnt(12)
	v_mfma_f32_16x16x32_f16 v[34:37], v[124:127], v[120:123], v[34:37]
	v_mfma_f32_16x16x32_f16 v[14:17], v[128:131], v[120:123], v[14:17]
	s_setprio 0
	ds_read_b128 v[96:99], v172
	ds_read_b128 v[112:115], v172 offset:8448
	s_setprio 1
	s_waitcnt vmcnt(11) lgkmcnt(1)
	v_mfma_f32_16x16x32_f16 v[100:103], v[96:99], v[30:33], v[100:103]
	s_waitcnt lgkmcnt(0)
	v_mfma_f32_16x16x32_f16 v[26:29], v[112:115], v[30:33], v[26:29]
	s_waitcnt vmcnt(10)
	v_mfma_f32_16x16x32_f16 v[30:33], v[96:99], v[92:95], v[42:45]
	v_mfma_f32_16x16x32_f16 v[22:25], v[112:115], v[92:95], v[22:25]
	s_waitcnt vmcnt(9)
	v_mfma_f32_16x16x32_f16 v[38:41], v[96:99], v[104:107], v[38:41]
	v_mfma_f32_16x16x32_f16 v[18:21], v[112:115], v[104:107], v[18:21]
	s_waitcnt vmcnt(8)
	v_mfma_f32_16x16x32_f16 v[34:37], v[96:99], v[108:111], v[34:37]
	v_mfma_f32_16x16x32_f16 v[14:17], v[112:115], v[108:111], v[14:17]
	s_setprio 0
	ds_read_b128 v[42:45], v173
	ds_read_b128 v[92:95], v173 offset:8448
	s_setprio 1
	s_waitcnt vmcnt(7) lgkmcnt(1)
	v_mfma_f32_16x16x32_f16 v[96:99], v[42:45], v[46:49], v[100:103]
	s_waitcnt lgkmcnt(0)
	v_mfma_f32_16x16x32_f16 v[26:29], v[92:95], v[46:49], v[26:29]
	s_waitcnt vmcnt(6)
	v_mfma_f32_16x16x32_f16 v[30:33], v[42:45], v[54:57], v[30:33]
	v_mfma_f32_16x16x32_f16 v[22:25], v[92:95], v[54:57], v[22:25]
	s_waitcnt vmcnt(5)
	v_mfma_f32_16x16x32_f16 v[38:41], v[42:45], v[58:61], v[38:41]
	v_mfma_f32_16x16x32_f16 v[18:21], v[92:95], v[58:61], v[18:21]
	s_waitcnt vmcnt(4)
	v_mfma_f32_16x16x32_f16 v[34:37], v[42:45], v[62:65], v[34:37]
	v_mfma_f32_16x16x32_f16 v[14:17], v[92:95], v[62:65], v[14:17]
	s_setprio 0
	ds_read_b128 v[42:45], v87
	ds_read_b128 v[46:49], v87 offset:8448
	s_setprio 1
	s_waitcnt vmcnt(3) lgkmcnt(1)
	v_mfma_f32_16x16x32_f16 v[54:57], v[42:45], v[66:69], v[96:99]
	s_waitcnt lgkmcnt(0)
	v_mfma_f32_16x16x32_f16 v[26:29], v[46:49], v[66:69], v[26:29]
	s_waitcnt vmcnt(2)
	v_mfma_f32_16x16x32_f16 v[30:33], v[42:45], v[70:73], v[30:33]
	v_mfma_f32_16x16x32_f16 v[22:25], v[46:49], v[70:73], v[22:25]
	s_waitcnt vmcnt(1)
	v_mfma_f32_16x16x32_f16 v[38:41], v[42:45], v[82:85], v[38:41]
	v_mfma_f32_16x16x32_f16 v[18:21], v[46:49], v[82:85], v[18:21]
	s_waitcnt vmcnt(0)
	v_mfma_f32_16x16x32_f16 v[34:37], v[42:45], v[88:91], v[34:37]
	v_mfma_f32_16x16x32_f16 v[14:17], v[46:49], v[88:91], v[14:17]
	s_setprio 0
	v_add_co_u32_e32 v78, vcc, s48, v148
	v_lshlrev_b32_e32 v116, 4, v1
	s_nop 0
	v_addc_co_u32_e32 v79, vcc, 0, v149, vcc
	v_add_co_u32_e32 v42, vcc, s49, v148
	v_or_b32_e32 v1, v116, v86
	s_nop 0
	v_addc_co_u32_e32 v43, vcc, 0, v149, vcc
	v_add_co_u32_e32 v66, vcc, s33, v148
	s_movk_i32 s2, 0x50
	s_nop 0
	v_addc_co_u32_e32 v67, vcc, 0, v149, vcc
	v_add_co_u32_e32 v108, vcc, s49, v150
	v_or_b32_e32 v117, 16, v116
	s_nop 0
	v_addc_co_u32_e32 v109, vcc, 0, v151, vcc
	v_add_co_u32_e32 v110, vcc, s49, v156
	global_load_dwordx4 v[42:45], v[42:43], off
	s_nop 0
	global_load_dwordx4 v[46:49], v[66:67], off
	global_load_dwordx4 v[58:61], v[148:149], off
	global_load_dwordx4 v[62:65], v[150:151], off
	s_nop 0
	global_load_dwordx4 v[66:69], v[152:153], off
	global_load_dwordx4 v[70:73], v[154:155], off
	global_load_dwordx4 v[82:85], v[156:157], off
	global_load_dwordx4 v[88:91], v[158:159], off
	v_addc_co_u32_e32 v111, vcc, 0, v157, vcc
	global_load_dwordx4 v[92:95], v[108:109], off
	global_load_dwordx4 v[96:99], v[110:111], off
	global_load_dwordx4 v[100:103], v[78:79], off
	global_load_dwordx4 v[104:107], v[160:161], off
	s_nop 0
	global_store_dwordx4 v[162:163], v[2:5], off sc0 sc1
	global_store_dwordx4 v[164:165], v[6:9], off sc0 sc1
	global_store_dwordx4 v[166:167], v[10:13], off sc0 sc1
	global_store_dwordx4 v[74:75], v[50:53], off sc0 sc1
	v_cvt_pk_f16_f32 v3, v56, v57
	v_cvt_pk_f16_f32 v2, v54, v55
	v_mad_u32_u24 v1, v1, s2, v81
	v_or_b32_e32 v4, v117, v86
	v_or_b32_e32 v118, 32, v116
	ds_write_b64 v1, v[2:3]
	v_cvt_pk_f16_f32 v3, v32, v33
	v_cvt_pk_f16_f32 v2, v30, v31
	v_mad_u32_u24 v4, v4, s2, v81
	v_or_b32_e32 v5, v118, v86
	v_and_or_b32 v119, v0, s50, 48
	ds_write_b64 v4, v[2:3]
	v_cvt_pk_f16_f32 v3, v40, v41
	v_cvt_pk_f16_f32 v2, v38, v39
	v_mad_u32_u24 v5, v5, s2, v81
	v_or_b32_e32 v6, v119, v86
	ds_write_b64 v5, v[2:3]
	v_cvt_pk_f16_f32 v3, v36, v37
	v_cvt_pk_f16_f32 v2, v34, v35
	v_mad_u32_u24 v6, v6, s2, v81
	ds_write_b64 v6, v[2:3]
	v_cvt_pk_f16_f32 v3, v28, v29
	v_cvt_pk_f16_f32 v2, v26, v27
	ds_write_b64 v1, v[2:3] offset:32
	v_cvt_pk_f16_f32 v3, v24, v25
	v_cvt_pk_f16_f32 v2, v22, v23
	v_lshl_add_u64 v[10:11], v[76:77], 0, s[16:17]
	ds_write_b64 v4, v[2:3] offset:32
	v_cvt_pk_f16_f32 v3, v20, v21
	v_cvt_pk_f16_f32 v2, v18, v19
	v_add_co_u32_e32 v18, vcc, s49, v10
	ds_write_b64 v5, v[2:3] offset:32
	v_cvt_pk_f16_f32 v3, v16, v17
	v_cvt_pk_f16_f32 v2, v14, v15
	v_lshl_add_u64 v[12:13], v[76:77], 0, s[14:15]
	v_addc_co_u32_e32 v19, vcc, 0, v11, vcc
	ds_write_b64 v6, v[2:3] offset:32
	s_waitcnt lgkmcnt(0)
	s_barrier
	global_load_dwordx4 v[2:5], v[10:11], off
	global_load_dwordx4 v[6:9], v[12:13], off
	v_lshl_add_u64 v[20:21], v[76:77], 0, s[18:19]
	global_load_dwordx4 v[10:13], v[18:19], off
	global_load_dwordx4 v[14:17], v[20:21], off
	ds_read_b128 v[18:21], v168
	ds_read_b128 v[22:25], v168 offset:8448
	s_mov_b32 s1, s3
	s_setprio 1
	s_waitcnt vmcnt(17) lgkmcnt(1)
	v_mfma_f32_16x16x32_f16 v[26:29], v[18:21], v[58:61], 0
	s_waitcnt lgkmcnt(0)
	v_mfma_f32_16x16x32_f16 v[30:33], v[22:25], v[58:61], 0
	s_waitcnt vmcnt(9)
	v_mfma_f32_16x16x32_f16 v[34:37], v[18:21], v[100:103], 0
	v_mfma_f32_16x16x32_f16 v[38:41], v[22:25], v[100:103], 0
	v_mfma_f32_16x16x32_f16 v[50:53], v[18:21], v[42:45], 0
	v_mfma_f32_16x16x32_f16 v[42:45], v[22:25], v[42:45], 0
	v_mfma_f32_16x16x32_f16 v[18:21], v[18:21], v[46:49], 0
	v_mfma_f32_16x16x32_f16 v[22:25], v[22:25], v[46:49], 0
	s_setprio 0
	v_lshl_add_u64 v[58:59], v[76:77], 0, s[44:45]
	v_add_co_u32_e32 v60, vcc, s48, v58
	s_nop 1
	v_addc_co_u32_e32 v61, vcc, 0, v59, vcc
	v_add_co_u32_e32 v74, vcc, s49, v58
	global_load_dwordx4 v[46:49], v[58:59], off
	global_load_dwordx4 v[54:57], v[60:61], off
	v_addc_co_u32_e32 v75, vcc, 0, v59, vcc
	v_add_co_u32_e32 v78, vcc, s33, v58
	s_nop 1
	v_addc_co_u32_e32 v79, vcc, 0, v59, vcc
	global_load_dwordx4 v[58:61], v[74:75], off
	global_load_dwordx4 v[100:103], v[78:79], off
	ds_read_b128 v[108:111], v80
	ds_read_b128 v[112:115], v80 offset:8448
	s_setprio 1
	s_waitcnt lgkmcnt(1)
	v_mfma_f32_16x16x32_f16 v[26:29], v[108:111], v[62:65], v[26:29]
	s_waitcnt lgkmcnt(0)
	v_mfma_f32_16x16x32_f16 v[30:33], v[112:115], v[62:65], v[30:33]
	v_mfma_f32_16x16x32_f16 v[34:37], v[108:111], v[66:69], v[34:37]
	v_mfma_f32_16x16x32_f16 v[38:41], v[112:115], v[66:69], v[38:41]
	v_mfma_f32_16x16x32_f16 v[50:53], v[108:111], v[92:95], v[50:53]
	v_mfma_f32_16x16x32_f16 v[42:45], v[112:115], v[92:95], v[42:45]
	v_mfma_f32_16x16x32_f16 v[18:21], v[108:111], v[70:73], v[18:21]
	v_mfma_f32_16x16x32_f16 v[22:25], v[112:115], v[70:73], v[22:25]
	s_setprio 0
	v_lshl_add_u64 v[70:71], v[76:77], 0, s[42:43]
	v_add_co_u32_e32 v74, vcc, s49, v70
	v_lshl_add_u64 v[72:73], v[76:77], 0, s[46:47]
	s_nop 0
	v_addc_co_u32_e32 v75, vcc, 0, v71, vcc
	global_load_dwordx4 v[62:65], v[70:71], off
	global_load_dwordx4 v[66:69], v[72:73], off
	v_lshl_add_u64 v[78:79], v[76:77], 0, s[40:41]
	global_load_dwordx4 v[70:73], v[74:75], off
	global_load_dwordx4 v[92:95], v[78:79], off
	ds_read_b128 v[108:111], v169
	ds_read_b128 v[112:115], v169 offset:8448
	s_setprio 1
	s_waitcnt lgkmcnt(1)
	v_mfma_f32_16x16x32_f16 v[26:29], v[108:111], v[82:85], v[26:29]
	s_waitcnt lgkmcnt(0)
	v_mfma_f32_16x16x32_f16 v[30:33], v[112:115], v[82:85], v[30:33]
	v_mfma_f32_16x16x32_f16 v[34:37], v[108:111], v[88:91], v[34:37]
	v_mfma_f32_16x16x32_f16 v[38:41], v[112:115], v[88:91], v[38:41]
	v_mfma_f32_16x16x32_f16 v[50:53], v[108:111], v[96:99], v[50:53]
	v_mfma_f32_16x16x32_f16 v[42:45], v[112:115], v[96:99], v[42:45]
	s_waitcnt vmcnt(16)
	v_mfma_f32_16x16x32_f16 v[18:21], v[108:111], v[104:107], v[18:21]
	v_mfma_f32_16x16x32_f16 v[22:25], v[112:115], v[104:107], v[22:25]
	s_setprio 0
	v_lshl_add_u64 v[74:75], v[76:77], 0, s[36:37]
	v_lshl_add_u64 v[78:79], v[76:77], 0, s[38:39]
	global_load_dwordx4 v[82:85], v[74:75], off
	global_load_dwordx4 v[88:91], v[78:79], off
	v_add_co_u32_e32 v74, vcc, s49, v74
	v_lshl_add_u64 v[78:79], v[76:77], 0, s[34:35]
	s_nop 0
	v_addc_co_u32_e32 v75, vcc, 0, v75, vcc
	global_load_dwordx4 v[96:99], v[74:75], off
	global_load_dwordx4 v[104:107], v[78:79], off
	ds_read_b128 v[108:111], v170
	ds_read_b128 v[112:115], v170 offset:8448
	s_setprio 1
	s_waitcnt vmcnt(15) lgkmcnt(1)
	v_mfma_f32_16x16x32_f16 v[26:29], v[108:111], v[2:5], v[26:29]
	s_waitcnt lgkmcnt(0)
	v_mfma_f32_16x16x32_f16 v[2:5], v[112:115], v[2:5], v[30:33]
	s_waitcnt vmcnt(14)
	v_mfma_f32_16x16x32_f16 v[30:33], v[108:111], v[6:9], v[34:37]
	v_mfma_f32_16x16x32_f16 v[6:9], v[112:115], v[6:9], v[38:41]
	s_waitcnt vmcnt(13)
	v_mfma_f32_16x16x32_f16 v[34:37], v[108:111], v[10:13], v[50:53]
	v_mfma_f32_16x16x32_f16 v[10:13], v[112:115], v[10:13], v[42:45]
	s_waitcnt vmcnt(12)
	v_mfma_f32_16x16x32_f16 v[18:21], v[108:111], v[14:17], v[18:21]
	v_mfma_f32_16x16x32_f16 v[14:17], v[112:115], v[14:17], v[22:25]
	s_setprio 0
	v_lshl_add_u64 v[42:43], v[76:77], 0, s[6:7]
	v_add_co_u32_e32 v74, vcc, s49, v42
	v_lshl_add_u64 v[44:45], v[76:77], 0, s[10:11]
	s_nop 0
	v_addc_co_u32_e32 v75, vcc, 0, v43, vcc
	global_load_dwordx4 v[22:25], v[42:43], off
	global_load_dwordx4 v[38:41], v[44:45], off
	v_lshl_add_u64 v[76:77], v[76:77], 0, s[4:5]
	global_load_dwordx4 v[42:45], v[74:75], off
	global_load_dwordx4 v[50:53], v[76:77], off
	ds_read_b128 v[74:77], v171
	ds_read_b128 v[108:111], v171 offset:8448
	s_setprio 1
	s_waitcnt vmcnt(15) lgkmcnt(1)
	v_mfma_f32_16x16x32_f16 v[26:29], v[74:77], v[46:49], v[26:29]
	s_waitcnt lgkmcnt(0)
	v_mfma_f32_16x16x32_f16 v[2:5], v[108:111], v[46:49], v[2:5]
	s_waitcnt vmcnt(14)
	v_mfma_f32_16x16x32_f16 v[30:33], v[74:77], v[54:57], v[30:33]
	v_mfma_f32_16x16x32_f16 v[6:9], v[108:111], v[54:57], v[6:9]
	s_waitcnt vmcnt(13)
	v_mfma_f32_16x16x32_f16 v[34:37], v[74:77], v[58:61], v[34:37]
	v_mfma_f32_16x16x32_f16 v[10:13], v[108:111], v[58:61], v[10:13]
	s_waitcnt vmcnt(12)
	v_mfma_f32_16x16x32_f16 v[18:21], v[74:77], v[100:103], v[18:21]
	v_mfma_f32_16x16x32_f16 v[14:17], v[108:111], v[100:103], v[14:17]
	s_setprio 0
	ds_read_b128 v[46:49], v172
	ds_read_b128 v[54:57], v172 offset:8448
	s_setprio 1
	s_waitcnt vmcnt(11) lgkmcnt(1)
	v_mfma_f32_16x16x32_f16 v[26:29], v[46:49], v[62:65], v[26:29]
	s_waitcnt lgkmcnt(0)
	v_mfma_f32_16x16x32_f16 v[2:5], v[54:57], v[62:65], v[2:5]
	s_waitcnt vmcnt(10)
	v_mfma_f32_16x16x32_f16 v[30:33], v[46:49], v[66:69], v[30:33]
	v_mfma_f32_16x16x32_f16 v[6:9], v[54:57], v[66:69], v[6:9]
	s_waitcnt vmcnt(9)
	v_mfma_f32_16x16x32_f16 v[34:37], v[46:49], v[70:73], v[34:37]
	v_mfma_f32_16x16x32_f16 v[10:13], v[54:57], v[70:73], v[10:13]
	s_waitcnt vmcnt(8)
	v_mfma_f32_16x16x32_f16 v[18:21], v[46:49], v[92:95], v[18:21]
	v_mfma_f32_16x16x32_f16 v[14:17], v[54:57], v[92:95], v[14:17]
	s_setprio 0
	ds_read_b128 v[46:49], v173
	ds_read_b128 v[54:57], v173 offset:8448
	s_setprio 1
	s_waitcnt vmcnt(7) lgkmcnt(1)
	v_mfma_f32_16x16x32_f16 v[26:29], v[46:49], v[82:85], v[26:29]
	s_waitcnt lgkmcnt(0)
	v_mfma_f32_16x16x32_f16 v[2:5], v[54:57], v[82:85], v[2:5]
	s_waitcnt vmcnt(6)
	v_mfma_f32_16x16x32_f16 v[30:33], v[46:49], v[88:91], v[30:33]
	v_mfma_f32_16x16x32_f16 v[6:9], v[54:57], v[88:91], v[6:9]
	s_waitcnt vmcnt(5)
	v_mfma_f32_16x16x32_f16 v[34:37], v[46:49], v[96:99], v[34:37]
	v_mfma_f32_16x16x32_f16 v[58:61], v[54:57], v[96:99], v[10:13]
	s_waitcnt vmcnt(4)
	v_mfma_f32_16x16x32_f16 v[18:21], v[46:49], v[104:107], v[18:21]
	v_mfma_f32_16x16x32_f16 v[46:49], v[54:57], v[104:107], v[14:17]
	s_setprio 0
	ds_read_b128 v[54:57], v87
	ds_read_b128 v[62:65], v87 offset:8448
	s_setprio 1
	s_waitcnt vmcnt(3) lgkmcnt(1)
	v_mfma_f32_16x16x32_f16 v[26:29], v[54:57], v[22:25], v[26:29]
	s_waitcnt lgkmcnt(0)
	v_mfma_f32_16x16x32_f16 v[14:17], v[62:65], v[22:25], v[2:5]
	s_waitcnt vmcnt(2)
	v_mfma_f32_16x16x32_f16 v[22:25], v[54:57], v[38:41], v[30:33]
	v_mfma_f32_16x16x32_f16 v[10:13], v[62:65], v[38:41], v[6:9]
	s_waitcnt vmcnt(1)
	v_mfma_f32_16x16x32_f16 v[30:33], v[54:57], v[42:45], v[34:37]
	v_mfma_f32_16x16x32_f16 v[6:9], v[62:65], v[42:45], v[58:61]
	s_waitcnt vmcnt(0)
	v_mfma_f32_16x16x32_f16 v[34:37], v[54:57], v[50:53], v[18:21]
	v_mfma_f32_16x16x32_f16 v[2:5], v[62:65], v[50:53], v[46:49]
	s_setprio 0
	v_mul_u32_u24_e32 v52, 0x50, v0
	ds_read_b128 v[18:21], v52
	s_lshl_b64 s[0:1], s[0:1], 15
	v_lshl_or_b32 v0, v0, 4, s0
	v_mov_b32_e32 v1, s1
	v_lshl_add_u64 v[50:51], s[12:13], 0, v[0:1]
	ds_read_b128 v[38:41], v52 offset:16
	ds_read_b128 v[42:45], v52 offset:32
	ds_read_b128 v[46:49], v52 offset:48
	s_waitcnt lgkmcnt(3)
	global_store_dwordx4 v[50:51], v[18:21], off sc0 sc1
	s_add_u32 s0, s12, 0x800000
	s_nop 0
	v_add_co_u32_e32 v18, vcc, s48, v50
	s_nop 1
	v_addc_co_u32_e32 v19, vcc, 0, v51, vcc
	s_waitcnt lgkmcnt(2)
	global_store_dwordx4 v[18:19], v[38:41], off sc0 sc1
	v_or_b32_e32 v18, 0x4000, v0
	v_mov_b32_e32 v19, s1
	v_lshl_add_u64 v[20:21], s[12:13], 0, v[18:19]
	s_waitcnt lgkmcnt(1)
	global_store_dwordx4 v[20:21], v[42:45], off sc0 sc1
	v_mul_f32_e32 v20, 0xbfb8aa3b, v26
	v_exp_f32_e32 v38, v20
	v_add_co_u32_e32 v20, vcc, s33, v50
	v_or_b32_e32 v39, 0x200, v86
	s_nop 0
	v_addc_co_u32_e32 v21, vcc, 0, v51, vcc
	s_waitcnt lgkmcnt(0)
	global_store_dwordx4 v[20:21], v[46:49], off sc0 sc1
	v_add_f32_e32 v20, 1.0, v38
	v_rcp_f32_e32 v20, v20
	v_mul_f32_e32 v21, 0xbfb8aa3b, v27
	v_mul_f32_e32 v38, 0xbfb8aa3b, v28
	v_exp_f32_e32 v21, v21
	v_exp_f32_e32 v38, v38
	v_fma_mixlo_f16 v40, v26, v20, 0
	v_mul_f32_e32 v26, 0xbfb8aa3b, v29
	v_add_f32_e32 v20, 1.0, v21
	v_add_f32_e32 v21, 1.0, v38
	v_exp_f32_e32 v38, v26
	v_rcp_f32_e32 v20, v20
	v_rcp_f32_e32 v21, v21
	v_mov_b32_e32 v26, v27
	v_mov_b32_e32 v27, v28
	v_add_f32_e32 v28, 1.0, v38
	v_rcp_f32_e32 v28, v28
	v_pk_mul_f32 v[20:21], v[26:27], v[20:21]
	v_or_b32_e32 v27, v116, v39
	v_cvt_pk_f16_f32 v21, v20, v21
	v_fma_mixlo_f16 v26, v29, v28, 0
	v_pack_b32_f16 v20, v40, v21
	v_alignbit_b32 v21, v26, v21, 16
	v_mul_f32_e32 v26, 0xbfb8aa3b, v22
	v_exp_f32_e32 v26, v26
	v_mad_u32_u24 v27, v27, s2, v81
	ds_write_b64 v27, v[20:21]
	v_mul_f32_e32 v21, 0xbfb8aa3b, v23
	v_add_f32_e32 v20, 1.0, v26
	v_rcp_f32_e32 v20, v20
	v_mul_f32_e32 v26, 0xbfb8aa3b, v24
	v_exp_f32_e32 v21, v21
	v_exp_f32_e32 v26, v26
	v_fma_mixlo_f16 v28, v22, v20, 0
	v_mul_f32_e32 v22, 0xbfb8aa3b, v25
	v_add_f32_e32 v20, 1.0, v21
	v_add_f32_e32 v21, 1.0, v26
	v_exp_f32_e32 v26, v22
	v_rcp_f32_e32 v20, v20
	v_rcp_f32_e32 v21, v21
	v_mov_b32_e32 v22, v23
	v_mov_b32_e32 v23, v24
	v_add_f32_e32 v24, 1.0, v26
	v_rcp_f32_e32 v24, v24
	v_pk_mul_f32 v[20:21], v[22:23], v[20:21]
	v_or_b32_e32 v23, v117, v39
	v_cvt_pk_f16_f32 v21, v20, v21
	v_fma_mixlo_f16 v22, v25, v24, 0
	v_pack_b32_f16 v20, v28, v21
	v_alignbit_b32 v21, v22, v21, 16
	v_mul_f32_e32 v22, 0xbfb8aa3b, v30
	v_exp_f32_e32 v22, v22
	v_mad_u32_u24 v24, v23, s2, v81
	ds_write_b64 v24, v[20:21]
	v_mul_f32_e32 v21, 0xbfb8aa3b, v31
	v_add_f32_e32 v20, 1.0, v22
	v_mul_f32_e32 v22, 0xbfb8aa3b, v32
	v_rcp_f32_e32 v20, v20
	v_exp_f32_e32 v21, v21
	v_exp_f32_e32 v22, v22
	v_mov_b32_e32 v23, v32
	v_fma_mixlo_f16 v25, v30, v20, 0
	v_add_f32_e32 v20, 1.0, v21
	v_add_f32_e32 v21, 1.0, v22
	v_mul_f32_e32 v22, 0xbfb8aa3b, v33
	v_exp_f32_e32 v26, v22
	v_rcp_f32_e32 v20, v20
	v_rcp_f32_e32 v21, v21
	v_mov_b32_e32 v22, v31
	v_add_f32_e32 v26, 1.0, v26
	v_rcp_f32_e32 v26, v26
	v_pk_mul_f32 v[20:21], v[22:23], v[20:21]
	v_or_b32_e32 v23, v118, v39
	v_cvt_pk_f16_f32 v21, v20, v21
	v_fma_mixlo_f16 v22, v33, v26, 0
	v_pack_b32_f16 v20, v25, v21
	v_alignbit_b32 v21, v22, v21, 16
	v_mul_f32_e32 v22, 0xbfb8aa3b, v34
	v_exp_f32_e32 v22, v22
	v_mad_u32_u24 v25, v23, s2, v81
	ds_write_b64 v25, v[20:21]
	v_mul_f32_e32 v21, 0xbfb8aa3b, v35
	v_add_f32_e32 v20, 1.0, v22
	v_mul_f32_e32 v22, 0xbfb8aa3b, v36
	v_rcp_f32_e32 v20, v20
	v_exp_f32_e32 v21, v21
	v_exp_f32_e32 v22, v22
	v_mov_b32_e32 v23, v36
	v_fma_mixlo_f16 v26, v34, v20, 0
	v_add_f32_e32 v20, 1.0, v21
	v_add_f32_e32 v21, 1.0, v22
	v_mul_f32_e32 v22, 0xbfb8aa3b, v37
	v_exp_f32_e32 v28, v22
	v_rcp_f32_e32 v20, v20
	v_rcp_f32_e32 v21, v21
	v_mov_b32_e32 v22, v35
	v_add_f32_e32 v28, 1.0, v28
	v_rcp_f32_e32 v28, v28
	v_pk_mul_f32 v[20:21], v[22:23], v[20:21]
	v_or_b32_e32 v23, v119, v39
	v_cvt_pk_f16_f32 v21, v20, v21
	v_fma_mixlo_f16 v22, v37, v28, 0
	v_pack_b32_f16 v20, v26, v21
	v_alignbit_b32 v21, v22, v21, 16
	v_mul_f32_e32 v22, 0xbfb8aa3b, v14
	v_exp_f32_e32 v22, v22
	v_mad_u32_u24 v23, v23, s2, v81
	ds_write_b64 v23, v[20:21]
	v_mul_f32_e32 v21, 0xbfb8aa3b, v15
	v_add_f32_e32 v20, 1.0, v22
	v_rcp_f32_e32 v20, v20
	v_exp_f32_e32 v21, v21
	v_mul_f32_e32 v22, 0xbfb8aa3b, v16
	v_exp_f32_e32 v22, v22
	v_fma_mixlo_f16 v26, v14, v20, 0
	v_add_f32_e32 v14, 1.0, v21
	v_rcp_f32_e32 v20, v14
	v_add_f32_e32 v14, 1.0, v22
	v_rcp_f32_e32 v21, v14
	v_mov_b32_e32 v14, v15
	v_mul_f32_e32 v15, 0xbfb8aa3b, v17
	v_exp_f32_e32 v22, v15
	v_mov_b32_e32 v15, v16
	v_pk_mul_f32 v[14:15], v[14:15], v[20:21]
	v_mul_f32_e32 v20, 0xbfb8aa3b, v10
	v_cvt_pk_f16_f32 v15, v14, v15
	v_add_f32_e32 v14, 1.0, v22
	v_rcp_f32_e32 v16, v14
	v_exp_f32_e32 v20, v20
	v_pack_b32_f16 v14, v26, v15
	s_addc_u32 s1, s13, 0
	v_fma_mixlo_f16 v16, v17, v16, 0
	v_alignbit_b32 v15, v16, v15, 16
	ds_write_b64 v27, v[14:15] offset:32
	v_add_f32_e32 v14, 1.0, v20
	v_mul_f32_e32 v15, 0xbfb8aa3b, v11
	v_rcp_f32_e32 v14, v14
	v_exp_f32_e32 v15, v15
	v_mul_f32_e32 v16, 0xbfb8aa3b, v12
	v_exp_f32_e32 v16, v16
	v_fma_mixlo_f16 v17, v10, v14, 0
	v_add_f32_e32 v10, 1.0, v15
	v_rcp_f32_e32 v14, v10
	v_add_f32_e32 v10, 1.0, v16
	v_rcp_f32_e32 v15, v10
	v_mov_b32_e32 v10, v11
	v_mul_f32_e32 v11, 0xbfb8aa3b, v13
	v_exp_f32_e32 v16, v11
	v_mov_b32_e32 v11, v12
	v_pk_mul_f32 v[10:11], v[10:11], v[14:15]
	v_mul_f32_e32 v14, 0xbfb8aa3b, v6
	v_cvt_pk_f16_f32 v11, v10, v11
	v_add_f32_e32 v10, 1.0, v16
	v_rcp_f32_e32 v12, v10
	v_exp_f32_e32 v14, v14
	v_pack_b32_f16 v10, v17, v11
	v_lshl_add_u64 v[0:1], s[0:1], 0, v[0:1]
	v_fma_mixlo_f16 v12, v13, v12, 0
	v_alignbit_b32 v11, v12, v11, 16
	ds_write_b64 v24, v[10:11] offset:32
	v_add_f32_e32 v10, 1.0, v14
	v_mul_f32_e32 v11, 0xbfb8aa3b, v7
	v_rcp_f32_e32 v10, v10
	v_exp_f32_e32 v11, v11
	v_mul_f32_e32 v12, 0xbfb8aa3b, v8
	v_exp_f32_e32 v12, v12
	v_fma_mixlo_f16 v13, v6, v10, 0
	v_add_f32_e32 v6, 1.0, v11
	v_rcp_f32_e32 v10, v6
	v_add_f32_e32 v6, 1.0, v12
	v_rcp_f32_e32 v11, v6
	v_mov_b32_e32 v6, v7
	v_mul_f32_e32 v7, 0xbfb8aa3b, v9
	v_exp_f32_e32 v12, v7
	v_mov_b32_e32 v7, v8
	v_pk_mul_f32 v[6:7], v[6:7], v[10:11]
	v_mul_f32_e32 v10, 0xbfb8aa3b, v2
	v_cvt_pk_f16_f32 v7, v6, v7
	v_add_f32_e32 v6, 1.0, v12
	v_rcp_f32_e32 v8, v6
	v_exp_f32_e32 v10, v10
	v_pack_b32_f16 v6, v13, v7
	v_fma_mixlo_f16 v8, v9, v8, 0
	v_alignbit_b32 v7, v8, v7, 16
	ds_write_b64 v25, v[6:7] offset:32
	v_add_f32_e32 v6, 1.0, v10
	v_mul_f32_e32 v7, 0xbfb8aa3b, v3
	v_rcp_f32_e32 v6, v6
	v_exp_f32_e32 v7, v7
	v_mul_f32_e32 v8, 0xbfb8aa3b, v4
	v_exp_f32_e32 v8, v8
	v_fma_mixlo_f16 v9, v2, v6, 0
	v_add_f32_e32 v2, 1.0, v7
	v_mul_f32_e32 v7, 0xbfb8aa3b, v5
	v_rcp_f32_e32 v6, v2
	v_add_f32_e32 v2, 1.0, v8
	v_exp_f32_e32 v8, v7
	v_rcp_f32_e32 v7, v2
	v_mov_b32_e32 v2, v3
	v_mov_b32_e32 v3, v4
	v_add_f32_e32 v4, 1.0, v8
	v_rcp_f32_e32 v4, v4
	v_pk_mul_f32 v[2:3], v[2:3], v[6:7]
	v_fma_mixlo_f16 v4, v5, v4, 0
	v_cvt_pk_f16_f32 v3, v2, v3
	v_pack_b32_f16 v2, v9, v3
	v_alignbit_b32 v3, v4, v3, 16
	ds_write_b64 v23, v[2:3] offset:32
	s_waitcnt lgkmcnt(0)
	s_barrier
	ds_read_b128 v[2:5], v52 offset:40960
	ds_read_b128 v[6:9], v52 offset:40976
	ds_read_b128 v[10:13], v52 offset:40992
	ds_read_b128 v[14:17], v52 offset:41008
	s_waitcnt lgkmcnt(3)
	global_store_dwordx4 v[0:1], v[2:5], off sc0 sc1
	s_nop 1
	v_add_co_u32_e32 v2, vcc, 0x2000, v0
	s_nop 1
	v_addc_co_u32_e32 v3, vcc, 0, v1, vcc
	v_add_co_u32_e32 v0, vcc, 0x6000, v0
	s_waitcnt lgkmcnt(2)
	global_store_dwordx4 v[2:3], v[6:9], off sc0 sc1
	v_lshl_add_u64 v[2:3], s[0:1], 0, v[18:19]
	v_addc_co_u32_e32 v1, vcc, 0, v1, vcc
	s_waitcnt lgkmcnt(1)
	global_store_dwordx4 v[2:3], v[10:13], off sc0 sc1
	s_waitcnt lgkmcnt(0)
	global_store_dwordx4 v[0:1], v[14:17], off sc0 sc1
	s_endpgm

.LBB2_5:
	v_and_b32_e32 v136, 0x1cf, v0
	v_lshlrev_b32_e32 v4, 6, v0
	s_movk_i32 s12, 0x7000
	v_lshlrev_b32_e32 v3, 2, v136
	v_and_or_b32 v2, v4, s12, v2
	v_or_b32_e32 v135, 48, v0
	global_load_dwordx4 v[34:37], v2, s[8:9]
	global_load_dwordx4 v[30:33], v2, s[8:9] offset:1024
	global_load_dword v134, v3, s[10:11]
	global_load_dword v133, v3, s[10:11] offset:64
	global_load_dword v131, v3, s[10:11] offset:128
	v_lshlrev_b32_e32 v3, 2, v135
	global_load_dword v121, v3, s[10:11]
	global_load_dwordx4 v[26:29], v2, s[8:9] offset:2048
	global_load_dwordx4 v[18:21], v2, s[8:9] offset:3072
	s_waitcnt lgkmcnt(0)
	v_lshl_add_u64 v[2:3], s[20:21], 0, v[118:119]
	s_movk_i32 s8, 0x2000
	v_add_co_u32_e32 v4, vcc, s8, v2
	s_movk_i32 s8, 0x4000
	s_nop 0
	v_addc_co_u32_e32 v5, vcc, 0, v3, vcc
	global_load_dwordx4 v[14:17], v[2:3], off
	global_load_dwordx4 v[10:13], v[4:5], off
	v_add_co_u32_e32 v4, vcc, s8, v2
	s_movk_i32 s8, 0x6000
	s_nop 0
	v_addc_co_u32_e32 v5, vcc, 0, v3, vcc
	v_add_co_u32_e32 v2, vcc, s8, v2
	s_nop 1
	v_addc_co_u32_e32 v3, vcc, 0, v3, vcc
	global_load_dwordx4 v[6:9], v[4:5], off
	s_nop 0
	global_load_dwordx4 v[2:5], v[2:3], off
	s_waitcnt vmcnt(12)
	v_cvt_f32_f16_sdwa v124, v122 dst_sel:DWORD dst_unused:UNUSED_PAD src0_sel:WORD_1
	v_cvt_f32_f16_e32 v125, v123
	v_cvt_f32_f16_sdwa v128, v123 dst_sel:DWORD dst_unused:UNUSED_PAD src0_sel:WORD_1
	v_cvt_f32_f16_e32 v129, v22
	v_cvt_f32_f16_sdwa v138, v22 dst_sel:DWORD dst_unused:UNUSED_PAD src0_sel:WORD_1
	v_cvt_f32_f16_e32 v139, v23
	s_waitcnt vmcnt(6)
	v_pk_fma_f32 v[122:123], v[106:107], v[124:125], v[120:121] op_sel_hi:[0,1,0]
	v_pk_mov_b32 v[124:125], v[124:125], v[128:129] op_sel:[1,0]
	v_cvt_f32_f16_sdwa v141, v25 dst_sel:DWORD dst_unused:UNUSED_PAD src0_sel:WORD_1
	v_pk_fma_f32 v[122:123], v[106:107], v[124:125], v[122:123] op_sel:[1,0,0]
	v_pk_mov_b32 v[148:149], v[128:129], v[138:139] op_sel:[1,0]
	v_pk_fma_f32 v[124:125], v[108:109], v[128:129], v[122:123] op_sel_hi:[0,1,1]
	v_mov_b32_e32 v122, v109
	v_pk_fma_f32 v[150:151], v[122:123], v[148:149], v[124:125] op_sel_hi:[0,1,1]
	v_mul_f32_e32 v22, 0xbfb8aa3b, v150
	v_exp_f32_e32 v22, v22
	v_mul_f32_e32 v123, 0xbfb8aa3b, v151
	v_exp_f32_e32 v123, v123
	v_cvt_f32_f16_sdwa v157, v102 dst_sel:DWORD dst_unused:UNUSED_PAD src0_sel:WORD_1
	v_add_f32_e32 v22, 1.0, v22
	v_rcp_f32_e32 v152, v22
	v_add_f32_e32 v22, 1.0, v123
	v_rcp_f32_e32 v153, v22
	v_cvt_f32_f16_e32 v156, v102
	v_mul_f32_e32 v155, v107, v141
	v_cvt_f32_f16_e32 v126, v103
	v_pk_mul_f32 v[150:151], v[150:151], v[152:153]
	v_cvt_f32_f16_sdwa v152, v23 dst_sel:DWORD dst_unused:UNUSED_PAD src0_sel:WORD_1
	v_cvt_f32_f16_e32 v153, v24
	v_pk_fma_f32 v[22:23], v[106:107], v[128:129], v[120:121] op_sel_hi:[0,1,0]
	v_pk_fma_f32 v[22:23], v[106:107], v[148:149], v[22:23] op_sel:[1,0,0]
	v_cvt_f32_f16_sdwa v158, v103 dst_sel:DWORD dst_unused:UNUSED_PAD src0_sel:WORD_1
	v_pk_fma_f32 v[22:23], v[108:109], v[138:139], v[22:23] op_sel_hi:[0,1,1]
	v_pk_mov_b32 v[128:129], v[138:139], v[152:153] op_sel:[1,0]
	v_cvt_f32_f16_e32 v159, v104
	v_pk_fma_f32 v[148:149], v[122:123], v[128:129], v[22:23] op_sel_hi:[0,1,1]
	v_mul_f32_e32 v22, 0xbfb8aa3b, v148
	v_exp_f32_e32 v23, v22
	v_mul_f32_e32 v22, 0xbfb8aa3b, v149
	v_exp_f32_e32 v123, v22
	v_cvt_pk_f16_f32 v22, v150, v151
	v_add_f32_e32 v23, 1.0, v23
	v_rcp_f32_e32 v150, v23
	v_add_f32_e32 v23, 1.0, v123
	v_rcp_f32_e32 v151, v23
	v_lshrrev_b32_e32 v123, 16, v22
	v_mov_b32_e32 v103, v158
	v_cvt_f32_f16_sdwa v127, v105 dst_sel:DWORD dst_unused:UNUSED_PAD src0_sel:WORD_1
	v_pk_mul_f32 v[148:149], v[148:149], v[150:151]
	v_cvt_f32_f16_sdwa v150, v24 dst_sel:DWORD dst_unused:UNUSED_PAD src0_sel:WORD_1
	v_cvt_f32_f16_e32 v151, v25
	v_pk_fma_f32 v[24:25], v[106:107], v[138:139], v[120:121] op_sel_hi:[0,1,0]
	v_pk_fma_f32 v[24:25], v[106:107], v[128:129], v[24:25] op_sel:[1,0,0]
	v_cvt_f32_f16_e32 v145, v115
	v_pk_fma_f32 v[24:25], v[108:109], v[152:153], v[24:25] op_sel_hi:[0,1,1]
	v_pk_mov_b32 v[128:129], v[152:153], v[150:151] op_sel:[1,0]
	v_mov_b32_e32 v140, v151
	v_pk_fma_f32 v[24:25], v[122:123], v[128:129], v[24:25] op_sel_hi:[0,1,1]
	v_mul_f32_e32 v23, 0xbfb8aa3b, v24
	v_exp_f32_e32 v124, v23
	v_mul_f32_e32 v23, 0xbfb8aa3b, v25
	v_exp_f32_e32 v137, v23
	v_cvt_pk_f16_f32 v23, v148, v149
	v_add_f32_e32 v124, 1.0, v124
	v_rcp_f32_e32 v138, v124
	v_add_f32_e32 v124, 1.0, v137
	v_rcp_f32_e32 v139, v124
	v_pk_fma_f32 v[148:149], v[106:107], v[152:153], v[120:121] op_sel_hi:[0,1,0]
	v_pk_fma_f32 v[128:129], v[106:107], v[128:129], v[148:149] op_sel:[1,0,0]
	v_cvt_f32_f16_sdwa v125, v117 dst_sel:DWORD dst_unused:UNUSED_PAD src0_sel:WORD_1
	v_pk_mul_f32 v[24:25], v[24:25], v[138:139]
	v_mul_f32_e32 v139, v109, v141
	v_pk_fma_f32 v[128:129], v[108:109], v[150:151], v[128:129] op_sel_hi:[0,1,1]
	v_mul_f32_e32 v138, v109, v151
	v_pk_add_f32 v[128:129], v[128:129], v[138:139]
	v_cvt_pk_f16_f32 v24, v24, v25
	v_mul_f32_e32 v124, 0xbfb8aa3b, v128
	v_exp_f32_e32 v124, v124
	v_mul_f32_e32 v138, 0xbfb8aa3b, v129
	v_exp_f32_e32 v138, v138
	v_pk_fma_f32 v[150:151], v[106:107], v[150:151], v[120:121] op_sel_hi:[0,1,0]
	v_add_f32_e32 v25, 1.0, v124
	v_rcp_f32_e32 v148, v25
	v_add_f32_e32 v25, 1.0, v138
	v_rcp_f32_e32 v149, v25
	v_cvt_f32_f16_e32 v146, v111
	v_cvt_f32_f16_sdwa v144, v113 dst_sel:DWORD dst_unused:UNUSED_PAD src0_sel:WORD_1
	v_cvt_f32_f16_e32 v113, v113
	v_pk_mul_f32 v[148:149], v[128:129], v[148:149]
	v_pk_mov_b32 v[128:129], v[106:107], v[108:109] op_sel:[1,0]
	v_lshlrev_b32_e32 v143, 1, v0
	v_pk_mul_f32 v[152:153], v[128:129], v[140:141]
	v_mov_b32_e32 v140, v141
	v_mov_b32_e32 v154, v152
	v_pk_add_f32 v[150:151], v[150:151], v[154:155]
	v_pk_mul_f32 v[154:155], v[108:109], v[156:157]
	v_lshrrev_b32_e32 v137, 16, v23
	v_pk_mov_b32 v[152:153], v[152:153], v[154:155] op_sel:[1,0]
	v_mul_f32_e32 v155, v108, v126
	v_pk_add_f32 v[150:151], v[150:151], v[152:153]
	v_pk_mul_f32 v[152:153], v[106:107], v[156:157]
	v_pk_fma_f32 v[150:151], v[122:123], v[156:157], v[150:151] op_sel_hi:[0,1,1]
	v_mul_f32_e32 v25, 0xbfb8aa3b, v150
	v_exp_f32_e32 v102, v25
	v_mul_f32_e32 v25, 0xbfb8aa3b, v151
	v_exp_f32_e32 v124, v25
	v_cvt_pk_f16_f32 v25, v148, v149
	v_add_f32_e32 v102, 1.0, v102
	v_rcp_f32_e32 v148, v102
	v_add_f32_e32 v102, 1.0, v124
	v_rcp_f32_e32 v149, v102
	v_lshrrev_b32_e32 v138, 16, v24
	v_lshrrev_b32_e32 v139, 16, v25
	ds_write_b16 v143, v22
	v_pk_mul_f32 v[148:149], v[150:151], v[148:149]
	ds_write_b16 v143, v123 offset:1040
	v_cvt_pk_f16_f32 v102, v148, v149
	v_pk_mov_b32 v[148:149], v[156:157], v[156:157] op_sel:[1,0]
	v_mov_b32_e32 v157, v152
	v_mov_b32_e32 v141, v149
	v_pk_mul_f32 v[140:141], v[106:107], v[140:141]
	v_mov_b32_e32 v149, v126
	v_mov_b32_e32 v156, v140
	v_pk_mul_f32 v[150:151], v[108:109], v[148:149]
	v_pk_add_f32 v[156:157], v[120:121], v[156:157] op_sel_hi:[0,1]
	v_mov_b32_e32 v152, v141
	v_pk_add_f32 v[140:141], v[156:157], v[152:153]
	v_mov_b32_e32 v154, v150
	v_pk_mul_f32 v[152:153], v[108:109], v[102:103]
	v_pk_add_f32 v[140:141], v[140:141], v[154:155]
	v_mov_b32_e32 v152, v151
	v_pk_add_f32 v[150:151], v[140:141], v[152:153]
	v_pk_mul_f32 v[148:149], v[106:107], v[148:149]
	v_mul_f32_e32 v124, 0xbfb8aa3b, v150
	v_exp_f32_e32 v124, v124
	v_mul_f32_e32 v140, 0xbfb8aa3b, v151
	v_exp_f32_e32 v141, v140
	v_cvt_f32_f16_sdwa v156, v104 dst_sel:DWORD dst_unused:UNUSED_PAD src0_sel:WORD_1
	v_add_f32_e32 v124, 1.0, v124
	v_rcp_f32_e32 v152, v124
	v_add_f32_e32 v124, 1.0, v141
	v_rcp_f32_e32 v153, v124
	v_cvt_f32_f16_e32 v157, v105
	v_pk_mul_f32 v[154:155], v[106:107], v[102:103]
	v_lshrrev_b32_e32 v140, 16, v102
	v_pk_mul_f32 v[150:151], v[150:151], v[152:153]
	v_mul_f32_e32 v153, v106, v126
	v_mov_b32_e32 v152, v148
	v_pk_add_f32 v[152:153], v[120:121], v[152:153] op_sel_hi:[0,1]
	v_mov_b32_e32 v154, v149
	v_pk_add_f32 v[104:105], v[152:153], v[154:155]
	v_pk_mov_b32 v[148:149], v[158:159], v[156:157] op_sel:[1,0]
	v_pk_fma_f32 v[104:105], v[108:109], v[158:159], v[104:105] op_sel_hi:[0,1,1]
	v_pk_fma_f32 v[104:105], v[122:123], v[148:149], v[104:105] op_sel_hi:[0,1,1]
	v_mul_f32_e32 v103, 0xbfb8aa3b, v104
	v_exp_f32_e32 v124, v103
	v_mul_f32_e32 v103, 0xbfb8aa3b, v105
	v_exp_f32_e32 v126, v103
	v_cvt_pk_f16_f32 v103, v150, v151
	v_add_f32_e32 v124, 1.0, v124
	v_rcp_f32_e32 v150, v124
	v_add_f32_e32 v124, 1.0, v126
	v_rcp_f32_e32 v151, v124
	v_pk_fma_f32 v[152:153], v[106:107], v[158:159], v[120:121] op_sel_hi:[0,1,0]
	v_pk_fma_f32 v[148:149], v[106:107], v[148:149], v[152:153] op_sel:[1,0,0]
	v_cvt_f32_f16_sdwa v155, v114 dst_sel:DWORD dst_unused:UNUSED_PAD src0_sel:WORD_1
	v_pk_mul_f32 v[104:105], v[104:105], v[150:151]
	v_mul_f32_e32 v151, v109, v127
	v_pk_fma_f32 v[148:149], v[108:109], v[156:157], v[148:149] op_sel_hi:[0,1,1]
	v_mul_f32_e32 v150, v109, v157
	v_pk_add_f32 v[148:149], v[148:149], v[150:151]
	v_cvt_pk_f16_f32 v104, v104, v105
	v_mul_f32_e32 v124, 0xbfb8aa3b, v148
	v_exp_f32_e32 v124, v124
	v_mul_f32_e32 v126, 0xbfb8aa3b, v149
	v_exp_f32_e32 v126, v126
	v_cvt_f32_f16_e32 v154, v114
	v_add_f32_e32 v105, 1.0, v124
	v_rcp_f32_e32 v150, v105
	v_add_f32_e32 v105, 1.0, v126
	v_rcp_f32_e32 v151, v105
	v_mov_b32_e32 v126, v157
	v_mul_f32_e32 v153, v107, v127
	v_pk_fma_f32 v[156:157], v[106:107], v[156:157], v[120:121] op_sel_hi:[0,1,0]
	v_pk_mul_f32 v[148:149], v[148:149], v[150:151]
	v_pk_mul_f32 v[150:151], v[128:129], v[126:127]
	v_lshrrev_b32_e32 v141, 16, v103
	v_mov_b32_e32 v152, v150
	v_pk_add_f32 v[152:153], v[156:157], v[152:153]
	v_pk_mul_f32 v[156:157], v[108:109], v[154:155]
	v_lshrrev_b32_e32 v142, 16, v104
	v_pk_mov_b32 v[150:151], v[150:151], v[156:157] op_sel:[1,0]
	v_mul_f32_e32 v157, v108, v145
	v_pk_add_f32 v[150:151], v[152:153], v[150:151]
	ds_write_b16 v143, v23 offset:2080
	v_pk_fma_f32 v[150:151], v[122:123], v[154:155], v[150:151] op_sel_hi:[0,1,1]
	v_mul_f32_e32 v105, 0xbfb8aa3b, v150
	v_exp_f32_e32 v114, v105
	v_mul_f32_e32 v105, 0xbfb8aa3b, v151
	v_exp_f32_e32 v124, v105
	v_cvt_pk_f16_f32 v105, v148, v149
	v_add_f32_e32 v114, 1.0, v114
	v_rcp_f32_e32 v148, v114
	v_add_f32_e32 v114, 1.0, v124
	v_rcp_f32_e32 v149, v114
	v_lshrrev_b32_e32 v126, 16, v105
	ds_write_b16 v143, v137 offset:3120
	ds_write_b16 v143, v24 offset:4160
	v_pk_mul_f32 v[148:149], v[150:151], v[148:149]
	v_mov_b32_e32 v150, v127
	v_cvt_pk_f16_f32 v114, v148, v149
	v_pk_mov_b32 v[148:149], v[154:155], v[154:155] op_sel:[1,0]
	v_pk_mul_f32 v[154:155], v[106:107], v[154:155]
	v_mov_b32_e32 v151, v149
	v_pk_mul_f32 v[150:151], v[106:107], v[150:151]
	v_mov_b32_e32 v149, v145
	v_mov_b32_e32 v158, v150
	v_cvt_f32_f16_sdwa v150, v115 dst_sel:DWORD dst_unused:UNUSED_PAD src0_sel:WORD_1
	v_mov_b32_e32 v159, v154
	v_pk_mul_f32 v[152:153], v[108:109], v[148:149]
	v_pk_add_f32 v[158:159], v[120:121], v[158:159] op_sel_hi:[0,1]
	v_mov_b32_e32 v154, v151
	v_pk_add_f32 v[154:155], v[158:159], v[154:155]
	v_mov_b32_e32 v156, v152
	v_mov_b32_e32 v115, v150
	v_pk_add_f32 v[154:155], v[154:155], v[156:157]
	v_pk_mul_f32 v[156:157], v[108:109], v[114:115]
	v_pk_mul_f32 v[148:149], v[106:107], v[148:149]
	v_mov_b32_e32 v156, v153
	v_pk_add_f32 v[152:153], v[154:155], v[156:157]
	v_cvt_f32_f16_e32 v151, v116
	v_mul_f32_e32 v124, 0xbfb8aa3b, v152
	v_exp_f32_e32 v124, v124
	v_mul_f32_e32 v127, 0xbfb8aa3b, v153
	v_exp_f32_e32 v147, v127
	v_cvt_f32_f16_sdwa v158, v116 dst_sel:DWORD dst_unused:UNUSED_PAD src0_sel:WORD_1
	v_add_f32_e32 v124, 1.0, v124
	v_rcp_f32_e32 v154, v124
	v_add_f32_e32 v124, 1.0, v147
	v_rcp_f32_e32 v155, v124
	v_cvt_f32_f16_e32 v159, v117
	v_pk_mul_f32 v[156:157], v[106:107], v[114:115]
	v_lshrrev_b32_e32 v127, 16, v114
	v_pk_mul_f32 v[152:153], v[152:153], v[154:155]
	v_mul_f32_e32 v155, v106, v145
	v_mov_b32_e32 v154, v148
	v_pk_add_f32 v[154:155], v[120:121], v[154:155] op_sel_hi:[0,1]
	v_mov_b32_e32 v156, v149
	v_pk_add_f32 v[116:117], v[154:155], v[156:157]
	v_pk_mov_b32 v[148:149], v[150:151], v[158:159] op_sel:[1,0]
	v_pk_fma_f32 v[116:117], v[108:109], v[150:151], v[116:117] op_sel_hi:[0,1,1]
	v_pk_fma_f32 v[116:117], v[122:123], v[148:149], v[116:117] op_sel_hi:[0,1,1]
	v_mul_f32_e32 v115, 0xbfb8aa3b, v116
	v_exp_f32_e32 v124, v115
	v_mul_f32_e32 v115, 0xbfb8aa3b, v117
	v_exp_f32_e32 v145, v115
	v_cvt_pk_f16_f32 v115, v152, v153
	v_add_f32_e32 v124, 1.0, v124
	v_rcp_f32_e32 v152, v124
	v_add_f32_e32 v124, 1.0, v145
	v_rcp_f32_e32 v153, v124
	v_pk_fma_f32 v[150:151], v[106:107], v[150:151], v[120:121] op_sel_hi:[0,1,0]
	v_pk_fma_f32 v[148:149], v[106:107], v[148:149], v[150:151] op_sel:[1,0,0]
	v_pk_fma_f32 v[154:155], v[106:107], v[158:159], v[120:121] op_sel_hi:[0,1,0]
	v_pk_mul_f32 v[116:117], v[116:117], v[152:153]
	v_mul_f32_e32 v153, v109, v125
	v_pk_fma_f32 v[148:149], v[108:109], v[158:159], v[148:149] op_sel_hi:[0,1,1]
	v_mul_f32_e32 v152, v109, v159
	v_pk_add_f32 v[148:149], v[148:149], v[152:153]
	v_cvt_pk_f16_f32 v116, v116, v117
	v_mul_f32_e32 v124, 0xbfb8aa3b, v148
	v_exp_f32_e32 v124, v124
	v_mul_f32_e32 v147, 0xbfb8aa3b, v149
	v_exp_f32_e32 v147, v147
	v_cvt_f32_f16_sdwa v153, v110 dst_sel:DWORD dst_unused:UNUSED_PAD src0_sel:WORD_1
	v_add_f32_e32 v117, 1.0, v124
	v_rcp_f32_e32 v150, v117
	v_add_f32_e32 v117, 1.0, v147
	v_rcp_f32_e32 v151, v117
	v_cvt_f32_f16_e32 v152, v110
	v_mov_b32_e32 v124, v159
	v_pk_mul_f32 v[128:129], v[128:129], v[124:125]
	v_pk_mul_f32 v[148:149], v[148:149], v[150:151]
	v_mul_f32_e32 v151, v107, v125
	v_mov_b32_e32 v150, v128
	v_pk_add_f32 v[150:151], v[154:155], v[150:151]
	v_pk_mul_f32 v[154:155], v[108:109], v[152:153]
	v_lshrrev_b32_e32 v145, 16, v115
	v_pk_mov_b32 v[128:129], v[128:129], v[154:155] op_sel:[1,0]
	v_mul_f32_e32 v155, v108, v146
	v_pk_add_f32 v[128:129], v[150:151], v[128:129]
	v_lshrrev_b32_e32 v147, 16, v116
	v_pk_fma_f32 v[128:129], v[122:123], v[152:153], v[128:129] op_sel_hi:[0,1,1]
	v_mul_f32_e32 v110, 0xbfb8aa3b, v128
	v_exp_f32_e32 v110, v110
	v_mul_f32_e32 v117, 0xbfb8aa3b, v129
	v_exp_f32_e32 v124, v117
	v_cvt_pk_f16_f32 v117, v148, v149
	v_add_f32_e32 v110, 1.0, v110
	v_rcp_f32_e32 v148, v110
	v_add_f32_e32 v110, 1.0, v124
	v_rcp_f32_e32 v149, v110
	v_lshrrev_b32_e32 v124, 16, v117
	ds_write_b16 v143, v138 offset:5200
	ds_write_b16 v143, v25 offset:6240
	v_pk_mul_f32 v[128:129], v[128:129], v[148:149]
	v_mov_b32_e32 v148, v125
	v_cvt_pk_f16_f32 v110, v128, v129
	v_pk_mov_b32 v[128:129], v[152:153], v[152:153] op_sel:[1,0]
	v_pk_mul_f32 v[152:153], v[106:107], v[152:153]
	v_mov_b32_e32 v149, v129
	v_pk_mul_f32 v[148:149], v[106:107], v[148:149]
	v_mov_b32_e32 v129, v146
	v_mov_b32_e32 v156, v148
	v_cvt_f32_f16_sdwa v148, v111 dst_sel:DWORD dst_unused:UNUSED_PAD src0_sel:WORD_1
	v_mov_b32_e32 v157, v152
	v_pk_mul_f32 v[150:151], v[108:109], v[128:129]
	v_pk_add_f32 v[156:157], v[120:121], v[156:157] op_sel_hi:[0,1]
	v_mov_b32_e32 v152, v149
	v_pk_add_f32 v[152:153], v[156:157], v[152:153]
	v_mov_b32_e32 v154, v150
	v_mov_b32_e32 v111, v148
	v_pk_add_f32 v[152:153], v[152:153], v[154:155]
	v_pk_mul_f32 v[154:155], v[108:109], v[110:111]
	v_pk_mul_f32 v[128:129], v[106:107], v[128:129]
	v_mov_b32_e32 v154, v151
	v_pk_add_f32 v[150:151], v[152:153], v[154:155]
	v_pk_mul_f32 v[154:155], v[106:107], v[110:111]
	v_mul_f32_e32 v125, 0xbfb8aa3b, v150
	v_exp_f32_e32 v149, v125
	v_mul_f32_e32 v125, 0xbfb8aa3b, v151
	v_exp_f32_e32 v153, v125
	v_mov_b32_e32 v154, v129
	v_add_f32_e32 v149, 1.0, v149
	v_rcp_f32_e32 v152, v149
	v_add_f32_e32 v149, 1.0, v153
	v_rcp_f32_e32 v153, v149
	v_cvt_f32_f16_e32 v149, v112
	v_cvt_f32_f16_sdwa v112, v112 dst_sel:DWORD dst_unused:UNUSED_PAD src0_sel:WORD_1
	v_lshrrev_b32_e32 v125, 16, v110
	v_pk_mul_f32 v[150:151], v[150:151], v[152:153]
	v_mul_f32_e32 v153, v106, v146
	v_mov_b32_e32 v152, v128
	v_pk_add_f32 v[152:153], v[120:121], v[152:153] op_sel_hi:[0,1]
	v_pk_add_f32 v[128:129], v[152:153], v[154:155]
	v_pk_mov_b32 v[152:153], v[148:149], v[112:113] op_sel:[1,0]
	v_pk_fma_f32 v[128:129], v[108:109], v[148:149], v[128:129] op_sel_hi:[0,1,1]
	v_pk_fma_f32 v[128:129], v[122:123], v[152:153], v[128:129] op_sel_hi:[0,1,1]
	v_mul_f32_e32 v111, 0xbfb8aa3b, v128
	v_exp_f32_e32 v122, v111
	v_mul_f32_e32 v111, 0xbfb8aa3b, v129
	v_exp_f32_e32 v146, v111
	v_cvt_pk_f16_f32 v111, v150, v151
	v_add_f32_e32 v122, 1.0, v122
	v_rcp_f32_e32 v150, v122
	v_add_f32_e32 v122, 1.0, v146
	v_rcp_f32_e32 v151, v122
	v_pk_fma_f32 v[148:149], v[106:107], v[148:149], v[120:121] op_sel_hi:[0,1,0]
	v_pk_fma_f32 v[106:107], v[106:107], v[152:153], v[148:149] op_sel:[1,0,0]
	v_lshrrev_b32_e32 v122, 16, v111
	v_pk_mul_f32 v[128:129], v[128:129], v[150:151]
	v_mul_f32_e32 v151, v109, v144
	v_pk_fma_f32 v[106:107], v[108:109], v[112:113], v[106:107] op_sel_hi:[0,1,1]
	v_mul_f32_e32 v150, v109, v113
	v_pk_add_f32 v[106:107], v[106:107], v[150:151]
	v_cvt_pk_f16_f32 v112, v128, v129
	v_mul_f32_e32 v108, 0xbfb8aa3b, v106
	v_exp_f32_e32 v108, v108
	v_mul_f32_e32 v109, 0xbfb8aa3b, v107
	v_exp_f32_e32 v109, v109
	ds_write_b16 v143, v139 offset:7280
	v_add_f32_e32 v108, 1.0, v108
	v_rcp_f32_e32 v128, v108
	v_add_f32_e32 v108, 1.0, v109
	v_rcp_f32_e32 v129, v108
	v_lshrrev_b32_e32 v108, 16, v112
	v_and_b32_e32 v109, 15, v0
	ds_write_b16 v143, v102 offset:8320
	v_pk_mul_f32 v[106:107], v[106:107], v[128:129]
	v_lshl_add_u64 v[128:129], s[2:3], 0, v[118:119]
	v_lshl_add_u64 v[148:149], v[128:129], 0, s[6:7]
	v_cvt_pk_f16_f32 v113, v106, v107
	global_store_dwordx4 v[148:149], v[22:25], off sc0 sc1
	v_lshl_add_u64 v[148:149], v[128:129], 0, s[14:15]
	v_lshrrev_b32_e32 v106, 16, v113
	global_store_dwordx4 v[148:149], v[102:105], off sc0 sc1
	v_lshl_add_u64 v[148:149], v[128:129], 0, s[16:17]
	v_lshl_add_u64 v[128:129], v[128:129], 0, s[18:19]
	v_lshrrev_b32_e32 v107, 4, v130
	ds_write_b16 v143, v140 offset:9360
	ds_write_b16 v143, v103 offset:10400
	ds_write_b16 v143, v141 offset:11440
	ds_write_b16 v143, v104 offset:12480
	ds_write_b16 v143, v142 offset:13520
	ds_write_b16 v143, v105 offset:14560
	ds_write_b16 v143, v126 offset:15600
	ds_write_b16 v143, v114 offset:16640
	ds_write_b16 v143, v127 offset:17680
	ds_write_b16 v143, v115 offset:18720
	ds_write_b16 v143, v145 offset:19760
	ds_write_b16 v143, v116 offset:20800
	ds_write_b16 v143, v147 offset:21840
	ds_write_b16 v143, v117 offset:22880
	ds_write_b16 v143, v124 offset:23920
	ds_write_b16 v143, v110 offset:24960
	ds_write_b16 v143, v125 offset:26000
	ds_write_b16 v143, v111 offset:27040
	ds_write_b16 v143, v122 offset:28080
	ds_write_b16 v143, v112 offset:29120
	ds_write_b16 v143, v108 offset:30160
	ds_write_b16 v143, v113 offset:31200
	ds_write_b16 v143, v106 offset:32240
	global_store_dwordx4 v[148:149], v[114:117], off sc0 sc1
	global_store_dwordx4 v[128:129], v[110:113], off sc0 sc1
	s_waitcnt lgkmcnt(0)
	s_barrier
	s_and_saveexec_b64 s[2:3], s[4:5]
	s_cbranch_execz .LBB2_7
	s_movk_i32 s4, 0xbf
	v_cmp_lt_u32_e32 vcc, s4, v0
	v_and_b32_e32 v129, 48, v0
	s_movk_i32 s4, 0x410
	v_cndmask_b32_e64 v120, 0, 16, vcc
	v_or_b32_e32 v128, v120, v109
	v_mad_u32_u24 v128, v128, s4, v129
	s_lshl_b32 s4, s24, 5
	s_and_b32 s5, s4, 0x1e0
	v_lshl_add_u32 v129, s5, 1, v128
	ds_read_b128 v[148:151], v129
	s_add_i32 s8, s4, 32
	s_and_b32 s8, s8, 0x1e0
	v_lshl_add_u32 v129, s8, 1, v128
	ds_read_b128 v[152:155], v129
	s_add_i32 s8, s4, 64
	s_waitcnt lgkmcnt(1)
	v_mfma_f32_16x16x32_f16 v[38:41], v[148:151], v[38:41], 0
	s_and_b32 s8, s8, 0x1e0
	s_xor_b32 s5, s5, 0x100
	s_waitcnt lgkmcnt(0)
	v_mfma_f32_16x16x32_f16 v[38:41], v[152:155], v[42:45], v[38:41]
	v_lshl_add_u32 v42, s8, 1, v128
	ds_read_b128 v[42:45], v42
	s_add_i32 s8, s4, 0x60
	s_and_b32 s8, s8, 0x1e0
	v_lshl_add_u32 v129, s8, 1, v128
	ds_read_b128 v[148:151], v129
	s_add_i32 s8, s4, 0x80
	s_and_b32 s8, s8, 0x1e0
	s_waitcnt lgkmcnt(1)
	v_mfma_f32_16x16x32_f16 v[38:41], v[42:45], v[46:49], v[38:41]
	v_lshl_add_u32 v42, s8, 1, v128
	ds_read_b128 v[42:45], v42
	s_add_i32 s8, s4, 0xa0
	s_and_b32 s8, s8, 0x1e0
	v_lshl_add_u32 v46, s8, 1, v128
	ds_read_b128 v[46:49], v46
	s_waitcnt lgkmcnt(2)
	v_mfma_f32_16x16x32_f16 v[38:41], v[148:151], v[50:53], v[38:41]
	s_add_i32 s8, s4, 0xc0
	s_and_b32 s8, s8, 0x1e0
	s_waitcnt lgkmcnt(1)
	v_mfma_f32_16x16x32_f16 v[38:41], v[42:45], v[54:57], v[38:41]
	v_lshl_add_u32 v42, s8, 1, v128
	ds_read_b128 v[42:45], v42
	s_add_i32 s8, s4, 0xe0
	s_and_b32 s8, s8, 0x1e0
	s_waitcnt lgkmcnt(1)
	v_mfma_f32_16x16x32_f16 v[38:41], v[46:49], v[58:61], v[38:41]
	v_lshl_add_u32 v46, s8, 1, v128
	ds_read_b128 v[46:49], v46
	s_waitcnt lgkmcnt(1)
	v_mfma_f32_16x16x32_f16 v[38:41], v[42:45], v[62:65], v[38:41]
	v_lshl_add_u32 v42, s5, 1, v128
	ds_read_b128 v[42:45], v42
	s_add_i32 s5, s4, 0x120
	s_and_b32 s5, s5, 0x1e0
	s_waitcnt lgkmcnt(1)
	v_mfma_f32_16x16x32_f16 v[38:41], v[46:49], v[66:69], v[38:41]
	v_lshl_add_u32 v46, s5, 1, v128
	ds_read_b128 v[46:49], v46
	s_add_i32 s5, s4, 0x140
	s_and_b32 s5, s5, 0x1e0
	s_waitcnt lgkmcnt(1)
	v_mfma_f32_16x16x32_f16 v[38:41], v[42:45], v[70:73], v[38:41]
	v_lshl_add_u32 v42, s5, 1, v128
	ds_read_b128 v[42:45], v42
	s_add_i32 s5, s4, 0x160
	s_and_b32 s5, s5, 0x1e0
	s_waitcnt lgkmcnt(1)
	v_mfma_f32_16x16x32_f16 v[38:41], v[46:49], v[74:77], v[38:41]
	v_lshl_add_u32 v46, s5, 1, v128
	ds_read_b128 v[46:49], v46
	s_add_i32 s5, s4, 0x180
	s_and_b32 s5, s5, 0x1e0
	s_waitcnt lgkmcnt(1)
	v_mfma_f32_16x16x32_f16 v[38:41], v[42:45], v[78:81], v[38:41]
	v_lshl_add_u32 v42, s5, 1, v128
	ds_read_b128 v[42:45], v42
	s_add_i32 s5, s4, 0x1a0
	s_and_b32 s5, s5, 0x1e0
	s_waitcnt lgkmcnt(1)
	v_mfma_f32_16x16x32_f16 v[38:41], v[46:49], v[82:85], v[38:41]
	v_lshl_add_u32 v46, s5, 1, v128
	ds_read_b128 v[46:49], v46
	s_add_i32 s5, s4, 0x1c0
	s_and_b32 s5, s5, 0x1e0
	s_waitcnt lgkmcnt(1)
	v_mfma_f32_16x16x32_f16 v[38:41], v[42:45], v[86:89], v[38:41]
	v_lshl_add_u32 v42, s5, 1, v128
	ds_read_b128 v[42:45], v42
	s_addk_i32 s4, 0x1e0
	s_and_b32 s4, s4, 0x1e0
	s_waitcnt lgkmcnt(1)
	v_mfma_f32_16x16x32_f16 v[38:41], v[46:49], v[90:93], v[38:41]
	v_lshl_add_u32 v46, s4, 1, v128
	ds_read_b128 v[46:49], v46
	s_waitcnt lgkmcnt(1)
	v_mfma_f32_16x16x32_f16 v[38:41], v[42:45], v[94:97], v[38:41]
	v_mul_lo_u16_e32 v42, 0x56, v132
	v_mov_b32_e32 v43, 3
	v_mul_lo_u16_sdwa v42, v42, v43 dst_sel:DWORD dst_unused:UNUSED_PAD src0_sel:BYTE_1 src1_sel:DWORD
	v_sub_u16_e32 v42, v132, v42
	v_mov_b32_e32 v45, 6
	s_waitcnt lgkmcnt(0)
	v_mfma_f32_16x16x32_f16 v[38:41], v[46:49], v[98:101], v[38:41]
	v_mul_u32_u24_e32 v43, 0xd0, v120
	v_mul_u32_u24_e32 v44, 0x340, v107
	v_lshlrev_b32_sdwa v42, v45, v42 dst_sel:DWORD dst_unused:UNUSED_PAD src0_sel:DWORD src1_sel:BYTE_0
	v_add3_u32 v42, v44, v43, v42
	v_lshl_or_b32 v42, v109, 2, v42
	v_add_u32_e32 v42, 0xa000, v42
	s_nop 1
	ds_write2_b32 v42, v38, v39 offset1:52
	ds_write2_b32 v42, v40, v41 offset0:104 offset1:156
.LBB2_7:
	s_or_b64 exec, exec, s[2:3]
	s_movk_i32 s2, 0x100
	v_cmp_gt_u32_e32 vcc, s2, v0
	s_waitcnt lgkmcnt(0)
	s_barrier
	s_and_saveexec_b64 s[2:3], vcc
	s_cbranch_execz .LBB2_9
	s_load_dwordx2 s[4:5], s[0:1], 0x40
	v_lshrrev_b32_e32 v38, 3, v0
	v_and_b32_e32 v42, 0x70, v118
	s_movk_i32 s8, 0xd0
	v_mad_u32_u24 v39, v38, s8, v42
	v_or_b32_e32 v44, s25, v38
	ds_read_b128 v[38:41], v39 offset:41024
	v_mov_b32_e32 v45, 0
	v_lshlrev_b64 v[46:47], 7, v[44:45]
	s_waitcnt lgkmcnt(0)
	v_lshl_add_u64 v[46:47], s[4:5], 0, v[46:47]
	v_mov_b32_e32 v43, v45
	v_lshl_add_u64 v[42:43], v[46:47], 0, v[42:43]
	global_store_dwordx4 v[42:43], v[38:41], off sc0 sc1

.LBB2_13:
	s_or_b64 exec, exec, s[10:11]
	v_mfma_f32_16x16x32_f16 v[92:95], v[42:45], v[34:37], 0
	v_cvt_f32_f16_e32 v89, v24
	v_lshlrev_b32_e32 v52, 3, v107
	s_movk_i32 s0, 0x50
	v_mfma_f32_16x16x32_f16 v[34:37], v[38:41], v[34:37], 0
	v_cvt_f32_f16_e32 v49, v108
	s_nop 2
	v_add_f32_e32 v24, v92, v134
	v_min_f32_e32 v46, 0x42a00000, v24
	v_mul_f32_e32 v46, 0x3fb8aa3b, v46
	v_exp_f32_e32 v46, v46
	v_add_f32_e32 v48, v93, v134
	v_min_f32_e32 v50, 0x42a00000, v48
	v_mul_f32_e32 v50, 0x3fb8aa3b, v50
	v_add_f32_e32 v46, 1.0, v46
	v_log_f32_e32 v46, v46
	v_exp_f32_e32 v50, v50
	v_add_f32_e32 v56, v95, v134
	v_min_f32_e32 v58, 0x42a00000, v56
	v_mul_f32_e32 v46, 0x3f317218, v46
	v_max_f32_e32 v24, v24, v46
	v_add_f32_e32 v46, 1.0, v50
	v_add_f32_e32 v50, v94, v134
	v_min_f32_e32 v54, 0x42a00000, v50
	v_mul_f32_e32 v54, 0x3fb8aa3b, v54
	v_exp_f32_e32 v54, v54
	v_mul_f32_e32 v58, 0x3fb8aa3b, v58
	v_exp_f32_e32 v58, v58
	v_log_f32_e32 v46, v46
	v_add_f32_e32 v54, 1.0, v54
	v_log_f32_e32 v54, v54
	v_add_f32_e32 v58, 1.0, v58
	v_log_f32_e32 v58, v58
	v_mul_f32_e32 v46, 0x3f317218, v46
	v_mfma_f32_16x16x32_f16 v[92:95], v[42:45], v[30:33], 0
	v_max_f32_e32 v46, v48, v46
	v_mul_f32_e32 v48, 0x3f317218, v54
	v_max_f32_e32 v48, v50, v48
	v_mul_f32_e32 v50, 0x3f317218, v58
	v_max_f32_e32 v50, v56, v50
	v_cvt_pk_f16_f32 v97, v48, v50
	s_nop 1
	v_add_f32_e32 v48, v92, v133
	v_min_f32_e32 v50, 0x42a00000, v48
	v_mul_f32_e32 v50, 0x3fb8aa3b, v50
	v_exp_f32_e32 v50, v50
	v_cvt_pk_f16_f32 v96, v24, v46
	v_add_f32_e32 v58, v95, v133
	v_min_f32_e32 v60, 0x42a00000, v58
	v_add_f32_e32 v46, 1.0, v50
	v_add_f32_e32 v50, v93, v133
	v_min_f32_e32 v54, 0x42a00000, v50
	v_log_f32_e32 v46, v46
	v_mul_f32_e32 v54, 0x3fb8aa3b, v54
	v_exp_f32_e32 v54, v54
	v_mul_f32_e32 v60, 0x3fb8aa3b, v60
	v_mul_f32_e32 v46, 0x3f317218, v46
	v_max_f32_e32 v46, v48, v46
	v_add_f32_e32 v48, 1.0, v54
	v_add_f32_e32 v54, v94, v133
	v_min_f32_e32 v56, 0x42a00000, v54
	v_mul_f32_e32 v56, 0x3fb8aa3b, v56
	v_exp_f32_e32 v56, v56
	v_exp_f32_e32 v60, v60
	v_log_f32_e32 v48, v48
	s_waitcnt vmcnt(9)
	v_mfma_f32_16x16x32_f16 v[92:95], v[42:45], v[26:29], 0
	v_add_f32_e32 v56, 1.0, v56
	v_log_f32_e32 v56, v56
	v_add_f32_e32 v60, 1.0, v60
	v_log_f32_e32 v60, v60
	v_mul_f32_e32 v48, 0x3f317218, v48
	v_max_f32_e32 v48, v50, v48
	v_mul_f32_e32 v50, 0x3f317218, v56
	s_nop 0
	v_add_f32_e32 v56, v92, v131
	v_max_f32_e32 v50, v54, v50
	v_mul_f32_e32 v54, 0x3f317218, v60
	v_min_f32_e32 v60, 0x42a00000, v56
	v_mul_f32_e32 v60, 0x3fb8aa3b, v60
	v_exp_f32_e32 v60, v60
	v_mad_u32_u24 v24, v136, s0, v52
	ds_write_b64 v24, v[96:97]
	v_cvt_pk_f16_f32 v96, v46, v48
	v_add_f32_e32 v46, 1.0, v60
	v_log_f32_e32 v46, v46
	v_max_f32_e32 v54, v58, v54
	v_add_f32_e32 v48, v93, v131
	v_cvt_pk_f16_f32 v97, v50, v54
	v_min_f32_e32 v50, 0x42a00000, v48
	v_mul_f32_e32 v46, 0x3f317218, v46
	v_add_f32_e32 v54, v94, v131
	v_mul_f32_e32 v50, 0x3fb8aa3b, v50
	v_max_f32_e32 v46, v56, v46
	v_min_f32_e32 v56, 0x42a00000, v54
	v_exp_f32_e32 v50, v50
	v_mul_f32_e32 v56, 0x3fb8aa3b, v56
	v_exp_f32_e32 v56, v56
	s_waitcnt vmcnt(8)
	v_mfma_f32_16x16x32_f16 v[42:45], v[42:45], v[18:21], 0
	v_add_f32_e32 v50, 1.0, v50
	v_log_f32_e32 v50, v50
	v_add_f32_e32 v56, 1.0, v56
	v_log_f32_e32 v56, v56
	v_add_f32_e32 v58, v95, v131
	v_mul_f32_e32 v50, 0x3f317218, v50
	s_nop 1
	v_add_f32_e32 v42, v42, v121
	v_min_f32_e32 v60, 0x42a00000, v58
	v_max_f32_e32 v48, v48, v50
	v_mul_f32_e32 v50, 0x3f317218, v56
	v_min_f32_e32 v56, 0x42a00000, v42
	v_mul_f32_e32 v60, 0x3fb8aa3b, v60
	v_mul_f32_e32 v56, 0x3fb8aa3b, v56
	v_exp_f32_e32 v60, v60
	v_exp_f32_e32 v56, v56
	v_add_f32_e32 v43, v43, v121
	v_cvt_pk_f16_f32 v92, v46, v48
	v_add_f32_e32 v60, 1.0, v60
	v_add_f32_e32 v46, 1.0, v56
	v_min_f32_e32 v48, 0x42a00000, v43
	v_log_f32_e32 v60, v60
	v_log_f32_e32 v46, v46
	v_mul_f32_e32 v48, 0x3fb8aa3b, v48
	v_exp_f32_e32 v48, v48
	v_max_f32_e32 v50, v54, v50
	v_mul_f32_e32 v54, 0x3f317218, v60
	v_mul_f32_e32 v46, 0x3f317218, v46
	v_add_f32_e32 v44, v44, v121
	v_max_f32_e32 v54, v58, v54
	v_max_f32_e32 v42, v42, v46
	v_add_f32_e32 v46, 1.0, v48
	v_min_f32_e32 v48, 0x42a00000, v44
	v_add_f32_e32 v45, v45, v121
	v_cvt_pk_f16_f32 v93, v50, v54
	v_mul_f32_e32 v48, 0x3fb8aa3b, v48
	v_min_f32_e32 v50, 0x42a00000, v45
	v_exp_f32_e32 v48, v48
	v_mul_f32_e32 v50, 0x3fb8aa3b, v50
	v_exp_f32_e32 v50, v50
	v_log_f32_e32 v46, v46
	v_add_f32_e32 v48, 1.0, v48
	v_log_f32_e32 v48, v48
	v_add_f32_e32 v50, 1.0, v50
	v_log_f32_e32 v50, v50
	v_mul_f32_e32 v46, 0x3f317218, v46
	v_max_f32_e32 v46, v43, v46
	v_mul_f32_e32 v43, 0x3f317218, v48
	v_max_f32_e32 v43, v44, v43
	v_mul_f32_e32 v44, 0x3f317218, v50
	v_add_f32_e32 v34, v34, v134
	v_max_f32_e32 v44, v45, v44
	v_min_f32_e32 v45, 0x42a00000, v34
	v_mul_f32_e32 v45, 0x3fb8aa3b, v45
	v_exp_f32_e32 v45, v45
	v_add_f32_e32 v35, v35, v134
	v_cvt_pk_f16_f32 v43, v43, v44
	v_cvt_pk_f16_f32 v42, v42, v46
	v_mad_u32_u24 v44, v135, s0, v52
	v_add_f32_e32 v45, 1.0, v45
	v_min_f32_e32 v46, 0x42a00000, v35
	v_add_f32_e32 v36, v36, v134
	ds_write_b64 v24, v[96:97] offset:1280
	ds_write_b64 v24, v[92:93] offset:2560
	v_log_f32_e32 v45, v45
	v_mul_f32_e32 v46, 0x3fb8aa3b, v46
	ds_write_b64 v44, v[42:43]
	v_min_f32_e32 v43, 0x42a00000, v36
	v_exp_f32_e32 v46, v46
	v_mul_f32_e32 v43, 0x3fb8aa3b, v43
	v_exp_f32_e32 v43, v43
	v_add_f32_e32 v37, v37, v134
	v_mul_f32_e32 v42, 0x3f317218, v45
	v_min_f32_e32 v45, 0x42a00000, v37
	v_max_f32_e32 v34, v34, v42
	v_add_f32_e32 v42, 1.0, v46
	v_mul_f32_e32 v45, 0x3fb8aa3b, v45
	v_log_f32_e32 v42, v42
	v_exp_f32_e32 v45, v45
	v_add_f32_e32 v43, 1.0, v43
	v_mfma_f32_16x16x32_f16 v[30:33], v[38:41], v[30:33], 0
	v_log_f32_e32 v43, v43
	v_mul_f32_e32 v42, 0x3f317218, v42
	v_add_f32_e32 v45, 1.0, v45
	v_log_f32_e32 v45, v45
	v_max_f32_e32 v42, v35, v42
	s_nop 2
	v_add_f32_e32 v30, v30, v133
	v_mul_f32_e32 v35, 0x3f317218, v43
	v_min_f32_e32 v43, 0x42a00000, v30
	v_mul_f32_e32 v43, 0x3fb8aa3b, v43
	v_exp_f32_e32 v43, v43
	v_max_f32_e32 v35, v36, v35
	v_mul_f32_e32 v36, 0x3f317218, v45
	v_max_f32_e32 v36, v37, v36
	v_add_f32_e32 v31, v31, v133
	v_cvt_pk_f16_f32 v35, v35, v36
	v_cvt_pk_f16_f32 v34, v34, v42
	v_add_f32_e32 v36, 1.0, v43
	v_min_f32_e32 v37, 0x42a00000, v31
	v_add_f32_e32 v32, v32, v133
	v_log_f32_e32 v36, v36
	v_mul_f32_e32 v37, 0x3fb8aa3b, v37
	ds_write_b64 v24, v[34:35] offset:32
	v_min_f32_e32 v35, 0x42a00000, v32
	v_exp_f32_e32 v37, v37
	v_mul_f32_e32 v35, 0x3fb8aa3b, v35
	v_exp_f32_e32 v35, v35
	v_add_f32_e32 v33, v33, v133
	v_mul_f32_e32 v34, 0x3f317218, v36
	v_min_f32_e32 v36, 0x42a00000, v33
	v_max_f32_e32 v30, v30, v34
	v_add_f32_e32 v34, 1.0, v37
	v_mul_f32_e32 v36, 0x3fb8aa3b, v36
	v_log_f32_e32 v34, v34
	v_exp_f32_e32 v36, v36
	v_add_f32_e32 v35, 1.0, v35
	v_mfma_f32_16x16x32_f16 v[26:29], v[38:41], v[26:29], 0
	v_log_f32_e32 v35, v35
	v_mul_f32_e32 v34, 0x3f317218, v34
	v_add_f32_e32 v36, 1.0, v36
	v_log_f32_e32 v36, v36
	v_max_f32_e32 v34, v31, v34
	s_nop 2
	v_add_f32_e32 v26, v26, v131
	v_mul_f32_e32 v31, 0x3f317218, v35
	v_min_f32_e32 v35, 0x42a00000, v26
	v_mul_f32_e32 v35, 0x3fb8aa3b, v35
	v_exp_f32_e32 v35, v35
	v_max_f32_e32 v31, v32, v31
	v_mul_f32_e32 v32, 0x3f317218, v36
	v_max_f32_e32 v32, v33, v32
	v_add_f32_e32 v27, v27, v131
	v_cvt_pk_f16_f32 v31, v31, v32
	v_cvt_pk_f16_f32 v30, v30, v34
	v_add_f32_e32 v32, 1.0, v35
	v_min_f32_e32 v33, 0x42a00000, v27
	v_add_f32_e32 v28, v28, v131
	v_log_f32_e32 v32, v32
	v_mul_f32_e32 v33, 0x3fb8aa3b, v33
	ds_write_b64 v24, v[30:31] offset:1312
	v_min_f32_e32 v31, 0x42a00000, v28
	v_exp_f32_e32 v33, v33
	v_mul_f32_e32 v31, 0x3fb8aa3b, v31
	v_exp_f32_e32 v31, v31
	v_add_f32_e32 v29, v29, v131
	v_mul_f32_e32 v30, 0x3f317218, v32
	v_min_f32_e32 v32, 0x42a00000, v29
	v_max_f32_e32 v26, v26, v30
	v_add_f32_e32 v30, 1.0, v33
	v_mul_f32_e32 v32, 0x3fb8aa3b, v32
	v_log_f32_e32 v30, v30
	v_exp_f32_e32 v32, v32
	v_add_f32_e32 v31, 1.0, v31
	v_mfma_f32_16x16x32_f16 v[18:21], v[38:41], v[18:21], 0
	v_log_f32_e32 v31, v31
	v_mul_f32_e32 v30, 0x3f317218, v30
	v_add_f32_e32 v32, 1.0, v32
	v_log_f32_e32 v32, v32
	v_max_f32_e32 v30, v27, v30
	s_nop 2
	v_add_f32_e32 v18, v18, v121
	v_mul_f32_e32 v27, 0x3f317218, v31
	v_min_f32_e32 v31, 0x42a00000, v18
	v_mul_f32_e32 v31, 0x3fb8aa3b, v31
	v_exp_f32_e32 v31, v31
	v_max_f32_e32 v27, v28, v27
	v_mul_f32_e32 v28, 0x3f317218, v32
	v_max_f32_e32 v28, v29, v28
	v_add_f32_e32 v19, v19, v121
	v_cvt_pk_f16_f32 v27, v27, v28
	v_cvt_pk_f16_f32 v26, v26, v30
	v_add_f32_e32 v28, 1.0, v31
	v_min_f32_e32 v29, 0x42a00000, v19
	v_add_f32_e32 v20, v20, v121
	v_log_f32_e32 v28, v28
	v_mul_f32_e32 v29, 0x3fb8aa3b, v29
	ds_write_b64 v24, v[26:27] offset:2592
	v_min_f32_e32 v26, 0x42a00000, v20
	v_add_f32_e32 v21, v21, v121
	v_exp_f32_e32 v29, v29
	v_mul_f32_e32 v26, 0x3fb8aa3b, v26
	v_min_f32_e32 v27, 0x42a00000, v21
	v_exp_f32_e32 v26, v26
	v_mul_f32_e32 v27, 0x3fb8aa3b, v27
	v_exp_f32_e32 v27, v27
	v_mul_f32_e32 v24, 0x3f317218, v28
	v_max_f32_e32 v18, v18, v24
	v_add_f32_e32 v24, 1.0, v29
	v_log_f32_e32 v24, v24
	v_add_f32_e32 v26, 1.0, v26
	v_log_f32_e32 v26, v26
	v_add_f32_e32 v27, 1.0, v27
	v_log_f32_e32 v27, v27
	v_mul_f32_e32 v24, 0x3f317218, v24
	v_max_f32_e32 v24, v19, v24
	v_mul_f32_e32 v19, 0x3f317218, v26
	v_max_f32_e32 v19, v20, v19
	v_mul_f32_e32 v20, 0x3f317218, v27
	v_max_f32_e32 v20, v21, v20
	v_cvt_pk_f16_f32 v19, v19, v20
	v_cvt_pk_f16_f32 v18, v18, v24
	ds_write_b64 v44, v[18:19] offset:32
	v_mul_u32_u24_e32 v18, 0x50, v0
	s_waitcnt lgkmcnt(0)
	s_barrier
	ds_read_b128 v[92:95], v18
	v_cvt_f32_f16_e32 v55, v111
	v_cvt_f32_f16_e32 v59, v110
	v_cvt_f32_f16_e32 v79, v105
	v_cvt_f32_f16_e32 v82, v104
	v_cvt_f32_f16_e32 v84, v103
	v_cvt_f32_f16_e32 v86, v102
	ds_read_b128 v[96:99], v18 offset:16
	ds_read_b128 v[100:103], v18 offset:32
	ds_read_b128 v[108:111], v18 offset:48
	v_lshl_add_u64 v[104:105], s[8:9], 0, v[118:119]
	v_cvt_f32_f16_e32 v47, v113
	v_cvt_f32_f16_e32 v51, v112
	v_lshl_add_u64 v[112:113], v[104:105], 0, s[6:7]
	s_waitcnt lgkmcnt(3)
	v_cvt_f32_f16_e32 v26, v94
	v_cvt_f32_f16_sdwa v28, v94 dst_sel:DWORD dst_unused:UNUSED_PAD src0_sel:WORD_1
	v_cvt_f32_f16_e32 v30, v95
	v_cvt_f32_f16_sdwa v32, v95 dst_sel:DWORD dst_unused:UNUSED_PAD src0_sel:WORD_1
	global_store_dwordx4 v[112:113], v[92:95], off sc0 sc1
	v_cvt_f32_f16_e32 v53, v122
	v_cvt_f32_f16_e32 v57, v125
	v_lshl_add_u64 v[94:95], v[104:105], 0, s[14:15]
	s_waitcnt lgkmcnt(2)
	global_store_dwordx4 v[94:95], v[96:99], off sc0 sc1
	v_lshl_add_u64 v[94:95], v[104:105], 0, s[16:17]
	s_waitcnt lgkmcnt(1)
	global_store_dwordx4 v[94:95], v[100:103], off sc0 sc1
	v_lshl_add_u64 v[94:95], v[104:105], 0, s[18:19]
	v_cvt_f32_f16_e32 v61, v124
	v_cvt_f32_f16_e32 v63, v117
	v_cvt_f32_f16_e32 v65, v147
	v_cvt_f32_f16_e32 v67, v116
	v_cvt_f32_f16_e32 v69, v145
	v_cvt_f32_f16_e32 v71, v115
	v_cvt_f32_f16_e32 v73, v127
	v_cvt_f32_f16_e32 v75, v114
	v_cvt_f32_f16_e32 v77, v126
	v_cvt_f32_f16_e32 v81, v142
	v_cvt_f32_f16_e32 v83, v141
	v_cvt_f32_f16_e32 v85, v140
	v_cvt_f32_f16_e32 v87, v139
	v_cvt_f32_f16_e32 v25, v25
	v_cvt_f32_f16_e32 v88, v138
	v_cvt_f32_f16_e32 v90, v137
	v_cvt_f32_f16_e32 v23, v23
	v_cvt_f32_f16_e32 v91, v123
	v_cvt_f32_f16_e32 v19, v22
	v_cvt_f32_f16_sdwa v20, v92 dst_sel:DWORD dst_unused:UNUSED_PAD src0_sel:WORD_1
	v_cvt_f32_f16_e32 v22, v93
	v_cvt_f32_f16_sdwa v24, v93 dst_sel:DWORD dst_unused:UNUSED_PAD src0_sel:WORD_1
	v_cvt_f32_f16_e32 v34, v96
	v_cvt_f32_f16_sdwa v36, v96 dst_sel:DWORD dst_unused:UNUSED_PAD src0_sel:WORD_1
	v_cvt_f32_f16_e32 v38, v97
	v_cvt_f32_f16_sdwa v40, v97 dst_sel:DWORD dst_unused:UNUSED_PAD src0_sel:WORD_1
	v_cvt_f32_f16_e32 v42, v98
	v_cvt_f32_f16_sdwa v44, v98 dst_sel:DWORD dst_unused:UNUSED_PAD src0_sel:WORD_1
	v_cvt_f32_f16_e32 v46, v99
	v_cvt_f32_f16_sdwa v48, v99 dst_sel:DWORD dst_unused:UNUSED_PAD src0_sel:WORD_1
	v_cvt_f32_f16_e32 v50, v100
	v_cvt_f32_f16_sdwa v52, v100 dst_sel:DWORD dst_unused:UNUSED_PAD src0_sel:WORD_1
	v_cvt_f32_f16_e32 v54, v101
	v_cvt_f32_f16_sdwa v56, v101 dst_sel:DWORD dst_unused:UNUSED_PAD src0_sel:WORD_1
	v_cvt_f32_f16_e32 v58, v102
	v_cvt_f32_f16_sdwa v60, v102 dst_sel:DWORD dst_unused:UNUSED_PAD src0_sel:WORD_1
	v_cvt_f32_f16_e32 v62, v103
	v_cvt_f32_f16_sdwa v64, v103 dst_sel:DWORD dst_unused:UNUSED_PAD src0_sel:WORD_1
	s_waitcnt lgkmcnt(0)
	v_cvt_f32_f16_e32 v66, v108
	v_cvt_f32_f16_sdwa v68, v108 dst_sel:DWORD dst_unused:UNUSED_PAD src0_sel:WORD_1
	v_cvt_f32_f16_e32 v70, v109
	v_cvt_f32_f16_sdwa v72, v109 dst_sel:DWORD dst_unused:UNUSED_PAD src0_sel:WORD_1
	v_cvt_f32_f16_e32 v74, v110
	v_cvt_f32_f16_sdwa v76, v110 dst_sel:DWORD dst_unused:UNUSED_PAD src0_sel:WORD_1
	v_cvt_f32_f16_e32 v78, v111
	v_cvt_f32_f16_sdwa v18, v111 dst_sel:DWORD dst_unused:UNUSED_PAD src0_sel:WORD_1
	global_store_dwordx4 v[94:95], v[108:111], off sc0 sc1
	v_cvt_f32_f16_e32 v80, v92
	v_mov_b32_e32 v21, 0xa000
	v_mov_b32_e32 v27, 0xa0d0
	ds_read_b128 v[92:95], v21 offset:64
	ds_read_b128 v[96:99], v21 offset:80
	ds_read_b128 v[100:103], v21 offset:96
	ds_read_b128 v[108:111], v21 offset:112
	s_waitcnt lgkmcnt(0)
	ds_read_b128 v[112:115], v27 offset:64
	ds_read_b128 v[116:119], v27 offset:80
	ds_read_b128 v[120:123], v27 offset:96
	ds_read_b128 v[124:127], v27 offset:112
	s_lshr_b32 s0, s23, 5
	s_waitcnt vmcnt(11)
	v_pk_mul_f32 v[128:129], v[80:81], v[14:15] op_sel_hi:[0,1]
	v_exp_f32_e32 v128, v128
	v_exp_f32_e32 v129, v129
	v_pk_mul_f32 v[130:131], v[80:81], v[16:17] op_sel_hi:[0,1]
	v_exp_f32_e32 v130, v130
	v_exp_f32_e32 v131, v131
	v_mul_f32_e32 v104, v80, v19
	v_pk_mul_f32 v[92:93], v[104:105], v[92:93] op_sel_hi:[0,1]
	v_pk_fma_f32 v[128:129], v[128:129], 0, v[92:93] op_sel_hi:[1,0,1]
	v_pk_mul_f32 v[92:93], v[104:105], v[94:95] op_sel_hi:[0,1]
	v_pk_fma_f32 v[130:131], v[130:131], 0, v[92:93] op_sel_hi:[1,0,1]
	s_waitcnt vmcnt(10)
	v_pk_mul_f32 v[92:93], v[80:81], v[10:11] op_sel_hi:[0,1]
	v_exp_f32_e32 v92, v92
	v_exp_f32_e32 v93, v93
	v_pk_mul_f32 v[94:95], v[80:81], v[12:13] op_sel_hi:[0,1]
	v_exp_f32_e32 v94, v94
	v_exp_f32_e32 v95, v95
	v_pk_mul_f32 v[96:97], v[104:105], v[96:97] op_sel_hi:[0,1]
	v_pk_fma_f32 v[132:133], v[92:93], 0, v[96:97] op_sel_hi:[1,0,1]
	v_pk_mul_f32 v[92:93], v[104:105], v[98:99] op_sel_hi:[0,1]
	v_pk_fma_f32 v[134:135], v[94:95], 0, v[92:93] op_sel_hi:[1,0,1]
	s_waitcnt vmcnt(9)
	v_pk_mul_f32 v[92:93], v[80:81], v[6:7] op_sel_hi:[0,1]
	v_exp_f32_e32 v92, v92
	v_exp_f32_e32 v93, v93
	v_pk_mul_f32 v[94:95], v[80:81], v[8:9] op_sel_hi:[0,1]
	v_exp_f32_e32 v94, v94
	v_exp_f32_e32 v95, v95
	v_pk_mul_f32 v[96:97], v[104:105], v[100:101] op_sel_hi:[0,1]
	v_pk_fma_f32 v[136:137], v[92:93], 0, v[96:97] op_sel_hi:[1,0,1]
	v_pk_mul_f32 v[92:93], v[104:105], v[102:103] op_sel_hi:[0,1]
	v_pk_fma_f32 v[138:139], v[94:95], 0, v[92:93] op_sel_hi:[1,0,1]
	s_waitcnt vmcnt(8)
	v_pk_mul_f32 v[92:93], v[80:81], v[2:3] op_sel_hi:[0,1]
	v_exp_f32_e32 v92, v92
	v_exp_f32_e32 v93, v93
	v_pk_mul_f32 v[94:95], v[80:81], v[4:5] op_sel_hi:[0,1]
	v_exp_f32_e32 v94, v94
	v_exp_f32_e32 v95, v95
	v_pk_mul_f32 v[96:97], v[104:105], v[108:109] op_sel_hi:[0,1]
	v_pk_fma_f32 v[140:141], v[92:93], 0, v[96:97] op_sel_hi:[1,0,1]
	v_pk_mul_f32 v[92:93], v[104:105], v[110:111] op_sel_hi:[0,1]
	v_pk_fma_f32 v[104:105], v[94:95], 0, v[92:93] op_sel_hi:[1,0,1]
	v_mov_b32_e32 v19, 0xa1a0
	s_waitcnt lgkmcnt(0)
	s_and_b32 s6, s22, 0x7ffffc0
	ds_read_b128 v[92:95], v19 offset:64
	ds_read_b128 v[96:99], v19 offset:80
	ds_read_b128 v[100:103], v19 offset:96
	ds_read_b128 v[108:111], v19 offset:112
	v_mov_b32_e32 v19, 0xa270
	v_pk_mul_f32 v[142:143], v[20:21], v[14:15] op_sel_hi:[0,1]
	v_exp_f32_e32 v142, v142
	v_exp_f32_e32 v143, v143
	v_mul_f32_e32 v144, v20, v91
	v_pk_mul_f32 v[112:113], v[144:145], v[112:113] op_sel_hi:[0,1]
	v_pk_mul_f32 v[114:115], v[144:145], v[114:115] op_sel_hi:[0,1]
	v_pk_fma_f32 v[128:129], v[128:129], v[142:143], v[112:113]
	v_pk_mul_f32 v[112:113], v[20:21], v[16:17] op_sel_hi:[0,1]
	v_exp_f32_e32 v112, v112
	v_exp_f32_e32 v113, v113
	v_pk_mul_f32 v[116:117], v[144:145], v[116:117] op_sel_hi:[0,1]
	s_or_b32 s0, s0, s6
	s_lshl_b64 s[6:7], s[0:1], 14
	v_pk_fma_f32 v[130:131], v[130:131], v[112:113], v[114:115]
	v_pk_mul_f32 v[112:113], v[20:21], v[10:11] op_sel_hi:[0,1]
	v_exp_f32_e32 v112, v112
	v_exp_f32_e32 v113, v113
	v_pk_mul_f32 v[114:115], v[20:21], v[12:13] op_sel_hi:[0,1]
	v_exp_f32_e32 v114, v114
	v_exp_f32_e32 v115, v115
	v_pk_fma_f32 v[132:133], v[132:133], v[112:113], v[116:117]
	v_pk_mul_f32 v[112:113], v[144:145], v[118:119] op_sel_hi:[0,1]
	v_pk_mul_f32 v[116:117], v[144:145], v[120:121] op_sel_hi:[0,1]
	v_pk_fma_f32 v[134:135], v[134:135], v[114:115], v[112:113]
	v_pk_mul_f32 v[112:113], v[20:21], v[6:7] op_sel_hi:[0,1]
	v_exp_f32_e32 v112, v112
	v_exp_f32_e32 v113, v113
	v_pk_mul_f32 v[114:115], v[20:21], v[8:9] op_sel_hi:[0,1]
	v_exp_f32_e32 v114, v114
	v_exp_f32_e32 v115, v115
	v_pk_fma_f32 v[136:137], v[136:137], v[112:113], v[116:117]
	v_pk_mul_f32 v[112:113], v[144:145], v[122:123] op_sel_hi:[0,1]
	v_pk_mul_f32 v[116:117], v[144:145], v[124:125] op_sel_hi:[0,1]
	v_pk_fma_f32 v[138:139], v[138:139], v[114:115], v[112:113]
	v_pk_mul_f32 v[112:113], v[20:21], v[2:3] op_sel_hi:[0,1]
	v_exp_f32_e32 v112, v112
	v_exp_f32_e32 v113, v113
	v_pk_mul_f32 v[114:115], v[20:21], v[4:5] op_sel_hi:[0,1]
	v_exp_f32_e32 v114, v114
	v_exp_f32_e32 v115, v115
	v_pk_fma_f32 v[140:141], v[140:141], v[112:113], v[116:117]
	v_pk_mul_f32 v[112:113], v[144:145], v[126:127] op_sel_hi:[0,1]
	s_lshl_b64 s[0:1], s[0:1], 11
	v_pk_fma_f32 v[104:105], v[104:105], v[114:115], v[112:113]
	s_add_u32 s0, s2, s0
	s_waitcnt lgkmcnt(0)
	s_addc_u32 s1, s3, s1
	ds_read_b128 v[112:115], v19 offset:64
	ds_read_b128 v[116:119], v19 offset:80
	ds_read_b128 v[120:123], v19 offset:96
	ds_read_b128 v[124:127], v19 offset:112
	v_mov_b32_e32 v19, 0xa340
	v_pk_mul_f32 v[142:143], v[22:23], v[14:15] op_sel_hi:[0,1]
	v_exp_f32_e32 v142, v142
	v_exp_f32_e32 v143, v143
	v_mul_f32_e32 v144, v22, v23
	v_pk_mul_f32 v[92:93], v[144:145], v[92:93] op_sel_hi:[0,1]
	v_pk_mul_f32 v[94:95], v[144:145], v[94:95] op_sel_hi:[0,1]
	v_pk_fma_f32 v[128:129], v[128:129], v[142:143], v[92:93]
	v_pk_mul_f32 v[92:93], v[22:23], v[16:17] op_sel_hi:[0,1]
	v_exp_f32_e32 v92, v92
	v_exp_f32_e32 v93, v93
	v_pk_mul_f32 v[96:97], v[144:145], v[96:97] op_sel_hi:[0,1]
	v_pk_fma_f32 v[130:131], v[130:131], v[92:93], v[94:95]
	v_pk_mul_f32 v[92:93], v[22:23], v[10:11] op_sel_hi:[0,1]
	v_exp_f32_e32 v92, v92
	v_exp_f32_e32 v93, v93
	v_pk_mul_f32 v[94:95], v[22:23], v[12:13] op_sel_hi:[0,1]
	v_exp_f32_e32 v94, v94
	v_exp_f32_e32 v95, v95
	v_pk_fma_f32 v[132:133], v[132:133], v[92:93], v[96:97]
	v_pk_mul_f32 v[92:93], v[144:145], v[98:99] op_sel_hi:[0,1]
	v_pk_mul_f32 v[96:97], v[144:145], v[100:101] op_sel_hi:[0,1]
	v_pk_fma_f32 v[134:135], v[134:135], v[94:95], v[92:93]
	v_pk_mul_f32 v[92:93], v[22:23], v[6:7] op_sel_hi:[0,1]
	v_exp_f32_e32 v92, v92
	v_exp_f32_e32 v93, v93
	v_pk_mul_f32 v[94:95], v[22:23], v[8:9] op_sel_hi:[0,1]
	v_exp_f32_e32 v94, v94
	v_exp_f32_e32 v95, v95
	v_pk_fma_f32 v[136:137], v[136:137], v[92:93], v[96:97]
	v_pk_mul_f32 v[92:93], v[144:145], v[102:103] op_sel_hi:[0,1]
	v_pk_mul_f32 v[96:97], v[144:145], v[108:109] op_sel_hi:[0,1]
	v_pk_fma_f32 v[138:139], v[138:139], v[94:95], v[92:93]
	v_pk_mul_f32 v[92:93], v[22:23], v[2:3] op_sel_hi:[0,1]
	v_exp_f32_e32 v92, v92
	v_exp_f32_e32 v93, v93
	v_pk_mul_f32 v[94:95], v[22:23], v[4:5] op_sel_hi:[0,1]
	v_exp_f32_e32 v94, v94
	v_exp_f32_e32 v95, v95
	v_pk_fma_f32 v[140:141], v[140:141], v[92:93], v[96:97]
	v_pk_mul_f32 v[92:93], v[144:145], v[110:111] op_sel_hi:[0,1]
	v_pk_fma_f32 v[104:105], v[104:105], v[94:95], v[92:93]
	s_nop 0
	s_waitcnt lgkmcnt(0)
	s_nop 0
	ds_read_b128 v[92:95], v19 offset:64
	ds_read_b128 v[96:99], v19 offset:80
	ds_read_b128 v[100:103], v19 offset:96
	ds_read_b128 v[108:111], v19 offset:112
	v_mov_b32_e32 v19, 0xa410
	v_pk_mul_f32 v[142:143], v[24:25], v[14:15] op_sel_hi:[0,1]
	v_exp_f32_e32 v142, v142
	v_exp_f32_e32 v143, v143
	v_mul_f32_e32 v90, v24, v90
	v_pk_mul_f32 v[112:113], v[90:91], v[112:113] op_sel_hi:[0,1]
	v_pk_mul_f32 v[114:115], v[90:91], v[114:115] op_sel_hi:[0,1]
	v_pk_fma_f32 v[128:129], v[128:129], v[142:143], v[112:113]
	v_pk_mul_f32 v[112:113], v[24:25], v[16:17] op_sel_hi:[0,1]
	v_exp_f32_e32 v112, v112
	v_exp_f32_e32 v113, v113
	v_pk_mul_f32 v[116:117], v[90:91], v[116:117] op_sel_hi:[0,1]
	v_pk_fma_f32 v[130:131], v[130:131], v[112:113], v[114:115]
	v_pk_mul_f32 v[112:113], v[24:25], v[10:11] op_sel_hi:[0,1]
	v_exp_f32_e32 v112, v112
	v_exp_f32_e32 v113, v113
	v_pk_mul_f32 v[114:115], v[24:25], v[12:13] op_sel_hi:[0,1]
	v_exp_f32_e32 v114, v114
	v_exp_f32_e32 v115, v115
	v_pk_fma_f32 v[132:133], v[132:133], v[112:113], v[116:117]
	v_pk_mul_f32 v[112:113], v[90:91], v[118:119] op_sel_hi:[0,1]
	v_pk_mul_f32 v[116:117], v[90:91], v[120:121] op_sel_hi:[0,1]
	v_pk_fma_f32 v[134:135], v[134:135], v[114:115], v[112:113]
	v_pk_mul_f32 v[112:113], v[24:25], v[6:7] op_sel_hi:[0,1]
	v_exp_f32_e32 v112, v112
	v_exp_f32_e32 v113, v113
	v_pk_mul_f32 v[114:115], v[24:25], v[8:9] op_sel_hi:[0,1]
	v_exp_f32_e32 v114, v114
	v_exp_f32_e32 v115, v115
	v_pk_fma_f32 v[136:137], v[136:137], v[112:113], v[116:117]
	v_pk_mul_f32 v[112:113], v[90:91], v[122:123] op_sel_hi:[0,1]
	v_pk_mul_f32 v[116:117], v[90:91], v[124:125] op_sel_hi:[0,1]
	v_pk_fma_f32 v[138:139], v[138:139], v[114:115], v[112:113]
	v_pk_mul_f32 v[112:113], v[24:25], v[2:3] op_sel_hi:[0,1]
	v_pk_mul_f32 v[114:115], v[24:25], v[4:5] op_sel_hi:[0,1]
	v_exp_f32_e32 v112, v112
	v_exp_f32_e32 v113, v113
	v_exp_f32_e32 v114, v114
	v_exp_f32_e32 v115, v115
	v_pk_mul_f32 v[90:91], v[90:91], v[126:127] op_sel_hi:[0,1]
	v_pk_fma_f32 v[140:141], v[140:141], v[112:113], v[116:117]
	v_pk_fma_f32 v[90:91], v[104:105], v[114:115], v[90:91]
	s_nop 0
	s_waitcnt lgkmcnt(0)
	s_nop 0
	ds_read_b128 v[112:115], v19 offset:64
	ds_read_b128 v[116:119], v19 offset:80
	ds_read_b128 v[120:123], v19 offset:96
	ds_read_b128 v[124:127], v19 offset:112
	v_mov_b32_e32 v19, 0xa4e0
	v_pk_mul_f32 v[104:105], v[26:27], v[14:15] op_sel_hi:[0,1]
	v_exp_f32_e32 v104, v104
	v_exp_f32_e32 v105, v105
	v_mul_f32_e32 v142, v26, v89
	v_pk_mul_f32 v[92:93], v[142:143], v[92:93] op_sel_hi:[0,1]
	v_pk_mul_f32 v[94:95], v[142:143], v[94:95] op_sel_hi:[0,1]
	v_pk_fma_f32 v[128:129], v[128:129], v[104:105], v[92:93]
	v_pk_mul_f32 v[92:93], v[26:27], v[16:17] op_sel_hi:[0,1]
	v_exp_f32_e32 v92, v92
	v_exp_f32_e32 v93, v93
	v_pk_mul_f32 v[96:97], v[142:143], v[96:97] op_sel_hi:[0,1]
	v_pk_fma_f32 v[130:131], v[130:131], v[92:93], v[94:95]
	v_pk_mul_f32 v[92:93], v[26:27], v[10:11] op_sel_hi:[0,1]
	v_exp_f32_e32 v92, v92
	v_exp_f32_e32 v93, v93
	v_pk_mul_f32 v[94:95], v[26:27], v[12:13] op_sel_hi:[0,1]
	v_exp_f32_e32 v94, v94
	v_exp_f32_e32 v95, v95
	v_pk_fma_f32 v[132:133], v[132:133], v[92:93], v[96:97]
	v_pk_mul_f32 v[92:93], v[142:143], v[98:99] op_sel_hi:[0,1]
	v_pk_mul_f32 v[96:97], v[142:143], v[100:101] op_sel_hi:[0,1]
	v_pk_fma_f32 v[134:135], v[134:135], v[94:95], v[92:93]
	v_pk_mul_f32 v[92:93], v[26:27], v[6:7] op_sel_hi:[0,1]
	v_exp_f32_e32 v92, v92
	v_exp_f32_e32 v93, v93
	v_pk_mul_f32 v[94:95], v[26:27], v[8:9] op_sel_hi:[0,1]
	v_exp_f32_e32 v94, v94
	v_exp_f32_e32 v95, v95
	v_pk_fma_f32 v[136:137], v[136:137], v[92:93], v[96:97]
	v_pk_mul_f32 v[92:93], v[142:143], v[102:103] op_sel_hi:[0,1]
	v_pk_mul_f32 v[96:97], v[142:143], v[108:109] op_sel_hi:[0,1]
	v_pk_fma_f32 v[138:139], v[138:139], v[94:95], v[92:93]
	v_pk_mul_f32 v[92:93], v[26:27], v[2:3] op_sel_hi:[0,1]
	v_exp_f32_e32 v92, v92
	v_exp_f32_e32 v93, v93
	v_pk_mul_f32 v[94:95], v[26:27], v[4:5] op_sel_hi:[0,1]
	v_exp_f32_e32 v94, v94
	v_exp_f32_e32 v95, v95
	v_pk_fma_f32 v[108:109], v[140:141], v[92:93], v[96:97]
	v_pk_mul_f32 v[92:93], v[142:143], v[110:111] op_sel_hi:[0,1]
	v_pk_fma_f32 v[110:111], v[90:91], v[94:95], v[92:93]
	s_nop 0
	s_waitcnt lgkmcnt(0)
	s_nop 0
	ds_read_b128 v[90:93], v19 offset:64
	ds_read_b128 v[94:97], v19 offset:80
	ds_read_b128 v[98:101], v19 offset:96
	ds_read_b128 v[102:105], v19 offset:112
	v_mov_b32_e32 v19, 0xa5b0
	v_pk_mul_f32 v[140:141], v[28:29], v[14:15] op_sel_hi:[0,1]
	v_exp_f32_e32 v140, v140
	v_exp_f32_e32 v141, v141
	v_pk_mul_f32 v[142:143], v[28:29], v[16:17] op_sel_hi:[0,1]
	v_exp_f32_e32 v142, v142
	v_exp_f32_e32 v143, v143
	v_mul_f32_e32 v88, v28, v88
	v_pk_mul_f32 v[112:113], v[88:89], v[112:113] op_sel_hi:[0,1]
	v_pk_fma_f32 v[128:129], v[128:129], v[140:141], v[112:113]
	v_pk_mul_f32 v[112:113], v[88:89], v[114:115] op_sel_hi:[0,1]
	v_pk_fma_f32 v[130:131], v[130:131], v[142:143], v[112:113]
	v_pk_mul_f32 v[112:113], v[28:29], v[10:11] op_sel_hi:[0,1]
	v_exp_f32_e32 v112, v112
	v_exp_f32_e32 v113, v113
	v_pk_mul_f32 v[114:115], v[28:29], v[12:13] op_sel_hi:[0,1]
	v_exp_f32_e32 v114, v114
	v_exp_f32_e32 v115, v115
	v_pk_mul_f32 v[116:117], v[88:89], v[116:117] op_sel_hi:[0,1]
	v_pk_fma_f32 v[132:133], v[132:133], v[112:113], v[116:117]
	v_pk_mul_f32 v[112:113], v[88:89], v[118:119] op_sel_hi:[0,1]
	v_pk_fma_f32 v[134:135], v[134:135], v[114:115], v[112:113]
	v_pk_mul_f32 v[112:113], v[28:29], v[6:7] op_sel_hi:[0,1]
	v_exp_f32_e32 v112, v112
	v_exp_f32_e32 v113, v113
	v_pk_mul_f32 v[114:115], v[28:29], v[8:9] op_sel_hi:[0,1]
	v_exp_f32_e32 v114, v114
	v_exp_f32_e32 v115, v115
	v_pk_mul_f32 v[116:117], v[88:89], v[120:121] op_sel_hi:[0,1]
	v_pk_fma_f32 v[136:137], v[136:137], v[112:113], v[116:117]
	v_pk_mul_f32 v[112:113], v[88:89], v[122:123] op_sel_hi:[0,1]
	v_pk_fma_f32 v[138:139], v[138:139], v[114:115], v[112:113]
	v_pk_mul_f32 v[112:113], v[28:29], v[2:3] op_sel_hi:[0,1]
	v_pk_mul_f32 v[114:115], v[28:29], v[4:5] op_sel_hi:[0,1]
	v_exp_f32_e32 v112, v112
	v_exp_f32_e32 v113, v113
	v_exp_f32_e32 v114, v114
	v_exp_f32_e32 v115, v115
	v_pk_mul_f32 v[116:117], v[88:89], v[124:125] op_sel_hi:[0,1]
	v_pk_mul_f32 v[88:89], v[88:89], v[126:127] op_sel_hi:[0,1]
	v_pk_fma_f32 v[124:125], v[108:109], v[112:113], v[116:117]
	v_pk_fma_f32 v[88:89], v[110:111], v[114:115], v[88:89]
	s_nop 0
	s_waitcnt lgkmcnt(0)
	s_nop 0
	ds_read_b128 v[108:111], v19 offset:64
	ds_read_b128 v[112:115], v19 offset:80
	ds_read_b128 v[116:119], v19 offset:96
	ds_read_b128 v[120:123], v19 offset:112
	v_mov_b32_e32 v19, 0xa680
	v_pk_mul_f32 v[140:141], v[30:31], v[14:15] op_sel_hi:[0,1]
	v_exp_f32_e32 v140, v140
	v_exp_f32_e32 v141, v141
	v_pk_mul_f32 v[142:143], v[30:31], v[16:17] op_sel_hi:[0,1]
	v_exp_f32_e32 v142, v142
	v_exp_f32_e32 v143, v143
	v_mul_f32_e32 v126, v30, v25
	v_pk_mul_f32 v[90:91], v[126:127], v[90:91] op_sel_hi:[0,1]
	v_pk_fma_f32 v[128:129], v[128:129], v[140:141], v[90:91]
	v_pk_mul_f32 v[90:91], v[126:127], v[92:93] op_sel_hi:[0,1]
	v_pk_fma_f32 v[130:131], v[130:131], v[142:143], v[90:91]
	v_pk_mul_f32 v[90:91], v[30:31], v[10:11] op_sel_hi:[0,1]
	v_exp_f32_e32 v90, v90
	v_exp_f32_e32 v91, v91
	v_pk_mul_f32 v[92:93], v[30:31], v[12:13] op_sel_hi:[0,1]
	v_exp_f32_e32 v92, v92
	v_exp_f32_e32 v93, v93
	v_pk_mul_f32 v[94:95], v[126:127], v[94:95] op_sel_hi:[0,1]
	v_pk_fma_f32 v[132:133], v[132:133], v[90:91], v[94:95]
	v_pk_mul_f32 v[90:91], v[126:127], v[96:97] op_sel_hi:[0,1]
	v_pk_fma_f32 v[134:135], v[134:135], v[92:93], v[90:91]
	v_pk_mul_f32 v[90:91], v[30:31], v[6:7] op_sel_hi:[0,1]
	v_exp_f32_e32 v90, v90
	v_exp_f32_e32 v91, v91
	v_pk_mul_f32 v[92:93], v[30:31], v[8:9] op_sel_hi:[0,1]
	v_exp_f32_e32 v92, v92
	v_exp_f32_e32 v93, v93
	v_pk_mul_f32 v[94:95], v[126:127], v[98:99] op_sel_hi:[0,1]
	v_pk_fma_f32 v[136:137], v[136:137], v[90:91], v[94:95]
	v_pk_mul_f32 v[90:91], v[126:127], v[100:101] op_sel_hi:[0,1]
	v_pk_fma_f32 v[138:139], v[138:139], v[92:93], v[90:91]
	v_pk_mul_f32 v[90:91], v[30:31], v[2:3] op_sel_hi:[0,1]
	v_exp_f32_e32 v90, v90
	v_exp_f32_e32 v91, v91
	v_pk_mul_f32 v[92:93], v[30:31], v[4:5] op_sel_hi:[0,1]
	v_exp_f32_e32 v92, v92
	v_exp_f32_e32 v93, v93
	v_pk_mul_f32 v[94:95], v[126:127], v[102:103] op_sel_hi:[0,1]
	v_pk_fma_f32 v[124:125], v[124:125], v[90:91], v[94:95]
	v_pk_mul_f32 v[90:91], v[126:127], v[104:105] op_sel_hi:[0,1]
	v_pk_fma_f32 v[104:105], v[88:89], v[92:93], v[90:91]
	s_nop 0
	s_waitcnt lgkmcnt(0)
	s_nop 0
	ds_read_b128 v[88:91], v19 offset:64
	ds_read_b128 v[92:95], v19 offset:80
	ds_read_b128 v[96:99], v19 offset:96
	ds_read_b128 v[100:103], v19 offset:112
	v_mov_b32_e32 v19, 0xa750
	v_pk_mul_f32 v[140:141], v[32:33], v[14:15] op_sel_hi:[0,1]
	v_exp_f32_e32 v140, v140
	v_exp_f32_e32 v141, v141
	v_pk_mul_f32 v[142:143], v[32:33], v[16:17] op_sel_hi:[0,1]
	v_exp_f32_e32 v142, v142
	v_exp_f32_e32 v143, v143
	v_mul_f32_e32 v126, v32, v87
	v_pk_mul_f32 v[108:109], v[126:127], v[108:109] op_sel_hi:[0,1]
	v_pk_fma_f32 v[128:129], v[128:129], v[140:141], v[108:109]
	v_pk_mul_f32 v[108:109], v[126:127], v[110:111] op_sel_hi:[0,1]
	v_pk_fma_f32 v[130:131], v[130:131], v[142:143], v[108:109]
	v_pk_mul_f32 v[108:109], v[32:33], v[10:11] op_sel_hi:[0,1]
	v_exp_f32_e32 v108, v108
	v_exp_f32_e32 v109, v109
	v_pk_mul_f32 v[110:111], v[32:33], v[12:13] op_sel_hi:[0,1]
	v_exp_f32_e32 v110, v110
	v_exp_f32_e32 v111, v111
	v_pk_mul_f32 v[112:113], v[126:127], v[112:113] op_sel_hi:[0,1]
	v_pk_fma_f32 v[132:133], v[132:133], v[108:109], v[112:113]
	v_pk_mul_f32 v[108:109], v[126:127], v[114:115] op_sel_hi:[0,1]
	v_pk_fma_f32 v[134:135], v[134:135], v[110:111], v[108:109]
	v_pk_mul_f32 v[108:109], v[32:33], v[6:7] op_sel_hi:[0,1]
	v_exp_f32_e32 v108, v108
	v_exp_f32_e32 v109, v109
	v_pk_mul_f32 v[110:111], v[32:33], v[8:9] op_sel_hi:[0,1]
	v_exp_f32_e32 v110, v110
	v_exp_f32_e32 v111, v111
	v_pk_mul_f32 v[112:113], v[126:127], v[116:117] op_sel_hi:[0,1]
	v_pk_fma_f32 v[136:137], v[136:137], v[108:109], v[112:113]
	v_pk_mul_f32 v[108:109], v[126:127], v[118:119] op_sel_hi:[0,1]
	v_pk_fma_f32 v[138:139], v[138:139], v[110:111], v[108:109]
	v_pk_mul_f32 v[108:109], v[32:33], v[2:3] op_sel_hi:[0,1]
	v_exp_f32_e32 v108, v108
	v_exp_f32_e32 v109, v109
	v_pk_mul_f32 v[110:111], v[32:33], v[4:5] op_sel_hi:[0,1]
	v_exp_f32_e32 v110, v110
	v_exp_f32_e32 v111, v111
	v_pk_mul_f32 v[112:113], v[126:127], v[120:121] op_sel_hi:[0,1]
	v_pk_fma_f32 v[124:125], v[124:125], v[108:109], v[112:113]
	v_pk_mul_f32 v[108:109], v[126:127], v[122:123] op_sel_hi:[0,1]
	v_pk_fma_f32 v[104:105], v[104:105], v[110:111], v[108:109]
	s_nop 0
	s_waitcnt lgkmcnt(0)
	s_nop 0
	ds_read_b128 v[108:111], v19 offset:64
	ds_read_b128 v[112:115], v19 offset:80
	ds_read_b128 v[116:119], v19 offset:96
	ds_read_b128 v[120:123], v19 offset:112
	v_mov_b32_e32 v19, 0xa820
	v_pk_mul_f32 v[126:127], v[34:35], v[14:15] op_sel_hi:[0,1]
	v_exp_f32_e32 v126, v126
	v_exp_f32_e32 v127, v127
	v_pk_mul_f32 v[140:141], v[34:35], v[16:17] op_sel_hi:[0,1]
	v_exp_f32_e32 v140, v140
	v_exp_f32_e32 v141, v141
	v_mul_f32_e32 v86, v34, v86
	v_pk_mul_f32 v[88:89], v[86:87], v[88:89] op_sel_hi:[0,1]
	v_pk_fma_f32 v[126:127], v[128:129], v[126:127], v[88:89]
	v_pk_mul_f32 v[88:89], v[86:87], v[90:91] op_sel_hi:[0,1]
	v_pk_fma_f32 v[128:129], v[130:131], v[140:141], v[88:89]
	v_pk_mul_f32 v[88:89], v[34:35], v[10:11] op_sel_hi:[0,1]
	v_exp_f32_e32 v88, v88
	v_exp_f32_e32 v89, v89
	v_pk_mul_f32 v[90:91], v[34:35], v[12:13] op_sel_hi:[0,1]
	v_exp_f32_e32 v90, v90
	v_exp_f32_e32 v91, v91
	v_pk_mul_f32 v[92:93], v[86:87], v[92:93] op_sel_hi:[0,1]
	v_pk_fma_f32 v[130:131], v[132:133], v[88:89], v[92:93]
	v_pk_mul_f32 v[88:89], v[86:87], v[94:95] op_sel_hi:[0,1]
	v_pk_fma_f32 v[132:133], v[134:135], v[90:91], v[88:89]
	v_pk_mul_f32 v[88:89], v[34:35], v[6:7] op_sel_hi:[0,1]
	v_exp_f32_e32 v88, v88
	v_exp_f32_e32 v89, v89
	v_pk_mul_f32 v[90:91], v[34:35], v[8:9] op_sel_hi:[0,1]
	v_exp_f32_e32 v90, v90
	v_exp_f32_e32 v91, v91
	v_pk_mul_f32 v[92:93], v[86:87], v[96:97] op_sel_hi:[0,1]
	v_pk_fma_f32 v[134:135], v[136:137], v[88:89], v[92:93]
	v_pk_mul_f32 v[88:89], v[86:87], v[98:99] op_sel_hi:[0,1]
	v_pk_fma_f32 v[136:137], v[138:139], v[90:91], v[88:89]
	v_pk_mul_f32 v[88:89], v[34:35], v[2:3] op_sel_hi:[0,1]
	v_pk_mul_f32 v[90:91], v[34:35], v[4:5] op_sel_hi:[0,1]
	v_exp_f32_e32 v88, v88
	v_exp_f32_e32 v89, v89
	v_exp_f32_e32 v90, v90
	v_exp_f32_e32 v91, v91
	v_pk_mul_f32 v[92:93], v[86:87], v[100:101] op_sel_hi:[0,1]
	v_pk_mul_f32 v[86:87], v[86:87], v[102:103] op_sel_hi:[0,1]
	v_pk_fma_f32 v[124:125], v[124:125], v[88:89], v[92:93]
	v_pk_fma_f32 v[102:103], v[104:105], v[90:91], v[86:87]
	s_nop 0
	s_waitcnt lgkmcnt(0)
	s_nop 0
	ds_read_b128 v[86:89], v19 offset:64
	ds_read_b128 v[90:93], v19 offset:80
	ds_read_b128 v[94:97], v19 offset:96
	ds_read_b128 v[98:101], v19 offset:112
	v_mov_b32_e32 v19, 0xa8f0
	v_pk_mul_f32 v[138:139], v[36:37], v[14:15] op_sel_hi:[0,1]
	v_exp_f32_e32 v138, v138
	v_exp_f32_e32 v139, v139
	v_pk_mul_f32 v[140:141], v[36:37], v[16:17] op_sel_hi:[0,1]
	v_exp_f32_e32 v140, v140
	v_exp_f32_e32 v141, v141
	v_mul_f32_e32 v104, v36, v85
	v_pk_mul_f32 v[108:109], v[104:105], v[108:109] op_sel_hi:[0,1]
	v_pk_fma_f32 v[126:127], v[126:127], v[138:139], v[108:109]
	v_pk_mul_f32 v[108:109], v[104:105], v[110:111] op_sel_hi:[0,1]
	v_pk_fma_f32 v[128:129], v[128:129], v[140:141], v[108:109]
	v_pk_mul_f32 v[108:109], v[36:37], v[10:11] op_sel_hi:[0,1]
	v_exp_f32_e32 v108, v108
	v_exp_f32_e32 v109, v109
	v_pk_mul_f32 v[110:111], v[36:37], v[12:13] op_sel_hi:[0,1]
	v_exp_f32_e32 v110, v110
	v_exp_f32_e32 v111, v111
	v_pk_mul_f32 v[112:113], v[104:105], v[112:113] op_sel_hi:[0,1]
	v_pk_fma_f32 v[130:131], v[130:131], v[108:109], v[112:113]
	v_pk_mul_f32 v[108:109], v[104:105], v[114:115] op_sel_hi:[0,1]
	v_pk_fma_f32 v[132:133], v[132:133], v[110:111], v[108:109]
	v_pk_mul_f32 v[108:109], v[36:37], v[6:7] op_sel_hi:[0,1]
	v_exp_f32_e32 v108, v108
	v_exp_f32_e32 v109, v109
	v_pk_mul_f32 v[110:111], v[36:37], v[8:9] op_sel_hi:[0,1]
	v_exp_f32_e32 v110, v110
	v_exp_f32_e32 v111, v111
	v_pk_mul_f32 v[112:113], v[104:105], v[116:117] op_sel_hi:[0,1]
	v_pk_fma_f32 v[134:135], v[134:135], v[108:109], v[112:113]
	v_pk_mul_f32 v[108:109], v[104:105], v[118:119] op_sel_hi:[0,1]
	v_pk_fma_f32 v[136:137], v[136:137], v[110:111], v[108:109]
	v_pk_mul_f32 v[108:109], v[36:37], v[2:3] op_sel_hi:[0,1]
	v_pk_mul_f32 v[110:111], v[36:37], v[4:5] op_sel_hi:[0,1]
	v_exp_f32_e32 v108, v108
	v_exp_f32_e32 v109, v109
	v_exp_f32_e32 v110, v110
	v_exp_f32_e32 v111, v111
	v_pk_mul_f32 v[112:113], v[104:105], v[120:121] op_sel_hi:[0,1]
	v_pk_mul_f32 v[104:105], v[104:105], v[122:123] op_sel_hi:[0,1]
	v_pk_fma_f32 v[120:121], v[124:125], v[108:109], v[112:113]
	v_pk_fma_f32 v[122:123], v[102:103], v[110:111], v[104:105]
	s_nop 0
	s_waitcnt lgkmcnt(0)
	s_nop 0
	ds_read_b128 v[102:105], v19 offset:64
	ds_read_b128 v[108:111], v19 offset:80
	ds_read_b128 v[112:115], v19 offset:96
	ds_read_b128 v[116:119], v19 offset:112
	v_mov_b32_e32 v19, 0xa9c0
	v_pk_mul_f32 v[124:125], v[38:39], v[14:15] op_sel_hi:[0,1]
	v_exp_f32_e32 v124, v124
	v_exp_f32_e32 v125, v125
	v_pk_mul_f32 v[138:139], v[38:39], v[16:17] op_sel_hi:[0,1]
	v_exp_f32_e32 v138, v138
	v_exp_f32_e32 v139, v139
	v_mul_f32_e32 v84, v38, v84
	v_pk_mul_f32 v[86:87], v[84:85], v[86:87] op_sel_hi:[0,1]
	v_pk_fma_f32 v[124:125], v[126:127], v[124:125], v[86:87]
	v_pk_mul_f32 v[86:87], v[84:85], v[88:89] op_sel_hi:[0,1]
	v_pk_fma_f32 v[126:127], v[128:129], v[138:139], v[86:87]
	v_pk_mul_f32 v[86:87], v[38:39], v[10:11] op_sel_hi:[0,1]
	v_exp_f32_e32 v86, v86
	v_exp_f32_e32 v87, v87
	v_pk_mul_f32 v[88:89], v[38:39], v[12:13] op_sel_hi:[0,1]
	v_exp_f32_e32 v88, v88
	v_exp_f32_e32 v89, v89
	v_pk_mul_f32 v[90:91], v[84:85], v[90:91] op_sel_hi:[0,1]
	v_pk_fma_f32 v[128:129], v[130:131], v[86:87], v[90:91]
	v_pk_mul_f32 v[86:87], v[84:85], v[92:93] op_sel_hi:[0,1]
	v_pk_fma_f32 v[130:131], v[132:133], v[88:89], v[86:87]
	v_pk_mul_f32 v[86:87], v[38:39], v[6:7] op_sel_hi:[0,1]
	v_exp_f32_e32 v86, v86
	v_exp_f32_e32 v87, v87
	v_pk_mul_f32 v[88:89], v[38:39], v[8:9] op_sel_hi:[0,1]
	v_exp_f32_e32 v88, v88
	v_exp_f32_e32 v89, v89
	v_pk_mul_f32 v[90:91], v[84:85], v[94:95] op_sel_hi:[0,1]
	v_pk_fma_f32 v[132:133], v[134:135], v[86:87], v[90:91]
	v_pk_mul_f32 v[86:87], v[84:85], v[96:97] op_sel_hi:[0,1]
	v_pk_fma_f32 v[134:135], v[136:137], v[88:89], v[86:87]
	v_pk_mul_f32 v[86:87], v[38:39], v[2:3] op_sel_hi:[0,1]
	v_pk_mul_f32 v[88:89], v[38:39], v[4:5] op_sel_hi:[0,1]
	v_exp_f32_e32 v86, v86
	v_exp_f32_e32 v87, v87
	v_exp_f32_e32 v88, v88
	v_exp_f32_e32 v89, v89
	v_pk_mul_f32 v[90:91], v[84:85], v[98:99] op_sel_hi:[0,1]
	v_pk_mul_f32 v[84:85], v[84:85], v[100:101] op_sel_hi:[0,1]
	v_pk_fma_f32 v[120:121], v[120:121], v[86:87], v[90:91]
	v_pk_fma_f32 v[100:101], v[122:123], v[88:89], v[84:85]
	s_nop 0
	s_waitcnt lgkmcnt(0)
	s_nop 0
	ds_read_b128 v[84:87], v19 offset:64
	ds_read_b128 v[88:91], v19 offset:80
	ds_read_b128 v[92:95], v19 offset:96
	ds_read_b128 v[96:99], v19 offset:112
	v_mov_b32_e32 v19, 0xaa90
	v_pk_mul_f32 v[136:137], v[40:41], v[14:15] op_sel_hi:[0,1]
	v_exp_f32_e32 v136, v136
	v_exp_f32_e32 v137, v137
	v_pk_mul_f32 v[138:139], v[40:41], v[16:17] op_sel_hi:[0,1]
	v_exp_f32_e32 v138, v138
	v_exp_f32_e32 v139, v139
	v_mul_f32_e32 v122, v40, v83
	v_pk_mul_f32 v[102:103], v[122:123], v[102:103] op_sel_hi:[0,1]
	v_pk_fma_f32 v[124:125], v[124:125], v[136:137], v[102:103]
	v_pk_mul_f32 v[102:103], v[122:123], v[104:105] op_sel_hi:[0,1]
	v_pk_fma_f32 v[104:105], v[126:127], v[138:139], v[102:103]
	v_pk_mul_f32 v[102:103], v[40:41], v[10:11] op_sel_hi:[0,1]
	v_exp_f32_e32 v102, v102
	v_exp_f32_e32 v103, v103
	v_pk_mul_f32 v[126:127], v[40:41], v[12:13] op_sel_hi:[0,1]
	v_exp_f32_e32 v126, v126
	v_exp_f32_e32 v127, v127
	v_pk_mul_f32 v[108:109], v[122:123], v[108:109] op_sel_hi:[0,1]
	v_pk_fma_f32 v[128:129], v[128:129], v[102:103], v[108:109]
	v_pk_mul_f32 v[102:103], v[122:123], v[110:111] op_sel_hi:[0,1]
	v_pk_fma_f32 v[126:127], v[130:131], v[126:127], v[102:103]
	v_pk_mul_f32 v[102:103], v[40:41], v[6:7] op_sel_hi:[0,1]
	v_exp_f32_e32 v102, v102
	v_exp_f32_e32 v103, v103
	v_pk_mul_f32 v[108:109], v[40:41], v[8:9] op_sel_hi:[0,1]
	v_exp_f32_e32 v108, v108
	v_exp_f32_e32 v109, v109
	v_pk_mul_f32 v[110:111], v[122:123], v[112:113] op_sel_hi:[0,1]
	v_pk_fma_f32 v[130:131], v[132:133], v[102:103], v[110:111]
	v_pk_mul_f32 v[102:103], v[122:123], v[114:115] op_sel_hi:[0,1]
	v_pk_fma_f32 v[132:133], v[134:135], v[108:109], v[102:103]
	v_pk_mul_f32 v[102:103], v[40:41], v[2:3] op_sel_hi:[0,1]
	v_exp_f32_e32 v102, v102
	v_exp_f32_e32 v103, v103
	v_pk_mul_f32 v[108:109], v[40:41], v[4:5] op_sel_hi:[0,1]
	v_exp_f32_e32 v108, v108
	v_exp_f32_e32 v109, v109
	v_pk_mul_f32 v[110:111], v[122:123], v[116:117] op_sel_hi:[0,1]
	v_pk_fma_f32 v[120:121], v[120:121], v[102:103], v[110:111]
	v_pk_mul_f32 v[102:103], v[122:123], v[118:119] op_sel_hi:[0,1]
	v_pk_fma_f32 v[122:123], v[100:101], v[108:109], v[102:103]
	s_nop 0
	s_waitcnt lgkmcnt(0)
	s_nop 0
	ds_read_b128 v[100:103], v19 offset:64
	ds_read_b128 v[108:111], v19 offset:80
	ds_read_b128 v[112:115], v19 offset:96
	ds_read_b128 v[116:119], v19 offset:112
	v_mov_b32_e32 v19, 0xab60
	v_pk_mul_f32 v[134:135], v[42:43], v[14:15] op_sel_hi:[0,1]
	v_exp_f32_e32 v134, v134
	v_exp_f32_e32 v135, v135
	v_pk_mul_f32 v[136:137], v[42:43], v[16:17] op_sel_hi:[0,1]
	v_exp_f32_e32 v136, v136
	v_exp_f32_e32 v137, v137
	v_mul_f32_e32 v82, v42, v82
	v_pk_mul_f32 v[84:85], v[82:83], v[84:85] op_sel_hi:[0,1]
	v_pk_fma_f32 v[124:125], v[124:125], v[134:135], v[84:85]
	v_pk_mul_f32 v[84:85], v[82:83], v[86:87] op_sel_hi:[0,1]
	v_pk_fma_f32 v[104:105], v[104:105], v[136:137], v[84:85]
	v_pk_mul_f32 v[84:85], v[42:43], v[10:11] op_sel_hi:[0,1]
	v_exp_f32_e32 v84, v84
	v_exp_f32_e32 v85, v85
	v_pk_mul_f32 v[86:87], v[42:43], v[12:13] op_sel_hi:[0,1]
	v_exp_f32_e32 v86, v86
	v_exp_f32_e32 v87, v87
	v_pk_mul_f32 v[88:89], v[82:83], v[88:89] op_sel_hi:[0,1]
	v_pk_fma_f32 v[128:129], v[128:129], v[84:85], v[88:89]
	v_pk_mul_f32 v[84:85], v[82:83], v[90:91] op_sel_hi:[0,1]
	v_pk_fma_f32 v[126:127], v[126:127], v[86:87], v[84:85]
	v_pk_mul_f32 v[84:85], v[42:43], v[6:7] op_sel_hi:[0,1]
	v_exp_f32_e32 v84, v84
	v_exp_f32_e32 v85, v85
	v_pk_mul_f32 v[86:87], v[42:43], v[8:9] op_sel_hi:[0,1]
	v_exp_f32_e32 v86, v86
	v_exp_f32_e32 v87, v87
	v_pk_mul_f32 v[88:89], v[82:83], v[92:93] op_sel_hi:[0,1]
	v_pk_fma_f32 v[130:131], v[130:131], v[84:85], v[88:89]
	v_pk_mul_f32 v[84:85], v[82:83], v[94:95] op_sel_hi:[0,1]
	v_pk_fma_f32 v[132:133], v[132:133], v[86:87], v[84:85]
	v_pk_mul_f32 v[84:85], v[42:43], v[2:3] op_sel_hi:[0,1]
	v_pk_mul_f32 v[86:87], v[42:43], v[4:5] op_sel_hi:[0,1]
	v_exp_f32_e32 v84, v84
	v_exp_f32_e32 v85, v85
	v_exp_f32_e32 v86, v86
	v_exp_f32_e32 v87, v87
	v_pk_mul_f32 v[88:89], v[82:83], v[96:97] op_sel_hi:[0,1]
	v_pk_mul_f32 v[82:83], v[82:83], v[98:99] op_sel_hi:[0,1]
	v_pk_fma_f32 v[120:121], v[120:121], v[84:85], v[88:89]
	v_pk_fma_f32 v[98:99], v[122:123], v[86:87], v[82:83]
	s_nop 0
	s_waitcnt lgkmcnt(0)
	s_nop 0
	ds_read_b128 v[82:85], v19 offset:64
	ds_read_b128 v[86:89], v19 offset:80
	ds_read_b128 v[90:93], v19 offset:96
	ds_read_b128 v[94:97], v19 offset:112
	v_mov_b32_e32 v19, 0xac30
	v_pk_mul_f32 v[134:135], v[44:45], v[14:15] op_sel_hi:[0,1]
	v_exp_f32_e32 v134, v134
	v_exp_f32_e32 v135, v135
	v_pk_mul_f32 v[136:137], v[44:45], v[16:17] op_sel_hi:[0,1]
	v_exp_f32_e32 v136, v136
	v_exp_f32_e32 v137, v137
	v_mul_f32_e32 v122, v44, v81
	v_pk_mul_f32 v[100:101], v[122:123], v[100:101] op_sel_hi:[0,1]
	v_pk_fma_f32 v[124:125], v[124:125], v[134:135], v[100:101]
	v_pk_mul_f32 v[100:101], v[122:123], v[102:103] op_sel_hi:[0,1]
	v_pk_fma_f32 v[134:135], v[104:105], v[136:137], v[100:101]
	v_pk_mul_f32 v[100:101], v[44:45], v[10:11] op_sel_hi:[0,1]
	v_exp_f32_e32 v100, v100
	v_exp_f32_e32 v101, v101
	v_pk_mul_f32 v[102:103], v[44:45], v[12:13] op_sel_hi:[0,1]
	v_exp_f32_e32 v102, v102
	v_exp_f32_e32 v103, v103
	v_pk_mul_f32 v[104:105], v[122:123], v[108:109] op_sel_hi:[0,1]
	v_pk_fma_f32 v[128:129], v[128:129], v[100:101], v[104:105]
	v_pk_mul_f32 v[100:101], v[122:123], v[110:111] op_sel_hi:[0,1]
	v_pk_fma_f32 v[126:127], v[126:127], v[102:103], v[100:101]
	v_pk_mul_f32 v[100:101], v[44:45], v[6:7] op_sel_hi:[0,1]
	v_exp_f32_e32 v100, v100
	v_exp_f32_e32 v101, v101
	v_pk_mul_f32 v[102:103], v[44:45], v[8:9] op_sel_hi:[0,1]
	v_exp_f32_e32 v102, v102
	v_exp_f32_e32 v103, v103
	v_pk_mul_f32 v[104:105], v[122:123], v[112:113] op_sel_hi:[0,1]
	v_pk_fma_f32 v[130:131], v[130:131], v[100:101], v[104:105]
	v_pk_mul_f32 v[100:101], v[122:123], v[114:115] op_sel_hi:[0,1]
	v_pk_fma_f32 v[132:133], v[132:133], v[102:103], v[100:101]
	v_pk_mul_f32 v[100:101], v[44:45], v[2:3] op_sel_hi:[0,1]
	v_exp_f32_e32 v100, v100
	v_exp_f32_e32 v101, v101
	v_pk_mul_f32 v[102:103], v[44:45], v[4:5] op_sel_hi:[0,1]
	v_exp_f32_e32 v102, v102
	v_exp_f32_e32 v103, v103
	v_pk_mul_f32 v[104:105], v[122:123], v[116:117] op_sel_hi:[0,1]
	v_pk_fma_f32 v[116:117], v[120:121], v[100:101], v[104:105]
	v_pk_mul_f32 v[100:101], v[122:123], v[118:119] op_sel_hi:[0,1]
	v_pk_fma_f32 v[118:119], v[98:99], v[102:103], v[100:101]
	s_nop 0
	s_waitcnt lgkmcnt(0)
	s_nop 0
	ds_read_b128 v[98:101], v19 offset:64
	ds_read_b128 v[102:105], v19 offset:80
	ds_read_b128 v[108:111], v19 offset:96
	ds_read_b128 v[112:115], v19 offset:112
	v_mov_b32_e32 v19, 0xad00
	v_pk_mul_f32 v[122:123], v[46:47], v[14:15] op_sel_hi:[0,1]
	v_exp_f32_e32 v122, v122
	v_exp_f32_e32 v123, v123
	v_pk_mul_f32 v[136:137], v[46:47], v[16:17] op_sel_hi:[0,1]
	v_exp_f32_e32 v136, v136
	v_exp_f32_e32 v137, v137
	v_mul_f32_e32 v120, v46, v79
	v_pk_mul_f32 v[82:83], v[120:121], v[82:83] op_sel_hi:[0,1]
	v_pk_fma_f32 v[122:123], v[124:125], v[122:123], v[82:83]
	v_pk_mul_f32 v[82:83], v[120:121], v[84:85] op_sel_hi:[0,1]
	v_pk_fma_f32 v[124:125], v[134:135], v[136:137], v[82:83]
	v_pk_mul_f32 v[82:83], v[46:47], v[10:11] op_sel_hi:[0,1]
	v_exp_f32_e32 v82, v82
	v_exp_f32_e32 v83, v83
	v_pk_mul_f32 v[84:85], v[46:47], v[12:13] op_sel_hi:[0,1]
	v_exp_f32_e32 v84, v84
	v_exp_f32_e32 v85, v85
	v_pk_mul_f32 v[86:87], v[120:121], v[86:87] op_sel_hi:[0,1]
	v_pk_fma_f32 v[128:129], v[128:129], v[82:83], v[86:87]
	v_pk_mul_f32 v[82:83], v[120:121], v[88:89] op_sel_hi:[0,1]
	v_pk_fma_f32 v[126:127], v[126:127], v[84:85], v[82:83]
	v_pk_mul_f32 v[82:83], v[46:47], v[6:7] op_sel_hi:[0,1]
	v_exp_f32_e32 v82, v82
	v_exp_f32_e32 v83, v83
	v_pk_mul_f32 v[84:85], v[46:47], v[8:9] op_sel_hi:[0,1]
	v_exp_f32_e32 v84, v84
	v_exp_f32_e32 v85, v85
	v_pk_mul_f32 v[86:87], v[120:121], v[90:91] op_sel_hi:[0,1]
	v_pk_fma_f32 v[130:131], v[130:131], v[82:83], v[86:87]
	v_pk_mul_f32 v[82:83], v[120:121], v[92:93] op_sel_hi:[0,1]
	v_pk_fma_f32 v[132:133], v[132:133], v[84:85], v[82:83]
	v_pk_mul_f32 v[82:83], v[46:47], v[2:3] op_sel_hi:[0,1]
	v_exp_f32_e32 v82, v82
	v_exp_f32_e32 v83, v83
	v_pk_mul_f32 v[84:85], v[46:47], v[4:5] op_sel_hi:[0,1]
	v_exp_f32_e32 v84, v84
	v_exp_f32_e32 v85, v85
	v_pk_mul_f32 v[86:87], v[120:121], v[94:95] op_sel_hi:[0,1]
	v_pk_fma_f32 v[116:117], v[116:117], v[82:83], v[86:87]
	v_pk_mul_f32 v[82:83], v[120:121], v[96:97] op_sel_hi:[0,1]
	v_pk_fma_f32 v[118:119], v[118:119], v[84:85], v[82:83]
	s_nop 0
	s_waitcnt lgkmcnt(0)
	s_nop 0
	ds_read_b128 v[82:85], v19 offset:64
	ds_read_b128 v[86:89], v19 offset:80
	ds_read_b128 v[90:93], v19 offset:96
	ds_read_b128 v[94:97], v19 offset:112
	v_mov_b32_e32 v19, 0xadd0
	v_pk_mul_f32 v[134:135], v[48:49], v[14:15] op_sel_hi:[0,1]
	v_exp_f32_e32 v134, v134
	v_exp_f32_e32 v135, v135
	v_pk_mul_f32 v[136:137], v[48:49], v[16:17] op_sel_hi:[0,1]
	v_exp_f32_e32 v136, v136
	v_exp_f32_e32 v137, v137
	v_mul_f32_e32 v120, v48, v77
	v_pk_mul_f32 v[98:99], v[120:121], v[98:99] op_sel_hi:[0,1]
	v_pk_fma_f32 v[122:123], v[122:123], v[134:135], v[98:99]
	v_pk_mul_f32 v[98:99], v[120:121], v[100:101] op_sel_hi:[0,1]
	v_pk_fma_f32 v[124:125], v[124:125], v[136:137], v[98:99]
	v_pk_mul_f32 v[98:99], v[48:49], v[10:11] op_sel_hi:[0,1]
	v_exp_f32_e32 v98, v98
	v_exp_f32_e32 v99, v99
	v_pk_mul_f32 v[100:101], v[48:49], v[12:13] op_sel_hi:[0,1]
	v_exp_f32_e32 v100, v100
	v_exp_f32_e32 v101, v101
	v_pk_mul_f32 v[102:103], v[120:121], v[102:103] op_sel_hi:[0,1]
	v_pk_fma_f32 v[128:129], v[128:129], v[98:99], v[102:103]
	v_pk_mul_f32 v[98:99], v[120:121], v[104:105] op_sel_hi:[0,1]
	v_pk_fma_f32 v[126:127], v[126:127], v[100:101], v[98:99]
	v_pk_mul_f32 v[98:99], v[48:49], v[6:7] op_sel_hi:[0,1]
	v_exp_f32_e32 v98, v98
	v_exp_f32_e32 v99, v99
	v_pk_mul_f32 v[100:101], v[48:49], v[8:9] op_sel_hi:[0,1]
	v_exp_f32_e32 v100, v100
	v_exp_f32_e32 v101, v101
	v_pk_mul_f32 v[102:103], v[120:121], v[108:109] op_sel_hi:[0,1]
	v_pk_fma_f32 v[130:131], v[130:131], v[98:99], v[102:103]
	v_pk_mul_f32 v[98:99], v[120:121], v[110:111] op_sel_hi:[0,1]
	v_pk_fma_f32 v[132:133], v[132:133], v[100:101], v[98:99]
	v_pk_mul_f32 v[98:99], v[48:49], v[2:3] op_sel_hi:[0,1]
	v_exp_f32_e32 v98, v98
	v_exp_f32_e32 v99, v99
	v_pk_mul_f32 v[100:101], v[48:49], v[4:5] op_sel_hi:[0,1]
	v_exp_f32_e32 v100, v100
	v_exp_f32_e32 v101, v101
	v_pk_mul_f32 v[102:103], v[120:121], v[112:113] op_sel_hi:[0,1]
	v_pk_fma_f32 v[116:117], v[116:117], v[98:99], v[102:103]
	v_pk_mul_f32 v[98:99], v[120:121], v[114:115] op_sel_hi:[0,1]
	v_pk_fma_f32 v[118:119], v[118:119], v[100:101], v[98:99]
	s_nop 0
	s_waitcnt lgkmcnt(0)
	s_nop 0
	ds_read_b128 v[98:101], v19 offset:64
	ds_read_b128 v[102:105], v19 offset:80
	ds_read_b128 v[108:111], v19 offset:96
	ds_read_b128 v[112:115], v19 offset:112
	v_mov_b32_e32 v19, 0xaea0
	v_pk_mul_f32 v[134:135], v[50:51], v[14:15] op_sel_hi:[0,1]
	v_exp_f32_e32 v134, v134
	v_exp_f32_e32 v135, v135
	v_pk_mul_f32 v[136:137], v[50:51], v[16:17] op_sel_hi:[0,1]
	v_exp_f32_e32 v136, v136
	v_exp_f32_e32 v137, v137
	v_mul_f32_e32 v120, v50, v75
	v_pk_mul_f32 v[82:83], v[120:121], v[82:83] op_sel_hi:[0,1]
	v_pk_fma_f32 v[122:123], v[122:123], v[134:135], v[82:83]
	v_pk_mul_f32 v[82:83], v[120:121], v[84:85] op_sel_hi:[0,1]
	v_pk_fma_f32 v[124:125], v[124:125], v[136:137], v[82:83]
	v_pk_mul_f32 v[82:83], v[50:51], v[10:11] op_sel_hi:[0,1]
	v_exp_f32_e32 v82, v82
	v_exp_f32_e32 v83, v83
	v_pk_mul_f32 v[84:85], v[50:51], v[12:13] op_sel_hi:[0,1]
	v_exp_f32_e32 v84, v84
	v_exp_f32_e32 v85, v85
	v_pk_mul_f32 v[86:87], v[120:121], v[86:87] op_sel_hi:[0,1]
	v_pk_fma_f32 v[128:129], v[128:129], v[82:83], v[86:87]
	v_pk_mul_f32 v[82:83], v[120:121], v[88:89] op_sel_hi:[0,1]
	v_pk_fma_f32 v[126:127], v[126:127], v[84:85], v[82:83]
	v_pk_mul_f32 v[82:83], v[50:51], v[6:7] op_sel_hi:[0,1]
	v_exp_f32_e32 v82, v82
	v_exp_f32_e32 v83, v83
	v_pk_mul_f32 v[84:85], v[50:51], v[8:9] op_sel_hi:[0,1]
	v_exp_f32_e32 v84, v84
	v_exp_f32_e32 v85, v85
	v_pk_mul_f32 v[86:87], v[120:121], v[90:91] op_sel_hi:[0,1]
	v_pk_fma_f32 v[130:131], v[130:131], v[82:83], v[86:87]
	v_pk_mul_f32 v[82:83], v[120:121], v[92:93] op_sel_hi:[0,1]
	v_pk_fma_f32 v[132:133], v[132:133], v[84:85], v[82:83]
	v_pk_mul_f32 v[82:83], v[50:51], v[2:3] op_sel_hi:[0,1]
	v_exp_f32_e32 v82, v82
	v_exp_f32_e32 v83, v83
	v_pk_mul_f32 v[84:85], v[50:51], v[4:5] op_sel_hi:[0,1]
	v_exp_f32_e32 v84, v84
	v_exp_f32_e32 v85, v85
	v_pk_mul_f32 v[86:87], v[120:121], v[94:95] op_sel_hi:[0,1]
	v_pk_fma_f32 v[116:117], v[116:117], v[82:83], v[86:87]
	v_pk_mul_f32 v[82:83], v[120:121], v[96:97] op_sel_hi:[0,1]
	v_pk_fma_f32 v[118:119], v[118:119], v[84:85], v[82:83]
	s_nop 0
	s_waitcnt lgkmcnt(0)
	s_nop 0
	ds_read_b128 v[82:85], v19 offset:64
	ds_read_b128 v[86:89], v19 offset:80
	ds_read_b128 v[90:93], v19 offset:96
	ds_read_b128 v[94:97], v19 offset:112
	v_mov_b32_e32 v19, 0xaf70
	v_pk_mul_f32 v[134:135], v[52:53], v[14:15] op_sel_hi:[0,1]
	v_exp_f32_e32 v134, v134
	v_exp_f32_e32 v135, v135
	v_pk_mul_f32 v[136:137], v[52:53], v[16:17] op_sel_hi:[0,1]
	v_exp_f32_e32 v136, v136
	v_exp_f32_e32 v137, v137
	v_mul_f32_e32 v120, v52, v73
	v_pk_mul_f32 v[98:99], v[120:121], v[98:99] op_sel_hi:[0,1]
	v_pk_fma_f32 v[122:123], v[122:123], v[134:135], v[98:99]
	v_pk_mul_f32 v[98:99], v[120:121], v[100:101] op_sel_hi:[0,1]
	v_pk_fma_f32 v[124:125], v[124:125], v[136:137], v[98:99]
	v_pk_mul_f32 v[98:99], v[52:53], v[10:11] op_sel_hi:[0,1]
	v_exp_f32_e32 v98, v98
	v_exp_f32_e32 v99, v99
	v_pk_mul_f32 v[100:101], v[52:53], v[12:13] op_sel_hi:[0,1]
	v_exp_f32_e32 v100, v100
	v_exp_f32_e32 v101, v101
	v_pk_mul_f32 v[102:103], v[120:121], v[102:103] op_sel_hi:[0,1]
	v_pk_fma_f32 v[128:129], v[128:129], v[98:99], v[102:103]
	v_pk_mul_f32 v[98:99], v[120:121], v[104:105] op_sel_hi:[0,1]
	v_pk_fma_f32 v[126:127], v[126:127], v[100:101], v[98:99]
	v_pk_mul_f32 v[98:99], v[52:53], v[6:7] op_sel_hi:[0,1]
	v_exp_f32_e32 v98, v98
	v_exp_f32_e32 v99, v99
	v_pk_mul_f32 v[100:101], v[52:53], v[8:9] op_sel_hi:[0,1]
	v_exp_f32_e32 v100, v100
	v_exp_f32_e32 v101, v101
	v_pk_mul_f32 v[102:103], v[120:121], v[108:109] op_sel_hi:[0,1]
	v_pk_fma_f32 v[130:131], v[130:131], v[98:99], v[102:103]
	v_pk_mul_f32 v[98:99], v[120:121], v[110:111] op_sel_hi:[0,1]
	v_pk_fma_f32 v[132:133], v[132:133], v[100:101], v[98:99]
	v_pk_mul_f32 v[98:99], v[52:53], v[2:3] op_sel_hi:[0,1]
	v_exp_f32_e32 v98, v98
	v_exp_f32_e32 v99, v99
	v_pk_mul_f32 v[100:101], v[52:53], v[4:5] op_sel_hi:[0,1]
	v_exp_f32_e32 v100, v100
	v_exp_f32_e32 v101, v101
	v_pk_mul_f32 v[102:103], v[120:121], v[112:113] op_sel_hi:[0,1]
	v_pk_fma_f32 v[116:117], v[116:117], v[98:99], v[102:103]
	v_pk_mul_f32 v[98:99], v[120:121], v[114:115] op_sel_hi:[0,1]
	v_pk_fma_f32 v[118:119], v[118:119], v[100:101], v[98:99]
	s_nop 0
	s_waitcnt lgkmcnt(0)
	s_nop 0
	ds_read_b128 v[98:101], v19 offset:64
	ds_read_b128 v[102:105], v19 offset:80
	ds_read_b128 v[108:111], v19 offset:96
	ds_read_b128 v[112:115], v19 offset:112
	v_mov_b32_e32 v19, 0xb040
	v_pk_mul_f32 v[134:135], v[54:55], v[14:15] op_sel_hi:[0,1]
	v_exp_f32_e32 v134, v134
	v_exp_f32_e32 v135, v135
	v_pk_mul_f32 v[136:137], v[54:55], v[16:17] op_sel_hi:[0,1]
	v_exp_f32_e32 v136, v136
	v_exp_f32_e32 v137, v137
	v_mul_f32_e32 v120, v54, v71
	v_pk_mul_f32 v[82:83], v[120:121], v[82:83] op_sel_hi:[0,1]
	v_pk_fma_f32 v[122:123], v[122:123], v[134:135], v[82:83]
	v_pk_mul_f32 v[82:83], v[120:121], v[84:85] op_sel_hi:[0,1]
	v_pk_fma_f32 v[124:125], v[124:125], v[136:137], v[82:83]
	v_pk_mul_f32 v[82:83], v[54:55], v[10:11] op_sel_hi:[0,1]
	v_exp_f32_e32 v82, v82
	v_exp_f32_e32 v83, v83
	v_pk_mul_f32 v[84:85], v[54:55], v[12:13] op_sel_hi:[0,1]
	v_exp_f32_e32 v84, v84
	v_exp_f32_e32 v85, v85
	v_pk_mul_f32 v[86:87], v[120:121], v[86:87] op_sel_hi:[0,1]
	v_pk_fma_f32 v[128:129], v[128:129], v[82:83], v[86:87]
	v_pk_mul_f32 v[82:83], v[120:121], v[88:89] op_sel_hi:[0,1]
	v_pk_fma_f32 v[126:127], v[126:127], v[84:85], v[82:83]
	v_pk_mul_f32 v[82:83], v[54:55], v[6:7] op_sel_hi:[0,1]
	v_exp_f32_e32 v82, v82
	v_exp_f32_e32 v83, v83
	v_pk_mul_f32 v[84:85], v[54:55], v[8:9] op_sel_hi:[0,1]
	v_exp_f32_e32 v84, v84
	v_exp_f32_e32 v85, v85
	v_pk_mul_f32 v[86:87], v[120:121], v[90:91] op_sel_hi:[0,1]
	v_pk_fma_f32 v[130:131], v[130:131], v[82:83], v[86:87]
	v_pk_mul_f32 v[82:83], v[120:121], v[92:93] op_sel_hi:[0,1]
	v_pk_fma_f32 v[132:133], v[132:133], v[84:85], v[82:83]
	v_pk_mul_f32 v[82:83], v[54:55], v[2:3] op_sel_hi:[0,1]
	v_exp_f32_e32 v82, v82
	v_exp_f32_e32 v83, v83
	v_pk_mul_f32 v[84:85], v[54:55], v[4:5] op_sel_hi:[0,1]
	v_exp_f32_e32 v84, v84
	v_exp_f32_e32 v85, v85
	v_pk_mul_f32 v[86:87], v[120:121], v[94:95] op_sel_hi:[0,1]
	v_pk_fma_f32 v[116:117], v[116:117], v[82:83], v[86:87]
	v_pk_mul_f32 v[82:83], v[120:121], v[96:97] op_sel_hi:[0,1]
	v_pk_fma_f32 v[118:119], v[118:119], v[84:85], v[82:83]
	s_nop 0
	s_waitcnt lgkmcnt(0)
	s_nop 0
	ds_read_b128 v[82:85], v19 offset:64
	ds_read_b128 v[86:89], v19 offset:80
	ds_read_b128 v[90:93], v19 offset:96
	ds_read_b128 v[94:97], v19 offset:112
	v_mov_b32_e32 v19, 0xb110
	v_pk_mul_f32 v[134:135], v[56:57], v[14:15] op_sel_hi:[0,1]
	v_exp_f32_e32 v134, v134
	v_exp_f32_e32 v135, v135
	v_pk_mul_f32 v[136:137], v[56:57], v[16:17] op_sel_hi:[0,1]
	v_exp_f32_e32 v136, v136
	v_exp_f32_e32 v137, v137
	v_mul_f32_e32 v120, v56, v69
	v_pk_mul_f32 v[98:99], v[120:121], v[98:99] op_sel_hi:[0,1]
	v_pk_fma_f32 v[122:123], v[122:123], v[134:135], v[98:99]
	v_pk_mul_f32 v[98:99], v[120:121], v[100:101] op_sel_hi:[0,1]
	v_pk_fma_f32 v[124:125], v[124:125], v[136:137], v[98:99]
	v_pk_mul_f32 v[98:99], v[56:57], v[10:11] op_sel_hi:[0,1]
	v_exp_f32_e32 v98, v98
	v_exp_f32_e32 v99, v99
	v_pk_mul_f32 v[100:101], v[56:57], v[12:13] op_sel_hi:[0,1]
	v_exp_f32_e32 v100, v100
	v_exp_f32_e32 v101, v101
	v_pk_mul_f32 v[102:103], v[120:121], v[102:103] op_sel_hi:[0,1]
	v_pk_fma_f32 v[128:129], v[128:129], v[98:99], v[102:103]
	v_pk_mul_f32 v[98:99], v[120:121], v[104:105] op_sel_hi:[0,1]
	v_pk_fma_f32 v[126:127], v[126:127], v[100:101], v[98:99]
	v_pk_mul_f32 v[98:99], v[56:57], v[6:7] op_sel_hi:[0,1]
	v_exp_f32_e32 v98, v98
	v_exp_f32_e32 v99, v99
	v_pk_mul_f32 v[100:101], v[56:57], v[8:9] op_sel_hi:[0,1]
	v_exp_f32_e32 v100, v100
	v_exp_f32_e32 v101, v101
	v_pk_mul_f32 v[102:103], v[120:121], v[108:109] op_sel_hi:[0,1]
	v_pk_fma_f32 v[130:131], v[130:131], v[98:99], v[102:103]
	v_pk_mul_f32 v[98:99], v[120:121], v[110:111] op_sel_hi:[0,1]
	v_pk_fma_f32 v[132:133], v[132:133], v[100:101], v[98:99]
	v_pk_mul_f32 v[98:99], v[56:57], v[2:3] op_sel_hi:[0,1]
	v_exp_f32_e32 v98, v98
	v_exp_f32_e32 v99, v99
	v_pk_mul_f32 v[100:101], v[56:57], v[4:5] op_sel_hi:[0,1]
	v_exp_f32_e32 v100, v100
	v_exp_f32_e32 v101, v101
	v_pk_mul_f32 v[102:103], v[120:121], v[112:113] op_sel_hi:[0,1]
	v_pk_fma_f32 v[116:117], v[116:117], v[98:99], v[102:103]
	v_pk_mul_f32 v[98:99], v[120:121], v[114:115] op_sel_hi:[0,1]
	v_pk_fma_f32 v[118:119], v[118:119], v[100:101], v[98:99]
	s_nop 0
	s_waitcnt lgkmcnt(0)
	s_nop 0
	ds_read_b128 v[98:101], v19 offset:64
	ds_read_b128 v[102:105], v19 offset:80
	ds_read_b128 v[108:111], v19 offset:96
	ds_read_b128 v[112:115], v19 offset:112
	v_mov_b32_e32 v19, 0xb1e0
	v_pk_mul_f32 v[134:135], v[58:59], v[14:15] op_sel_hi:[0,1]
	v_exp_f32_e32 v134, v134
	v_exp_f32_e32 v135, v135
	v_pk_mul_f32 v[136:137], v[58:59], v[16:17] op_sel_hi:[0,1]
	v_exp_f32_e32 v136, v136
	v_exp_f32_e32 v137, v137
	v_mul_f32_e32 v120, v58, v67
	v_pk_mul_f32 v[82:83], v[120:121], v[82:83] op_sel_hi:[0,1]
	v_pk_fma_f32 v[122:123], v[122:123], v[134:135], v[82:83]
	v_pk_mul_f32 v[82:83], v[120:121], v[84:85] op_sel_hi:[0,1]
	v_pk_fma_f32 v[124:125], v[124:125], v[136:137], v[82:83]
	v_pk_mul_f32 v[82:83], v[58:59], v[10:11] op_sel_hi:[0,1]
	v_exp_f32_e32 v82, v82
	v_exp_f32_e32 v83, v83
	v_pk_mul_f32 v[84:85], v[58:59], v[12:13] op_sel_hi:[0,1]
	v_exp_f32_e32 v84, v84
	v_exp_f32_e32 v85, v85
	v_pk_mul_f32 v[86:87], v[120:121], v[86:87] op_sel_hi:[0,1]
	v_pk_fma_f32 v[128:129], v[128:129], v[82:83], v[86:87]
	v_pk_mul_f32 v[82:83], v[120:121], v[88:89] op_sel_hi:[0,1]
	v_pk_fma_f32 v[126:127], v[126:127], v[84:85], v[82:83]
	v_pk_mul_f32 v[82:83], v[58:59], v[6:7] op_sel_hi:[0,1]
	v_exp_f32_e32 v82, v82
	v_exp_f32_e32 v83, v83
	v_pk_mul_f32 v[84:85], v[58:59], v[8:9] op_sel_hi:[0,1]
	v_exp_f32_e32 v84, v84
	v_exp_f32_e32 v85, v85
	v_pk_mul_f32 v[86:87], v[120:121], v[90:91] op_sel_hi:[0,1]
	v_pk_fma_f32 v[130:131], v[130:131], v[82:83], v[86:87]
	v_pk_mul_f32 v[82:83], v[120:121], v[92:93] op_sel_hi:[0,1]
	v_pk_fma_f32 v[132:133], v[132:133], v[84:85], v[82:83]
	v_pk_mul_f32 v[82:83], v[58:59], v[2:3] op_sel_hi:[0,1]
	v_exp_f32_e32 v82, v82
	v_exp_f32_e32 v83, v83
	v_pk_mul_f32 v[84:85], v[58:59], v[4:5] op_sel_hi:[0,1]
	v_exp_f32_e32 v84, v84
	v_exp_f32_e32 v85, v85
	v_pk_mul_f32 v[86:87], v[120:121], v[94:95] op_sel_hi:[0,1]
	v_pk_fma_f32 v[116:117], v[116:117], v[82:83], v[86:87]
	v_pk_mul_f32 v[82:83], v[120:121], v[96:97] op_sel_hi:[0,1]
	v_pk_fma_f32 v[118:119], v[118:119], v[84:85], v[82:83]
	s_nop 0
	s_waitcnt lgkmcnt(0)
	s_nop 0
	ds_read_b128 v[82:85], v19 offset:64
	ds_read_b128 v[86:89], v19 offset:80
	ds_read_b128 v[90:93], v19 offset:96
	ds_read_b128 v[94:97], v19 offset:112
	v_mov_b32_e32 v19, 0xb2b0
	v_pk_mul_f32 v[134:135], v[60:61], v[14:15] op_sel_hi:[0,1]
	v_exp_f32_e32 v134, v134
	v_exp_f32_e32 v135, v135
	v_pk_mul_f32 v[136:137], v[60:61], v[16:17] op_sel_hi:[0,1]
	v_exp_f32_e32 v136, v136
	v_exp_f32_e32 v137, v137
	v_mul_f32_e32 v120, v60, v65
	v_pk_mul_f32 v[98:99], v[120:121], v[98:99] op_sel_hi:[0,1]
	v_pk_fma_f32 v[122:123], v[122:123], v[134:135], v[98:99]
	v_pk_mul_f32 v[98:99], v[120:121], v[100:101] op_sel_hi:[0,1]
	v_pk_fma_f32 v[124:125], v[124:125], v[136:137], v[98:99]
	v_pk_mul_f32 v[98:99], v[60:61], v[10:11] op_sel_hi:[0,1]
	v_exp_f32_e32 v98, v98
	v_exp_f32_e32 v99, v99
	v_pk_mul_f32 v[100:101], v[60:61], v[12:13] op_sel_hi:[0,1]
	v_exp_f32_e32 v100, v100
	v_exp_f32_e32 v101, v101
	v_pk_mul_f32 v[102:103], v[120:121], v[102:103] op_sel_hi:[0,1]
	v_pk_fma_f32 v[128:129], v[128:129], v[98:99], v[102:103]
	v_pk_mul_f32 v[98:99], v[120:121], v[104:105] op_sel_hi:[0,1]
	v_pk_fma_f32 v[126:127], v[126:127], v[100:101], v[98:99]
	v_pk_mul_f32 v[98:99], v[60:61], v[6:7] op_sel_hi:[0,1]
	v_exp_f32_e32 v98, v98
	v_exp_f32_e32 v99, v99
	v_pk_mul_f32 v[100:101], v[60:61], v[8:9] op_sel_hi:[0,1]
	v_exp_f32_e32 v100, v100
	v_exp_f32_e32 v101, v101
	v_pk_mul_f32 v[102:103], v[120:121], v[108:109] op_sel_hi:[0,1]
	v_pk_fma_f32 v[130:131], v[130:131], v[98:99], v[102:103]
	v_pk_mul_f32 v[98:99], v[120:121], v[110:111] op_sel_hi:[0,1]
	v_pk_fma_f32 v[132:133], v[132:133], v[100:101], v[98:99]
	v_pk_mul_f32 v[98:99], v[60:61], v[2:3] op_sel_hi:[0,1]
	v_exp_f32_e32 v98, v98
	v_exp_f32_e32 v99, v99
	v_pk_mul_f32 v[100:101], v[60:61], v[4:5] op_sel_hi:[0,1]
	v_exp_f32_e32 v100, v100
	v_exp_f32_e32 v101, v101
	v_pk_mul_f32 v[102:103], v[120:121], v[112:113] op_sel_hi:[0,1]
	v_pk_fma_f32 v[116:117], v[116:117], v[98:99], v[102:103]
	v_pk_mul_f32 v[98:99], v[120:121], v[114:115] op_sel_hi:[0,1]
	v_pk_fma_f32 v[118:119], v[118:119], v[100:101], v[98:99]
	s_nop 0
	s_waitcnt lgkmcnt(0)
	s_nop 0
	ds_read_b128 v[98:101], v19 offset:64
	ds_read_b128 v[102:105], v19 offset:80
	ds_read_b128 v[108:111], v19 offset:96
	ds_read_b128 v[112:115], v19 offset:112
	v_mov_b32_e32 v19, 0xb380
	v_pk_mul_f32 v[134:135], v[62:63], v[14:15] op_sel_hi:[0,1]
	v_exp_f32_e32 v134, v134
	v_exp_f32_e32 v135, v135
	v_pk_mul_f32 v[136:137], v[62:63], v[16:17] op_sel_hi:[0,1]
	v_exp_f32_e32 v136, v136
	v_exp_f32_e32 v137, v137
	v_mul_f32_e32 v120, v62, v63
	v_pk_mul_f32 v[82:83], v[120:121], v[82:83] op_sel_hi:[0,1]
	v_pk_fma_f32 v[122:123], v[122:123], v[134:135], v[82:83]
	v_pk_mul_f32 v[82:83], v[120:121], v[84:85] op_sel_hi:[0,1]
	v_pk_fma_f32 v[124:125], v[124:125], v[136:137], v[82:83]
	v_pk_mul_f32 v[82:83], v[62:63], v[10:11] op_sel_hi:[0,1]
	v_exp_f32_e32 v82, v82
	v_exp_f32_e32 v83, v83
	v_pk_mul_f32 v[84:85], v[62:63], v[12:13] op_sel_hi:[0,1]
	v_exp_f32_e32 v84, v84
	v_exp_f32_e32 v85, v85
	v_pk_mul_f32 v[86:87], v[120:121], v[86:87] op_sel_hi:[0,1]
	v_pk_fma_f32 v[128:129], v[128:129], v[82:83], v[86:87]
	v_pk_mul_f32 v[82:83], v[120:121], v[88:89] op_sel_hi:[0,1]
	v_pk_fma_f32 v[126:127], v[126:127], v[84:85], v[82:83]
	v_pk_mul_f32 v[82:83], v[62:63], v[6:7] op_sel_hi:[0,1]
	v_exp_f32_e32 v82, v82
	v_exp_f32_e32 v83, v83
	v_pk_mul_f32 v[84:85], v[62:63], v[8:9] op_sel_hi:[0,1]
	v_exp_f32_e32 v84, v84
	v_exp_f32_e32 v85, v85
	v_pk_mul_f32 v[86:87], v[120:121], v[90:91] op_sel_hi:[0,1]
	v_pk_fma_f32 v[130:131], v[130:131], v[82:83], v[86:87]
	v_pk_mul_f32 v[82:83], v[120:121], v[92:93] op_sel_hi:[0,1]
	v_pk_fma_f32 v[132:133], v[132:133], v[84:85], v[82:83]
	v_pk_mul_f32 v[82:83], v[62:63], v[2:3] op_sel_hi:[0,1]
	v_exp_f32_e32 v82, v82
	v_exp_f32_e32 v83, v83
	v_pk_mul_f32 v[84:85], v[62:63], v[4:5] op_sel_hi:[0,1]
	v_exp_f32_e32 v84, v84
	v_exp_f32_e32 v85, v85
	v_pk_mul_f32 v[86:87], v[120:121], v[94:95] op_sel_hi:[0,1]
	v_pk_fma_f32 v[116:117], v[116:117], v[82:83], v[86:87]
	v_pk_mul_f32 v[82:83], v[120:121], v[96:97] op_sel_hi:[0,1]
	v_pk_fma_f32 v[118:119], v[118:119], v[84:85], v[82:83]
	s_nop 0
	s_waitcnt lgkmcnt(0)
	s_nop 0
	ds_read_b128 v[82:85], v19 offset:64
	ds_read_b128 v[86:89], v19 offset:80
	ds_read_b128 v[90:93], v19 offset:96
	ds_read_b128 v[94:97], v19 offset:112
	v_mov_b32_e32 v19, 0xb450
	v_pk_mul_f32 v[134:135], v[64:65], v[14:15] op_sel_hi:[0,1]
	v_exp_f32_e32 v134, v134
	v_exp_f32_e32 v135, v135
	v_pk_mul_f32 v[136:137], v[64:65], v[16:17] op_sel_hi:[0,1]
	v_exp_f32_e32 v136, v136
	v_exp_f32_e32 v137, v137
	v_mul_f32_e32 v120, v64, v61
	v_pk_mul_f32 v[98:99], v[120:121], v[98:99] op_sel_hi:[0,1]
	v_pk_fma_f32 v[122:123], v[122:123], v[134:135], v[98:99]
	v_pk_mul_f32 v[98:99], v[120:121], v[100:101] op_sel_hi:[0,1]
	v_pk_fma_f32 v[124:125], v[124:125], v[136:137], v[98:99]
	v_pk_mul_f32 v[98:99], v[64:65], v[10:11] op_sel_hi:[0,1]
	v_exp_f32_e32 v98, v98
	v_exp_f32_e32 v99, v99
	v_pk_mul_f32 v[100:101], v[64:65], v[12:13] op_sel_hi:[0,1]
	v_exp_f32_e32 v100, v100
	v_exp_f32_e32 v101, v101
	v_pk_mul_f32 v[102:103], v[120:121], v[102:103] op_sel_hi:[0,1]
	v_pk_fma_f32 v[128:129], v[128:129], v[98:99], v[102:103]
	v_pk_mul_f32 v[98:99], v[120:121], v[104:105] op_sel_hi:[0,1]
	v_pk_fma_f32 v[126:127], v[126:127], v[100:101], v[98:99]
	v_pk_mul_f32 v[98:99], v[64:65], v[6:7] op_sel_hi:[0,1]
	v_exp_f32_e32 v98, v98
	v_exp_f32_e32 v99, v99
	v_pk_mul_f32 v[100:101], v[64:65], v[8:9] op_sel_hi:[0,1]
	v_exp_f32_e32 v100, v100
	v_exp_f32_e32 v101, v101
	v_pk_mul_f32 v[102:103], v[120:121], v[108:109] op_sel_hi:[0,1]
	v_pk_fma_f32 v[130:131], v[130:131], v[98:99], v[102:103]
	v_pk_mul_f32 v[98:99], v[120:121], v[110:111] op_sel_hi:[0,1]
	v_pk_fma_f32 v[132:133], v[132:133], v[100:101], v[98:99]
	v_pk_mul_f32 v[98:99], v[64:65], v[2:3] op_sel_hi:[0,1]
	v_exp_f32_e32 v98, v98
	v_exp_f32_e32 v99, v99
	v_pk_mul_f32 v[100:101], v[64:65], v[4:5] op_sel_hi:[0,1]
	v_exp_f32_e32 v100, v100
	v_exp_f32_e32 v101, v101
	v_pk_mul_f32 v[102:103], v[120:121], v[112:113] op_sel_hi:[0,1]
	v_pk_fma_f32 v[116:117], v[116:117], v[98:99], v[102:103]
	v_pk_mul_f32 v[98:99], v[120:121], v[114:115] op_sel_hi:[0,1]
	v_pk_fma_f32 v[118:119], v[118:119], v[100:101], v[98:99]
	s_nop 0
	s_waitcnt lgkmcnt(0)
	s_nop 0
	ds_read_b128 v[98:101], v19 offset:64
	ds_read_b128 v[102:105], v19 offset:80
	ds_read_b128 v[108:111], v19 offset:96
	ds_read_b128 v[112:115], v19 offset:112
	v_mov_b32_e32 v19, 0xb520
	v_pk_mul_f32 v[134:135], v[66:67], v[14:15] op_sel_hi:[0,1]
	v_exp_f32_e32 v134, v134
	v_exp_f32_e32 v135, v135
	v_pk_mul_f32 v[136:137], v[66:67], v[16:17] op_sel_hi:[0,1]
	v_exp_f32_e32 v136, v136
	v_exp_f32_e32 v137, v137
	v_mul_f32_e32 v120, v66, v59
	v_pk_mul_f32 v[82:83], v[120:121], v[82:83] op_sel_hi:[0,1]
	v_pk_fma_f32 v[122:123], v[122:123], v[134:135], v[82:83]
	v_pk_mul_f32 v[82:83], v[120:121], v[84:85] op_sel_hi:[0,1]
	v_pk_fma_f32 v[124:125], v[124:125], v[136:137], v[82:83]
	v_pk_mul_f32 v[82:83], v[66:67], v[10:11] op_sel_hi:[0,1]
	v_exp_f32_e32 v82, v82
	v_exp_f32_e32 v83, v83
	v_pk_mul_f32 v[84:85], v[66:67], v[12:13] op_sel_hi:[0,1]
	v_exp_f32_e32 v84, v84
	v_exp_f32_e32 v85, v85
	v_pk_mul_f32 v[86:87], v[120:121], v[86:87] op_sel_hi:[0,1]
	v_pk_fma_f32 v[128:129], v[128:129], v[82:83], v[86:87]
	v_pk_mul_f32 v[82:83], v[120:121], v[88:89] op_sel_hi:[0,1]
	v_pk_fma_f32 v[126:127], v[126:127], v[84:85], v[82:83]
	v_pk_mul_f32 v[82:83], v[66:67], v[6:7] op_sel_hi:[0,1]
	v_exp_f32_e32 v82, v82
	v_exp_f32_e32 v83, v83
	v_pk_mul_f32 v[84:85], v[66:67], v[8:9] op_sel_hi:[0,1]
	v_exp_f32_e32 v84, v84
	v_exp_f32_e32 v85, v85
	v_pk_mul_f32 v[86:87], v[120:121], v[90:91] op_sel_hi:[0,1]
	v_pk_fma_f32 v[130:131], v[130:131], v[82:83], v[86:87]
	v_pk_mul_f32 v[82:83], v[120:121], v[92:93] op_sel_hi:[0,1]
	v_pk_fma_f32 v[132:133], v[132:133], v[84:85], v[82:83]
	v_pk_mul_f32 v[82:83], v[66:67], v[2:3] op_sel_hi:[0,1]
	v_exp_f32_e32 v82, v82
	v_exp_f32_e32 v83, v83
	v_pk_mul_f32 v[84:85], v[66:67], v[4:5] op_sel_hi:[0,1]
	v_exp_f32_e32 v84, v84
	v_exp_f32_e32 v85, v85
	v_pk_mul_f32 v[86:87], v[120:121], v[94:95] op_sel_hi:[0,1]
	v_pk_fma_f32 v[116:117], v[116:117], v[82:83], v[86:87]
	v_pk_mul_f32 v[82:83], v[120:121], v[96:97] op_sel_hi:[0,1]
	v_pk_fma_f32 v[118:119], v[118:119], v[84:85], v[82:83]
	s_nop 0
	s_waitcnt lgkmcnt(0)
	s_nop 0
	ds_read_b128 v[82:85], v19 offset:64
	ds_read_b128 v[86:89], v19 offset:80
	ds_read_b128 v[90:93], v19 offset:96
	ds_read_b128 v[94:97], v19 offset:112
	v_mov_b32_e32 v19, 0xb5f0
	v_pk_mul_f32 v[134:135], v[68:69], v[14:15] op_sel_hi:[0,1]
	v_exp_f32_e32 v134, v134
	v_exp_f32_e32 v135, v135
	v_pk_mul_f32 v[136:137], v[68:69], v[16:17] op_sel_hi:[0,1]
	v_exp_f32_e32 v136, v136
	v_exp_f32_e32 v137, v137
	v_mul_f32_e32 v120, v68, v57
	v_pk_mul_f32 v[98:99], v[120:121], v[98:99] op_sel_hi:[0,1]
	v_pk_fma_f32 v[122:123], v[122:123], v[134:135], v[98:99]
	v_pk_mul_f32 v[98:99], v[120:121], v[100:101] op_sel_hi:[0,1]
	v_pk_fma_f32 v[124:125], v[124:125], v[136:137], v[98:99]
	v_pk_mul_f32 v[98:99], v[68:69], v[10:11] op_sel_hi:[0,1]
	v_exp_f32_e32 v98, v98
	v_exp_f32_e32 v99, v99
	v_pk_mul_f32 v[100:101], v[68:69], v[12:13] op_sel_hi:[0,1]
	v_exp_f32_e32 v100, v100
	v_exp_f32_e32 v101, v101
	v_pk_mul_f32 v[102:103], v[120:121], v[102:103] op_sel_hi:[0,1]
	v_pk_fma_f32 v[128:129], v[128:129], v[98:99], v[102:103]
	v_pk_mul_f32 v[98:99], v[120:121], v[104:105] op_sel_hi:[0,1]
	v_pk_fma_f32 v[126:127], v[126:127], v[100:101], v[98:99]
	v_pk_mul_f32 v[98:99], v[68:69], v[6:7] op_sel_hi:[0,1]
	v_exp_f32_e32 v98, v98
	v_exp_f32_e32 v99, v99
	v_pk_mul_f32 v[100:101], v[68:69], v[8:9] op_sel_hi:[0,1]
	v_exp_f32_e32 v100, v100
	v_exp_f32_e32 v101, v101
	v_pk_mul_f32 v[102:103], v[120:121], v[108:109] op_sel_hi:[0,1]
	v_pk_fma_f32 v[130:131], v[130:131], v[98:99], v[102:103]
	v_pk_mul_f32 v[98:99], v[120:121], v[110:111] op_sel_hi:[0,1]
	v_pk_fma_f32 v[132:133], v[132:133], v[100:101], v[98:99]
	v_pk_mul_f32 v[98:99], v[68:69], v[2:3] op_sel_hi:[0,1]
	v_exp_f32_e32 v98, v98
	v_exp_f32_e32 v99, v99
	v_pk_mul_f32 v[100:101], v[68:69], v[4:5] op_sel_hi:[0,1]
	v_exp_f32_e32 v100, v100
	v_exp_f32_e32 v101, v101
	v_pk_mul_f32 v[102:103], v[120:121], v[112:113] op_sel_hi:[0,1]
	v_pk_fma_f32 v[116:117], v[116:117], v[98:99], v[102:103]
	v_pk_mul_f32 v[98:99], v[120:121], v[114:115] op_sel_hi:[0,1]
	v_pk_fma_f32 v[118:119], v[118:119], v[100:101], v[98:99]
	s_nop 0
	s_waitcnt lgkmcnt(0)
	s_nop 0
	ds_read_b128 v[98:101], v19 offset:64
	ds_read_b128 v[102:105], v19 offset:80
	ds_read_b128 v[108:111], v19 offset:96
	ds_read_b128 v[112:115], v19 offset:112
	v_mov_b32_e32 v19, 0xb6c0
	v_pk_mul_f32 v[134:135], v[70:71], v[14:15] op_sel_hi:[0,1]
	v_exp_f32_e32 v134, v134
	v_exp_f32_e32 v135, v135
	v_pk_mul_f32 v[136:137], v[70:71], v[16:17] op_sel_hi:[0,1]
	v_exp_f32_e32 v136, v136
	v_exp_f32_e32 v137, v137
	v_mul_f32_e32 v120, v70, v55
	v_pk_mul_f32 v[82:83], v[120:121], v[82:83] op_sel_hi:[0,1]
	v_pk_fma_f32 v[122:123], v[122:123], v[134:135], v[82:83]
	v_pk_mul_f32 v[82:83], v[120:121], v[84:85] op_sel_hi:[0,1]
	v_pk_fma_f32 v[124:125], v[124:125], v[136:137], v[82:83]
	v_pk_mul_f32 v[82:83], v[70:71], v[10:11] op_sel_hi:[0,1]
	v_exp_f32_e32 v82, v82
	v_exp_f32_e32 v83, v83
	v_pk_mul_f32 v[84:85], v[70:71], v[12:13] op_sel_hi:[0,1]
	v_exp_f32_e32 v84, v84
	v_exp_f32_e32 v85, v85
	v_pk_mul_f32 v[86:87], v[120:121], v[86:87] op_sel_hi:[0,1]
	v_pk_fma_f32 v[128:129], v[128:129], v[82:83], v[86:87]
	v_pk_mul_f32 v[82:83], v[120:121], v[88:89] op_sel_hi:[0,1]
	v_pk_fma_f32 v[126:127], v[126:127], v[84:85], v[82:83]
	v_pk_mul_f32 v[82:83], v[70:71], v[6:7] op_sel_hi:[0,1]
	v_exp_f32_e32 v82, v82
	v_exp_f32_e32 v83, v83
	v_pk_mul_f32 v[84:85], v[70:71], v[8:9] op_sel_hi:[0,1]
	v_exp_f32_e32 v84, v84
	v_exp_f32_e32 v85, v85
	v_pk_mul_f32 v[86:87], v[120:121], v[90:91] op_sel_hi:[0,1]
	v_pk_fma_f32 v[130:131], v[130:131], v[82:83], v[86:87]
	v_pk_mul_f32 v[82:83], v[120:121], v[92:93] op_sel_hi:[0,1]
	v_pk_fma_f32 v[132:133], v[132:133], v[84:85], v[82:83]
	v_pk_mul_f32 v[82:83], v[70:71], v[2:3] op_sel_hi:[0,1]
	v_exp_f32_e32 v82, v82
	v_exp_f32_e32 v83, v83
	v_pk_mul_f32 v[84:85], v[70:71], v[4:5] op_sel_hi:[0,1]
	v_exp_f32_e32 v84, v84
	v_exp_f32_e32 v85, v85
	v_pk_mul_f32 v[86:87], v[120:121], v[94:95] op_sel_hi:[0,1]
	v_pk_fma_f32 v[116:117], v[116:117], v[82:83], v[86:87]
	v_pk_mul_f32 v[82:83], v[120:121], v[96:97] op_sel_hi:[0,1]
	v_pk_fma_f32 v[118:119], v[118:119], v[84:85], v[82:83]
	s_nop 0
	s_waitcnt lgkmcnt(0)
	s_nop 0
	ds_read_b128 v[82:85], v19 offset:64
	ds_read_b128 v[86:89], v19 offset:80
	ds_read_b128 v[90:93], v19 offset:96
	ds_read_b128 v[94:97], v19 offset:112
	v_mov_b32_e32 v19, 0xb790
	v_pk_mul_f32 v[134:135], v[72:73], v[14:15] op_sel_hi:[0,1]
	v_exp_f32_e32 v134, v134
	v_exp_f32_e32 v135, v135
	v_pk_mul_f32 v[136:137], v[72:73], v[16:17] op_sel_hi:[0,1]
	v_exp_f32_e32 v136, v136
	v_exp_f32_e32 v137, v137
	v_mul_f32_e32 v120, v72, v53
	v_pk_mul_f32 v[98:99], v[120:121], v[98:99] op_sel_hi:[0,1]
	v_pk_fma_f32 v[122:123], v[122:123], v[134:135], v[98:99]
	v_pk_mul_f32 v[98:99], v[120:121], v[100:101] op_sel_hi:[0,1]
	v_pk_fma_f32 v[124:125], v[124:125], v[136:137], v[98:99]
	v_pk_mul_f32 v[98:99], v[72:73], v[10:11] op_sel_hi:[0,1]
	v_exp_f32_e32 v98, v98
	v_exp_f32_e32 v99, v99
	v_pk_mul_f32 v[100:101], v[72:73], v[12:13] op_sel_hi:[0,1]
	v_exp_f32_e32 v100, v100
	v_exp_f32_e32 v101, v101
	v_pk_mul_f32 v[102:103], v[120:121], v[102:103] op_sel_hi:[0,1]
	v_pk_fma_f32 v[128:129], v[128:129], v[98:99], v[102:103]
	v_pk_mul_f32 v[98:99], v[120:121], v[104:105] op_sel_hi:[0,1]
	v_pk_fma_f32 v[126:127], v[126:127], v[100:101], v[98:99]
	v_pk_mul_f32 v[98:99], v[72:73], v[6:7] op_sel_hi:[0,1]
	v_exp_f32_e32 v98, v98
	v_exp_f32_e32 v99, v99
	v_pk_mul_f32 v[100:101], v[72:73], v[8:9] op_sel_hi:[0,1]
	v_exp_f32_e32 v100, v100
	v_exp_f32_e32 v101, v101
	v_pk_mul_f32 v[102:103], v[120:121], v[108:109] op_sel_hi:[0,1]
	v_pk_fma_f32 v[130:131], v[130:131], v[98:99], v[102:103]
	v_pk_mul_f32 v[98:99], v[120:121], v[110:111] op_sel_hi:[0,1]
	v_pk_fma_f32 v[132:133], v[132:133], v[100:101], v[98:99]
	v_pk_mul_f32 v[98:99], v[72:73], v[2:3] op_sel_hi:[0,1]
	v_exp_f32_e32 v98, v98
	v_exp_f32_e32 v99, v99
	v_pk_mul_f32 v[100:101], v[72:73], v[4:5] op_sel_hi:[0,1]
	v_exp_f32_e32 v100, v100
	v_exp_f32_e32 v101, v101
	v_pk_mul_f32 v[102:103], v[120:121], v[112:113] op_sel_hi:[0,1]
	v_pk_fma_f32 v[116:117], v[116:117], v[98:99], v[102:103]
	v_pk_mul_f32 v[98:99], v[120:121], v[114:115] op_sel_hi:[0,1]
	v_pk_fma_f32 v[118:119], v[118:119], v[100:101], v[98:99]
	s_nop 0
	s_waitcnt lgkmcnt(0)
	s_nop 0
	ds_read_b128 v[98:101], v19 offset:64
	ds_read_b128 v[102:105], v19 offset:80
	ds_read_b128 v[108:111], v19 offset:96
	ds_read_b128 v[112:115], v19 offset:112
	v_mov_b32_e32 v19, 0xb860
	v_pk_mul_f32 v[134:135], v[74:75], v[14:15] op_sel_hi:[0,1]
	v_exp_f32_e32 v134, v134
	v_exp_f32_e32 v135, v135
	v_pk_mul_f32 v[136:137], v[74:75], v[16:17] op_sel_hi:[0,1]
	v_exp_f32_e32 v136, v136
	v_exp_f32_e32 v137, v137
	v_mul_f32_e32 v120, v74, v51
	v_pk_mul_f32 v[82:83], v[120:121], v[82:83] op_sel_hi:[0,1]
	v_pk_fma_f32 v[122:123], v[122:123], v[134:135], v[82:83]
	v_pk_mul_f32 v[82:83], v[120:121], v[84:85] op_sel_hi:[0,1]
	v_pk_fma_f32 v[124:125], v[124:125], v[136:137], v[82:83]
	v_pk_mul_f32 v[82:83], v[74:75], v[10:11] op_sel_hi:[0,1]
	v_exp_f32_e32 v82, v82
	v_exp_f32_e32 v83, v83
	v_pk_mul_f32 v[84:85], v[74:75], v[12:13] op_sel_hi:[0,1]
	v_exp_f32_e32 v84, v84
	v_exp_f32_e32 v85, v85
	v_pk_mul_f32 v[86:87], v[120:121], v[86:87] op_sel_hi:[0,1]
	v_pk_fma_f32 v[128:129], v[128:129], v[82:83], v[86:87]
	v_pk_mul_f32 v[82:83], v[120:121], v[88:89] op_sel_hi:[0,1]
	v_pk_fma_f32 v[126:127], v[126:127], v[84:85], v[82:83]
	v_pk_mul_f32 v[82:83], v[74:75], v[6:7] op_sel_hi:[0,1]
	v_exp_f32_e32 v82, v82
	v_exp_f32_e32 v83, v83
	v_pk_mul_f32 v[84:85], v[74:75], v[8:9] op_sel_hi:[0,1]
	v_exp_f32_e32 v84, v84
	v_exp_f32_e32 v85, v85
	v_pk_mul_f32 v[86:87], v[120:121], v[90:91] op_sel_hi:[0,1]
	v_pk_fma_f32 v[130:131], v[130:131], v[82:83], v[86:87]
	v_pk_mul_f32 v[82:83], v[120:121], v[92:93] op_sel_hi:[0,1]
	v_pk_fma_f32 v[132:133], v[132:133], v[84:85], v[82:83]
	v_pk_mul_f32 v[82:83], v[74:75], v[2:3] op_sel_hi:[0,1]
	v_exp_f32_e32 v82, v82
	v_exp_f32_e32 v83, v83
	v_pk_mul_f32 v[84:85], v[74:75], v[4:5] op_sel_hi:[0,1]
	v_exp_f32_e32 v84, v84
	v_exp_f32_e32 v85, v85
	v_pk_mul_f32 v[86:87], v[120:121], v[94:95] op_sel_hi:[0,1]
	v_pk_fma_f32 v[116:117], v[116:117], v[82:83], v[86:87]
	v_pk_mul_f32 v[82:83], v[120:121], v[96:97] op_sel_hi:[0,1]
	v_pk_fma_f32 v[118:119], v[118:119], v[84:85], v[82:83]
	s_nop 0
	s_waitcnt lgkmcnt(0)
	s_nop 0
	ds_read_b128 v[82:85], v19 offset:64
	ds_read_b128 v[86:89], v19 offset:80
	ds_read_b128 v[90:93], v19 offset:96
	ds_read_b128 v[94:97], v19 offset:112
	v_mov_b32_e32 v19, 0xb930
	v_pk_mul_f32 v[134:135], v[76:77], v[14:15] op_sel_hi:[0,1]
	v_exp_f32_e32 v134, v134
	v_exp_f32_e32 v135, v135
	v_pk_mul_f32 v[136:137], v[76:77], v[16:17] op_sel_hi:[0,1]
	v_exp_f32_e32 v136, v136
	v_exp_f32_e32 v137, v137
	v_mul_f32_e32 v120, v76, v49
	v_pk_mul_f32 v[98:99], v[120:121], v[98:99] op_sel_hi:[0,1]
	v_pk_fma_f32 v[122:123], v[122:123], v[134:135], v[98:99]
	v_pk_mul_f32 v[98:99], v[120:121], v[100:101] op_sel_hi:[0,1]
	v_pk_fma_f32 v[124:125], v[124:125], v[136:137], v[98:99]
	v_pk_mul_f32 v[98:99], v[76:77], v[10:11] op_sel_hi:[0,1]
	v_exp_f32_e32 v98, v98
	v_exp_f32_e32 v99, v99
	v_pk_mul_f32 v[100:101], v[76:77], v[12:13] op_sel_hi:[0,1]
	v_exp_f32_e32 v100, v100
	v_exp_f32_e32 v101, v101
	v_pk_mul_f32 v[102:103], v[120:121], v[102:103] op_sel_hi:[0,1]
	v_pk_fma_f32 v[128:129], v[128:129], v[98:99], v[102:103]
	v_pk_mul_f32 v[98:99], v[120:121], v[104:105] op_sel_hi:[0,1]
	v_pk_fma_f32 v[126:127], v[126:127], v[100:101], v[98:99]
	v_pk_mul_f32 v[98:99], v[76:77], v[6:7] op_sel_hi:[0,1]
	v_exp_f32_e32 v98, v98
	v_exp_f32_e32 v99, v99
	v_pk_mul_f32 v[100:101], v[76:77], v[8:9] op_sel_hi:[0,1]
	v_exp_f32_e32 v100, v100
	v_exp_f32_e32 v101, v101
	v_pk_mul_f32 v[102:103], v[120:121], v[108:109] op_sel_hi:[0,1]
	v_pk_fma_f32 v[130:131], v[130:131], v[98:99], v[102:103]
	v_pk_mul_f32 v[98:99], v[120:121], v[110:111] op_sel_hi:[0,1]
	v_pk_fma_f32 v[132:133], v[132:133], v[100:101], v[98:99]
	v_pk_mul_f32 v[98:99], v[76:77], v[2:3] op_sel_hi:[0,1]
	v_exp_f32_e32 v98, v98
	v_exp_f32_e32 v99, v99
	v_pk_mul_f32 v[100:101], v[76:77], v[4:5] op_sel_hi:[0,1]
	v_exp_f32_e32 v100, v100
	v_exp_f32_e32 v101, v101
	v_pk_mul_f32 v[102:103], v[120:121], v[112:113] op_sel_hi:[0,1]
	v_pk_fma_f32 v[116:117], v[116:117], v[98:99], v[102:103]
	v_pk_mul_f32 v[98:99], v[120:121], v[114:115] op_sel_hi:[0,1]
	v_pk_fma_f32 v[118:119], v[118:119], v[100:101], v[98:99]
	s_nop 0
	s_waitcnt lgkmcnt(0)
	s_nop 0
	ds_read_b128 v[98:101], v19 offset:64
	ds_read_b128 v[102:105], v19 offset:80
	ds_read_b128 v[108:111], v19 offset:96
	ds_read_b128 v[112:115], v19 offset:112
	v_add_f32_e32 v19, 0, v80
	v_add_f32_e32 v19, v19, v20
	v_add_f32_e32 v19, v19, v22
	v_add_f32_e32 v19, v19, v24
	v_add_f32_e32 v19, v19, v26
	v_add_f32_e32 v19, v19, v28
	v_add_f32_e32 v19, v19, v30
	v_add_f32_e32 v19, v19, v32
	v_add_f32_e32 v19, v19, v34
	v_add_f32_e32 v19, v19, v36
	v_pk_mul_f32 v[134:135], v[78:79], v[14:15] op_sel_hi:[0,1]
	v_pk_mul_f32 v[136:137], v[78:79], v[16:17] op_sel_hi:[0,1]
	v_add_f32_e32 v19, v19, v38
	v_exp_f32_e32 v134, v134
	v_exp_f32_e32 v135, v135
	v_exp_f32_e32 v136, v136
	v_exp_f32_e32 v137, v137
	v_add_f32_e32 v19, v19, v40
	v_add_f32_e32 v19, v19, v42
	v_mul_f32_e32 v120, v78, v47
	v_add_f32_e32 v19, v19, v44
	v_pk_mul_f32 v[82:83], v[120:121], v[82:83] op_sel_hi:[0,1]
	v_pk_mul_f32 v[84:85], v[120:121], v[84:85] op_sel_hi:[0,1]
	v_add_f32_e32 v19, v19, v46
	v_pk_fma_f32 v[82:83], v[122:123], v[134:135], v[82:83]
	v_pk_fma_f32 v[84:85], v[124:125], v[136:137], v[84:85]
	v_pk_mul_f32 v[122:123], v[78:79], v[10:11] op_sel_hi:[0,1]
	v_pk_mul_f32 v[124:125], v[78:79], v[12:13] op_sel_hi:[0,1]
	v_add_f32_e32 v19, v19, v48
	v_exp_f32_e32 v122, v122
	v_exp_f32_e32 v123, v123
	v_exp_f32_e32 v124, v124
	v_exp_f32_e32 v125, v125
	v_add_f32_e32 v19, v19, v50
	v_add_f32_e32 v19, v19, v52
	v_add_f32_e32 v19, v19, v54
	v_pk_mul_f32 v[86:87], v[120:121], v[86:87] op_sel_hi:[0,1]
	v_pk_mul_f32 v[88:89], v[120:121], v[88:89] op_sel_hi:[0,1]
	v_add_f32_e32 v19, v19, v56
	v_pk_fma_f32 v[86:87], v[128:129], v[122:123], v[86:87]
	v_pk_fma_f32 v[88:89], v[126:127], v[124:125], v[88:89]
	v_pk_mul_f32 v[122:123], v[78:79], v[6:7] op_sel_hi:[0,1]
	v_pk_mul_f32 v[124:125], v[78:79], v[8:9] op_sel_hi:[0,1]
	v_add_f32_e32 v19, v19, v58
	v_exp_f32_e32 v122, v122
	v_exp_f32_e32 v123, v123
	v_exp_f32_e32 v124, v124
	v_exp_f32_e32 v125, v125
	v_add_f32_e32 v19, v19, v60
	v_add_f32_e32 v19, v19, v62
	v_add_f32_e32 v19, v19, v64
	v_pk_mul_f32 v[90:91], v[120:121], v[90:91] op_sel_hi:[0,1]
	v_pk_mul_f32 v[92:93], v[120:121], v[92:93] op_sel_hi:[0,1]
	v_add_f32_e32 v19, v19, v66
	v_pk_fma_f32 v[90:91], v[130:131], v[122:123], v[90:91]
	v_pk_fma_f32 v[92:93], v[132:133], v[124:125], v[92:93]
	v_pk_mul_f32 v[122:123], v[78:79], v[2:3] op_sel_hi:[0,1]
	v_pk_mul_f32 v[124:125], v[78:79], v[4:5] op_sel_hi:[0,1]
	v_add_f32_e32 v19, v19, v68
	v_exp_f32_e32 v122, v122
	v_exp_f32_e32 v123, v123
	v_exp_f32_e32 v124, v124
	v_exp_f32_e32 v125, v125
	v_add_f32_e32 v19, v19, v70
	v_add_f32_e32 v19, v19, v72
	v_add_f32_e32 v19, v19, v74
	v_pk_mul_f32 v[94:95], v[120:121], v[94:95] op_sel_hi:[0,1]
	v_pk_mul_f32 v[96:97], v[120:121], v[96:97] op_sel_hi:[0,1]
	v_add_f32_e32 v19, v19, v76
	v_pk_fma_f32 v[94:95], v[116:117], v[122:123], v[94:95]
	v_pk_fma_f32 v[96:97], v[118:119], v[124:125], v[96:97]
	v_add_f32_e32 v19, v19, v78
	s_waitcnt lgkmcnt(0)
	v_cvt_f32_f16_e32 v20, v106
	v_add_f32_e32 v19, v19, v18
	v_pk_mul_f32 v[4:5], v[18:19], v[4:5] op_sel_hi:[0,1]
	v_exp_f32_e32 v4, v4
	v_exp_f32_e32 v5, v5
	v_pk_mul_f32 v[14:15], v[18:19], v[14:15] op_sel_hi:[0,1]
	v_exp_f32_e32 v14, v14
	v_exp_f32_e32 v15, v15
	v_mul_f32_e32 v20, v18, v20
	v_pk_mul_f32 v[22:23], v[20:21], v[114:115] op_sel_hi:[0,1]
	v_pk_fma_f32 v[22:23], v[96:97], v[4:5], v[22:23]
	v_pk_mul_f32 v[4:5], v[20:21], v[98:99] op_sel_hi:[0,1]
	v_pk_fma_f32 v[14:15], v[82:83], v[14:15], v[4:5]
	v_pk_mul_f32 v[4:5], v[18:19], v[16:17] op_sel_hi:[0,1]
	v_exp_f32_e32 v4, v4
	v_exp_f32_e32 v5, v5
	v_pk_mul_f32 v[10:11], v[18:19], v[10:11] op_sel_hi:[0,1]
	v_exp_f32_e32 v10, v10
	v_exp_f32_e32 v11, v11
	v_pk_mul_f32 v[16:17], v[20:21], v[100:101] op_sel_hi:[0,1]
	v_pk_fma_f32 v[16:17], v[84:85], v[4:5], v[16:17]
	v_pk_mul_f32 v[4:5], v[20:21], v[102:103] op_sel_hi:[0,1]
	v_pk_fma_f32 v[10:11], v[86:87], v[10:11], v[4:5]
	v_pk_mul_f32 v[4:5], v[18:19], v[12:13] op_sel_hi:[0,1]
	v_exp_f32_e32 v4, v4
	v_exp_f32_e32 v5, v5
	v_pk_mul_f32 v[6:7], v[18:19], v[6:7] op_sel_hi:[0,1]
	v_exp_f32_e32 v6, v6
	v_exp_f32_e32 v7, v7
	v_pk_mul_f32 v[8:9], v[18:19], v[8:9] op_sel_hi:[0,1]
	v_exp_f32_e32 v8, v8
	v_exp_f32_e32 v9, v9
	v_pk_mul_f32 v[2:3], v[18:19], v[2:3] op_sel_hi:[0,1]
	v_pk_mul_f32 v[12:13], v[20:21], v[104:105] op_sel_hi:[0,1]
	v_exp_f32_e32 v2, v2
	v_exp_f32_e32 v3, v3
	v_pk_fma_f32 v[4:5], v[88:89], v[4:5], v[12:13]
	v_pk_mul_f32 v[12:13], v[20:21], v[108:109] op_sel_hi:[0,1]
	v_pk_fma_f32 v[6:7], v[90:91], v[6:7], v[12:13]
	v_pk_mul_f32 v[12:13], v[20:21], v[110:111] op_sel_hi:[0,1]
	v_pk_fma_f32 v[8:9], v[92:93], v[8:9], v[12:13]
	v_pk_mul_f32 v[12:13], v[20:21], v[112:113] op_sel_hi:[0,1]
	v_cvt_pk_f16_f32 v5, v4, v5
	v_cvt_pk_f16_f32 v4, v10, v11
	v_lshl_or_b32 v10, v0, 4, s6
	v_mov_b32_e32 v11, s7
	v_pk_fma_f32 v[12:13], v[94:95], v[2:3], v[12:13]
	v_cvt_pk_f16_f32 v3, v16, v17
	v_cvt_pk_f16_f32 v2, v14, v15
	v_lshl_add_u64 v[10:11], s[4:5], 0, v[10:11]
	s_movk_i32 s4, 0x2000
	global_store_dwordx4 v[10:11], v[2:5], off sc0 sc1
	global_store_dword v1, v19, s[0:1] sc0 sc1
	s_nop 0
	v_cvt_pk_f16_f32 v2, v6, v7
	v_add_co_u32_e32 v6, vcc, s4, v10
	v_cvt_pk_f16_f32 v5, v22, v23
	v_cvt_pk_f16_f32 v4, v12, v13
	v_cvt_pk_f16_f32 v3, v8, v9
	v_addc_co_u32_e32 v7, vcc, 0, v11, vcc
	global_store_dwordx4 v[6:7], v[2:5], off sc0 sc1
	s_endpgm

.LBB3_10:
	s_or_b64 exec, exec, s[0:1]
	v_lshl_add_u64 v[0:1], v[6:7], 1, s[10:11]
	v_cvt_pk_f16_f32 v5, v80, v81
	v_cvt_pk_f16_f32 v4, v78, v79
	v_lshl_add_u64 v[6:7], v[0:1], 0, v[8:9]
	global_store_dwordx2 v[6:7], v[4:5], off sc0 sc1
	v_cvt_pk_f16_f32 v3, v2, v3
	v_cvt_pk_f16_f32 v2, v82, v83
	v_lshl_add_u64 v[4:5], v[0:1], 0, v[10:11]
	global_store_dwordx2 v[4:5], v[2:3], off sc0 sc1
	v_cvt_pk_f16_f32 v3, v84, v85
	v_cvt_pk_f16_f32 v2, v86, v87
	v_lshl_add_u64 v[4:5], v[0:1], 0, v[12:13]
	global_store_dwordx2 v[4:5], v[2:3], off sc0 sc1
	v_cvt_pk_f16_f32 v3, v88, v89
	v_cvt_pk_f16_f32 v2, v90, v91
	v_lshl_add_u64 v[4:5], v[0:1], 0, v[14:15]
	global_store_dwordx2 v[4:5], v[2:3], off sc0 sc1
	v_cvt_pk_f16_f32 v3, v92, v93
	v_cvt_pk_f16_f32 v2, v94, v95
	v_lshl_add_u64 v[4:5], v[0:1], 0, v[16:17]
	global_store_dwordx2 v[4:5], v[2:3], off sc0 sc1
	v_cvt_pk_f16_f32 v3, v96, v97
	v_cvt_pk_f16_f32 v2, v98, v99
	v_lshl_add_u64 v[4:5], v[0:1], 0, v[18:19]
	global_store_dwordx2 v[4:5], v[2:3], off sc0 sc1
	v_cvt_pk_f16_f32 v3, v100, v101
	v_cvt_pk_f16_f32 v2, v102, v103
	v_lshl_add_u64 v[4:5], v[0:1], 0, v[20:21]
	global_store_dwordx2 v[4:5], v[2:3], off sc0 sc1
	v_cvt_pk_f16_f32 v3, v104, v105
	v_cvt_pk_f16_f32 v2, v106, v107
	v_lshl_add_u64 v[0:1], v[0:1], 0, v[22:23]
	global_store_dwordx2 v[0:1], v[2:3], off sc0 sc1
	s_endpgm

_Z6k_headPKfS0_S0_S0_Pf:
	s_load_dwordx8 s[4:11], s[0:1], 0x0
	s_load_dwordx2 s[12:13], s[0:1], 0x20
	s_ashr_i32 s3, s2, 31
	s_lshl_b64 s[0:1], s[2:3], 16
	s_lshl_b32 s14, s2, 8
	v_lshlrev_b32_e32 v1, 2, v0
	s_waitcnt lgkmcnt(0)
	s_add_u32 s0, s4, s0
	s_addc_u32 s1, s5, s1
	s_add_u32 s14, s6, s14
	s_addc_u32 s15, s7, 0
	s_load_dwordx16 s[16:31], s[14:15], 0x0
	s_load_dwordx16 s[32:47], s[14:15], 0x40
	s_load_dwordx16 s[48:63], s[14:15], 0x80
	s_load_dwordx16 s[64:79], s[14:15], 0xc0
	global_load_dword v4, v1, s[8:9]
	global_load_dword v5, v1, s[8:9] offset:1024
	global_load_dword v24, v1, s[0:1]
	global_load_dword v25, v1, s[0:1] offset:1024
	global_load_dword v26, v1, s[0:1] offset:2048
	global_load_dword v27, v1, s[0:1] offset:3072
	v_add_u32_e32 v88, 0x1000, v1
	global_load_dword v28, v88, s[0:1]
	global_load_dword v29, v88, s[0:1] offset:1024
	global_load_dword v30, v88, s[0:1] offset:2048
	global_load_dword v31, v88, s[0:1] offset:3072
	v_add_u32_e32 v88, 0x1000, v88
	global_load_dword v32, v88, s[0:1]
	global_load_dword v33, v88, s[0:1] offset:1024
	global_load_dword v34, v88, s[0:1] offset:2048
	global_load_dword v35, v88, s[0:1] offset:3072
	v_add_u32_e32 v88, 0x1000, v88
	global_load_dword v36, v88, s[0:1]
	global_load_dword v37, v88, s[0:1] offset:1024
	global_load_dword v38, v88, s[0:1] offset:2048
	global_load_dword v39, v88, s[0:1] offset:3072
	v_add_u32_e32 v88, 0x1000, v88
	global_load_dword v40, v88, s[0:1]
	global_load_dword v41, v88, s[0:1] offset:1024
	global_load_dword v42, v88, s[0:1] offset:2048
	global_load_dword v43, v88, s[0:1] offset:3072
	v_add_u32_e32 v88, 0x1000, v88
	global_load_dword v44, v88, s[0:1]
	global_load_dword v45, v88, s[0:1] offset:1024
	global_load_dword v46, v88, s[0:1] offset:2048
	global_load_dword v47, v88, s[0:1] offset:3072
	v_add_u32_e32 v88, 0x1000, v88
	global_load_dword v48, v88, s[0:1]
	global_load_dword v49, v88, s[0:1] offset:1024
	global_load_dword v50, v88, s[0:1] offset:2048
	global_load_dword v51, v88, s[0:1] offset:3072
	v_add_u32_e32 v88, 0x1000, v88
	global_load_dword v52, v88, s[0:1]
	global_load_dword v53, v88, s[0:1] offset:1024
	global_load_dword v54, v88, s[0:1] offset:2048
	global_load_dword v55, v88, s[0:1] offset:3072
	v_add_u32_e32 v88, 0x1000, v88
	global_load_dword v56, v88, s[0:1]
	global_load_dword v57, v88, s[0:1] offset:1024
	global_load_dword v58, v88, s[0:1] offset:2048
	global_load_dword v59, v88, s[0:1] offset:3072
	v_add_u32_e32 v88, 0x1000, v88
	global_load_dword v60, v88, s[0:1]
	global_load_dword v61, v88, s[0:1] offset:1024
	global_load_dword v62, v88, s[0:1] offset:2048
	global_load_dword v63, v88, s[0:1] offset:3072
	v_add_u32_e32 v88, 0x1000, v88
	global_load_dword v64, v88, s[0:1]
	global_load_dword v65, v88, s[0:1] offset:1024
	global_load_dword v66, v88, s[0:1] offset:2048
	global_load_dword v67, v88, s[0:1] offset:3072
	v_add_u32_e32 v88, 0x1000, v88
	global_load_dword v68, v88, s[0:1]
	global_load_dword v69, v88, s[0:1] offset:1024
	global_load_dword v70, v88, s[0:1] offset:2048
	global_load_dword v71, v88, s[0:1] offset:3072
	v_add_u32_e32 v88, 0x1000, v88
	global_load_dword v72, v88, s[0:1]
	global_load_dword v73, v88, s[0:1] offset:1024
	global_load_dword v74, v88, s[0:1] offset:2048
	global_load_dword v75, v88, s[0:1] offset:3072
	v_add_u32_e32 v88, 0x1000, v88
	global_load_dword v76, v88, s[0:1]
	global_load_dword v77, v88, s[0:1] offset:1024
	global_load_dword v78, v88, s[0:1] offset:2048
	global_load_dword v79, v88, s[0:1] offset:3072
	v_add_u32_e32 v88, 0x1000, v88
	global_load_dword v80, v88, s[0:1]
	global_load_dword v81, v88, s[0:1] offset:1024
	global_load_dword v82, v88, s[0:1] offset:2048
	global_load_dword v83, v88, s[0:1] offset:3072
	v_add_u32_e32 v88, 0x1000, v88
	global_load_dword v84, v88, s[0:1]
	global_load_dword v85, v88, s[0:1] offset:1024
	global_load_dword v86, v88, s[0:1] offset:2048
	global_load_dword v87, v88, s[0:1] offset:3072
	v_mov_b32_e32 v2, 0
	v_mov_b32_e32 v3, 0
	s_waitcnt lgkmcnt(0)
	s_waitcnt vmcnt(56)
	v_add_f32_e32 v2, v2, v24
	v_add_f32_e32 v3, s16, v3
	v_add_f32_e32 v2, v2, v25
	v_add_f32_e32 v3, s17, v3
	v_add_f32_e32 v2, v2, v26
	v_add_f32_e32 v3, s18, v3
	v_add_f32_e32 v2, v2, v27
	v_add_f32_e32 v3, s19, v3
	v_add_f32_e32 v2, v2, v28
	v_add_f32_e32 v3, s20, v3
	v_add_f32_e32 v2, v2, v29
	v_add_f32_e32 v3, s21, v3
	v_add_f32_e32 v2, v2, v30
	v_add_f32_e32 v3, s22, v3
	v_add_f32_e32 v2, v2, v31
	v_add_f32_e32 v3, s23, v3
	s_waitcnt vmcnt(48)
	v_add_f32_e32 v2, v2, v32
	v_add_f32_e32 v3, s24, v3
	v_add_f32_e32 v2, v2, v33
	v_add_f32_e32 v3, s25, v3
	v_add_f32_e32 v2, v2, v34
	v_add_f32_e32 v3, s26, v3
	v_add_f32_e32 v2, v2, v35
	v_add_f32_e32 v3, s27, v3
	v_add_f32_e32 v2, v2, v36
	v_add_f32_e32 v3, s28, v3
	v_add_f32_e32 v2, v2, v37
	v_add_f32_e32 v3, s29, v3
	v_add_f32_e32 v2, v2, v38
	v_add_f32_e32 v3, s30, v3
	v_add_f32_e32 v2, v2, v39
	v_add_f32_e32 v3, s31, v3
	s_waitcnt vmcnt(40)
	v_add_f32_e32 v2, v2, v40
	v_add_f32_e32 v3, s32, v3
	v_add_f32_e32 v2, v2, v41
	v_add_f32_e32 v3, s33, v3
	v_add_f32_e32 v2, v2, v42
	v_add_f32_e32 v3, s34, v3
	v_add_f32_e32 v2, v2, v43
	v_add_f32_e32 v3, s35, v3
	v_add_f32_e32 v2, v2, v44
	v_add_f32_e32 v3, s36, v3
	v_add_f32_e32 v2, v2, v45
	v_add_f32_e32 v3, s37, v3
	v_add_f32_e32 v2, v2, v46
	v_add_f32_e32 v3, s38, v3
	v_add_f32_e32 v2, v2, v47
	v_add_f32_e32 v3, s39, v3
	s_waitcnt vmcnt(32)
	v_add_f32_e32 v2, v2, v48
	v_add_f32_e32 v3, s40, v3
	v_add_f32_e32 v2, v2, v49
	v_add_f32_e32 v3, s41, v3
	v_add_f32_e32 v2, v2, v50
	v_add_f32_e32 v3, s42, v3
	v_add_f32_e32 v2, v2, v51
	v_add_f32_e32 v3, s43, v3
	v_add_f32_e32 v2, v2, v52
	v_add_f32_e32 v3, s44, v3
	v_add_f32_e32 v2, v2, v53
	v_add_f32_e32 v3, s45, v3
	v_add_f32_e32 v2, v2, v54
	v_add_f32_e32 v3, s46, v3
	v_add_f32_e32 v2, v2, v55
	v_add_f32_e32 v3, s47, v3
	s_waitcnt vmcnt(24)
	v_add_f32_e32 v2, v2, v56
	v_add_f32_e32 v3, s48, v3
	v_add_f32_e32 v2, v2, v57
	v_add_f32_e32 v3, s49, v3
	v_add_f32_e32 v2, v2, v58
	v_add_f32_e32 v3, s50, v3
	v_add_f32_e32 v2, v2, v59
	v_add_f32_e32 v3, s51, v3
	v_add_f32_e32 v2, v2, v60
	v_add_f32_e32 v3, s52, v3
	v_add_f32_e32 v2, v2, v61
	v_add_f32_e32 v3, s53, v3
	v_add_f32_e32 v2, v2, v62
	v_add_f32_e32 v3, s54, v3
	v_add_f32_e32 v2, v2, v63
	v_add_f32_e32 v3, s55, v3
	s_waitcnt vmcnt(16)
	v_add_f32_e32 v2, v2, v64
	v_add_f32_e32 v3, s56, v3
	v_add_f32_e32 v2, v2, v65
	v_add_f32_e32 v3, s57, v3
	v_add_f32_e32 v2, v2, v66
	v_add_f32_e32 v3, s58, v3
	v_add_f32_e32 v2, v2, v67
	v_add_f32_e32 v3, s59, v3
	v_add_f32_e32 v2, v2, v68
	v_add_f32_e32 v3, s60, v3
	v_add_f32_e32 v2, v2, v69
	v_add_f32_e32 v3, s61, v3
	v_add_f32_e32 v2, v2, v70
	v_add_f32_e32 v3, s62, v3
	v_add_f32_e32 v2, v2, v71
	v_add_f32_e32 v3, s63, v3
	s_waitcnt vmcnt(8)
	v_add_f32_e32 v2, v2, v72
	v_add_f32_e32 v3, s64, v3
	v_add_f32_e32 v2, v2, v73
	v_add_f32_e32 v3, s65, v3
	v_add_f32_e32 v2, v2, v74
	v_add_f32_e32 v3, s66, v3
	v_add_f32_e32 v2, v2, v75
	v_add_f32_e32 v3, s67, v3
	v_add_f32_e32 v2, v2, v76
	v_add_f32_e32 v3, s68, v3
	v_add_f32_e32 v2, v2, v77
	v_add_f32_e32 v3, s69, v3
	v_add_f32_e32 v2, v2, v78
	v_add_f32_e32 v3, s70, v3
	v_add_f32_e32 v2, v2, v79
	v_add_f32_e32 v3, s71, v3
	s_waitcnt vmcnt(0)
	v_add_f32_e32 v2, v2, v80
	v_add_f32_e32 v3, s72, v3
	v_add_f32_e32 v2, v2, v81
	v_add_f32_e32 v3, s73, v3
	v_add_f32_e32 v2, v2, v82
	v_add_f32_e32 v3, s74, v3
	v_add_f32_e32 v2, v2, v83
	v_add_f32_e32 v3, s75, v3
	v_add_f32_e32 v2, v2, v84
	v_add_f32_e32 v3, s76, v3
	v_add_f32_e32 v2, v2, v85
	v_add_f32_e32 v3, s77, v3
	v_add_f32_e32 v2, v2, v86
	v_add_f32_e32 v3, s78, v3
	v_add_f32_e32 v2, v2, v87
	v_add_f32_e32 v3, s79, v3
	v_lshlrev_b32_e32 v1, 2, v0
	v_max_f32_e32 v3, v3, v3
	v_max_f32_e32 v3, 1.0, v3
	v_div_scale_f32 v6, s[0:1], v3, v3, v2
	v_rcp_f32_e32 v7, v6
	v_div_scale_f32 v9, vcc, v2, v3, v2
	v_and_b32_e32 v8, 63, v0
	v_fma_f32 v10, -v6, v7, 1.0
	v_fmac_f32_e32 v7, v10, v7
	v_mul_f32_e32 v10, v9, v7
	v_fma_f32 v11, -v6, v10, v9
	v_fmac_f32_e32 v10, v11, v7
	v_fma_f32 v6, -v6, v10, v9
	v_div_fmas_f32 v6, v6, v7, v10
	v_div_fixup_f32 v2, v6, v3, v2
	v_cmp_eq_u32_e32 vcc, 0, v8
	s_waitcnt vmcnt(1)
	v_mul_f32_e32 v3, v2, v4
	s_waitcnt vmcnt(0)
	v_mul_f32_e32 v6, v2, v5
	v_mov_b32_dpp v3, v3 quad_perm:[1,0,3,2] row_mask:0xf bank_mask:0xf bound_ctrl:1
	v_fmac_f32_e32 v3, v2, v4
	v_mov_b32_dpp v6, v6 quad_perm:[1,0,3,2] row_mask:0xf bank_mask:0xf bound_ctrl:1
	v_fmac_f32_e32 v6, v2, v5
	v_add_f32_dpp v2, v3, v3 quad_perm:[2,3,0,1] row_mask:0xf bank_mask:0xf bound_ctrl:1
	s_nop 0
	v_add_f32_dpp v3, v6, v6 quad_perm:[2,3,0,1] row_mask:0xf bank_mask:0xf bound_ctrl:1
	v_add_f32_dpp v2, v2, v2 row_half_mirror row_mask:0xf bank_mask:0xf bound_ctrl:1
	s_nop 0
	v_add_f32_dpp v3, v3, v3 row_half_mirror row_mask:0xf bank_mask:0xf bound_ctrl:1
	v_add_f32_dpp v2, v2, v2 row_mirror row_mask:0xf bank_mask:0xf bound_ctrl:1
	s_nop 0
	v_add_f32_dpp v3, v3, v3 row_mirror row_mask:0xf bank_mask:0xf bound_ctrl:1
	v_readlane_b32 s3, v2, 0
	v_readlane_b32 s5, v2, 16
	v_readlane_b32 s4, v2, 32
	v_readlane_b32 s6, v2, 48
	v_readlane_b32 s7, v3, 0
	v_readlane_b32 s9, v3, 16
	v_readlane_b32 s8, v3, 32
	v_readlane_b32 s14, v3, 48
	s_and_saveexec_b64 s[0:1], vcc
	s_cbranch_execz .LBB4_4
	v_mov_b32_e32 v3, s9
	v_mov_b32_e32 v4, s14
	v_add_f32_e32 v3, s7, v3
	v_add_f32_e32 v4, s8, v4
	v_add_f32_e32 v3, v3, v4
	v_mov_b32_e32 v4, s5
	v_mov_b32_e32 v5, s6
	v_add_f32_e32 v4, s3, v4
	v_add_f32_e32 v5, s4, v5
	v_lshrrev_b32_e32 v2, 4, v0
	v_add_f32_e32 v4, v4, v5
	ds_write2_b32 v2, v4, v3 offset1:4

	.amdhsa_kernel _Z6k_headPKfS0_S0_S0_Pf
		.amdhsa_group_segment_fixed_size 32
		.amdhsa_private_segment_fixed_size 0
		.amdhsa_kernarg_size 40
		.amdhsa_user_sgpr_count 2
		.amdhsa_user_sgpr_dispatch_ptr 0
		.amdhsa_user_sgpr_queue_ptr 0
		.amdhsa_user_sgpr_kernarg_segment_ptr 1
		.amdhsa_user_sgpr_dispatch_id 0
		.amdhsa_user_sgpr_kernarg_preload_length 0
		.amdhsa_user_sgpr_kernarg_preload_offset 0
		.amdhsa_user_sgpr_private_segment_size 0
		.amdhsa_uses_dynamic_stack 0
		.amdhsa_enable_private_segment 0
		.amdhsa_system_sgpr_workgroup_id_x 1
		.amdhsa_system_sgpr_workgroup_id_y 0
		.amdhsa_system_sgpr_workgroup_id_z 0
		.amdhsa_system_sgpr_workgroup_info 0
		.amdhsa_system_vgpr_workitem_id 0
		.amdhsa_next_free_vgpr 92
		.amdhsa_next_free_sgpr 80
		.amdhsa_accum_offset 92
		.amdhsa_reserve_vcc 1
		.amdhsa_float_round_mode_32 0
		.amdhsa_float_round_mode_16_64 0
		.amdhsa_float_denorm_mode_32 3
		.amdhsa_float_denorm_mode_16_64 3
		.amdhsa_dx10_clamp 1
		.amdhsa_ieee_mode 1
		.amdhsa_fp16_overflow 0
		.amdhsa_tg_split 0
		.amdhsa_exception_fp_ieee_invalid_op 0
		.amdhsa_exception_fp_denorm_src 0
		.amdhsa_exception_fp_ieee_div_zero 0
		.amdhsa_exception_fp_ieee_overflow 0
		.amdhsa_exception_fp_ieee_underflow 0
		.amdhsa_exception_fp_ieee_inexact 0
		.amdhsa_exception_int_div_zero 0
	.end_amdhsa_kernel

.Lk2f_bc_done:
	s_or_b64 exec, exec, s[56:57]
	s_waitcnt lgkmcnt(0)
	s_barrier
	s_waitcnt vmcnt(18)
	v_cvt_f32_f16_e32 v134, v68
	v_cvt_f32_f16_sdwa v135, v68 dst_sel:DWORD dst_unused:UNUSED_PAD src0_sel:WORD_1
	v_cvt_f32_f16_e32 v136, v69
	v_cvt_f32_f16_sdwa v137, v69 dst_sel:DWORD dst_unused:UNUSED_PAD src0_sel:WORD_1
	v_cvt_f32_f16_e32 v138, v70
	v_cvt_f32_f16_sdwa v139, v70 dst_sel:DWORD dst_unused:UNUSED_PAD src0_sel:WORD_1
	v_cvt_f32_f16_e32 v140, v71
	v_cvt_f32_f16_sdwa v141, v71 dst_sel:DWORD dst_unused:UNUSED_PAD src0_sel:WORD_1
	s_waitcnt vmcnt(17)
	v_cvt_f32_f16_e32 v142, v72
	v_cvt_f32_f16_sdwa v143, v72 dst_sel:DWORD dst_unused:UNUSED_PAD src0_sel:WORD_1
	v_cvt_f32_f16_e32 v144, v73
	v_cvt_f32_f16_sdwa v145, v73 dst_sel:DWORD dst_unused:UNUSED_PAD src0_sel:WORD_1
	v_cvt_f32_f16_e32 v146, v74
	v_cvt_f32_f16_sdwa v147, v74 dst_sel:DWORD dst_unused:UNUSED_PAD src0_sel:WORD_1
	v_cvt_f32_f16_e32 v148, v75
	v_cvt_f32_f16_sdwa v149, v75 dst_sel:DWORD dst_unused:UNUSED_PAD src0_sel:WORD_1
	ds_read_b128 v[70:73], v67
	ds_read_b128 v[74:77], v67 offset:16
	ds_read_b128 v[78:81], v67 offset:32
	ds_read_b128 v[82:85], v67 offset:48
	ds_read_b128 v[86:89], v67 offset:64
	ds_read_b128 v[90:93], v67 offset:80
	ds_read_b128 v[94:97], v67 offset:96
	ds_read_b128 v[98:101], v67 offset:112
	ds_read_b128 v[102:105], v67 offset:128
	ds_read_b128 v[106:109], v67 offset:144
	ds_read_b128 v[110:113], v67 offset:160
	ds_read_b128 v[114:117], v67 offset:176
	ds_read_b128 v[118:121], v67 offset:192
	ds_read_b128 v[122:125], v67 offset:208
	ds_read_b128 v[126:129], v67 offset:224
	ds_read_b128 v[130:133], v67 offset:240
	v_lshlrev_b32_e32 v68, 1, v0
	s_waitcnt vmcnt(11)
	v_cvt_f32_f16_e32 v150, v62
	s_waitcnt vmcnt(10)
	v_cvt_f32_f16_e32 v69, v54
	v_pk_mul_f32 v[154:155], v[150:151], v[14:15] op_sel_hi:[0,1]
	v_exp_f32_e32 v154, v154
	v_exp_f32_e32 v155, v155
	v_pk_mul_f32 v[156:157], v[150:151], v[16:17] op_sel_hi:[0,1]
	v_exp_f32_e32 v156, v156
	v_exp_f32_e32 v157, v157
	v_mul_f32_e32 v152, v150, v69
	v_pk_mul_f32 v[134:135], v[154:155], v[134:135]
	s_waitcnt lgkmcnt(14)
	v_pk_fma_f32 v[134:135], v[152:153], v[70:71], v[134:135] op_sel_hi:[0,1,1]
	s_waitcnt lgkmcnt(11)
	v_pk_fma_f32 v[70:71], v[86:87], v[134:135], 0 op_sel_hi:[1,1,0]
	v_pk_mul_f32 v[86:87], v[156:157], v[136:137]
	s_nop 0
	v_pk_fma_f32 v[136:137], v[152:153], v[72:73], v[86:87] op_sel_hi:[0,1,1]
	v_pk_mul_f32 v[72:73], v[150:151], v[10:11] op_sel_hi:[0,1]
	v_exp_f32_e32 v72, v72
	v_exp_f32_e32 v73, v73
	v_pk_mul_f32 v[86:87], v[150:151], v[12:13] op_sel_hi:[0,1]
	v_exp_f32_e32 v86, v86
	v_exp_f32_e32 v87, v87
	v_pk_mul_f32 v[72:73], v[72:73], v[138:139]
	v_pk_fma_f32 v[70:71], v[88:89], v[136:137], v[70:71]
	v_pk_fma_f32 v[138:139], v[152:153], v[74:75], v[72:73] op_sel_hi:[0,1,1]
	v_pk_mul_f32 v[72:73], v[86:87], v[140:141]
	v_pk_mul_f32 v[74:75], v[150:151], v[8:9] op_sel_hi:[0,1]
	v_pk_fma_f32 v[140:141], v[152:153], v[76:77], v[72:73] op_sel_hi:[0,1,1]
	v_pk_mul_f32 v[72:73], v[150:151], v[6:7] op_sel_hi:[0,1]
	v_exp_f32_e32 v72, v72
	v_exp_f32_e32 v73, v73
	v_exp_f32_e32 v74, v74
	v_exp_f32_e32 v75, v75
	s_waitcnt lgkmcnt(10)
	v_pk_fma_f32 v[70:71], v[90:91], v[138:139], v[70:71]
	v_pk_mul_f32 v[72:73], v[72:73], v[142:143]
	v_pk_fma_f32 v[70:71], v[92:93], v[140:141], v[70:71]
	v_pk_fma_f32 v[142:143], v[152:153], v[78:79], v[72:73] op_sel_hi:[0,1,1]
	v_pk_mul_f32 v[72:73], v[74:75], v[144:145]
	v_pk_mul_f32 v[74:75], v[150:151], v[4:5] op_sel_hi:[0,1]
	v_pk_fma_f32 v[144:145], v[152:153], v[80:81], v[72:73] op_sel_hi:[0,1,1]
	v_pk_mul_f32 v[72:73], v[150:151], v[2:3] op_sel_hi:[0,1]
	v_exp_f32_e32 v72, v72
	v_exp_f32_e32 v73, v73
	v_exp_f32_e32 v74, v74
	v_exp_f32_e32 v75, v75
	s_waitcnt lgkmcnt(9)
	v_pk_fma_f32 v[70:71], v[94:95], v[142:143], v[70:71]
	v_pk_mul_f32 v[72:73], v[72:73], v[146:147]
	v_pk_fma_f32 v[70:71], v[96:97], v[144:145], v[70:71]
	v_pk_fma_f32 v[146:147], v[152:153], v[82:83], v[72:73] op_sel_hi:[0,1,1]
	v_pk_mul_f32 v[72:73], v[74:75], v[148:149]
	s_waitcnt lgkmcnt(8)
	v_pk_fma_f32 v[70:71], v[98:99], v[146:147], v[70:71]
	v_pk_fma_f32 v[148:149], v[152:153], v[84:85], v[72:73] op_sel_hi:[0,1,1]
	v_pk_fma_f32 v[70:71], v[100:101], v[148:149], v[70:71]
	s_nop 0
	v_add_f32_e32 v69, v70, v71
	v_fma_mix_f32 v69, v1, v54, v69 op_sel_hi:[0,1,0]
	s_waitcnt vmcnt(9)
	v_fma_mixlo_f16 v69, v69, v58, 0 op_sel_hi:[0,1,0]
	ds_write_b16 v68, v69 offset:4096
	ds_read_b128 v[70:73], v67 offset:256
	ds_read_b128 v[74:77], v67 offset:272
	ds_read_b128 v[78:81], v67 offset:288
	ds_read_b128 v[82:85], v67 offset:304
	ds_read_b128 v[86:89], v67 offset:320
	ds_read_b128 v[90:93], v67 offset:336
	ds_read_b128 v[94:97], v67 offset:352
	ds_read_b128 v[98:101], v67 offset:368
	v_cvt_f32_f16_sdwa v62, v62 dst_sel:DWORD dst_unused:UNUSED_PAD src0_sel:WORD_1
	v_cvt_f32_f16_sdwa v69, v54 dst_sel:DWORD dst_unused:UNUSED_PAD src0_sel:WORD_1
	v_pk_mul_f32 v[152:153], v[62:63], v[14:15] op_sel_hi:[0,1]
	v_exp_f32_e32 v152, v152
	v_exp_f32_e32 v153, v153
	v_pk_mul_f32 v[154:155], v[62:63], v[16:17] op_sel_hi:[0,1]
	v_exp_f32_e32 v154, v154
	v_exp_f32_e32 v155, v155
	v_mul_f32_e32 v150, v62, v69
	v_pk_mul_f32 v[134:135], v[152:153], v[134:135]
	s_waitcnt lgkmcnt(14)
	v_pk_fma_f32 v[134:135], v[150:151], v[102:103], v[134:135] op_sel_hi:[0,1,1]
	s_waitcnt lgkmcnt(12)
	v_pk_fma_f32 v[102:103], v[118:119], v[134:135], 0 op_sel_hi:[1,1,0]
	v_pk_mul_f32 v[118:119], v[154:155], v[136:137]
	s_nop 0
	v_pk_fma_f32 v[136:137], v[150:151], v[104:105], v[118:119] op_sel_hi:[0,1,1]
	v_pk_mul_f32 v[104:105], v[62:63], v[10:11] op_sel_hi:[0,1]
	v_exp_f32_e32 v104, v104
	v_exp_f32_e32 v105, v105
	v_pk_mul_f32 v[118:119], v[62:63], v[12:13] op_sel_hi:[0,1]
	v_exp_f32_e32 v118, v118
	v_exp_f32_e32 v119, v119
	v_pk_mul_f32 v[104:105], v[104:105], v[138:139]
	v_pk_fma_f32 v[102:103], v[120:121], v[136:137], v[102:103]
	v_pk_fma_f32 v[138:139], v[150:151], v[106:107], v[104:105] op_sel_hi:[0,1,1]
	v_pk_mul_f32 v[104:105], v[118:119], v[140:141]
	v_pk_mul_f32 v[106:107], v[62:63], v[8:9] op_sel_hi:[0,1]
	v_pk_fma_f32 v[140:141], v[150:151], v[108:109], v[104:105] op_sel_hi:[0,1,1]
	v_pk_mul_f32 v[104:105], v[62:63], v[6:7] op_sel_hi:[0,1]
	v_exp_f32_e32 v104, v104
	v_exp_f32_e32 v105, v105
	v_exp_f32_e32 v106, v106
	v_exp_f32_e32 v107, v107
	s_waitcnt lgkmcnt(11)
	v_pk_fma_f32 v[102:103], v[122:123], v[138:139], v[102:103]
	v_pk_mul_f32 v[104:105], v[104:105], v[142:143]
	v_pk_fma_f32 v[102:103], v[124:125], v[140:141], v[102:103]
	v_pk_fma_f32 v[142:143], v[150:151], v[110:111], v[104:105] op_sel_hi:[0,1,1]
	v_pk_mul_f32 v[104:105], v[106:107], v[144:145]
	v_pk_mul_f32 v[106:107], v[62:63], v[4:5] op_sel_hi:[0,1]
	v_pk_fma_f32 v[144:145], v[150:151], v[112:113], v[104:105] op_sel_hi:[0,1,1]
	v_pk_mul_f32 v[104:105], v[62:63], v[2:3] op_sel_hi:[0,1]
	v_exp_f32_e32 v104, v104
	v_exp_f32_e32 v105, v105
	v_exp_f32_e32 v106, v106
	v_exp_f32_e32 v107, v107
	s_waitcnt lgkmcnt(10)
	v_pk_fma_f32 v[102:103], v[126:127], v[142:143], v[102:103]
	v_pk_mul_f32 v[104:105], v[104:105], v[146:147]
	v_pk_fma_f32 v[102:103], v[128:129], v[144:145], v[102:103]
	v_pk_fma_f32 v[146:147], v[150:151], v[114:115], v[104:105] op_sel_hi:[0,1,1]
	v_pk_mul_f32 v[104:105], v[106:107], v[148:149]
	s_waitcnt lgkmcnt(9)
	v_pk_fma_f32 v[102:103], v[130:131], v[146:147], v[102:103]
	v_pk_fma_f32 v[148:149], v[150:151], v[116:117], v[104:105] op_sel_hi:[0,1,1]
	v_pk_fma_f32 v[102:103], v[132:133], v[148:149], v[102:103]
	s_nop 0
	v_add_f32_e32 v62, v102, v103
	v_fma_mix_f32 v54, v1, v54, v62 op_sel:[0,1,0] op_sel_hi:[0,1,0]
	v_fma_mixlo_f16 v54, v54, v58, 0 op_sel:[0,1,0] op_sel_hi:[0,1,0]
	ds_write_b16 v68, v54 offset:5136
	ds_read_b128 v[102:105], v67 offset:384
	ds_read_b128 v[106:109], v67 offset:400
	ds_read_b128 v[110:113], v67 offset:416
	ds_read_b128 v[114:117], v67 offset:432
	ds_read_b128 v[118:121], v67 offset:448
	ds_read_b128 v[122:125], v67 offset:464
	ds_read_b128 v[126:129], v67 offset:480
	ds_read_b128 v[130:133], v67 offset:496
	v_cvt_f32_f16_e32 v54, v63
	v_cvt_f32_f16_e32 v58, v55
	v_pk_mul_f32 v[150:151], v[54:55], v[14:15] op_sel_hi:[0,1]
	v_exp_f32_e32 v150, v150
	v_exp_f32_e32 v151, v151
	v_pk_mul_f32 v[152:153], v[54:55], v[16:17] op_sel_hi:[0,1]
	v_exp_f32_e32 v152, v152
	v_exp_f32_e32 v153, v153
	v_mul_f32_e32 v58, v54, v58
	v_pk_mul_f32 v[134:135], v[150:151], v[134:135]
	s_waitcnt lgkmcnt(14)
	v_pk_fma_f32 v[134:135], v[58:59], v[70:71], v[134:135] op_sel_hi:[0,1,1]
	s_waitcnt lgkmcnt(12)
	v_pk_fma_f32 v[70:71], v[86:87], v[134:135], 0 op_sel_hi:[1,1,0]
	v_pk_mul_f32 v[86:87], v[152:153], v[136:137]
	s_nop 0
	v_pk_fma_f32 v[136:137], v[58:59], v[72:73], v[86:87] op_sel_hi:[0,1,1]
	v_pk_mul_f32 v[72:73], v[54:55], v[10:11] op_sel_hi:[0,1]
	v_exp_f32_e32 v72, v72
	v_exp_f32_e32 v73, v73
	v_pk_mul_f32 v[86:87], v[54:55], v[12:13] op_sel_hi:[0,1]
	v_exp_f32_e32 v86, v86
	v_exp_f32_e32 v87, v87
	v_pk_mul_f32 v[72:73], v[72:73], v[138:139]
	v_pk_fma_f32 v[70:71], v[88:89], v[136:137], v[70:71]
	v_pk_fma_f32 v[138:139], v[58:59], v[74:75], v[72:73] op_sel_hi:[0,1,1]
	v_pk_mul_f32 v[72:73], v[86:87], v[140:141]
	v_pk_mul_f32 v[74:75], v[54:55], v[8:9] op_sel_hi:[0,1]
	v_pk_fma_f32 v[140:141], v[58:59], v[76:77], v[72:73] op_sel_hi:[0,1,1]
	v_pk_mul_f32 v[72:73], v[54:55], v[6:7] op_sel_hi:[0,1]
	v_exp_f32_e32 v72, v72
	v_exp_f32_e32 v73, v73
	v_exp_f32_e32 v74, v74
	v_exp_f32_e32 v75, v75
	s_waitcnt lgkmcnt(11)
	v_pk_fma_f32 v[70:71], v[90:91], v[138:139], v[70:71]
	v_pk_mul_f32 v[72:73], v[72:73], v[142:143]
	v_pk_fma_f32 v[70:71], v[92:93], v[140:141], v[70:71]
	v_pk_fma_f32 v[142:143], v[58:59], v[78:79], v[72:73] op_sel_hi:[0,1,1]
	v_pk_mul_f32 v[72:73], v[74:75], v[144:145]
	v_pk_mul_f32 v[74:75], v[54:55], v[4:5] op_sel_hi:[0,1]
	v_pk_fma_f32 v[144:145], v[58:59], v[80:81], v[72:73] op_sel_hi:[0,1,1]
	v_pk_mul_f32 v[72:73], v[54:55], v[2:3] op_sel_hi:[0,1]
	v_exp_f32_e32 v72, v72
	v_exp_f32_e32 v73, v73
	v_exp_f32_e32 v74, v74
	v_exp_f32_e32 v75, v75
	s_waitcnt lgkmcnt(10)
	v_pk_fma_f32 v[70:71], v[94:95], v[142:143], v[70:71]
	v_pk_mul_f32 v[72:73], v[72:73], v[146:147]
	v_pk_fma_f32 v[70:71], v[96:97], v[144:145], v[70:71]
	v_pk_fma_f32 v[146:147], v[58:59], v[82:83], v[72:73] op_sel_hi:[0,1,1]
	v_pk_mul_f32 v[72:73], v[74:75], v[148:149]
	s_waitcnt lgkmcnt(9)
	v_pk_fma_f32 v[70:71], v[98:99], v[146:147], v[70:71]
	v_pk_fma_f32 v[148:149], v[58:59], v[84:85], v[72:73] op_sel_hi:[0,1,1]
	v_pk_fma_f32 v[70:71], v[100:101], v[148:149], v[70:71]
	s_nop 0
	v_add_f32_e32 v54, v70, v71
	v_fma_mix_f32 v54, v1, v55, v54 op_sel_hi:[0,1,0]
	v_fma_mixlo_f16 v54, v54, v59, 0 op_sel_hi:[0,1,0]
	ds_write_b16 v68, v54 offset:6176
	ds_read_b128 v[70:73], v67 offset:512
	ds_read_b128 v[74:77], v67 offset:528
	ds_read_b128 v[78:81], v67 offset:544
	ds_read_b128 v[82:85], v67 offset:560
	ds_read_b128 v[86:89], v67 offset:576
	ds_read_b128 v[90:93], v67 offset:592
	ds_read_b128 v[94:97], v67 offset:608
	ds_read_b128 v[98:101], v67 offset:624
	v_cvt_f32_f16_sdwa v54, v63 dst_sel:DWORD dst_unused:UNUSED_PAD src0_sel:WORD_1
	v_cvt_f32_f16_sdwa v58, v55 dst_sel:DWORD dst_unused:UNUSED_PAD src0_sel:WORD_1
	v_pk_mul_f32 v[62:63], v[54:55], v[14:15] op_sel_hi:[0,1]
	v_exp_f32_e32 v62, v62
	v_exp_f32_e32 v63, v63
	v_pk_mul_f32 v[150:151], v[54:55], v[16:17] op_sel_hi:[0,1]
	v_exp_f32_e32 v150, v150
	v_exp_f32_e32 v151, v151
	v_mul_f32_e32 v58, v54, v58
	v_pk_mul_f32 v[62:63], v[62:63], v[134:135]
	s_waitcnt lgkmcnt(14)
	v_pk_fma_f32 v[62:63], v[58:59], v[102:103], v[62:63] op_sel_hi:[0,1,1]
	s_waitcnt lgkmcnt(12)
	v_pk_fma_f32 v[102:103], v[118:119], v[62:63], 0 op_sel_hi:[1,1,0]
	v_pk_mul_f32 v[118:119], v[150:151], v[136:137]
	s_nop 0
	v_pk_fma_f32 v[134:135], v[58:59], v[104:105], v[118:119] op_sel_hi:[0,1,1]
	v_pk_mul_f32 v[104:105], v[54:55], v[10:11] op_sel_hi:[0,1]
	v_exp_f32_e32 v104, v104
	v_exp_f32_e32 v105, v105
	v_pk_mul_f32 v[118:119], v[54:55], v[12:13] op_sel_hi:[0,1]
	v_exp_f32_e32 v118, v118
	v_exp_f32_e32 v119, v119
	v_pk_mul_f32 v[104:105], v[104:105], v[138:139]
	v_pk_fma_f32 v[102:103], v[120:121], v[134:135], v[102:103]
	v_pk_fma_f32 v[136:137], v[58:59], v[106:107], v[104:105] op_sel_hi:[0,1,1]
	v_pk_mul_f32 v[104:105], v[118:119], v[140:141]
	v_pk_mul_f32 v[106:107], v[54:55], v[8:9] op_sel_hi:[0,1]
	v_pk_fma_f32 v[138:139], v[58:59], v[108:109], v[104:105] op_sel_hi:[0,1,1]
	v_pk_mul_f32 v[104:105], v[54:55], v[6:7] op_sel_hi:[0,1]
	v_exp_f32_e32 v104, v104
	v_exp_f32_e32 v105, v105
	v_exp_f32_e32 v106, v106
	v_exp_f32_e32 v107, v107
	s_waitcnt lgkmcnt(11)
	v_pk_fma_f32 v[102:103], v[122:123], v[136:137], v[102:103]
	v_pk_mul_f32 v[104:105], v[104:105], v[142:143]
	v_pk_fma_f32 v[102:103], v[124:125], v[138:139], v[102:103]
	v_pk_fma_f32 v[140:141], v[58:59], v[110:111], v[104:105] op_sel_hi:[0,1,1]
	v_pk_mul_f32 v[104:105], v[106:107], v[144:145]
	v_pk_mul_f32 v[106:107], v[54:55], v[4:5] op_sel_hi:[0,1]
	v_pk_fma_f32 v[142:143], v[58:59], v[112:113], v[104:105] op_sel_hi:[0,1,1]
	v_pk_mul_f32 v[104:105], v[54:55], v[2:3] op_sel_hi:[0,1]
	v_exp_f32_e32 v104, v104
	v_exp_f32_e32 v105, v105
	v_exp_f32_e32 v106, v106
	v_exp_f32_e32 v107, v107
	s_waitcnt lgkmcnt(10)
	v_pk_fma_f32 v[102:103], v[126:127], v[140:141], v[102:103]
	v_pk_mul_f32 v[104:105], v[104:105], v[146:147]
	v_pk_fma_f32 v[102:103], v[128:129], v[142:143], v[102:103]
	v_pk_fma_f32 v[144:145], v[58:59], v[114:115], v[104:105] op_sel_hi:[0,1,1]
	v_pk_mul_f32 v[104:105], v[106:107], v[148:149]
	s_waitcnt lgkmcnt(9)
	v_pk_fma_f32 v[102:103], v[130:131], v[144:145], v[102:103]
	v_pk_fma_f32 v[146:147], v[58:59], v[116:117], v[104:105] op_sel_hi:[0,1,1]
	v_pk_fma_f32 v[102:103], v[132:133], v[146:147], v[102:103]
	s_nop 0
	v_add_f32_e32 v54, v102, v103
	v_fma_mix_f32 v54, v1, v55, v54 op_sel:[0,1,0] op_sel_hi:[0,1,0]
	v_fma_mixlo_f16 v54, v54, v59, 0 op_sel:[0,1,0] op_sel_hi:[0,1,0]
	ds_write_b16 v68, v54 offset:7216
	ds_read_b128 v[102:105], v67 offset:640
	ds_read_b128 v[106:109], v67 offset:656
	ds_read_b128 v[110:113], v67 offset:672
	ds_read_b128 v[114:117], v67 offset:688
	ds_read_b128 v[118:121], v67 offset:704
	ds_read_b128 v[122:125], v67 offset:720
	ds_read_b128 v[126:129], v67 offset:736
	ds_read_b128 v[130:133], v67 offset:752
	v_cvt_f32_f16_e32 v54, v64
	v_cvt_f32_f16_e32 v55, v56
	v_pk_mul_f32 v[148:149], v[54:55], v[14:15] op_sel_hi:[0,1]
	v_exp_f32_e32 v148, v148
	v_exp_f32_e32 v149, v149
	v_pk_mul_f32 v[150:151], v[54:55], v[16:17] op_sel_hi:[0,1]
	v_exp_f32_e32 v150, v150
	v_exp_f32_e32 v151, v151
	v_mul_f32_e32 v58, v54, v55
	v_pk_mul_f32 v[62:63], v[148:149], v[62:63]
	s_waitcnt lgkmcnt(14)
	v_pk_fma_f32 v[62:63], v[58:59], v[70:71], v[62:63] op_sel_hi:[0,1,1]
	s_waitcnt lgkmcnt(12)
	v_pk_fma_f32 v[70:71], v[86:87], v[62:63], 0 op_sel_hi:[1,1,0]
	v_pk_mul_f32 v[86:87], v[150:151], v[134:135]
	s_nop 0
	v_pk_fma_f32 v[134:135], v[58:59], v[72:73], v[86:87] op_sel_hi:[0,1,1]
	v_pk_mul_f32 v[72:73], v[54:55], v[10:11] op_sel_hi:[0,1]
	v_exp_f32_e32 v72, v72
	v_exp_f32_e32 v73, v73
	v_pk_mul_f32 v[86:87], v[54:55], v[12:13] op_sel_hi:[0,1]
	v_exp_f32_e32 v86, v86
	v_exp_f32_e32 v87, v87
	v_pk_mul_f32 v[72:73], v[72:73], v[136:137]
	v_pk_fma_f32 v[70:71], v[88:89], v[134:135], v[70:71]
	v_pk_fma_f32 v[136:137], v[58:59], v[74:75], v[72:73] op_sel_hi:[0,1,1]
	v_pk_mul_f32 v[72:73], v[86:87], v[138:139]
	v_pk_mul_f32 v[74:75], v[54:55], v[8:9] op_sel_hi:[0,1]
	v_pk_fma_f32 v[138:139], v[58:59], v[76:77], v[72:73] op_sel_hi:[0,1,1]
	v_pk_mul_f32 v[72:73], v[54:55], v[6:7] op_sel_hi:[0,1]
	v_exp_f32_e32 v72, v72
	v_exp_f32_e32 v73, v73
	v_exp_f32_e32 v74, v74
	v_exp_f32_e32 v75, v75
	s_waitcnt lgkmcnt(11)
	v_pk_fma_f32 v[70:71], v[90:91], v[136:137], v[70:71]
	v_pk_mul_f32 v[72:73], v[72:73], v[140:141]
	v_pk_fma_f32 v[70:71], v[92:93], v[138:139], v[70:71]
	v_pk_fma_f32 v[140:141], v[58:59], v[78:79], v[72:73] op_sel_hi:[0,1,1]
	v_pk_mul_f32 v[72:73], v[74:75], v[142:143]
	s_waitcnt lgkmcnt(10)
	v_pk_fma_f32 v[70:71], v[94:95], v[140:141], v[70:71]
	v_pk_fma_f32 v[142:143], v[58:59], v[80:81], v[72:73] op_sel_hi:[0,1,1]
	v_pk_mul_f32 v[72:73], v[54:55], v[2:3] op_sel_hi:[0,1]
	v_exp_f32_e32 v72, v72
	v_exp_f32_e32 v73, v73
	v_pk_mul_f32 v[54:55], v[54:55], v[4:5] op_sel_hi:[0,1]
	v_exp_f32_e32 v54, v54
	v_exp_f32_e32 v55, v55
	v_pk_mul_f32 v[72:73], v[72:73], v[144:145]
	v_pk_fma_f32 v[70:71], v[96:97], v[142:143], v[70:71]
	v_pk_fma_f32 v[144:145], v[58:59], v[82:83], v[72:73] op_sel_hi:[0,1,1]
	v_pk_mul_f32 v[54:55], v[54:55], v[146:147]
	s_waitcnt lgkmcnt(9)
	v_pk_fma_f32 v[70:71], v[98:99], v[144:145], v[70:71]
	v_pk_fma_f32 v[54:55], v[58:59], v[84:85], v[54:55] op_sel_hi:[0,1,1]
	v_pk_fma_f32 v[58:59], v[100:101], v[54:55], v[70:71]
	s_nop 0
	v_add_f32_e32 v58, v58, v59
	v_fma_mix_f32 v58, v1, v56, v58 op_sel_hi:[0,1,0]
	v_fma_mixlo_f16 v58, v58, v60, 0 op_sel_hi:[0,1,0]
	ds_write_b16 v68, v58 offset:8256
	ds_read_b128 v[70:73], v67 offset:768
	ds_read_b128 v[74:77], v67 offset:784
	ds_read_b128 v[78:81], v67 offset:800
	ds_read_b128 v[82:85], v67 offset:816
	ds_read_b128 v[86:89], v67 offset:832
	ds_read_b128 v[90:93], v67 offset:848
	ds_read_b128 v[94:97], v67 offset:864
	ds_read_b128 v[98:101], v67 offset:880
	v_cvt_f32_f16_sdwa v58, v64 dst_sel:DWORD dst_unused:UNUSED_PAD src0_sel:WORD_1
	v_cvt_f32_f16_sdwa v59, v56 dst_sel:DWORD dst_unused:UNUSED_PAD src0_sel:WORD_1
	v_pk_mul_f32 v[146:147], v[58:59], v[14:15] op_sel_hi:[0,1]
	v_exp_f32_e32 v146, v146
	v_exp_f32_e32 v147, v147
	v_pk_mul_f32 v[148:149], v[58:59], v[16:17] op_sel_hi:[0,1]
	v_exp_f32_e32 v148, v148
	v_exp_f32_e32 v149, v149
	v_mul_f32_e32 v64, v58, v59
	v_pk_mul_f32 v[62:63], v[146:147], v[62:63]
	s_waitcnt lgkmcnt(14)
	v_pk_fma_f32 v[62:63], v[64:65], v[102:103], v[62:63] op_sel_hi:[0,1,1]
	s_waitcnt lgkmcnt(12)
	v_pk_fma_f32 v[102:103], v[118:119], v[62:63], 0 op_sel_hi:[1,1,0]
	v_pk_mul_f32 v[118:119], v[148:149], v[134:135]
	s_nop 0
	v_pk_fma_f32 v[134:135], v[64:65], v[104:105], v[118:119] op_sel_hi:[0,1,1]
	v_pk_mul_f32 v[104:105], v[58:59], v[10:11] op_sel_hi:[0,1]
	v_exp_f32_e32 v104, v104
	v_exp_f32_e32 v105, v105
	v_pk_mul_f32 v[118:119], v[58:59], v[12:13] op_sel_hi:[0,1]
	v_exp_f32_e32 v118, v118
	v_exp_f32_e32 v119, v119
	v_pk_mul_f32 v[104:105], v[104:105], v[136:137]
	v_pk_fma_f32 v[102:103], v[120:121], v[134:135], v[102:103]
	v_pk_fma_f32 v[136:137], v[64:65], v[106:107], v[104:105] op_sel_hi:[0,1,1]
	v_pk_mul_f32 v[104:105], v[118:119], v[138:139]
	v_pk_mul_f32 v[106:107], v[58:59], v[8:9] op_sel_hi:[0,1]
	v_pk_fma_f32 v[138:139], v[64:65], v[108:109], v[104:105] op_sel_hi:[0,1,1]
	v_pk_mul_f32 v[104:105], v[58:59], v[6:7] op_sel_hi:[0,1]
	v_exp_f32_e32 v104, v104
	v_exp_f32_e32 v105, v105
	v_exp_f32_e32 v106, v106
	v_exp_f32_e32 v107, v107
	s_waitcnt lgkmcnt(11)
	v_pk_fma_f32 v[102:103], v[122:123], v[136:137], v[102:103]
	v_pk_mul_f32 v[104:105], v[104:105], v[140:141]
	v_pk_fma_f32 v[102:103], v[124:125], v[138:139], v[102:103]
	v_pk_fma_f32 v[140:141], v[64:65], v[110:111], v[104:105] op_sel_hi:[0,1,1]
	v_pk_mul_f32 v[104:105], v[106:107], v[142:143]
	s_waitcnt lgkmcnt(10)
	v_pk_fma_f32 v[102:103], v[126:127], v[140:141], v[102:103]
	v_pk_fma_f32 v[142:143], v[64:65], v[112:113], v[104:105] op_sel_hi:[0,1,1]
	v_pk_mul_f32 v[104:105], v[58:59], v[2:3] op_sel_hi:[0,1]
	v_exp_f32_e32 v104, v104
	v_exp_f32_e32 v105, v105
	v_pk_mul_f32 v[58:59], v[58:59], v[4:5] op_sel_hi:[0,1]
	v_exp_f32_e32 v58, v58
	v_exp_f32_e32 v59, v59
	v_pk_mul_f32 v[104:105], v[104:105], v[144:145]
	v_pk_fma_f32 v[102:103], v[128:129], v[142:143], v[102:103]
	v_pk_fma_f32 v[144:145], v[64:65], v[114:115], v[104:105] op_sel_hi:[0,1,1]
	v_pk_mul_f32 v[54:55], v[58:59], v[54:55]
	s_waitcnt lgkmcnt(9)
	v_pk_fma_f32 v[102:103], v[130:131], v[144:145], v[102:103]
	v_pk_fma_f32 v[54:55], v[64:65], v[116:117], v[54:55] op_sel_hi:[0,1,1]
	v_pk_fma_f32 v[58:59], v[132:133], v[54:55], v[102:103]
	s_nop 0
	v_add_f32_e32 v58, v58, v59
	v_fma_mix_f32 v56, v1, v56, v58 op_sel:[0,1,0] op_sel_hi:[0,1,0]
	v_fma_mixlo_f16 v56, v56, v60, 0 op_sel:[0,1,0] op_sel_hi:[0,1,0]
	ds_write_b16 v68, v56 offset:9296
	ds_read_b128 v[102:105], v67 offset:896
	ds_read_b128 v[106:109], v67 offset:912
	ds_read_b128 v[110:113], v67 offset:928
	ds_read_b128 v[114:117], v67 offset:944
	ds_read_b128 v[118:121], v67 offset:960
	ds_read_b128 v[122:125], v67 offset:976
	ds_read_b128 v[126:129], v67 offset:992
	ds_read_b128 v[130:133], v67 offset:1008
	v_cvt_f32_f16_e32 v56, v65
	v_cvt_f32_f16_e32 v58, v57
	v_pk_mul_f32 v[146:147], v[56:57], v[14:15] op_sel_hi:[0,1]
	v_exp_f32_e32 v146, v146
	v_exp_f32_e32 v147, v147
	v_pk_mul_f32 v[148:149], v[56:57], v[16:17] op_sel_hi:[0,1]
	v_exp_f32_e32 v148, v148
	v_exp_f32_e32 v149, v149
	v_mul_f32_e32 v58, v56, v58
	v_pk_mul_f32 v[62:63], v[146:147], v[62:63]
	s_waitcnt lgkmcnt(14)
	v_pk_fma_f32 v[62:63], v[58:59], v[70:71], v[62:63] op_sel_hi:[0,1,1]
	s_waitcnt lgkmcnt(12)
	v_pk_fma_f32 v[70:71], v[86:87], v[62:63], 0 op_sel_hi:[1,1,0]
	v_pk_mul_f32 v[86:87], v[148:149], v[134:135]
	s_nop 0
	v_pk_fma_f32 v[134:135], v[58:59], v[72:73], v[86:87] op_sel_hi:[0,1,1]
	v_pk_mul_f32 v[72:73], v[56:57], v[10:11] op_sel_hi:[0,1]
	v_exp_f32_e32 v72, v72
	v_exp_f32_e32 v73, v73
	v_pk_mul_f32 v[86:87], v[56:57], v[12:13] op_sel_hi:[0,1]
	v_exp_f32_e32 v86, v86
	v_exp_f32_e32 v87, v87
	v_pk_mul_f32 v[72:73], v[72:73], v[136:137]
	v_pk_fma_f32 v[70:71], v[88:89], v[134:135], v[70:71]
	v_pk_fma_f32 v[136:137], v[58:59], v[74:75], v[72:73] op_sel_hi:[0,1,1]
	v_pk_mul_f32 v[72:73], v[86:87], v[138:139]
	v_pk_mul_f32 v[74:75], v[56:57], v[8:9] op_sel_hi:[0,1]
	v_pk_fma_f32 v[138:139], v[58:59], v[76:77], v[72:73] op_sel_hi:[0,1,1]
	v_pk_mul_f32 v[72:73], v[56:57], v[6:7] op_sel_hi:[0,1]
	v_exp_f32_e32 v72, v72
	v_exp_f32_e32 v73, v73
	v_exp_f32_e32 v74, v74
	v_exp_f32_e32 v75, v75
	s_waitcnt lgkmcnt(11)
	v_pk_fma_f32 v[70:71], v[90:91], v[136:137], v[70:71]
	v_pk_mul_f32 v[72:73], v[72:73], v[140:141]
	v_pk_fma_f32 v[70:71], v[92:93], v[138:139], v[70:71]
	v_pk_fma_f32 v[140:141], v[58:59], v[78:79], v[72:73] op_sel_hi:[0,1,1]
	v_pk_mul_f32 v[72:73], v[74:75], v[142:143]
	v_pk_mul_f32 v[74:75], v[56:57], v[4:5] op_sel_hi:[0,1]
	v_pk_fma_f32 v[142:143], v[58:59], v[80:81], v[72:73] op_sel_hi:[0,1,1]
	v_pk_mul_f32 v[72:73], v[56:57], v[2:3] op_sel_hi:[0,1]
	v_exp_f32_e32 v72, v72
	v_exp_f32_e32 v73, v73
	v_exp_f32_e32 v74, v74
	v_exp_f32_e32 v75, v75
	s_waitcnt lgkmcnt(10)
	v_pk_fma_f32 v[70:71], v[94:95], v[140:141], v[70:71]
	v_pk_mul_f32 v[72:73], v[72:73], v[144:145]
	v_pk_fma_f32 v[70:71], v[96:97], v[142:143], v[70:71]
	v_pk_fma_f32 v[144:145], v[58:59], v[82:83], v[72:73] op_sel_hi:[0,1,1]
	v_pk_mul_f32 v[54:55], v[74:75], v[54:55]
	s_waitcnt lgkmcnt(9)
	v_pk_fma_f32 v[70:71], v[98:99], v[144:145], v[70:71]
	v_pk_fma_f32 v[54:55], v[58:59], v[84:85], v[54:55] op_sel_hi:[0,1,1]
	v_pk_fma_f32 v[58:59], v[100:101], v[54:55], v[70:71]
	s_nop 0
	v_add_f32_e32 v56, v58, v59
	v_fma_mix_f32 v56, v1, v57, v56 op_sel_hi:[0,1,0]
	v_fma_mixlo_f16 v56, v56, v61, 0 op_sel_hi:[0,1,0]
	ds_write_b16 v68, v56 offset:10336
	ds_read_b128 v[70:73], v67 offset:1024
	ds_read_b128 v[74:77], v67 offset:1040
	ds_read_b128 v[78:81], v67 offset:1056
	ds_read_b128 v[82:85], v67 offset:1072
	ds_read_b128 v[86:89], v67 offset:1088
	ds_read_b128 v[90:93], v67 offset:1104
	ds_read_b128 v[94:97], v67 offset:1120
	ds_read_b128 v[98:101], v67 offset:1136
	v_cvt_f32_f16_sdwa v56, v65 dst_sel:DWORD dst_unused:UNUSED_PAD src0_sel:WORD_1
	v_cvt_f32_f16_sdwa v58, v57 dst_sel:DWORD dst_unused:UNUSED_PAD src0_sel:WORD_1
	v_pk_mul_f32 v[64:65], v[56:57], v[14:15] op_sel_hi:[0,1]
	v_pk_mul_f32 v[146:147], v[56:57], v[16:17] op_sel_hi:[0,1]
	v_exp_f32_e32 v64, v64
	v_exp_f32_e32 v65, v65
	v_exp_f32_e32 v146, v146
	v_exp_f32_e32 v147, v147
	v_mul_f32_e32 v58, v56, v58
	v_pk_mul_f32 v[62:63], v[64:65], v[62:63]
	v_pk_mul_f32 v[64:65], v[146:147], v[134:135]
	s_waitcnt lgkmcnt(14)
	v_pk_fma_f32 v[134:135], v[58:59], v[104:105], v[64:65] op_sel_hi:[0,1,1]
	v_pk_mul_f32 v[64:65], v[56:57], v[10:11] op_sel_hi:[0,1]
	v_pk_fma_f32 v[148:149], v[58:59], v[102:103], v[62:63] op_sel_hi:[0,1,1]
	v_exp_f32_e32 v64, v64
	v_exp_f32_e32 v65, v65
	v_pk_mul_f32 v[102:103], v[56:57], v[12:13] op_sel_hi:[0,1]
	v_exp_f32_e32 v102, v102
	v_exp_f32_e32 v103, v103
	s_waitcnt lgkmcnt(12)
	v_pk_fma_f32 v[62:63], v[118:119], v[148:149], 0 op_sel_hi:[1,1,0]
	v_pk_mul_f32 v[64:65], v[64:65], v[136:137]
	v_pk_fma_f32 v[62:63], v[120:121], v[134:135], v[62:63]
	v_pk_fma_f32 v[136:137], v[58:59], v[106:107], v[64:65] op_sel_hi:[0,1,1]
	v_pk_mul_f32 v[64:65], v[102:103], v[138:139]
	s_waitcnt lgkmcnt(11)
	v_pk_fma_f32 v[62:63], v[122:123], v[136:137], v[62:63]
	v_pk_fma_f32 v[122:123], v[58:59], v[108:109], v[64:65] op_sel_hi:[0,1,1]
	v_pk_mul_f32 v[64:65], v[56:57], v[6:7] op_sel_hi:[0,1]
	v_exp_f32_e32 v64, v64
	v_exp_f32_e32 v65, v65
	v_pk_mul_f32 v[102:103], v[56:57], v[8:9] op_sel_hi:[0,1]
	v_exp_f32_e32 v102, v102
	v_exp_f32_e32 v103, v103
	v_pk_mul_f32 v[64:65], v[64:65], v[140:141]
	v_pk_fma_f32 v[62:63], v[124:125], v[122:123], v[62:63]
	v_pk_fma_f32 v[124:125], v[58:59], v[110:111], v[64:65] op_sel_hi:[0,1,1]
	v_pk_mul_f32 v[64:65], v[102:103], v[142:143]
	s_waitcnt lgkmcnt(10)
	v_pk_fma_f32 v[62:63], v[126:127], v[124:125], v[62:63]
	v_pk_fma_f32 v[126:127], v[58:59], v[112:113], v[64:65] op_sel_hi:[0,1,1]
	v_pk_mul_f32 v[64:65], v[56:57], v[2:3] op_sel_hi:[0,1]
	v_exp_f32_e32 v64, v64
	v_exp_f32_e32 v65, v65
	v_pk_mul_f32 v[102:103], v[56:57], v[4:5] op_sel_hi:[0,1]
	v_exp_f32_e32 v102, v102
	v_exp_f32_e32 v103, v103
	v_pk_mul_f32 v[64:65], v[64:65], v[144:145]
	v_pk_fma_f32 v[62:63], v[128:129], v[126:127], v[62:63]
	v_pk_fma_f32 v[128:129], v[58:59], v[114:115], v[64:65] op_sel_hi:[0,1,1]
	v_pk_mul_f32 v[54:55], v[102:103], v[54:55]
	s_waitcnt lgkmcnt(9)
	v_pk_fma_f32 v[62:63], v[130:131], v[128:129], v[62:63]
	v_pk_fma_f32 v[130:131], v[58:59], v[116:117], v[54:55] op_sel_hi:[0,1,1]
	v_pk_fma_f32 v[54:55], v[132:133], v[130:131], v[62:63]
	s_nop 0
	v_add_f32_e32 v54, v54, v55
	v_fma_mix_f32 v54, v1, v57, v54 op_sel:[0,1,0] op_sel_hi:[0,1,0]
	v_fma_mixlo_f16 v54, v54, v61, 0 op_sel:[0,1,0] op_sel_hi:[0,1,0]
	ds_write_b16 v68, v54 offset:11376
	ds_read_b128 v[54:57], v67 offset:1152
	ds_read_b128 v[58:61], v67 offset:1168
	ds_read_b128 v[62:65], v67 offset:1184
	ds_read_b128 v[102:105], v67 offset:1200
	ds_read_b128 v[106:109], v67 offset:1216
	ds_read_b128 v[110:113], v67 offset:1232
	ds_read_b128 v[114:117], v67 offset:1248
	ds_read_b128 v[118:121], v67 offset:1264
	s_waitcnt vmcnt(8)
	v_cvt_f32_f16_e32 v132, v50
	s_waitcnt vmcnt(7)
	v_cvt_f32_f16_e32 v69, v42
	v_pk_mul_f32 v[140:141], v[132:133], v[14:15] op_sel_hi:[0,1]
	v_exp_f32_e32 v140, v140
	v_exp_f32_e32 v141, v141
	v_pk_mul_f32 v[142:143], v[132:133], v[16:17] op_sel_hi:[0,1]
	v_exp_f32_e32 v142, v142
	v_exp_f32_e32 v143, v143
	v_mul_f32_e32 v138, v132, v69
	v_pk_mul_f32 v[140:141], v[140:141], v[148:149]
	s_waitcnt lgkmcnt(14)
	v_pk_fma_f32 v[140:141], v[138:139], v[70:71], v[140:141] op_sel_hi:[0,1,1]
	s_waitcnt lgkmcnt(12)
	v_pk_fma_f32 v[70:71], v[86:87], v[140:141], 0 op_sel_hi:[1,1,0]
	v_pk_mul_f32 v[86:87], v[142:143], v[134:135]
	s_nop 0
	v_pk_fma_f32 v[134:135], v[138:139], v[72:73], v[86:87] op_sel_hi:[0,1,1]
	v_pk_mul_f32 v[72:73], v[132:133], v[10:11] op_sel_hi:[0,1]
	v_exp_f32_e32 v72, v72
	v_exp_f32_e32 v73, v73
	v_pk_mul_f32 v[86:87], v[132:133], v[12:13] op_sel_hi:[0,1]
	v_exp_f32_e32 v86, v86
	v_exp_f32_e32 v87, v87
	v_pk_mul_f32 v[72:73], v[72:73], v[136:137]
	v_pk_fma_f32 v[70:71], v[88:89], v[134:135], v[70:71]
	v_pk_fma_f32 v[136:137], v[138:139], v[74:75], v[72:73] op_sel_hi:[0,1,1]
	v_pk_mul_f32 v[72:73], v[86:87], v[122:123]
	v_pk_mul_f32 v[74:75], v[132:133], v[8:9] op_sel_hi:[0,1]
	v_pk_fma_f32 v[122:123], v[138:139], v[76:77], v[72:73] op_sel_hi:[0,1,1]
	v_pk_mul_f32 v[72:73], v[132:133], v[6:7] op_sel_hi:[0,1]
	v_exp_f32_e32 v72, v72
	v_exp_f32_e32 v73, v73
	v_exp_f32_e32 v74, v74
	v_exp_f32_e32 v75, v75
	s_waitcnt lgkmcnt(11)
	v_pk_fma_f32 v[70:71], v[90:91], v[136:137], v[70:71]
	v_pk_mul_f32 v[72:73], v[72:73], v[124:125]
	v_pk_fma_f32 v[70:71], v[92:93], v[122:123], v[70:71]
	v_pk_fma_f32 v[124:125], v[138:139], v[78:79], v[72:73] op_sel_hi:[0,1,1]
	v_pk_mul_f32 v[72:73], v[74:75], v[126:127]
	v_pk_mul_f32 v[74:75], v[132:133], v[4:5] op_sel_hi:[0,1]
	v_pk_fma_f32 v[126:127], v[138:139], v[80:81], v[72:73] op_sel_hi:[0,1,1]
	v_pk_mul_f32 v[72:73], v[132:133], v[2:3] op_sel_hi:[0,1]
	v_exp_f32_e32 v72, v72
	v_exp_f32_e32 v73, v73
	v_exp_f32_e32 v74, v74
	v_exp_f32_e32 v75, v75
	s_waitcnt lgkmcnt(10)
	v_pk_fma_f32 v[70:71], v[94:95], v[124:125], v[70:71]
	v_pk_mul_f32 v[72:73], v[72:73], v[128:129]
	v_pk_fma_f32 v[70:71], v[96:97], v[126:127], v[70:71]
	v_pk_fma_f32 v[128:129], v[138:139], v[82:83], v[72:73] op_sel_hi:[0,1,1]
	v_pk_mul_f32 v[72:73], v[74:75], v[130:131]
	s_waitcnt lgkmcnt(9)
	v_pk_fma_f32 v[70:71], v[98:99], v[128:129], v[70:71]
	v_pk_fma_f32 v[130:131], v[138:139], v[84:85], v[72:73] op_sel_hi:[0,1,1]
	v_pk_fma_f32 v[70:71], v[100:101], v[130:131], v[70:71]
	s_nop 0
	v_add_f32_e32 v69, v70, v71
	v_fma_mix_f32 v69, v1, v42, v69 op_sel_hi:[0,1,0]
	s_waitcnt vmcnt(6)
	v_fma_mixlo_f16 v69, v69, v46, 0 op_sel_hi:[0,1,0]
	ds_write_b16 v68, v69 offset:12416
	ds_read_b128 v[70:73], v67 offset:1280
	ds_read_b128 v[74:77], v67 offset:1296
	ds_read_b128 v[78:81], v67 offset:1312
	ds_read_b128 v[82:85], v67 offset:1328
	ds_read_b128 v[86:89], v67 offset:1344
	ds_read_b128 v[90:93], v67 offset:1360
	ds_read_b128 v[94:97], v67 offset:1376
	ds_read_b128 v[98:101], v67 offset:1392
	v_cvt_f32_f16_sdwa v50, v50 dst_sel:DWORD dst_unused:UNUSED_PAD src0_sel:WORD_1
	v_cvt_f32_f16_sdwa v69, v42 dst_sel:DWORD dst_unused:UNUSED_PAD src0_sel:WORD_1
	v_pk_mul_f32 v[138:139], v[50:51], v[14:15] op_sel_hi:[0,1]
	v_exp_f32_e32 v138, v138
	v_exp_f32_e32 v139, v139
	v_pk_mul_f32 v[142:143], v[50:51], v[16:17] op_sel_hi:[0,1]
	v_exp_f32_e32 v142, v142
	v_exp_f32_e32 v143, v143
	v_mul_f32_e32 v132, v50, v69
	v_pk_mul_f32 v[138:139], v[138:139], v[140:141]
	s_waitcnt lgkmcnt(14)
	v_pk_fma_f32 v[138:139], v[132:133], v[54:55], v[138:139] op_sel_hi:[0,1,1]
	s_waitcnt lgkmcnt(12)
	v_pk_fma_f32 v[54:55], v[106:107], v[138:139], 0 op_sel_hi:[1,1,0]
	v_pk_mul_f32 v[106:107], v[142:143], v[134:135]
	s_nop 0
	v_pk_fma_f32 v[134:135], v[132:133], v[56:57], v[106:107] op_sel_hi:[0,1,1]
	v_pk_mul_f32 v[56:57], v[50:51], v[10:11] op_sel_hi:[0,1]
	v_exp_f32_e32 v56, v56
	v_exp_f32_e32 v57, v57
	v_pk_mul_f32 v[106:107], v[50:51], v[12:13] op_sel_hi:[0,1]
	v_exp_f32_e32 v106, v106
	v_exp_f32_e32 v107, v107
	v_pk_mul_f32 v[56:57], v[56:57], v[136:137]
	v_pk_fma_f32 v[54:55], v[108:109], v[134:135], v[54:55]
	v_pk_fma_f32 v[136:137], v[132:133], v[58:59], v[56:57] op_sel_hi:[0,1,1]
	v_pk_mul_f32 v[56:57], v[106:107], v[122:123]
	v_pk_mul_f32 v[58:59], v[50:51], v[8:9] op_sel_hi:[0,1]
	v_pk_fma_f32 v[122:123], v[132:133], v[60:61], v[56:57] op_sel_hi:[0,1,1]
	v_pk_mul_f32 v[56:57], v[50:51], v[6:7] op_sel_hi:[0,1]
	v_exp_f32_e32 v56, v56
	v_exp_f32_e32 v57, v57
	v_exp_f32_e32 v58, v58
	v_exp_f32_e32 v59, v59
	s_waitcnt lgkmcnt(11)
	v_pk_fma_f32 v[54:55], v[110:111], v[136:137], v[54:55]
	v_pk_mul_f32 v[56:57], v[56:57], v[124:125]
	v_pk_fma_f32 v[54:55], v[112:113], v[122:123], v[54:55]
	v_pk_fma_f32 v[124:125], v[132:133], v[62:63], v[56:57] op_sel_hi:[0,1,1]
	v_pk_mul_f32 v[56:57], v[58:59], v[126:127]
	v_pk_mul_f32 v[58:59], v[50:51], v[4:5] op_sel_hi:[0,1]
	v_pk_fma_f32 v[126:127], v[132:133], v[64:65], v[56:57] op_sel_hi:[0,1,1]
	v_pk_mul_f32 v[56:57], v[50:51], v[2:3] op_sel_hi:[0,1]
	v_exp_f32_e32 v56, v56
	v_exp_f32_e32 v57, v57
	v_exp_f32_e32 v58, v58
	v_exp_f32_e32 v59, v59
	s_waitcnt lgkmcnt(10)
	v_pk_fma_f32 v[54:55], v[114:115], v[124:125], v[54:55]
	v_pk_mul_f32 v[56:57], v[56:57], v[128:129]
	v_pk_fma_f32 v[54:55], v[116:117], v[126:127], v[54:55]
	v_pk_fma_f32 v[128:129], v[132:133], v[102:103], v[56:57] op_sel_hi:[0,1,1]
	v_pk_mul_f32 v[56:57], v[58:59], v[130:131]
	s_waitcnt lgkmcnt(9)
	v_pk_fma_f32 v[54:55], v[118:119], v[128:129], v[54:55]
	v_pk_fma_f32 v[130:131], v[132:133], v[104:105], v[56:57] op_sel_hi:[0,1,1]
	v_pk_fma_f32 v[54:55], v[120:121], v[130:131], v[54:55]
	s_nop 0
	v_add_f32_e32 v50, v54, v55
	v_fma_mix_f32 v42, v1, v42, v50 op_sel:[0,1,0] op_sel_hi:[0,1,0]
	v_fma_mixlo_f16 v42, v42, v46, 0 op_sel:[0,1,0] op_sel_hi:[0,1,0]
	ds_write_b16 v68, v42 offset:13456
	ds_read_b128 v[54:57], v67 offset:1408
	ds_read_b128 v[58:61], v67 offset:1424
	ds_read_b128 v[62:65], v67 offset:1440
	ds_read_b128 v[102:105], v67 offset:1456
	ds_read_b128 v[106:109], v67 offset:1472
	ds_read_b128 v[110:113], v67 offset:1488
	ds_read_b128 v[114:117], v67 offset:1504
	ds_read_b128 v[118:121], v67 offset:1520
	v_cvt_f32_f16_e32 v42, v51
	v_cvt_f32_f16_e32 v46, v43
	v_pk_mul_f32 v[132:133], v[42:43], v[14:15] op_sel_hi:[0,1]
	v_exp_f32_e32 v132, v132
	v_exp_f32_e32 v133, v133
	v_pk_mul_f32 v[140:141], v[42:43], v[16:17] op_sel_hi:[0,1]
	v_exp_f32_e32 v140, v140
	v_exp_f32_e32 v141, v141
	v_mul_f32_e32 v46, v42, v46
	v_pk_mul_f32 v[132:133], v[132:133], v[138:139]
	s_waitcnt lgkmcnt(14)
	v_pk_fma_f32 v[132:133], v[46:47], v[70:71], v[132:133] op_sel_hi:[0,1,1]
	s_waitcnt lgkmcnt(12)
	v_pk_fma_f32 v[70:71], v[86:87], v[132:133], 0 op_sel_hi:[1,1,0]
	v_pk_mul_f32 v[86:87], v[140:141], v[134:135]
	s_nop 0
	v_pk_fma_f32 v[134:135], v[46:47], v[72:73], v[86:87] op_sel_hi:[0,1,1]
	v_pk_mul_f32 v[72:73], v[42:43], v[10:11] op_sel_hi:[0,1]
	v_exp_f32_e32 v72, v72
	v_exp_f32_e32 v73, v73
	v_pk_mul_f32 v[86:87], v[42:43], v[12:13] op_sel_hi:[0,1]
	v_exp_f32_e32 v86, v86
	v_exp_f32_e32 v87, v87
	v_pk_mul_f32 v[72:73], v[72:73], v[136:137]
	v_pk_fma_f32 v[70:71], v[88:89], v[134:135], v[70:71]
	v_pk_fma_f32 v[136:137], v[46:47], v[74:75], v[72:73] op_sel_hi:[0,1,1]
	v_pk_mul_f32 v[72:73], v[86:87], v[122:123]
	v_pk_mul_f32 v[74:75], v[42:43], v[8:9] op_sel_hi:[0,1]
	v_pk_fma_f32 v[122:123], v[46:47], v[76:77], v[72:73] op_sel_hi:[0,1,1]
	v_pk_mul_f32 v[72:73], v[42:43], v[6:7] op_sel_hi:[0,1]
	v_exp_f32_e32 v72, v72
	v_exp_f32_e32 v73, v73
	v_exp_f32_e32 v74, v74
	v_exp_f32_e32 v75, v75
	s_waitcnt lgkmcnt(11)
	v_pk_fma_f32 v[70:71], v[90:91], v[136:137], v[70:71]
	v_pk_mul_f32 v[72:73], v[72:73], v[124:125]
	v_pk_fma_f32 v[70:71], v[92:93], v[122:123], v[70:71]
	v_pk_fma_f32 v[124:125], v[46:47], v[78:79], v[72:73] op_sel_hi:[0,1,1]
	v_pk_mul_f32 v[72:73], v[74:75], v[126:127]
	v_pk_mul_f32 v[74:75], v[42:43], v[4:5] op_sel_hi:[0,1]
	v_pk_fma_f32 v[126:127], v[46:47], v[80:81], v[72:73] op_sel_hi:[0,1,1]
	v_pk_mul_f32 v[72:73], v[42:43], v[2:3] op_sel_hi:[0,1]
	v_exp_f32_e32 v72, v72
	v_exp_f32_e32 v73, v73
	v_exp_f32_e32 v74, v74
	v_exp_f32_e32 v75, v75
	s_waitcnt lgkmcnt(10)
	v_pk_fma_f32 v[70:71], v[94:95], v[124:125], v[70:71]
	v_pk_mul_f32 v[72:73], v[72:73], v[128:129]
	v_pk_fma_f32 v[70:71], v[96:97], v[126:127], v[70:71]
	v_pk_fma_f32 v[128:129], v[46:47], v[82:83], v[72:73] op_sel_hi:[0,1,1]
	v_pk_mul_f32 v[72:73], v[74:75], v[130:131]
	s_waitcnt lgkmcnt(9)
	v_pk_fma_f32 v[70:71], v[98:99], v[128:129], v[70:71]
	v_pk_fma_f32 v[130:131], v[46:47], v[84:85], v[72:73] op_sel_hi:[0,1,1]
	v_pk_fma_f32 v[70:71], v[100:101], v[130:131], v[70:71]
	s_nop 0
	v_add_f32_e32 v42, v70, v71
	v_fma_mix_f32 v42, v1, v43, v42 op_sel_hi:[0,1,0]
	v_fma_mixlo_f16 v42, v42, v47, 0 op_sel_hi:[0,1,0]
	ds_write_b16 v68, v42 offset:14496
	ds_read_b128 v[70:73], v67 offset:1536
	ds_read_b128 v[74:77], v67 offset:1552
	ds_read_b128 v[78:81], v67 offset:1568
	ds_read_b128 v[82:85], v67 offset:1584
	ds_read_b128 v[86:89], v67 offset:1600
	ds_read_b128 v[90:93], v67 offset:1616
	ds_read_b128 v[94:97], v67 offset:1632
	ds_read_b128 v[98:101], v67 offset:1648
	v_cvt_f32_f16_sdwa v42, v51 dst_sel:DWORD dst_unused:UNUSED_PAD src0_sel:WORD_1
	v_cvt_f32_f16_sdwa v46, v43 dst_sel:DWORD dst_unused:UNUSED_PAD src0_sel:WORD_1
	v_pk_mul_f32 v[50:51], v[42:43], v[14:15] op_sel_hi:[0,1]
	v_exp_f32_e32 v50, v50
	v_exp_f32_e32 v51, v51
	v_pk_mul_f32 v[138:139], v[42:43], v[16:17] op_sel_hi:[0,1]
	v_exp_f32_e32 v138, v138
	v_exp_f32_e32 v139, v139
	v_mul_f32_e32 v46, v42, v46
	v_pk_mul_f32 v[50:51], v[50:51], v[132:133]
	s_waitcnt lgkmcnt(14)
	v_pk_fma_f32 v[50:51], v[46:47], v[54:55], v[50:51] op_sel_hi:[0,1,1]
	s_waitcnt lgkmcnt(12)
	v_pk_fma_f32 v[54:55], v[106:107], v[50:51], 0 op_sel_hi:[1,1,0]
	v_pk_mul_f32 v[106:107], v[138:139], v[134:135]
	s_nop 0
	v_pk_fma_f32 v[132:133], v[46:47], v[56:57], v[106:107] op_sel_hi:[0,1,1]
	v_pk_mul_f32 v[56:57], v[42:43], v[10:11] op_sel_hi:[0,1]
	v_exp_f32_e32 v56, v56
	v_exp_f32_e32 v57, v57
	v_pk_mul_f32 v[106:107], v[42:43], v[12:13] op_sel_hi:[0,1]
	v_exp_f32_e32 v106, v106
	v_exp_f32_e32 v107, v107
	v_pk_mul_f32 v[56:57], v[56:57], v[136:137]
	v_pk_fma_f32 v[54:55], v[108:109], v[132:133], v[54:55]
	v_pk_fma_f32 v[134:135], v[46:47], v[58:59], v[56:57] op_sel_hi:[0,1,1]
	v_pk_mul_f32 v[56:57], v[106:107], v[122:123]
	v_pk_mul_f32 v[58:59], v[42:43], v[8:9] op_sel_hi:[0,1]
	v_pk_fma_f32 v[122:123], v[46:47], v[60:61], v[56:57] op_sel_hi:[0,1,1]
	v_pk_mul_f32 v[56:57], v[42:43], v[6:7] op_sel_hi:[0,1]
	v_exp_f32_e32 v56, v56
	v_exp_f32_e32 v57, v57
	v_exp_f32_e32 v58, v58
	v_exp_f32_e32 v59, v59
	s_waitcnt lgkmcnt(11)
	v_pk_fma_f32 v[54:55], v[110:111], v[134:135], v[54:55]
	v_pk_mul_f32 v[56:57], v[56:57], v[124:125]
	v_pk_fma_f32 v[54:55], v[112:113], v[122:123], v[54:55]
	v_pk_fma_f32 v[124:125], v[46:47], v[62:63], v[56:57] op_sel_hi:[0,1,1]
	v_pk_mul_f32 v[56:57], v[58:59], v[126:127]
	v_pk_mul_f32 v[58:59], v[42:43], v[4:5] op_sel_hi:[0,1]
	v_pk_fma_f32 v[126:127], v[46:47], v[64:65], v[56:57] op_sel_hi:[0,1,1]
	v_pk_mul_f32 v[56:57], v[42:43], v[2:3] op_sel_hi:[0,1]
	v_exp_f32_e32 v56, v56
	v_exp_f32_e32 v57, v57
	v_exp_f32_e32 v58, v58
	v_exp_f32_e32 v59, v59
	s_waitcnt lgkmcnt(10)
	v_pk_fma_f32 v[54:55], v[114:115], v[124:125], v[54:55]
	v_pk_mul_f32 v[56:57], v[56:57], v[128:129]
	v_pk_fma_f32 v[54:55], v[116:117], v[126:127], v[54:55]
	v_pk_fma_f32 v[128:129], v[46:47], v[102:103], v[56:57] op_sel_hi:[0,1,1]
	v_pk_mul_f32 v[56:57], v[58:59], v[130:131]
	s_waitcnt lgkmcnt(9)
	v_pk_fma_f32 v[54:55], v[118:119], v[128:129], v[54:55]
	v_pk_fma_f32 v[130:131], v[46:47], v[104:105], v[56:57] op_sel_hi:[0,1,1]
	v_pk_fma_f32 v[54:55], v[120:121], v[130:131], v[54:55]
	s_nop 0
	v_add_f32_e32 v42, v54, v55
	v_fma_mix_f32 v42, v1, v43, v42 op_sel:[0,1,0] op_sel_hi:[0,1,0]
	v_fma_mixlo_f16 v42, v42, v47, 0 op_sel:[0,1,0] op_sel_hi:[0,1,0]
	ds_write_b16 v68, v42 offset:15536
	ds_read_b128 v[54:57], v67 offset:1664
	ds_read_b128 v[58:61], v67 offset:1680
	ds_read_b128 v[62:65], v67 offset:1696
	ds_read_b128 v[102:105], v67 offset:1712
	ds_read_b128 v[106:109], v67 offset:1728
	ds_read_b128 v[110:113], v67 offset:1744
	ds_read_b128 v[114:117], v67 offset:1760
	ds_read_b128 v[118:121], v67 offset:1776
	v_cvt_f32_f16_e32 v42, v52
	v_cvt_f32_f16_e32 v43, v44
	v_pk_mul_f32 v[136:137], v[42:43], v[14:15] op_sel_hi:[0,1]
	v_exp_f32_e32 v136, v136
	v_exp_f32_e32 v137, v137
	v_pk_mul_f32 v[138:139], v[42:43], v[16:17] op_sel_hi:[0,1]
	v_exp_f32_e32 v138, v138
	v_exp_f32_e32 v139, v139
	v_mul_f32_e32 v46, v42, v43
	v_pk_mul_f32 v[50:51], v[136:137], v[50:51]
	s_waitcnt lgkmcnt(14)
	v_pk_fma_f32 v[50:51], v[46:47], v[70:71], v[50:51] op_sel_hi:[0,1,1]
	s_waitcnt lgkmcnt(12)
	v_pk_fma_f32 v[70:71], v[86:87], v[50:51], 0 op_sel_hi:[1,1,0]
	v_pk_mul_f32 v[86:87], v[138:139], v[132:133]
	s_nop 0
	v_pk_fma_f32 v[132:133], v[46:47], v[72:73], v[86:87] op_sel_hi:[0,1,1]
	v_pk_mul_f32 v[72:73], v[42:43], v[10:11] op_sel_hi:[0,1]
	v_exp_f32_e32 v72, v72
	v_exp_f32_e32 v73, v73
	v_pk_mul_f32 v[86:87], v[42:43], v[12:13] op_sel_hi:[0,1]
	v_exp_f32_e32 v86, v86
	v_exp_f32_e32 v87, v87
	v_pk_mul_f32 v[72:73], v[72:73], v[134:135]
	v_pk_fma_f32 v[70:71], v[88:89], v[132:133], v[70:71]
	v_pk_fma_f32 v[134:135], v[46:47], v[74:75], v[72:73] op_sel_hi:[0,1,1]
	v_pk_mul_f32 v[72:73], v[86:87], v[122:123]
	v_pk_mul_f32 v[74:75], v[42:43], v[8:9] op_sel_hi:[0,1]
	v_pk_fma_f32 v[122:123], v[46:47], v[76:77], v[72:73] op_sel_hi:[0,1,1]
	v_pk_mul_f32 v[72:73], v[42:43], v[6:7] op_sel_hi:[0,1]
	v_exp_f32_e32 v72, v72
	v_exp_f32_e32 v73, v73
	v_exp_f32_e32 v74, v74
	v_exp_f32_e32 v75, v75
	s_waitcnt lgkmcnt(11)
	v_pk_fma_f32 v[70:71], v[90:91], v[134:135], v[70:71]
	v_pk_mul_f32 v[72:73], v[72:73], v[124:125]
	v_pk_fma_f32 v[70:71], v[92:93], v[122:123], v[70:71]
	v_pk_fma_f32 v[124:125], v[46:47], v[78:79], v[72:73] op_sel_hi:[0,1,1]
	v_pk_mul_f32 v[72:73], v[74:75], v[126:127]
	s_waitcnt lgkmcnt(10)
	v_pk_fma_f32 v[70:71], v[94:95], v[124:125], v[70:71]
	v_pk_fma_f32 v[126:127], v[46:47], v[80:81], v[72:73] op_sel_hi:[0,1,1]
	v_pk_mul_f32 v[72:73], v[42:43], v[2:3] op_sel_hi:[0,1]
	v_exp_f32_e32 v72, v72
	v_exp_f32_e32 v73, v73
	v_pk_mul_f32 v[42:43], v[42:43], v[4:5] op_sel_hi:[0,1]
	v_exp_f32_e32 v42, v42
	v_exp_f32_e32 v43, v43
	v_pk_mul_f32 v[72:73], v[72:73], v[128:129]
	v_pk_fma_f32 v[70:71], v[96:97], v[126:127], v[70:71]
	v_pk_fma_f32 v[128:129], v[46:47], v[82:83], v[72:73] op_sel_hi:[0,1,1]
	v_pk_mul_f32 v[42:43], v[42:43], v[130:131]
	s_waitcnt lgkmcnt(9)
	v_pk_fma_f32 v[70:71], v[98:99], v[128:129], v[70:71]
	v_pk_fma_f32 v[42:43], v[46:47], v[84:85], v[42:43] op_sel_hi:[0,1,1]
	v_pk_fma_f32 v[46:47], v[100:101], v[42:43], v[70:71]
	s_nop 0
	v_add_f32_e32 v46, v46, v47
	v_fma_mix_f32 v46, v1, v44, v46 op_sel_hi:[0,1,0]
	v_fma_mixlo_f16 v46, v46, v48, 0 op_sel_hi:[0,1,0]
	ds_write_b16 v68, v46 offset:16576
	ds_read_b128 v[70:73], v67 offset:1792
	ds_read_b128 v[74:77], v67 offset:1808
	ds_read_b128 v[78:81], v67 offset:1824
	ds_read_b128 v[82:85], v67 offset:1840
	ds_read_b128 v[86:89], v67 offset:1856
	ds_read_b128 v[90:93], v67 offset:1872
	ds_read_b128 v[94:97], v67 offset:1888
	ds_read_b128 v[98:101], v67 offset:1904
	v_cvt_f32_f16_sdwa v46, v52 dst_sel:DWORD dst_unused:UNUSED_PAD src0_sel:WORD_1
	v_cvt_f32_f16_sdwa v47, v44 dst_sel:DWORD dst_unused:UNUSED_PAD src0_sel:WORD_1
	v_pk_mul_f32 v[130:131], v[46:47], v[14:15] op_sel_hi:[0,1]
	v_exp_f32_e32 v130, v130
	v_exp_f32_e32 v131, v131
	v_pk_mul_f32 v[136:137], v[46:47], v[16:17] op_sel_hi:[0,1]
	v_exp_f32_e32 v136, v136
	v_exp_f32_e32 v137, v137
	v_mul_f32_e32 v52, v46, v47
	v_pk_mul_f32 v[50:51], v[130:131], v[50:51]
	s_waitcnt lgkmcnt(14)
	v_pk_fma_f32 v[50:51], v[52:53], v[54:55], v[50:51] op_sel_hi:[0,1,1]
	s_waitcnt lgkmcnt(12)
	v_pk_fma_f32 v[54:55], v[106:107], v[50:51], 0 op_sel_hi:[1,1,0]
	v_pk_mul_f32 v[106:107], v[136:137], v[132:133]
	s_nop 0
	v_pk_fma_f32 v[130:131], v[52:53], v[56:57], v[106:107] op_sel_hi:[0,1,1]
	v_pk_mul_f32 v[56:57], v[46:47], v[10:11] op_sel_hi:[0,1]
	v_exp_f32_e32 v56, v56
	v_exp_f32_e32 v57, v57
	v_pk_mul_f32 v[106:107], v[46:47], v[12:13] op_sel_hi:[0,1]
	v_exp_f32_e32 v106, v106
	v_exp_f32_e32 v107, v107
	v_pk_mul_f32 v[56:57], v[56:57], v[134:135]
	v_pk_fma_f32 v[54:55], v[108:109], v[130:131], v[54:55]
	v_pk_fma_f32 v[132:133], v[52:53], v[58:59], v[56:57] op_sel_hi:[0,1,1]
	v_pk_mul_f32 v[56:57], v[106:107], v[122:123]
	v_pk_mul_f32 v[58:59], v[46:47], v[8:9] op_sel_hi:[0,1]
	v_pk_fma_f32 v[122:123], v[52:53], v[60:61], v[56:57] op_sel_hi:[0,1,1]
	v_pk_mul_f32 v[56:57], v[46:47], v[6:7] op_sel_hi:[0,1]
	v_exp_f32_e32 v56, v56
	v_exp_f32_e32 v57, v57
	v_exp_f32_e32 v58, v58
	v_exp_f32_e32 v59, v59
	s_waitcnt lgkmcnt(11)
	v_pk_fma_f32 v[54:55], v[110:111], v[132:133], v[54:55]
	v_pk_mul_f32 v[56:57], v[56:57], v[124:125]
	v_pk_fma_f32 v[54:55], v[112:113], v[122:123], v[54:55]
	v_pk_fma_f32 v[124:125], v[52:53], v[62:63], v[56:57] op_sel_hi:[0,1,1]
	v_pk_mul_f32 v[56:57], v[58:59], v[126:127]
	s_waitcnt lgkmcnt(10)
	v_pk_fma_f32 v[54:55], v[114:115], v[124:125], v[54:55]
	v_pk_fma_f32 v[126:127], v[52:53], v[64:65], v[56:57] op_sel_hi:[0,1,1]
	v_pk_mul_f32 v[56:57], v[46:47], v[2:3] op_sel_hi:[0,1]
	v_exp_f32_e32 v56, v56
	v_exp_f32_e32 v57, v57
	v_pk_mul_f32 v[46:47], v[46:47], v[4:5] op_sel_hi:[0,1]
	v_exp_f32_e32 v46, v46
	v_exp_f32_e32 v47, v47
	v_pk_mul_f32 v[56:57], v[56:57], v[128:129]
	v_pk_fma_f32 v[54:55], v[116:117], v[126:127], v[54:55]
	v_pk_fma_f32 v[128:129], v[52:53], v[102:103], v[56:57] op_sel_hi:[0,1,1]
	v_pk_mul_f32 v[42:43], v[46:47], v[42:43]
	s_waitcnt lgkmcnt(9)
	v_pk_fma_f32 v[54:55], v[118:119], v[128:129], v[54:55]
	v_pk_fma_f32 v[42:43], v[52:53], v[104:105], v[42:43] op_sel_hi:[0,1,1]
	v_pk_fma_f32 v[46:47], v[120:121], v[42:43], v[54:55]
	s_nop 0
	v_add_f32_e32 v46, v46, v47
	v_fma_mix_f32 v44, v1, v44, v46 op_sel:[0,1,0] op_sel_hi:[0,1,0]
	v_fma_mixlo_f16 v44, v44, v48, 0 op_sel:[0,1,0] op_sel_hi:[0,1,0]
	ds_write_b16 v68, v44 offset:17616
	ds_read_b128 v[54:57], v67 offset:1920
	ds_read_b128 v[58:61], v67 offset:1936
	ds_read_b128 v[62:65], v67 offset:1952
	ds_read_b128 v[102:105], v67 offset:1968
	ds_read_b128 v[106:109], v67 offset:1984
	ds_read_b128 v[110:113], v67 offset:2000
	ds_read_b128 v[114:117], v67 offset:2016
	ds_read_b128 v[118:121], v67 offset:2032
	v_cvt_f32_f16_e32 v44, v53
	v_cvt_f32_f16_e32 v46, v45
	v_pk_mul_f32 v[134:135], v[44:45], v[14:15] op_sel_hi:[0,1]
	v_exp_f32_e32 v134, v134
	v_exp_f32_e32 v135, v135
	v_pk_mul_f32 v[136:137], v[44:45], v[16:17] op_sel_hi:[0,1]
	v_exp_f32_e32 v136, v136
	v_exp_f32_e32 v137, v137
	v_mul_f32_e32 v46, v44, v46
	v_pk_mul_f32 v[50:51], v[134:135], v[50:51]
	s_waitcnt lgkmcnt(14)
	v_pk_fma_f32 v[50:51], v[46:47], v[70:71], v[50:51] op_sel_hi:[0,1,1]
	s_waitcnt lgkmcnt(12)
	v_pk_fma_f32 v[70:71], v[86:87], v[50:51], 0 op_sel_hi:[1,1,0]
	v_pk_mul_f32 v[86:87], v[136:137], v[130:131]
	s_nop 0
	v_pk_fma_f32 v[130:131], v[46:47], v[72:73], v[86:87] op_sel_hi:[0,1,1]
	v_pk_mul_f32 v[72:73], v[44:45], v[10:11] op_sel_hi:[0,1]
	v_exp_f32_e32 v72, v72
	v_exp_f32_e32 v73, v73
	v_pk_mul_f32 v[86:87], v[44:45], v[12:13] op_sel_hi:[0,1]
	v_exp_f32_e32 v86, v86
	v_exp_f32_e32 v87, v87
	v_pk_mul_f32 v[72:73], v[72:73], v[132:133]
	v_pk_fma_f32 v[70:71], v[88:89], v[130:131], v[70:71]
	v_pk_fma_f32 v[132:133], v[46:47], v[74:75], v[72:73] op_sel_hi:[0,1,1]
	v_pk_mul_f32 v[72:73], v[86:87], v[122:123]
	v_pk_mul_f32 v[74:75], v[44:45], v[8:9] op_sel_hi:[0,1]
	v_pk_fma_f32 v[122:123], v[46:47], v[76:77], v[72:73] op_sel_hi:[0,1,1]
	v_pk_mul_f32 v[72:73], v[44:45], v[6:7] op_sel_hi:[0,1]
	v_exp_f32_e32 v72, v72
	v_exp_f32_e32 v73, v73
	v_exp_f32_e32 v74, v74
	v_exp_f32_e32 v75, v75
	s_waitcnt lgkmcnt(11)
	v_pk_fma_f32 v[70:71], v[90:91], v[132:133], v[70:71]
	v_pk_mul_f32 v[72:73], v[72:73], v[124:125]
	v_pk_fma_f32 v[70:71], v[92:93], v[122:123], v[70:71]
	v_pk_fma_f32 v[124:125], v[46:47], v[78:79], v[72:73] op_sel_hi:[0,1,1]
	v_pk_mul_f32 v[72:73], v[74:75], v[126:127]
	v_pk_mul_f32 v[74:75], v[44:45], v[4:5] op_sel_hi:[0,1]
	v_pk_fma_f32 v[126:127], v[46:47], v[80:81], v[72:73] op_sel_hi:[0,1,1]
	v_pk_mul_f32 v[72:73], v[44:45], v[2:3] op_sel_hi:[0,1]
	v_exp_f32_e32 v72, v72
	v_exp_f32_e32 v73, v73
	v_exp_f32_e32 v74, v74
	v_exp_f32_e32 v75, v75
	s_waitcnt lgkmcnt(10)
	v_pk_fma_f32 v[70:71], v[94:95], v[124:125], v[70:71]
	v_pk_mul_f32 v[72:73], v[72:73], v[128:129]
	v_pk_fma_f32 v[70:71], v[96:97], v[126:127], v[70:71]
	v_pk_fma_f32 v[128:129], v[46:47], v[82:83], v[72:73] op_sel_hi:[0,1,1]
	v_pk_mul_f32 v[42:43], v[74:75], v[42:43]
	s_waitcnt lgkmcnt(9)
	v_pk_fma_f32 v[70:71], v[98:99], v[128:129], v[70:71]
	v_pk_fma_f32 v[42:43], v[46:47], v[84:85], v[42:43] op_sel_hi:[0,1,1]
	v_pk_fma_f32 v[46:47], v[100:101], v[42:43], v[70:71]
	s_nop 0
	v_add_f32_e32 v44, v46, v47
	v_fma_mix_f32 v44, v1, v45, v44 op_sel_hi:[0,1,0]
	v_fma_mixlo_f16 v44, v44, v49, 0 op_sel_hi:[0,1,0]
	ds_write_b16 v68, v44 offset:18656
	ds_read_b128 v[70:73], v67 offset:2048
	ds_read_b128 v[74:77], v67 offset:2064
	ds_read_b128 v[78:81], v67 offset:2080
	ds_read_b128 v[82:85], v67 offset:2096
	ds_read_b128 v[86:89], v67 offset:2112
	ds_read_b128 v[90:93], v67 offset:2128
	ds_read_b128 v[94:97], v67 offset:2144
	ds_read_b128 v[98:101], v67 offset:2160
	v_cvt_f32_f16_sdwa v44, v53 dst_sel:DWORD dst_unused:UNUSED_PAD src0_sel:WORD_1
	v_cvt_f32_f16_sdwa v46, v45 dst_sel:DWORD dst_unused:UNUSED_PAD src0_sel:WORD_1
	v_pk_mul_f32 v[52:53], v[44:45], v[14:15] op_sel_hi:[0,1]
	v_pk_mul_f32 v[134:135], v[44:45], v[16:17] op_sel_hi:[0,1]
	v_exp_f32_e32 v52, v52
	v_exp_f32_e32 v53, v53
	v_exp_f32_e32 v134, v134
	v_exp_f32_e32 v135, v135
	v_mul_f32_e32 v46, v44, v46
	v_pk_mul_f32 v[50:51], v[52:53], v[50:51]
	v_pk_mul_f32 v[52:53], v[134:135], v[130:131]
	s_waitcnt lgkmcnt(14)
	v_pk_fma_f32 v[130:131], v[46:47], v[56:57], v[52:53] op_sel_hi:[0,1,1]
	v_pk_mul_f32 v[52:53], v[44:45], v[10:11] op_sel_hi:[0,1]
	v_pk_fma_f32 v[136:137], v[46:47], v[54:55], v[50:51] op_sel_hi:[0,1,1]
	v_exp_f32_e32 v52, v52
	v_exp_f32_e32 v53, v53
	v_pk_mul_f32 v[54:55], v[44:45], v[12:13] op_sel_hi:[0,1]
	v_exp_f32_e32 v54, v54
	v_exp_f32_e32 v55, v55
	s_waitcnt lgkmcnt(12)
	v_pk_fma_f32 v[50:51], v[106:107], v[136:137], 0 op_sel_hi:[1,1,0]
	v_pk_mul_f32 v[52:53], v[52:53], v[132:133]
	v_pk_fma_f32 v[50:51], v[108:109], v[130:131], v[50:51]
	v_pk_fma_f32 v[132:133], v[46:47], v[58:59], v[52:53] op_sel_hi:[0,1,1]
	v_pk_mul_f32 v[52:53], v[54:55], v[122:123]
	s_waitcnt lgkmcnt(11)
	v_pk_fma_f32 v[50:51], v[110:111], v[132:133], v[50:51]
	v_pk_fma_f32 v[110:111], v[46:47], v[60:61], v[52:53] op_sel_hi:[0,1,1]
	v_pk_mul_f32 v[52:53], v[44:45], v[6:7] op_sel_hi:[0,1]
	v_exp_f32_e32 v52, v52
	v_exp_f32_e32 v53, v53
	v_pk_mul_f32 v[54:55], v[44:45], v[8:9] op_sel_hi:[0,1]
	v_exp_f32_e32 v54, v54
	v_exp_f32_e32 v55, v55
	v_pk_mul_f32 v[52:53], v[52:53], v[124:125]
	v_pk_fma_f32 v[50:51], v[112:113], v[110:111], v[50:51]
	v_pk_fma_f32 v[112:113], v[46:47], v[62:63], v[52:53] op_sel_hi:[0,1,1]
	v_pk_mul_f32 v[52:53], v[54:55], v[126:127]
	s_waitcnt lgkmcnt(10)
	v_pk_fma_f32 v[50:51], v[114:115], v[112:113], v[50:51]
	v_pk_fma_f32 v[114:115], v[46:47], v[64:65], v[52:53] op_sel_hi:[0,1,1]
	v_pk_mul_f32 v[52:53], v[44:45], v[2:3] op_sel_hi:[0,1]
	v_exp_f32_e32 v52, v52
	v_exp_f32_e32 v53, v53
	v_pk_mul_f32 v[54:55], v[44:45], v[4:5] op_sel_hi:[0,1]
	v_exp_f32_e32 v54, v54
	v_exp_f32_e32 v55, v55
	v_pk_mul_f32 v[52:53], v[52:53], v[128:129]
	v_pk_fma_f32 v[50:51], v[116:117], v[114:115], v[50:51]
	v_pk_fma_f32 v[116:117], v[46:47], v[102:103], v[52:53] op_sel_hi:[0,1,1]
	v_pk_mul_f32 v[42:43], v[54:55], v[42:43]
	s_waitcnt lgkmcnt(9)
	v_pk_fma_f32 v[50:51], v[118:119], v[116:117], v[50:51]
	v_pk_fma_f32 v[118:119], v[46:47], v[104:105], v[42:43] op_sel_hi:[0,1,1]
	v_pk_fma_f32 v[42:43], v[120:121], v[118:119], v[50:51]
	s_nop 0
	v_add_f32_e32 v42, v42, v43
	v_fma_mix_f32 v42, v1, v45, v42 op_sel:[0,1,0] op_sel_hi:[0,1,0]
	v_fma_mixlo_f16 v42, v42, v49, 0 op_sel:[0,1,0] op_sel_hi:[0,1,0]
	ds_write_b16 v68, v42 offset:19696
	ds_read_b128 v[42:45], v67 offset:2176
	ds_read_b128 v[46:49], v67 offset:2192
	ds_read_b128 v[50:53], v67 offset:2208
	ds_read_b128 v[54:57], v67 offset:2224
	ds_read_b128 v[58:61], v67 offset:2240
	ds_read_b128 v[62:65], v67 offset:2256
	ds_read_b128 v[102:105], v67 offset:2272
	ds_read_b128 v[106:109], v67 offset:2288
	s_waitcnt vmcnt(5)
	v_cvt_f32_f16_e32 v120, v38
	s_waitcnt vmcnt(4)
	v_cvt_f32_f16_e32 v69, v30
	v_pk_mul_f32 v[124:125], v[120:121], v[14:15] op_sel_hi:[0,1]
	v_exp_f32_e32 v124, v124
	v_exp_f32_e32 v125, v125
	v_pk_mul_f32 v[126:127], v[120:121], v[16:17] op_sel_hi:[0,1]
	v_exp_f32_e32 v126, v126
	v_exp_f32_e32 v127, v127
	v_mul_f32_e32 v122, v120, v69
	v_pk_mul_f32 v[124:125], v[124:125], v[136:137]
	s_waitcnt lgkmcnt(14)
	v_pk_fma_f32 v[124:125], v[122:123], v[70:71], v[124:125] op_sel_hi:[0,1,1]
	s_waitcnt lgkmcnt(12)
	v_pk_fma_f32 v[70:71], v[86:87], v[124:125], 0 op_sel_hi:[1,1,0]
	v_pk_mul_f32 v[86:87], v[126:127], v[130:131]
	s_nop 0
	v_pk_fma_f32 v[126:127], v[122:123], v[72:73], v[86:87] op_sel_hi:[0,1,1]
	v_pk_mul_f32 v[72:73], v[120:121], v[10:11] op_sel_hi:[0,1]
	v_exp_f32_e32 v72, v72
	v_exp_f32_e32 v73, v73
	v_pk_mul_f32 v[86:87], v[120:121], v[12:13] op_sel_hi:[0,1]
	v_exp_f32_e32 v86, v86
	v_exp_f32_e32 v87, v87
	v_pk_mul_f32 v[72:73], v[72:73], v[132:133]
	v_pk_fma_f32 v[70:71], v[88:89], v[126:127], v[70:71]
	v_pk_fma_f32 v[128:129], v[122:123], v[74:75], v[72:73] op_sel_hi:[0,1,1]
	v_pk_mul_f32 v[72:73], v[86:87], v[110:111]
	v_pk_mul_f32 v[74:75], v[120:121], v[8:9] op_sel_hi:[0,1]
	v_pk_fma_f32 v[110:111], v[122:123], v[76:77], v[72:73] op_sel_hi:[0,1,1]
	v_pk_mul_f32 v[72:73], v[120:121], v[6:7] op_sel_hi:[0,1]
	v_exp_f32_e32 v72, v72
	v_exp_f32_e32 v73, v73
	v_exp_f32_e32 v74, v74
	v_exp_f32_e32 v75, v75
	s_waitcnt lgkmcnt(11)
	v_pk_fma_f32 v[70:71], v[90:91], v[128:129], v[70:71]
	v_pk_mul_f32 v[72:73], v[72:73], v[112:113]
	v_pk_fma_f32 v[70:71], v[92:93], v[110:111], v[70:71]
	v_pk_fma_f32 v[112:113], v[122:123], v[78:79], v[72:73] op_sel_hi:[0,1,1]
	v_pk_mul_f32 v[72:73], v[74:75], v[114:115]
	v_pk_mul_f32 v[74:75], v[120:121], v[4:5] op_sel_hi:[0,1]
	v_pk_fma_f32 v[114:115], v[122:123], v[80:81], v[72:73] op_sel_hi:[0,1,1]
	v_pk_mul_f32 v[72:73], v[120:121], v[2:3] op_sel_hi:[0,1]
	v_exp_f32_e32 v72, v72
	v_exp_f32_e32 v73, v73
	v_exp_f32_e32 v74, v74
	v_exp_f32_e32 v75, v75
	s_waitcnt lgkmcnt(10)
	v_pk_fma_f32 v[70:71], v[94:95], v[112:113], v[70:71]
	v_pk_mul_f32 v[72:73], v[72:73], v[116:117]
	v_pk_fma_f32 v[70:71], v[96:97], v[114:115], v[70:71]
	v_pk_fma_f32 v[116:117], v[122:123], v[82:83], v[72:73] op_sel_hi:[0,1,1]
	v_pk_mul_f32 v[72:73], v[74:75], v[118:119]
	s_waitcnt lgkmcnt(9)
	v_pk_fma_f32 v[70:71], v[98:99], v[116:117], v[70:71]
	v_pk_fma_f32 v[118:119], v[122:123], v[84:85], v[72:73] op_sel_hi:[0,1,1]
	v_pk_fma_f32 v[70:71], v[100:101], v[118:119], v[70:71]
	s_nop 0
	v_add_f32_e32 v69, v70, v71
	v_fma_mix_f32 v69, v1, v30, v69 op_sel_hi:[0,1,0]
	s_waitcnt vmcnt(3)
	v_fma_mixlo_f16 v69, v69, v34, 0 op_sel_hi:[0,1,0]
	ds_write_b16 v68, v69 offset:20736
	ds_read_b128 v[70:73], v67 offset:2304
	ds_read_b128 v[74:77], v67 offset:2320
	ds_read_b128 v[78:81], v67 offset:2336
	ds_read_b128 v[82:85], v67 offset:2352
	ds_read_b128 v[86:89], v67 offset:2368
	ds_read_b128 v[90:93], v67 offset:2384
	ds_read_b128 v[94:97], v67 offset:2400
	ds_read_b128 v[98:101], v67 offset:2416
	v_cvt_f32_f16_sdwa v38, v38 dst_sel:DWORD dst_unused:UNUSED_PAD src0_sel:WORD_1
	v_cvt_f32_f16_sdwa v69, v30 dst_sel:DWORD dst_unused:UNUSED_PAD src0_sel:WORD_1
	v_pk_mul_f32 v[122:123], v[38:39], v[14:15] op_sel_hi:[0,1]
	v_exp_f32_e32 v122, v122
	v_exp_f32_e32 v123, v123
	v_pk_mul_f32 v[130:131], v[38:39], v[16:17] op_sel_hi:[0,1]
	v_exp_f32_e32 v130, v130
	v_exp_f32_e32 v131, v131
	v_mul_f32_e32 v120, v38, v69
	v_pk_mul_f32 v[122:123], v[122:123], v[124:125]
	s_waitcnt lgkmcnt(14)
	v_pk_fma_f32 v[122:123], v[120:121], v[42:43], v[122:123] op_sel_hi:[0,1,1]
	s_waitcnt lgkmcnt(12)
	v_pk_fma_f32 v[42:43], v[58:59], v[122:123], 0 op_sel_hi:[1,1,0]
	v_pk_mul_f32 v[58:59], v[130:131], v[126:127]
	s_nop 0
	v_pk_fma_f32 v[124:125], v[120:121], v[44:45], v[58:59] op_sel_hi:[0,1,1]
	v_pk_mul_f32 v[44:45], v[38:39], v[10:11] op_sel_hi:[0,1]
	v_exp_f32_e32 v44, v44
	v_exp_f32_e32 v45, v45
	v_pk_mul_f32 v[58:59], v[38:39], v[12:13] op_sel_hi:[0,1]
	v_exp_f32_e32 v58, v58
	v_exp_f32_e32 v59, v59
	v_pk_mul_f32 v[44:45], v[44:45], v[128:129]
	v_pk_fma_f32 v[42:43], v[60:61], v[124:125], v[42:43]
	v_pk_fma_f32 v[126:127], v[120:121], v[46:47], v[44:45] op_sel_hi:[0,1,1]
	v_pk_mul_f32 v[44:45], v[58:59], v[110:111]
	v_pk_mul_f32 v[46:47], v[38:39], v[8:9] op_sel_hi:[0,1]
	v_pk_fma_f32 v[110:111], v[120:121], v[48:49], v[44:45] op_sel_hi:[0,1,1]
	v_pk_mul_f32 v[44:45], v[38:39], v[6:7] op_sel_hi:[0,1]
	v_exp_f32_e32 v44, v44
	v_exp_f32_e32 v45, v45
	v_exp_f32_e32 v46, v46
	v_exp_f32_e32 v47, v47
	s_waitcnt lgkmcnt(11)
	v_pk_fma_f32 v[42:43], v[62:63], v[126:127], v[42:43]
	v_pk_mul_f32 v[44:45], v[44:45], v[112:113]
	v_pk_fma_f32 v[42:43], v[64:65], v[110:111], v[42:43]
	v_pk_fma_f32 v[112:113], v[120:121], v[50:51], v[44:45] op_sel_hi:[0,1,1]
	v_pk_mul_f32 v[44:45], v[46:47], v[114:115]
	v_pk_mul_f32 v[46:47], v[38:39], v[4:5] op_sel_hi:[0,1]
	v_pk_fma_f32 v[114:115], v[120:121], v[52:53], v[44:45] op_sel_hi:[0,1,1]
	v_pk_mul_f32 v[44:45], v[38:39], v[2:3] op_sel_hi:[0,1]
	v_exp_f32_e32 v44, v44
	v_exp_f32_e32 v45, v45
	v_exp_f32_e32 v46, v46
	v_exp_f32_e32 v47, v47
	s_waitcnt lgkmcnt(10)
	v_pk_fma_f32 v[42:43], v[102:103], v[112:113], v[42:43]
	v_pk_mul_f32 v[44:45], v[44:45], v[116:117]
	v_pk_fma_f32 v[42:43], v[104:105], v[114:115], v[42:43]
	v_pk_fma_f32 v[116:117], v[120:121], v[54:55], v[44:45] op_sel_hi:[0,1,1]
	v_pk_mul_f32 v[44:45], v[46:47], v[118:119]
	s_waitcnt lgkmcnt(9)
	v_pk_fma_f32 v[42:43], v[106:107], v[116:117], v[42:43]
	v_pk_fma_f32 v[118:119], v[120:121], v[56:57], v[44:45] op_sel_hi:[0,1,1]
	v_pk_fma_f32 v[42:43], v[108:109], v[118:119], v[42:43]
	s_nop 0
	v_add_f32_e32 v38, v42, v43
	v_fma_mix_f32 v30, v1, v30, v38 op_sel:[0,1,0] op_sel_hi:[0,1,0]
	v_fma_mixlo_f16 v30, v30, v34, 0 op_sel:[0,1,0] op_sel_hi:[0,1,0]
	ds_write_b16 v68, v30 offset:21776
	ds_read_b128 v[42:45], v67 offset:2432
	ds_read_b128 v[46:49], v67 offset:2448
	ds_read_b128 v[50:53], v67 offset:2464
	ds_read_b128 v[54:57], v67 offset:2480
	ds_read_b128 v[58:61], v67 offset:2496
	ds_read_b128 v[62:65], v67 offset:2512
	ds_read_b128 v[102:105], v67 offset:2528
	ds_read_b128 v[106:109], v67 offset:2544
	v_cvt_f32_f16_e32 v30, v39
	v_cvt_f32_f16_e32 v34, v31
	v_pk_mul_f32 v[120:121], v[30:31], v[14:15] op_sel_hi:[0,1]
	v_exp_f32_e32 v120, v120
	v_exp_f32_e32 v121, v121
	v_pk_mul_f32 v[128:129], v[30:31], v[16:17] op_sel_hi:[0,1]
	v_exp_f32_e32 v128, v128
	v_exp_f32_e32 v129, v129
	v_mul_f32_e32 v34, v30, v34
	v_pk_mul_f32 v[120:121], v[120:121], v[122:123]
	s_waitcnt lgkmcnt(14)
	v_pk_fma_f32 v[120:121], v[34:35], v[70:71], v[120:121] op_sel_hi:[0,1,1]
	s_waitcnt lgkmcnt(12)
	v_pk_fma_f32 v[70:71], v[86:87], v[120:121], 0 op_sel_hi:[1,1,0]
	v_pk_mul_f32 v[86:87], v[128:129], v[124:125]
	s_nop 0
	v_pk_fma_f32 v[122:123], v[34:35], v[72:73], v[86:87] op_sel_hi:[0,1,1]
	v_pk_mul_f32 v[72:73], v[30:31], v[10:11] op_sel_hi:[0,1]
	v_exp_f32_e32 v72, v72
	v_exp_f32_e32 v73, v73
	v_pk_mul_f32 v[86:87], v[30:31], v[12:13] op_sel_hi:[0,1]
	v_exp_f32_e32 v86, v86
	v_exp_f32_e32 v87, v87
	v_pk_mul_f32 v[72:73], v[72:73], v[126:127]
	v_pk_fma_f32 v[70:71], v[88:89], v[122:123], v[70:71]
	v_pk_fma_f32 v[124:125], v[34:35], v[74:75], v[72:73] op_sel_hi:[0,1,1]
	v_pk_mul_f32 v[72:73], v[86:87], v[110:111]
	v_pk_mul_f32 v[74:75], v[30:31], v[8:9] op_sel_hi:[0,1]
	v_pk_fma_f32 v[110:111], v[34:35], v[76:77], v[72:73] op_sel_hi:[0,1,1]
	v_pk_mul_f32 v[72:73], v[30:31], v[6:7] op_sel_hi:[0,1]
	v_exp_f32_e32 v72, v72
	v_exp_f32_e32 v73, v73
	v_exp_f32_e32 v74, v74
	v_exp_f32_e32 v75, v75
	s_waitcnt lgkmcnt(11)
	v_pk_fma_f32 v[70:71], v[90:91], v[124:125], v[70:71]
	v_pk_mul_f32 v[72:73], v[72:73], v[112:113]
	v_pk_fma_f32 v[70:71], v[92:93], v[110:111], v[70:71]
	v_pk_fma_f32 v[112:113], v[34:35], v[78:79], v[72:73] op_sel_hi:[0,1,1]
	v_pk_mul_f32 v[72:73], v[74:75], v[114:115]
	v_pk_mul_f32 v[74:75], v[30:31], v[4:5] op_sel_hi:[0,1]
	v_pk_fma_f32 v[114:115], v[34:35], v[80:81], v[72:73] op_sel_hi:[0,1,1]
	v_pk_mul_f32 v[72:73], v[30:31], v[2:3] op_sel_hi:[0,1]
	v_exp_f32_e32 v72, v72
	v_exp_f32_e32 v73, v73
	v_exp_f32_e32 v74, v74
	v_exp_f32_e32 v75, v75
	s_waitcnt lgkmcnt(10)
	v_pk_fma_f32 v[70:71], v[94:95], v[112:113], v[70:71]
	v_pk_mul_f32 v[72:73], v[72:73], v[116:117]
	v_pk_fma_f32 v[70:71], v[96:97], v[114:115], v[70:71]
	v_pk_fma_f32 v[116:117], v[34:35], v[82:83], v[72:73] op_sel_hi:[0,1,1]
	v_pk_mul_f32 v[72:73], v[74:75], v[118:119]
	s_waitcnt lgkmcnt(9)
	v_pk_fma_f32 v[70:71], v[98:99], v[116:117], v[70:71]
	v_pk_fma_f32 v[118:119], v[34:35], v[84:85], v[72:73] op_sel_hi:[0,1,1]
	v_pk_fma_f32 v[70:71], v[100:101], v[118:119], v[70:71]
	s_nop 0
	v_add_f32_e32 v30, v70, v71
	v_fma_mix_f32 v30, v1, v31, v30 op_sel_hi:[0,1,0]
	v_fma_mixlo_f16 v30, v30, v35, 0 op_sel_hi:[0,1,0]
	ds_write_b16 v68, v30 offset:22816
	ds_read_b128 v[70:73], v67 offset:2560
	ds_read_b128 v[74:77], v67 offset:2576
	ds_read_b128 v[78:81], v67 offset:2592
	ds_read_b128 v[82:85], v67 offset:2608
	ds_read_b128 v[86:89], v67 offset:2624
	ds_read_b128 v[90:93], v67 offset:2640
	ds_read_b128 v[94:97], v67 offset:2656
	ds_read_b128 v[98:101], v67 offset:2672
	v_cvt_f32_f16_sdwa v30, v39 dst_sel:DWORD dst_unused:UNUSED_PAD src0_sel:WORD_1
	v_cvt_f32_f16_sdwa v34, v31 dst_sel:DWORD dst_unused:UNUSED_PAD src0_sel:WORD_1
	v_pk_mul_f32 v[38:39], v[30:31], v[14:15] op_sel_hi:[0,1]
	v_exp_f32_e32 v38, v38
	v_exp_f32_e32 v39, v39
	v_pk_mul_f32 v[126:127], v[30:31], v[16:17] op_sel_hi:[0,1]
	v_exp_f32_e32 v126, v126
	v_exp_f32_e32 v127, v127
	v_mul_f32_e32 v34, v30, v34
	v_pk_mul_f32 v[38:39], v[38:39], v[120:121]
	s_waitcnt lgkmcnt(14)
	v_pk_fma_f32 v[38:39], v[34:35], v[42:43], v[38:39] op_sel_hi:[0,1,1]
	s_waitcnt lgkmcnt(12)
	v_pk_fma_f32 v[42:43], v[58:59], v[38:39], 0 op_sel_hi:[1,1,0]
	v_pk_mul_f32 v[58:59], v[126:127], v[122:123]
	s_nop 0
	v_pk_fma_f32 v[120:121], v[34:35], v[44:45], v[58:59] op_sel_hi:[0,1,1]
	v_pk_mul_f32 v[44:45], v[30:31], v[10:11] op_sel_hi:[0,1]
	v_exp_f32_e32 v44, v44
	v_exp_f32_e32 v45, v45
	v_pk_mul_f32 v[58:59], v[30:31], v[12:13] op_sel_hi:[0,1]
	v_exp_f32_e32 v58, v58
	v_exp_f32_e32 v59, v59
	v_pk_mul_f32 v[44:45], v[44:45], v[124:125]
	v_pk_fma_f32 v[42:43], v[60:61], v[120:121], v[42:43]
	v_pk_fma_f32 v[122:123], v[34:35], v[46:47], v[44:45] op_sel_hi:[0,1,1]
	v_pk_mul_f32 v[44:45], v[58:59], v[110:111]
	v_pk_mul_f32 v[46:47], v[30:31], v[8:9] op_sel_hi:[0,1]
	v_pk_fma_f32 v[110:111], v[34:35], v[48:49], v[44:45] op_sel_hi:[0,1,1]
	v_pk_mul_f32 v[44:45], v[30:31], v[6:7] op_sel_hi:[0,1]
	v_exp_f32_e32 v44, v44
	v_exp_f32_e32 v45, v45
	v_exp_f32_e32 v46, v46
	v_exp_f32_e32 v47, v47
	s_waitcnt lgkmcnt(11)
	v_pk_fma_f32 v[42:43], v[62:63], v[122:123], v[42:43]
	v_pk_mul_f32 v[44:45], v[44:45], v[112:113]
	v_pk_fma_f32 v[42:43], v[64:65], v[110:111], v[42:43]
	v_pk_fma_f32 v[112:113], v[34:35], v[50:51], v[44:45] op_sel_hi:[0,1,1]
	v_pk_mul_f32 v[44:45], v[46:47], v[114:115]
	v_pk_mul_f32 v[46:47], v[30:31], v[4:5] op_sel_hi:[0,1]
	v_pk_fma_f32 v[114:115], v[34:35], v[52:53], v[44:45] op_sel_hi:[0,1,1]
	v_pk_mul_f32 v[44:45], v[30:31], v[2:3] op_sel_hi:[0,1]
	v_exp_f32_e32 v44, v44
	v_exp_f32_e32 v45, v45
	v_exp_f32_e32 v46, v46
	v_exp_f32_e32 v47, v47
	s_waitcnt lgkmcnt(10)
	v_pk_fma_f32 v[42:43], v[102:103], v[112:113], v[42:43]
	v_pk_mul_f32 v[44:45], v[44:45], v[116:117]
	v_pk_fma_f32 v[42:43], v[104:105], v[114:115], v[42:43]
	v_pk_fma_f32 v[116:117], v[34:35], v[54:55], v[44:45] op_sel_hi:[0,1,1]
	v_pk_mul_f32 v[44:45], v[46:47], v[118:119]
	s_waitcnt lgkmcnt(9)
	v_pk_fma_f32 v[42:43], v[106:107], v[116:117], v[42:43]
	v_pk_fma_f32 v[118:119], v[34:35], v[56:57], v[44:45] op_sel_hi:[0,1,1]
	v_pk_fma_f32 v[42:43], v[108:109], v[118:119], v[42:43]
	s_nop 0
	v_add_f32_e32 v30, v42, v43
	v_fma_mix_f32 v30, v1, v31, v30 op_sel:[0,1,0] op_sel_hi:[0,1,0]
	v_fma_mixlo_f16 v30, v30, v35, 0 op_sel:[0,1,0] op_sel_hi:[0,1,0]
	ds_write_b16 v68, v30 offset:23856
	ds_read_b128 v[42:45], v67 offset:2688
	ds_read_b128 v[46:49], v67 offset:2704
	ds_read_b128 v[50:53], v67 offset:2720
	ds_read_b128 v[54:57], v67 offset:2736
	ds_read_b128 v[58:61], v67 offset:2752
	ds_read_b128 v[62:65], v67 offset:2768
	ds_read_b128 v[102:105], v67 offset:2784
	ds_read_b128 v[106:109], v67 offset:2800
	v_cvt_f32_f16_e32 v30, v40
	v_cvt_f32_f16_e32 v31, v32
	v_pk_mul_f32 v[124:125], v[30:31], v[14:15] op_sel_hi:[0,1]
	v_exp_f32_e32 v124, v124
	v_exp_f32_e32 v125, v125
	v_pk_mul_f32 v[126:127], v[30:31], v[16:17] op_sel_hi:[0,1]
	v_exp_f32_e32 v126, v126
	v_exp_f32_e32 v127, v127
	v_mul_f32_e32 v34, v30, v31
	v_pk_mul_f32 v[38:39], v[124:125], v[38:39]
	s_waitcnt lgkmcnt(14)
	v_pk_fma_f32 v[38:39], v[34:35], v[70:71], v[38:39] op_sel_hi:[0,1,1]
	s_waitcnt lgkmcnt(12)
	v_pk_fma_f32 v[70:71], v[86:87], v[38:39], 0 op_sel_hi:[1,1,0]
	v_pk_mul_f32 v[86:87], v[126:127], v[120:121]
	s_nop 0
	v_pk_fma_f32 v[120:121], v[34:35], v[72:73], v[86:87] op_sel_hi:[0,1,1]
	v_pk_mul_f32 v[72:73], v[30:31], v[10:11] op_sel_hi:[0,1]
	v_exp_f32_e32 v72, v72
	v_exp_f32_e32 v73, v73
	v_pk_mul_f32 v[86:87], v[30:31], v[12:13] op_sel_hi:[0,1]
	v_exp_f32_e32 v86, v86
	v_exp_f32_e32 v87, v87
	v_pk_mul_f32 v[72:73], v[72:73], v[122:123]
	v_pk_fma_f32 v[70:71], v[88:89], v[120:121], v[70:71]
	v_pk_fma_f32 v[122:123], v[34:35], v[74:75], v[72:73] op_sel_hi:[0,1,1]
	v_pk_mul_f32 v[72:73], v[86:87], v[110:111]
	v_pk_mul_f32 v[74:75], v[30:31], v[8:9] op_sel_hi:[0,1]
	v_pk_fma_f32 v[110:111], v[34:35], v[76:77], v[72:73] op_sel_hi:[0,1,1]
	v_pk_mul_f32 v[72:73], v[30:31], v[6:7] op_sel_hi:[0,1]
	v_exp_f32_e32 v72, v72
	v_exp_f32_e32 v73, v73
	v_exp_f32_e32 v74, v74
	v_exp_f32_e32 v75, v75
	s_waitcnt lgkmcnt(11)
	v_pk_fma_f32 v[70:71], v[90:91], v[122:123], v[70:71]
	v_pk_mul_f32 v[72:73], v[72:73], v[112:113]
	v_pk_fma_f32 v[70:71], v[92:93], v[110:111], v[70:71]
	v_pk_fma_f32 v[112:113], v[34:35], v[78:79], v[72:73] op_sel_hi:[0,1,1]
	v_pk_mul_f32 v[72:73], v[74:75], v[114:115]
	s_waitcnt lgkmcnt(10)
	v_pk_fma_f32 v[70:71], v[94:95], v[112:113], v[70:71]
	v_pk_fma_f32 v[114:115], v[34:35], v[80:81], v[72:73] op_sel_hi:[0,1,1]
	v_pk_mul_f32 v[72:73], v[30:31], v[2:3] op_sel_hi:[0,1]
	v_exp_f32_e32 v72, v72
	v_exp_f32_e32 v73, v73
	v_pk_mul_f32 v[30:31], v[30:31], v[4:5] op_sel_hi:[0,1]
	v_exp_f32_e32 v30, v30
	v_exp_f32_e32 v31, v31
	v_pk_mul_f32 v[72:73], v[72:73], v[116:117]
	v_pk_fma_f32 v[70:71], v[96:97], v[114:115], v[70:71]
	v_pk_fma_f32 v[116:117], v[34:35], v[82:83], v[72:73] op_sel_hi:[0,1,1]
	v_pk_mul_f32 v[30:31], v[30:31], v[118:119]
	s_waitcnt lgkmcnt(9)
	v_pk_fma_f32 v[70:71], v[98:99], v[116:117], v[70:71]
	v_pk_fma_f32 v[30:31], v[34:35], v[84:85], v[30:31] op_sel_hi:[0,1,1]
	v_pk_fma_f32 v[34:35], v[100:101], v[30:31], v[70:71]
	s_nop 0
	v_add_f32_e32 v34, v34, v35
	v_fma_mix_f32 v34, v1, v32, v34 op_sel_hi:[0,1,0]
	v_fma_mixlo_f16 v34, v34, v36, 0 op_sel_hi:[0,1,0]
	ds_write_b16 v68, v34 offset:24896
	ds_read_b128 v[70:73], v67 offset:2816
	ds_read_b128 v[74:77], v67 offset:2832
	ds_read_b128 v[78:81], v67 offset:2848
	ds_read_b128 v[82:85], v67 offset:2864
	ds_read_b128 v[86:89], v67 offset:2880
	ds_read_b128 v[90:93], v67 offset:2896
	ds_read_b128 v[94:97], v67 offset:2912
	ds_read_b128 v[98:101], v67 offset:2928
	v_cvt_f32_f16_sdwa v34, v40 dst_sel:DWORD dst_unused:UNUSED_PAD src0_sel:WORD_1
	v_cvt_f32_f16_sdwa v35, v32 dst_sel:DWORD dst_unused:UNUSED_PAD src0_sel:WORD_1
	v_pk_mul_f32 v[118:119], v[34:35], v[14:15] op_sel_hi:[0,1]
	v_exp_f32_e32 v118, v118
	v_exp_f32_e32 v119, v119
	v_pk_mul_f32 v[124:125], v[34:35], v[16:17] op_sel_hi:[0,1]
	v_exp_f32_e32 v124, v124
	v_exp_f32_e32 v125, v125
	v_mul_f32_e32 v40, v34, v35
	v_pk_mul_f32 v[38:39], v[118:119], v[38:39]
	s_waitcnt lgkmcnt(14)
	v_pk_fma_f32 v[38:39], v[40:41], v[42:43], v[38:39] op_sel_hi:[0,1,1]
	s_waitcnt lgkmcnt(12)
	v_pk_fma_f32 v[42:43], v[58:59], v[38:39], 0 op_sel_hi:[1,1,0]
	v_pk_mul_f32 v[58:59], v[124:125], v[120:121]
	s_nop 0
	v_pk_fma_f32 v[118:119], v[40:41], v[44:45], v[58:59] op_sel_hi:[0,1,1]
	v_pk_mul_f32 v[44:45], v[34:35], v[10:11] op_sel_hi:[0,1]
	v_exp_f32_e32 v44, v44
	v_exp_f32_e32 v45, v45
	v_pk_mul_f32 v[58:59], v[34:35], v[12:13] op_sel_hi:[0,1]
	v_exp_f32_e32 v58, v58
	v_exp_f32_e32 v59, v59
	v_pk_mul_f32 v[44:45], v[44:45], v[122:123]
	v_pk_fma_f32 v[42:43], v[60:61], v[118:119], v[42:43]
	v_pk_fma_f32 v[120:121], v[40:41], v[46:47], v[44:45] op_sel_hi:[0,1,1]
	v_pk_mul_f32 v[44:45], v[58:59], v[110:111]
	v_pk_mul_f32 v[46:47], v[34:35], v[8:9] op_sel_hi:[0,1]
	v_pk_fma_f32 v[110:111], v[40:41], v[48:49], v[44:45] op_sel_hi:[0,1,1]
	v_pk_mul_f32 v[44:45], v[34:35], v[6:7] op_sel_hi:[0,1]
	v_exp_f32_e32 v44, v44
	v_exp_f32_e32 v45, v45
	v_exp_f32_e32 v46, v46
	v_exp_f32_e32 v47, v47
	s_waitcnt lgkmcnt(11)
	v_pk_fma_f32 v[42:43], v[62:63], v[120:121], v[42:43]
	v_pk_mul_f32 v[44:45], v[44:45], v[112:113]
	v_pk_fma_f32 v[42:43], v[64:65], v[110:111], v[42:43]
	v_pk_fma_f32 v[112:113], v[40:41], v[50:51], v[44:45] op_sel_hi:[0,1,1]
	v_pk_mul_f32 v[44:45], v[46:47], v[114:115]
	s_waitcnt lgkmcnt(10)
	v_pk_fma_f32 v[42:43], v[102:103], v[112:113], v[42:43]
	v_pk_fma_f32 v[114:115], v[40:41], v[52:53], v[44:45] op_sel_hi:[0,1,1]
	v_pk_mul_f32 v[44:45], v[34:35], v[2:3] op_sel_hi:[0,1]
	v_exp_f32_e32 v44, v44
	v_exp_f32_e32 v45, v45
	v_pk_mul_f32 v[34:35], v[34:35], v[4:5] op_sel_hi:[0,1]
	v_exp_f32_e32 v34, v34
	v_exp_f32_e32 v35, v35
	v_pk_mul_f32 v[44:45], v[44:45], v[116:117]
	v_pk_fma_f32 v[42:43], v[104:105], v[114:115], v[42:43]
	v_pk_fma_f32 v[116:117], v[40:41], v[54:55], v[44:45] op_sel_hi:[0,1,1]
	v_pk_mul_f32 v[30:31], v[34:35], v[30:31]
	s_waitcnt lgkmcnt(9)
	v_pk_fma_f32 v[42:43], v[106:107], v[116:117], v[42:43]
	v_pk_fma_f32 v[30:31], v[40:41], v[56:57], v[30:31] op_sel_hi:[0,1,1]
	v_pk_fma_f32 v[34:35], v[108:109], v[30:31], v[42:43]
	s_nop 0
	v_add_f32_e32 v34, v34, v35
	v_fma_mix_f32 v32, v1, v32, v34 op_sel:[0,1,0] op_sel_hi:[0,1,0]
	v_fma_mixlo_f16 v32, v32, v36, 0 op_sel:[0,1,0] op_sel_hi:[0,1,0]
	ds_write_b16 v68, v32 offset:25936
	ds_read_b128 v[42:45], v67 offset:2944
	ds_read_b128 v[46:49], v67 offset:2960
	ds_read_b128 v[50:53], v67 offset:2976
	ds_read_b128 v[54:57], v67 offset:2992
	ds_read_b128 v[58:61], v67 offset:3008
	ds_read_b128 v[62:65], v67 offset:3024
	ds_read_b128 v[102:105], v67 offset:3040
	ds_read_b128 v[106:109], v67 offset:3056
	v_cvt_f32_f16_e32 v32, v41
	v_cvt_f32_f16_e32 v34, v33
	v_pk_mul_f32 v[122:123], v[32:33], v[14:15] op_sel_hi:[0,1]
	v_exp_f32_e32 v122, v122
	v_exp_f32_e32 v123, v123
	v_pk_mul_f32 v[124:125], v[32:33], v[16:17] op_sel_hi:[0,1]
	v_exp_f32_e32 v124, v124
	v_exp_f32_e32 v125, v125
	v_mul_f32_e32 v34, v32, v34
	v_pk_mul_f32 v[38:39], v[122:123], v[38:39]
	s_waitcnt lgkmcnt(14)
	v_pk_fma_f32 v[38:39], v[34:35], v[70:71], v[38:39] op_sel_hi:[0,1,1]
	s_waitcnt lgkmcnt(12)
	v_pk_fma_f32 v[70:71], v[86:87], v[38:39], 0 op_sel_hi:[1,1,0]
	v_pk_mul_f32 v[86:87], v[124:125], v[118:119]
	s_nop 0
	v_pk_fma_f32 v[118:119], v[34:35], v[72:73], v[86:87] op_sel_hi:[0,1,1]
	v_pk_mul_f32 v[72:73], v[32:33], v[10:11] op_sel_hi:[0,1]
	v_exp_f32_e32 v72, v72
	v_exp_f32_e32 v73, v73
	v_pk_mul_f32 v[86:87], v[32:33], v[12:13] op_sel_hi:[0,1]
	v_exp_f32_e32 v86, v86
	v_exp_f32_e32 v87, v87
	v_pk_mul_f32 v[72:73], v[72:73], v[120:121]
	v_pk_fma_f32 v[70:71], v[88:89], v[118:119], v[70:71]
	v_pk_fma_f32 v[120:121], v[34:35], v[74:75], v[72:73] op_sel_hi:[0,1,1]
	v_pk_mul_f32 v[72:73], v[86:87], v[110:111]
	v_pk_mul_f32 v[74:75], v[32:33], v[8:9] op_sel_hi:[0,1]
	v_pk_fma_f32 v[110:111], v[34:35], v[76:77], v[72:73] op_sel_hi:[0,1,1]
	v_pk_mul_f32 v[72:73], v[32:33], v[6:7] op_sel_hi:[0,1]
	v_exp_f32_e32 v72, v72
	v_exp_f32_e32 v73, v73
	v_exp_f32_e32 v74, v74
	v_exp_f32_e32 v75, v75
	s_waitcnt lgkmcnt(11)
	v_pk_fma_f32 v[70:71], v[90:91], v[120:121], v[70:71]
	v_pk_mul_f32 v[72:73], v[72:73], v[112:113]
	v_pk_fma_f32 v[70:71], v[92:93], v[110:111], v[70:71]
	v_pk_fma_f32 v[112:113], v[34:35], v[78:79], v[72:73] op_sel_hi:[0,1,1]
	v_pk_mul_f32 v[72:73], v[74:75], v[114:115]
	v_pk_mul_f32 v[74:75], v[32:33], v[4:5] op_sel_hi:[0,1]
	v_pk_fma_f32 v[114:115], v[34:35], v[80:81], v[72:73] op_sel_hi:[0,1,1]
	v_pk_mul_f32 v[72:73], v[32:33], v[2:3] op_sel_hi:[0,1]
	v_exp_f32_e32 v72, v72
	v_exp_f32_e32 v73, v73
	v_exp_f32_e32 v74, v74
	v_exp_f32_e32 v75, v75
	s_waitcnt lgkmcnt(10)
	v_pk_fma_f32 v[70:71], v[94:95], v[112:113], v[70:71]
	v_pk_mul_f32 v[72:73], v[72:73], v[116:117]
	v_pk_fma_f32 v[70:71], v[96:97], v[114:115], v[70:71]
	v_pk_fma_f32 v[116:117], v[34:35], v[82:83], v[72:73] op_sel_hi:[0,1,1]
	v_pk_mul_f32 v[30:31], v[74:75], v[30:31]
	s_waitcnt lgkmcnt(9)
	v_pk_fma_f32 v[70:71], v[98:99], v[116:117], v[70:71]
	v_pk_fma_f32 v[30:31], v[34:35], v[84:85], v[30:31] op_sel_hi:[0,1,1]
	v_pk_fma_f32 v[34:35], v[100:101], v[30:31], v[70:71]
	s_nop 0
	v_add_f32_e32 v32, v34, v35
	v_fma_mix_f32 v32, v1, v33, v32 op_sel_hi:[0,1,0]
	v_fma_mixlo_f16 v32, v32, v37, 0 op_sel_hi:[0,1,0]
	ds_write_b16 v68, v32 offset:26976
	ds_read_b128 v[70:73], v67 offset:3072
	ds_read_b128 v[74:77], v67 offset:3088
	ds_read_b128 v[78:81], v67 offset:3104
	ds_read_b128 v[82:85], v67 offset:3120
	ds_read_b128 v[86:89], v67 offset:3136
	ds_read_b128 v[90:93], v67 offset:3152
	ds_read_b128 v[94:97], v67 offset:3168
	ds_read_b128 v[98:101], v67 offset:3184
	v_cvt_f32_f16_sdwa v32, v41 dst_sel:DWORD dst_unused:UNUSED_PAD src0_sel:WORD_1
	v_cvt_f32_f16_sdwa v34, v33 dst_sel:DWORD dst_unused:UNUSED_PAD src0_sel:WORD_1
	v_pk_mul_f32 v[40:41], v[32:33], v[14:15] op_sel_hi:[0,1]
	v_pk_mul_f32 v[122:123], v[32:33], v[16:17] op_sel_hi:[0,1]
	v_exp_f32_e32 v40, v40
	v_exp_f32_e32 v41, v41
	v_exp_f32_e32 v122, v122
	v_exp_f32_e32 v123, v123
	v_mul_f32_e32 v34, v32, v34
	v_pk_mul_f32 v[38:39], v[40:41], v[38:39]
	v_pk_mul_f32 v[40:41], v[122:123], v[118:119]
	s_waitcnt lgkmcnt(14)
	v_pk_fma_f32 v[118:119], v[34:35], v[44:45], v[40:41] op_sel_hi:[0,1,1]
	v_pk_mul_f32 v[40:41], v[32:33], v[10:11] op_sel_hi:[0,1]
	v_pk_fma_f32 v[124:125], v[34:35], v[42:43], v[38:39] op_sel_hi:[0,1,1]
	v_exp_f32_e32 v40, v40
	v_exp_f32_e32 v41, v41
	v_pk_mul_f32 v[42:43], v[32:33], v[12:13] op_sel_hi:[0,1]
	v_exp_f32_e32 v42, v42
	v_exp_f32_e32 v43, v43
	s_waitcnt lgkmcnt(12)
	v_pk_fma_f32 v[38:39], v[58:59], v[124:125], 0 op_sel_hi:[1,1,0]
	v_pk_mul_f32 v[40:41], v[40:41], v[120:121]
	v_pk_fma_f32 v[38:39], v[60:61], v[118:119], v[38:39]
	v_pk_fma_f32 v[120:121], v[34:35], v[46:47], v[40:41] op_sel_hi:[0,1,1]
	v_pk_mul_f32 v[40:41], v[42:43], v[110:111]
	s_waitcnt lgkmcnt(11)
	v_pk_fma_f32 v[38:39], v[62:63], v[120:121], v[38:39]
	v_pk_fma_f32 v[62:63], v[34:35], v[48:49], v[40:41] op_sel_hi:[0,1,1]
	v_pk_mul_f32 v[40:41], v[32:33], v[6:7] op_sel_hi:[0,1]
	v_exp_f32_e32 v40, v40
	v_exp_f32_e32 v41, v41
	v_pk_mul_f32 v[42:43], v[32:33], v[8:9] op_sel_hi:[0,1]
	v_exp_f32_e32 v42, v42
	v_exp_f32_e32 v43, v43
	v_pk_mul_f32 v[40:41], v[40:41], v[112:113]
	v_pk_fma_f32 v[38:39], v[64:65], v[62:63], v[38:39]
	v_pk_fma_f32 v[64:65], v[34:35], v[50:51], v[40:41] op_sel_hi:[0,1,1]
	v_pk_mul_f32 v[40:41], v[42:43], v[114:115]
	s_waitcnt lgkmcnt(10)
	v_pk_fma_f32 v[38:39], v[102:103], v[64:65], v[38:39]
	v_pk_fma_f32 v[102:103], v[34:35], v[52:53], v[40:41] op_sel_hi:[0,1,1]
	v_pk_mul_f32 v[40:41], v[32:33], v[2:3] op_sel_hi:[0,1]
	v_exp_f32_e32 v40, v40
	v_exp_f32_e32 v41, v41
	v_pk_mul_f32 v[42:43], v[32:33], v[4:5] op_sel_hi:[0,1]
	v_exp_f32_e32 v42, v42
	v_exp_f32_e32 v43, v43
	v_pk_mul_f32 v[40:41], v[40:41], v[116:117]
	v_pk_fma_f32 v[38:39], v[104:105], v[102:103], v[38:39]
	v_pk_fma_f32 v[104:105], v[34:35], v[54:55], v[40:41] op_sel_hi:[0,1,1]
	v_pk_mul_f32 v[30:31], v[42:43], v[30:31]
	s_waitcnt lgkmcnt(9)
	v_pk_fma_f32 v[38:39], v[106:107], v[104:105], v[38:39]
	v_pk_fma_f32 v[106:107], v[34:35], v[56:57], v[30:31] op_sel_hi:[0,1,1]
	v_pk_fma_f32 v[30:31], v[108:109], v[106:107], v[38:39]
	s_nop 0
	v_add_f32_e32 v30, v30, v31
	v_fma_mix_f32 v30, v1, v33, v30 op_sel:[0,1,0] op_sel_hi:[0,1,0]
	v_fma_mixlo_f16 v30, v30, v37, 0 op_sel:[0,1,0] op_sel_hi:[0,1,0]
	ds_write_b16 v68, v30 offset:28016
	ds_read_b128 v[30:33], v67 offset:3200
	ds_read_b128 v[34:37], v67 offset:3216
	ds_read_b128 v[38:41], v67 offset:3232
	ds_read_b128 v[42:45], v67 offset:3248
	ds_read_b128 v[46:49], v67 offset:3264
	ds_read_b128 v[50:53], v67 offset:3280
	ds_read_b128 v[54:57], v67 offset:3296
	ds_read_b128 v[58:61], v67 offset:3312
	s_waitcnt vmcnt(2)
	v_cvt_f32_f16_e32 v108, v26
	s_waitcnt vmcnt(1)
	v_cvt_f32_f16_e32 v69, v18
	v_pk_mul_f32 v[112:113], v[108:109], v[14:15] op_sel_hi:[0,1]
	v_exp_f32_e32 v112, v112
	v_exp_f32_e32 v113, v113
	v_pk_mul_f32 v[114:115], v[108:109], v[16:17] op_sel_hi:[0,1]
	v_exp_f32_e32 v114, v114
	v_exp_f32_e32 v115, v115
	v_mul_f32_e32 v110, v108, v69
	v_pk_mul_f32 v[112:113], v[112:113], v[124:125]
	s_waitcnt lgkmcnt(14)
	v_pk_fma_f32 v[112:113], v[110:111], v[70:71], v[112:113] op_sel_hi:[0,1,1]
	s_waitcnt lgkmcnt(12)
	v_pk_fma_f32 v[70:71], v[86:87], v[112:113], 0 op_sel_hi:[1,1,0]
	v_pk_mul_f32 v[86:87], v[114:115], v[118:119]
	s_nop 0
	v_pk_fma_f32 v[114:115], v[110:111], v[72:73], v[86:87] op_sel_hi:[0,1,1]
	v_pk_mul_f32 v[72:73], v[108:109], v[10:11] op_sel_hi:[0,1]
	v_exp_f32_e32 v72, v72
	v_exp_f32_e32 v73, v73
	v_pk_mul_f32 v[86:87], v[108:109], v[12:13] op_sel_hi:[0,1]
	v_exp_f32_e32 v86, v86
	v_exp_f32_e32 v87, v87
	v_pk_mul_f32 v[72:73], v[72:73], v[120:121]
	v_pk_fma_f32 v[70:71], v[88:89], v[114:115], v[70:71]
	v_pk_fma_f32 v[116:117], v[110:111], v[74:75], v[72:73] op_sel_hi:[0,1,1]
	v_pk_mul_f32 v[62:63], v[86:87], v[62:63]
	s_waitcnt lgkmcnt(11)
	v_pk_fma_f32 v[70:71], v[90:91], v[116:117], v[70:71]
	v_pk_fma_f32 v[118:119], v[110:111], v[76:77], v[62:63] op_sel_hi:[0,1,1]
	v_pk_fma_f32 v[62:63], v[92:93], v[118:119], v[70:71]
	v_pk_mul_f32 v[70:71], v[108:109], v[6:7] op_sel_hi:[0,1]
	v_exp_f32_e32 v70, v70
	v_exp_f32_e32 v71, v71
	v_pk_mul_f32 v[72:73], v[108:109], v[8:9] op_sel_hi:[0,1]
	v_exp_f32_e32 v72, v72
	v_exp_f32_e32 v73, v73
	v_pk_mul_f32 v[64:65], v[70:71], v[64:65]
	v_pk_mul_f32 v[70:71], v[108:109], v[4:5] op_sel_hi:[0,1]
	v_pk_fma_f32 v[120:121], v[110:111], v[78:79], v[64:65] op_sel_hi:[0,1,1]
	v_pk_mul_f32 v[64:65], v[72:73], v[102:103]
	v_exp_f32_e32 v70, v70
	v_pk_fma_f32 v[102:103], v[110:111], v[80:81], v[64:65] op_sel_hi:[0,1,1]
	v_pk_mul_f32 v[64:65], v[108:109], v[2:3] op_sel_hi:[0,1]
	v_exp_f32_e32 v64, v64
	v_exp_f32_e32 v65, v65
	v_exp_f32_e32 v71, v71
	s_waitcnt lgkmcnt(10)
	v_pk_fma_f32 v[62:63], v[94:95], v[120:121], v[62:63]
	v_pk_mul_f32 v[64:65], v[64:65], v[104:105]
	v_pk_fma_f32 v[62:63], v[96:97], v[102:103], v[62:63]
	v_pk_fma_f32 v[104:105], v[110:111], v[82:83], v[64:65] op_sel_hi:[0,1,1]
	v_pk_mul_f32 v[64:65], v[70:71], v[106:107]
	s_waitcnt lgkmcnt(9)
	v_pk_fma_f32 v[62:63], v[98:99], v[104:105], v[62:63]
	v_pk_fma_f32 v[98:99], v[110:111], v[84:85], v[64:65] op_sel_hi:[0,1,1]
	v_pk_fma_f32 v[62:63], v[100:101], v[98:99], v[62:63]
	s_nop 0
	v_add_f32_e32 v62, v62, v63
	v_fma_mix_f32 v62, v1, v18, v62 op_sel_hi:[0,1,0]
	s_waitcnt vmcnt(0)
	v_fma_mixlo_f16 v62, v62, v22, 0 op_sel_hi:[0,1,0]
	ds_write_b16 v68, v62 offset:29056
	v_lshrrev_b32_e32 v196, 6, v0
	v_and_b32_e32 v197, 48, v0
	v_lshl_or_b32 v196, v196, 7, v197
	v_and_b32_e32 v197, 15, v0
	v_or_b32_e32 v197, s28, v197
	v_lshl_or_b32 v196, v197, 10, v196
	v_add_u32_e32 v197, 0x4000, v196
	global_load_dwordx4 v[180:183], v196, s[4:5]
	global_load_dwordx4 v[184:187], v196, s[4:5] offset:64
	global_load_dwordx4 v[188:191], v197, s[4:5]
	global_load_dwordx4 v[192:195], v197, s[4:5] offset:64
	v_and_b32_e32 v196, 63, v0
	v_lshlrev_b32_e32 v196, 4, v196
	global_load_dwordx4 v[204:207], v196, s[6:7]
	global_load_dwordx4 v[208:211], v196, s[8:9]
	ds_read_b128 v[62:65], v67 offset:3328
	ds_read_b128 v[70:73], v67 offset:3344
	ds_read_b128 v[74:77], v67 offset:3360
	ds_read_b128 v[78:81], v67 offset:3376
	ds_read_b128 v[82:85], v67 offset:3392
	ds_read_b128 v[86:89], v67 offset:3408
	ds_read_b128 v[90:93], v67 offset:3424
	ds_read_b128 v[94:97], v67 offset:3440
	v_cvt_f32_f16_sdwa v26, v26 dst_sel:DWORD dst_unused:UNUSED_PAD src0_sel:WORD_1
	v_cvt_f32_f16_sdwa v69, v18 dst_sel:DWORD dst_unused:UNUSED_PAD src0_sel:WORD_1
	v_pk_mul_f32 v[106:107], v[26:27], v[14:15] op_sel_hi:[0,1]
	v_exp_f32_e32 v106, v106
	v_exp_f32_e32 v107, v107
	v_pk_mul_f32 v[108:109], v[26:27], v[16:17] op_sel_hi:[0,1]
	v_exp_f32_e32 v108, v108
	v_exp_f32_e32 v109, v109
	v_mul_f32_e32 v100, v26, v69
	v_pk_mul_f32 v[106:107], v[106:107], v[112:113]
	s_waitcnt lgkmcnt(14)
	v_pk_fma_f32 v[106:107], v[100:101], v[30:31], v[106:107] op_sel_hi:[0,1,1]
	s_waitcnt lgkmcnt(12)
	v_pk_fma_f32 v[30:31], v[46:47], v[106:107], 0 op_sel_hi:[1,1,0]
	v_pk_mul_f32 v[46:47], v[108:109], v[114:115]
	s_nop 0
	v_pk_fma_f32 v[108:109], v[100:101], v[32:33], v[46:47] op_sel_hi:[0,1,1]
	v_pk_mul_f32 v[32:33], v[26:27], v[10:11] op_sel_hi:[0,1]
	v_exp_f32_e32 v32, v32
	v_exp_f32_e32 v33, v33
	v_pk_mul_f32 v[46:47], v[26:27], v[12:13] op_sel_hi:[0,1]
	v_exp_f32_e32 v46, v46
	v_exp_f32_e32 v47, v47
	v_pk_mul_f32 v[32:33], v[32:33], v[116:117]
	v_pk_fma_f32 v[30:31], v[48:49], v[108:109], v[30:31]
	v_pk_fma_f32 v[110:111], v[100:101], v[34:35], v[32:33] op_sel_hi:[0,1,1]
	v_pk_mul_f32 v[32:33], v[46:47], v[118:119]
	v_pk_mul_f32 v[34:35], v[26:27], v[8:9] op_sel_hi:[0,1]
	v_pk_fma_f32 v[112:113], v[100:101], v[36:37], v[32:33] op_sel_hi:[0,1,1]
	v_pk_mul_f32 v[32:33], v[26:27], v[6:7] op_sel_hi:[0,1]
	v_exp_f32_e32 v32, v32
	v_exp_f32_e32 v33, v33
	v_exp_f32_e32 v34, v34
	v_exp_f32_e32 v35, v35
	s_waitcnt lgkmcnt(11)
	v_pk_fma_f32 v[30:31], v[50:51], v[110:111], v[30:31]
	v_pk_mul_f32 v[32:33], v[32:33], v[120:121]
	v_pk_fma_f32 v[30:31], v[52:53], v[112:113], v[30:31]
	v_pk_fma_f32 v[114:115], v[100:101], v[38:39], v[32:33] op_sel_hi:[0,1,1]
	v_pk_mul_f32 v[32:33], v[34:35], v[102:103]
	v_pk_mul_f32 v[34:35], v[26:27], v[4:5] op_sel_hi:[0,1]
	v_pk_fma_f32 v[102:103], v[100:101], v[40:41], v[32:33] op_sel_hi:[0,1,1]
	v_pk_mul_f32 v[32:33], v[26:27], v[2:3] op_sel_hi:[0,1]
	v_exp_f32_e32 v32, v32
	v_exp_f32_e32 v33, v33
	v_exp_f32_e32 v34, v34
	v_exp_f32_e32 v35, v35
	s_waitcnt lgkmcnt(10)
	v_pk_fma_f32 v[30:31], v[54:55], v[114:115], v[30:31]
	v_pk_mul_f32 v[32:33], v[32:33], v[104:105]
	v_pk_fma_f32 v[30:31], v[56:57], v[102:103], v[30:31]
	v_pk_fma_f32 v[104:105], v[100:101], v[42:43], v[32:33] op_sel_hi:[0,1,1]
	v_pk_mul_f32 v[32:33], v[34:35], v[98:99]
	s_waitcnt lgkmcnt(9)
	v_pk_fma_f32 v[30:31], v[58:59], v[104:105], v[30:31]
	v_pk_fma_f32 v[98:99], v[100:101], v[44:45], v[32:33] op_sel_hi:[0,1,1]
	v_pk_fma_f32 v[30:31], v[60:61], v[98:99], v[30:31]
	s_nop 0
	v_add_f32_e32 v26, v30, v31
	v_fma_mix_f32 v18, v1, v18, v26 op_sel:[0,1,0] op_sel_hi:[0,1,0]
	v_fma_mixlo_f16 v18, v18, v22, 0 op_sel:[0,1,0] op_sel_hi:[0,1,0]
	ds_write_b16 v68, v18 offset:30096
	ds_read_b128 v[30:33], v67 offset:3456
	ds_read_b128 v[34:37], v67 offset:3472
	ds_read_b128 v[38:41], v67 offset:3488
	ds_read_b128 v[42:45], v67 offset:3504
	ds_read_b128 v[46:49], v67 offset:3520
	ds_read_b128 v[50:53], v67 offset:3536
	ds_read_b128 v[54:57], v67 offset:3552
	ds_read_b128 v[58:61], v67 offset:3568
	v_cvt_f32_f16_e32 v18, v27
	v_cvt_f32_f16_e32 v22, v19
	v_pk_mul_f32 v[100:101], v[18:19], v[14:15] op_sel_hi:[0,1]
	v_exp_f32_e32 v100, v100
	v_exp_f32_e32 v101, v101
	v_pk_mul_f32 v[116:117], v[18:19], v[16:17] op_sel_hi:[0,1]
	v_exp_f32_e32 v116, v116
	v_exp_f32_e32 v117, v117
	v_mul_f32_e32 v22, v18, v22
	v_pk_mul_f32 v[100:101], v[100:101], v[106:107]
	s_waitcnt lgkmcnt(14)
	v_pk_fma_f32 v[100:101], v[22:23], v[62:63], v[100:101] op_sel_hi:[0,1,1]
	s_waitcnt lgkmcnt(12)
	v_pk_fma_f32 v[62:63], v[82:83], v[100:101], 0 op_sel_hi:[1,1,0]
	v_pk_mul_f32 v[82:83], v[116:117], v[108:109]
	s_nop 0
	v_pk_fma_f32 v[106:107], v[22:23], v[64:65], v[82:83] op_sel_hi:[0,1,1]
	v_pk_mul_f32 v[64:65], v[18:19], v[10:11] op_sel_hi:[0,1]
	v_exp_f32_e32 v64, v64
	v_exp_f32_e32 v65, v65
	v_pk_mul_f32 v[82:83], v[18:19], v[12:13] op_sel_hi:[0,1]
	v_exp_f32_e32 v82, v82
	v_exp_f32_e32 v83, v83
	v_pk_mul_f32 v[64:65], v[64:65], v[110:111]
	v_pk_fma_f32 v[62:63], v[84:85], v[106:107], v[62:63]
	v_pk_fma_f32 v[108:109], v[22:23], v[70:71], v[64:65] op_sel_hi:[0,1,1]
	v_pk_mul_f32 v[64:65], v[82:83], v[112:113]
	v_pk_mul_f32 v[70:71], v[18:19], v[8:9] op_sel_hi:[0,1]
	v_pk_fma_f32 v[110:111], v[22:23], v[72:73], v[64:65] op_sel_hi:[0,1,1]
	v_pk_mul_f32 v[64:65], v[18:19], v[6:7] op_sel_hi:[0,1]
	v_exp_f32_e32 v64, v64
	v_exp_f32_e32 v65, v65
	v_exp_f32_e32 v70, v70
	v_exp_f32_e32 v71, v71
	s_waitcnt lgkmcnt(11)
	v_pk_fma_f32 v[62:63], v[86:87], v[108:109], v[62:63]
	v_pk_mul_f32 v[64:65], v[64:65], v[114:115]
	v_pk_fma_f32 v[62:63], v[88:89], v[110:111], v[62:63]
	v_pk_fma_f32 v[112:113], v[22:23], v[74:75], v[64:65] op_sel_hi:[0,1,1]
	v_pk_mul_f32 v[64:65], v[70:71], v[102:103]
	v_pk_mul_f32 v[70:71], v[18:19], v[4:5] op_sel_hi:[0,1]
	v_pk_fma_f32 v[102:103], v[22:23], v[76:77], v[64:65] op_sel_hi:[0,1,1]
	v_pk_mul_f32 v[64:65], v[18:19], v[2:3] op_sel_hi:[0,1]
	v_exp_f32_e32 v64, v64
	v_exp_f32_e32 v65, v65
	v_exp_f32_e32 v70, v70
	v_exp_f32_e32 v71, v71
	s_waitcnt lgkmcnt(10)
	v_pk_fma_f32 v[62:63], v[90:91], v[112:113], v[62:63]
	v_pk_mul_f32 v[64:65], v[64:65], v[104:105]
	v_pk_fma_f32 v[62:63], v[92:93], v[102:103], v[62:63]
	v_pk_fma_f32 v[104:105], v[22:23], v[78:79], v[64:65] op_sel_hi:[0,1,1]
	v_pk_mul_f32 v[64:65], v[70:71], v[98:99]
	s_waitcnt lgkmcnt(9)
	v_pk_fma_f32 v[62:63], v[94:95], v[104:105], v[62:63]
	v_pk_fma_f32 v[98:99], v[22:23], v[80:81], v[64:65] op_sel_hi:[0,1,1]
	v_pk_fma_f32 v[62:63], v[96:97], v[98:99], v[62:63]
	s_nop 0
	v_add_f32_e32 v18, v62, v63
	v_fma_mix_f32 v18, v1, v19, v18 op_sel_hi:[0,1,0]
	v_fma_mixlo_f16 v18, v18, v23, 0 op_sel_hi:[0,1,0]
	ds_write_b16 v68, v18 offset:31136
	ds_read_b128 v[62:65], v67 offset:3584
	ds_read_b128 v[70:73], v67 offset:3600
	ds_read_b128 v[74:77], v67 offset:3616
	ds_read_b128 v[78:81], v67 offset:3632
	ds_read_b128 v[82:85], v67 offset:3648
	ds_read_b128 v[86:89], v67 offset:3664
	ds_read_b128 v[90:93], v67 offset:3680
	ds_read_b128 v[94:97], v67 offset:3696
	v_cvt_f32_f16_sdwa v18, v27 dst_sel:DWORD dst_unused:UNUSED_PAD src0_sel:WORD_1
	v_cvt_f32_f16_sdwa v22, v19 dst_sel:DWORD dst_unused:UNUSED_PAD src0_sel:WORD_1
	v_pk_mul_f32 v[26:27], v[18:19], v[14:15] op_sel_hi:[0,1]
	v_exp_f32_e32 v26, v26
	v_exp_f32_e32 v27, v27
	v_pk_mul_f32 v[114:115], v[18:19], v[16:17] op_sel_hi:[0,1]
	v_exp_f32_e32 v114, v114
	v_exp_f32_e32 v115, v115
	v_mul_f32_e32 v22, v18, v22
	v_pk_mul_f32 v[26:27], v[26:27], v[100:101]
	s_waitcnt lgkmcnt(14)
	v_pk_fma_f32 v[26:27], v[22:23], v[30:31], v[26:27] op_sel_hi:[0,1,1]
	s_waitcnt lgkmcnt(12)
	v_pk_fma_f32 v[30:31], v[46:47], v[26:27], 0 op_sel_hi:[1,1,0]
	v_pk_mul_f32 v[46:47], v[114:115], v[106:107]
	s_nop 0
	v_pk_fma_f32 v[100:101], v[22:23], v[32:33], v[46:47] op_sel_hi:[0,1,1]
	v_pk_mul_f32 v[32:33], v[18:19], v[10:11] op_sel_hi:[0,1]
	v_exp_f32_e32 v32, v32
	v_exp_f32_e32 v33, v33
	v_pk_mul_f32 v[46:47], v[18:19], v[12:13] op_sel_hi:[0,1]
	v_exp_f32_e32 v46, v46
	v_exp_f32_e32 v47, v47
	v_pk_mul_f32 v[32:33], v[32:33], v[108:109]
	v_pk_fma_f32 v[30:31], v[48:49], v[100:101], v[30:31]
	v_pk_fma_f32 v[106:107], v[22:23], v[34:35], v[32:33] op_sel_hi:[0,1,1]
	v_pk_mul_f32 v[32:33], v[46:47], v[110:111]
	v_pk_mul_f32 v[34:35], v[18:19], v[8:9] op_sel_hi:[0,1]
	v_pk_fma_f32 v[108:109], v[22:23], v[36:37], v[32:33] op_sel_hi:[0,1,1]
	v_pk_mul_f32 v[32:33], v[18:19], v[6:7] op_sel_hi:[0,1]
	v_exp_f32_e32 v32, v32
	v_exp_f32_e32 v33, v33
	v_exp_f32_e32 v34, v34
	v_exp_f32_e32 v35, v35
	s_waitcnt lgkmcnt(11)
	v_pk_fma_f32 v[30:31], v[50:51], v[106:107], v[30:31]
	v_pk_mul_f32 v[32:33], v[32:33], v[112:113]
	v_pk_fma_f32 v[30:31], v[52:53], v[108:109], v[30:31]
	v_pk_fma_f32 v[110:111], v[22:23], v[38:39], v[32:33] op_sel_hi:[0,1,1]
	v_pk_mul_f32 v[32:33], v[34:35], v[102:103]
	v_pk_mul_f32 v[34:35], v[18:19], v[4:5] op_sel_hi:[0,1]
	v_pk_fma_f32 v[102:103], v[22:23], v[40:41], v[32:33] op_sel_hi:[0,1,1]
	v_pk_mul_f32 v[32:33], v[18:19], v[2:3] op_sel_hi:[0,1]
	v_exp_f32_e32 v32, v32
	v_exp_f32_e32 v33, v33
	v_exp_f32_e32 v34, v34
	v_exp_f32_e32 v35, v35
	s_waitcnt lgkmcnt(10)
	v_pk_fma_f32 v[30:31], v[54:55], v[110:111], v[30:31]
	v_pk_mul_f32 v[32:33], v[32:33], v[104:105]
	v_pk_fma_f32 v[30:31], v[56:57], v[102:103], v[30:31]
	v_pk_fma_f32 v[104:105], v[22:23], v[42:43], v[32:33] op_sel_hi:[0,1,1]
	v_pk_mul_f32 v[32:33], v[34:35], v[98:99]
	s_waitcnt lgkmcnt(9)
	v_pk_fma_f32 v[30:31], v[58:59], v[104:105], v[30:31]
	v_pk_fma_f32 v[98:99], v[22:23], v[44:45], v[32:33] op_sel_hi:[0,1,1]
	v_pk_fma_f32 v[30:31], v[60:61], v[98:99], v[30:31]
	s_nop 0
	v_add_f32_e32 v18, v30, v31
	v_fma_mix_f32 v18, v1, v19, v18 op_sel:[0,1,0] op_sel_hi:[0,1,0]
	v_fma_mixlo_f16 v18, v18, v23, 0 op_sel:[0,1,0] op_sel_hi:[0,1,0]
	ds_write_b16 v68, v18 offset:32176
	ds_read_b128 v[30:33], v67 offset:3712
	ds_read_b128 v[34:37], v67 offset:3728
	ds_read_b128 v[38:41], v67 offset:3744
	ds_read_b128 v[42:45], v67 offset:3760
	ds_read_b128 v[46:49], v67 offset:3776
	ds_read_b128 v[50:53], v67 offset:3792
	ds_read_b128 v[54:57], v67 offset:3808
	ds_read_b128 v[58:61], v67 offset:3824
	v_cvt_f32_f16_e32 v18, v28
	v_cvt_f32_f16_e32 v19, v20
	v_pk_mul_f32 v[112:113], v[18:19], v[14:15] op_sel_hi:[0,1]
	v_exp_f32_e32 v112, v112
	v_exp_f32_e32 v113, v113
	v_pk_mul_f32 v[114:115], v[18:19], v[16:17] op_sel_hi:[0,1]
	v_exp_f32_e32 v114, v114
	v_exp_f32_e32 v115, v115
	v_mul_f32_e32 v22, v18, v19
	v_pk_mul_f32 v[26:27], v[112:113], v[26:27]
	s_waitcnt lgkmcnt(14)
	v_pk_fma_f32 v[26:27], v[22:23], v[62:63], v[26:27] op_sel_hi:[0,1,1]
	s_waitcnt lgkmcnt(12)
	v_pk_fma_f32 v[62:63], v[82:83], v[26:27], 0 op_sel_hi:[1,1,0]
	v_pk_mul_f32 v[82:83], v[114:115], v[100:101]
	s_nop 0
	v_pk_fma_f32 v[100:101], v[22:23], v[64:65], v[82:83] op_sel_hi:[0,1,1]
	v_pk_mul_f32 v[64:65], v[18:19], v[10:11] op_sel_hi:[0,1]
	v_exp_f32_e32 v64, v64
	v_exp_f32_e32 v65, v65
	v_pk_mul_f32 v[82:83], v[18:19], v[12:13] op_sel_hi:[0,1]
	v_exp_f32_e32 v82, v82
	v_exp_f32_e32 v83, v83
	v_pk_mul_f32 v[64:65], v[64:65], v[106:107]
	v_pk_fma_f32 v[62:63], v[84:85], v[100:101], v[62:63]
	v_pk_fma_f32 v[106:107], v[22:23], v[70:71], v[64:65] op_sel_hi:[0,1,1]
	v_pk_mul_f32 v[64:65], v[82:83], v[108:109]
	v_pk_mul_f32 v[70:71], v[18:19], v[8:9] op_sel_hi:[0,1]
	v_pk_fma_f32 v[108:109], v[22:23], v[72:73], v[64:65] op_sel_hi:[0,1,1]
	v_pk_mul_f32 v[64:65], v[18:19], v[6:7] op_sel_hi:[0,1]
	v_exp_f32_e32 v64, v64
	v_exp_f32_e32 v65, v65
	v_exp_f32_e32 v70, v70
	v_exp_f32_e32 v71, v71
	s_waitcnt lgkmcnt(11)
	v_pk_fma_f32 v[62:63], v[86:87], v[106:107], v[62:63]
	v_pk_mul_f32 v[64:65], v[64:65], v[110:111]
	v_pk_fma_f32 v[62:63], v[88:89], v[108:109], v[62:63]
	v_pk_fma_f32 v[110:111], v[22:23], v[74:75], v[64:65] op_sel_hi:[0,1,1]
	v_pk_mul_f32 v[64:65], v[70:71], v[102:103]
	s_waitcnt lgkmcnt(10)
	v_pk_fma_f32 v[62:63], v[90:91], v[110:111], v[62:63]
	v_pk_fma_f32 v[102:103], v[22:23], v[76:77], v[64:65] op_sel_hi:[0,1,1]
	v_pk_mul_f32 v[64:65], v[18:19], v[2:3] op_sel_hi:[0,1]
	v_exp_f32_e32 v64, v64
	v_exp_f32_e32 v65, v65
	v_pk_mul_f32 v[18:19], v[18:19], v[4:5] op_sel_hi:[0,1]
	v_exp_f32_e32 v18, v18
	v_exp_f32_e32 v19, v19
	v_pk_mul_f32 v[64:65], v[64:65], v[104:105]
	v_pk_fma_f32 v[62:63], v[92:93], v[102:103], v[62:63]
	v_pk_fma_f32 v[104:105], v[22:23], v[78:79], v[64:65] op_sel_hi:[0,1,1]
	v_pk_mul_f32 v[18:19], v[18:19], v[98:99]
	s_waitcnt lgkmcnt(9)
	v_pk_fma_f32 v[62:63], v[94:95], v[104:105], v[62:63]
	v_pk_fma_f32 v[18:19], v[22:23], v[80:81], v[18:19] op_sel_hi:[0,1,1]
	v_pk_fma_f32 v[22:23], v[96:97], v[18:19], v[62:63]
	s_nop 0
	v_add_f32_e32 v22, v22, v23
	v_fma_mix_f32 v22, v1, v20, v22 op_sel_hi:[0,1,0]
	v_fma_mixlo_f16 v22, v22, v24, 0 op_sel_hi:[0,1,0]
	ds_write_b16 v68, v22 offset:33216
	ds_read_b128 v[62:65], v67 offset:3840
	ds_read_b128 v[70:73], v67 offset:3856
	ds_read_b128 v[74:77], v67 offset:3872
	ds_read_b128 v[78:81], v67 offset:3888
	ds_read_b128 v[82:85], v67 offset:3904
	ds_read_b128 v[86:89], v67 offset:3920
	ds_read_b128 v[90:93], v67 offset:3936
	ds_read_b128 v[94:97], v67 offset:3952
	v_cvt_f32_f16_sdwa v22, v28 dst_sel:DWORD dst_unused:UNUSED_PAD src0_sel:WORD_1
	v_cvt_f32_f16_sdwa v23, v20 dst_sel:DWORD dst_unused:UNUSED_PAD src0_sel:WORD_1
	v_pk_mul_f32 v[98:99], v[22:23], v[14:15] op_sel_hi:[0,1]
	v_exp_f32_e32 v98, v98
	v_exp_f32_e32 v99, v99
	v_pk_mul_f32 v[112:113], v[22:23], v[16:17] op_sel_hi:[0,1]
	v_exp_f32_e32 v112, v112
	v_exp_f32_e32 v113, v113
	v_mul_f32_e32 v28, v22, v23
	v_pk_mul_f32 v[26:27], v[98:99], v[26:27]
	s_waitcnt lgkmcnt(14)
	v_pk_fma_f32 v[26:27], v[28:29], v[30:31], v[26:27] op_sel_hi:[0,1,1]
	s_waitcnt lgkmcnt(12)
	v_pk_fma_f32 v[30:31], v[46:47], v[26:27], 0 op_sel_hi:[1,1,0]
	v_pk_mul_f32 v[46:47], v[112:113], v[100:101]
	s_nop 0
	v_pk_fma_f32 v[98:99], v[28:29], v[32:33], v[46:47] op_sel_hi:[0,1,1]
	v_pk_mul_f32 v[32:33], v[22:23], v[10:11] op_sel_hi:[0,1]
	v_exp_f32_e32 v32, v32
	v_exp_f32_e32 v33, v33
	v_pk_mul_f32 v[46:47], v[22:23], v[12:13] op_sel_hi:[0,1]
	v_exp_f32_e32 v46, v46
	v_exp_f32_e32 v47, v47
	v_pk_mul_f32 v[32:33], v[32:33], v[106:107]
	v_pk_fma_f32 v[30:31], v[48:49], v[98:99], v[30:31]
	v_pk_fma_f32 v[100:101], v[28:29], v[34:35], v[32:33] op_sel_hi:[0,1,1]
	v_pk_mul_f32 v[32:33], v[46:47], v[108:109]
	v_pk_mul_f32 v[34:35], v[22:23], v[8:9] op_sel_hi:[0,1]
	v_pk_fma_f32 v[106:107], v[28:29], v[36:37], v[32:33] op_sel_hi:[0,1,1]
	v_pk_mul_f32 v[32:33], v[22:23], v[6:7] op_sel_hi:[0,1]
	v_exp_f32_e32 v32, v32
	v_exp_f32_e32 v33, v33
	v_exp_f32_e32 v34, v34
	v_exp_f32_e32 v35, v35
	s_waitcnt lgkmcnt(11)
	v_pk_fma_f32 v[30:31], v[50:51], v[100:101], v[30:31]
	v_pk_mul_f32 v[32:33], v[32:33], v[110:111]
	v_pk_fma_f32 v[30:31], v[52:53], v[106:107], v[30:31]
	v_pk_fma_f32 v[108:109], v[28:29], v[38:39], v[32:33] op_sel_hi:[0,1,1]
	v_pk_mul_f32 v[32:33], v[34:35], v[102:103]
	s_waitcnt lgkmcnt(10)
	v_pk_fma_f32 v[30:31], v[54:55], v[108:109], v[30:31]
	v_pk_fma_f32 v[102:103], v[28:29], v[40:41], v[32:33] op_sel_hi:[0,1,1]
	v_pk_mul_f32 v[32:33], v[22:23], v[2:3] op_sel_hi:[0,1]
	v_exp_f32_e32 v32, v32
	v_exp_f32_e32 v33, v33
	v_pk_mul_f32 v[22:23], v[22:23], v[4:5] op_sel_hi:[0,1]
	v_exp_f32_e32 v22, v22
	v_exp_f32_e32 v23, v23
	v_pk_mul_f32 v[32:33], v[32:33], v[104:105]
	v_pk_fma_f32 v[30:31], v[56:57], v[102:103], v[30:31]
	v_pk_fma_f32 v[104:105], v[28:29], v[42:43], v[32:33] op_sel_hi:[0,1,1]
	v_pk_mul_f32 v[18:19], v[22:23], v[18:19]
	s_waitcnt lgkmcnt(9)
	v_pk_fma_f32 v[30:31], v[58:59], v[104:105], v[30:31]
	v_pk_fma_f32 v[18:19], v[28:29], v[44:45], v[18:19] op_sel_hi:[0,1,1]
	v_pk_fma_f32 v[22:23], v[60:61], v[18:19], v[30:31]
	s_nop 0
	v_add_f32_e32 v22, v22, v23
	v_fma_mix_f32 v20, v1, v20, v22 op_sel:[0,1,0] op_sel_hi:[0,1,0]
	v_fma_mixlo_f16 v20, v20, v24, 0 op_sel:[0,1,0] op_sel_hi:[0,1,0]
	ds_write_b16 v68, v20 offset:34256
	ds_read_b128 v[30:33], v67 offset:3968
	ds_read_b128 v[34:37], v67 offset:3984
	ds_read_b128 v[38:41], v67 offset:4000
	ds_read_b128 v[42:45], v67 offset:4016
	ds_read_b128 v[46:49], v67 offset:4032
	ds_read_b128 v[50:53], v67 offset:4048
	ds_read_b128 v[54:57], v67 offset:4064
	ds_read_b128 v[58:61], v67 offset:4080
	v_cvt_f32_f16_e32 v20, v29
	v_cvt_f32_f16_e32 v22, v21
	v_pk_mul_f32 v[110:111], v[20:21], v[14:15] op_sel_hi:[0,1]
	v_exp_f32_e32 v110, v110
	v_exp_f32_e32 v111, v111
	v_pk_mul_f32 v[112:113], v[20:21], v[16:17] op_sel_hi:[0,1]
	v_exp_f32_e32 v112, v112
	v_exp_f32_e32 v113, v113
	v_mul_f32_e32 v22, v20, v22
	v_pk_mul_f32 v[26:27], v[110:111], v[26:27]
	s_waitcnt lgkmcnt(14)
	v_pk_fma_f32 v[26:27], v[22:23], v[62:63], v[26:27] op_sel_hi:[0,1,1]
	s_waitcnt lgkmcnt(12)
	v_pk_fma_f32 v[62:63], v[82:83], v[26:27], 0 op_sel_hi:[1,1,0]
	v_pk_mul_f32 v[82:83], v[112:113], v[98:99]
	s_nop 0
	v_pk_fma_f32 v[64:65], v[22:23], v[64:65], v[82:83] op_sel_hi:[0,1,1]
	v_pk_mul_f32 v[82:83], v[20:21], v[10:11] op_sel_hi:[0,1]
	v_pk_fma_f32 v[62:63], v[84:85], v[64:65], v[62:63]
	v_exp_f32_e32 v82, v82
	v_exp_f32_e32 v83, v83
	v_pk_mul_f32 v[84:85], v[20:21], v[12:13] op_sel_hi:[0,1]
	v_exp_f32_e32 v84, v84
	v_exp_f32_e32 v85, v85
	v_pk_mul_f32 v[82:83], v[82:83], v[100:101]
	s_nop 0
	v_pk_fma_f32 v[70:71], v[22:23], v[70:71], v[82:83] op_sel_hi:[0,1,1]
	v_pk_mul_f32 v[82:83], v[84:85], v[106:107]
	v_pk_mul_f32 v[84:85], v[20:21], v[8:9] op_sel_hi:[0,1]
	v_pk_fma_f32 v[72:73], v[22:23], v[72:73], v[82:83] op_sel_hi:[0,1,1]
	v_pk_mul_f32 v[82:83], v[20:21], v[6:7] op_sel_hi:[0,1]
	v_exp_f32_e32 v82, v82
	v_exp_f32_e32 v83, v83
	v_exp_f32_e32 v84, v84
	v_exp_f32_e32 v85, v85
	s_waitcnt lgkmcnt(11)
	v_pk_fma_f32 v[62:63], v[86:87], v[70:71], v[62:63]
	v_pk_mul_f32 v[82:83], v[82:83], v[108:109]
	v_pk_fma_f32 v[62:63], v[88:89], v[72:73], v[62:63]
	v_pk_fma_f32 v[74:75], v[22:23], v[74:75], v[82:83] op_sel_hi:[0,1,1]
	v_pk_mul_f32 v[82:83], v[84:85], v[102:103]
	v_pk_mul_f32 v[84:85], v[20:21], v[4:5] op_sel_hi:[0,1]
	v_pk_fma_f32 v[76:77], v[22:23], v[76:77], v[82:83] op_sel_hi:[0,1,1]
	v_pk_mul_f32 v[82:83], v[20:21], v[2:3] op_sel_hi:[0,1]
	v_exp_f32_e32 v82, v82
	v_exp_f32_e32 v83, v83
	v_exp_f32_e32 v84, v84
	v_exp_f32_e32 v85, v85
	s_waitcnt lgkmcnt(10)
	v_pk_fma_f32 v[62:63], v[90:91], v[74:75], v[62:63]
	v_pk_mul_f32 v[82:83], v[82:83], v[104:105]
	v_pk_fma_f32 v[62:63], v[92:93], v[76:77], v[62:63]
	v_pk_fma_f32 v[78:79], v[22:23], v[78:79], v[82:83] op_sel_hi:[0,1,1]
	v_pk_mul_f32 v[18:19], v[84:85], v[18:19]
	s_waitcnt lgkmcnt(9)
	v_pk_fma_f32 v[62:63], v[94:95], v[78:79], v[62:63]
	v_pk_fma_f32 v[18:19], v[22:23], v[80:81], v[18:19] op_sel_hi:[0,1,1]
	v_pk_fma_f32 v[22:23], v[96:97], v[18:19], v[62:63]
	s_nop 0
	v_add_f32_e32 v20, v22, v23
	v_fma_mix_f32 v20, v1, v21, v20 op_sel_hi:[0,1,0]
	v_fma_mixlo_f16 v20, v20, v25, 0 op_sel_hi:[0,1,0]
	ds_write_b16 v68, v20 offset:35296
	v_cvt_f32_f16_sdwa v20, v29 dst_sel:DWORD dst_unused:UNUSED_PAD src0_sel:WORD_1
	v_cvt_f32_f16_sdwa v22, v21 dst_sel:DWORD dst_unused:UNUSED_PAD src0_sel:WORD_1
	v_pk_mul_f32 v[14:15], v[20:21], v[14:15] op_sel_hi:[0,1]
	v_exp_f32_e32 v14, v14
	v_exp_f32_e32 v15, v15
	v_pk_mul_f32 v[16:17], v[20:21], v[16:17] op_sel_hi:[0,1]
	v_exp_f32_e32 v16, v16
	v_exp_f32_e32 v17, v17
	v_pk_mul_f32 v[10:11], v[20:21], v[10:11] op_sel_hi:[0,1]
	v_exp_f32_e32 v10, v10
	v_exp_f32_e32 v11, v11
	v_pk_mul_f32 v[12:13], v[20:21], v[12:13] op_sel_hi:[0,1]
	v_exp_f32_e32 v12, v12
	v_exp_f32_e32 v13, v13
	v_pk_mul_f32 v[6:7], v[20:21], v[6:7] op_sel_hi:[0,1]
	v_mul_f32_e32 v22, v20, v22
	v_pk_mul_f32 v[14:15], v[14:15], v[26:27]
	v_exp_f32_e32 v6, v6
	v_exp_f32_e32 v7, v7
	v_pk_mul_f32 v[8:9], v[20:21], v[8:9] op_sel_hi:[0,1]
	s_waitcnt lgkmcnt(8)
	v_pk_fma_f32 v[14:15], v[22:23], v[30:31], v[14:15] op_sel_hi:[0,1,1]
	v_pk_mul_f32 v[16:17], v[16:17], v[64:65]
	v_exp_f32_e32 v8, v8
	v_exp_f32_e32 v9, v9
	v_pk_mul_f32 v[2:3], v[20:21], v[2:3] op_sel_hi:[0,1]
	s_waitcnt lgkmcnt(4)
	v_pk_fma_f32 v[14:15], v[46:47], v[14:15], 0 op_sel_hi:[1,1,0]
	v_pk_fma_f32 v[16:17], v[22:23], v[32:33], v[16:17] op_sel_hi:[0,1,1]
	v_pk_mul_f32 v[10:11], v[10:11], v[70:71]
	v_exp_f32_e32 v2, v2
	v_exp_f32_e32 v3, v3
	v_pk_mul_f32 v[4:5], v[20:21], v[4:5] op_sel_hi:[0,1]
	v_pk_fma_f32 v[14:15], v[48:49], v[16:17], v[14:15]
	v_pk_fma_f32 v[10:11], v[22:23], v[34:35], v[10:11] op_sel_hi:[0,1,1]
	v_pk_mul_f32 v[12:13], v[12:13], v[72:73]
	v_exp_f32_e32 v4, v4
	v_exp_f32_e32 v5, v5
	s_waitcnt lgkmcnt(3)
	v_pk_fma_f32 v[10:11], v[50:51], v[10:11], v[14:15]
	v_pk_fma_f32 v[12:13], v[22:23], v[36:37], v[12:13] op_sel_hi:[0,1,1]
	v_pk_mul_f32 v[6:7], v[6:7], v[74:75]
	v_pk_fma_f32 v[10:11], v[52:53], v[12:13], v[10:11]
	v_pk_fma_f32 v[6:7], v[22:23], v[38:39], v[6:7] op_sel_hi:[0,1,1]
	v_pk_mul_f32 v[8:9], v[8:9], v[76:77]
	s_waitcnt lgkmcnt(2)
	v_pk_fma_f32 v[6:7], v[54:55], v[6:7], v[10:11]
	v_pk_fma_f32 v[8:9], v[22:23], v[40:41], v[8:9] op_sel_hi:[0,1,1]
	v_pk_mul_f32 v[2:3], v[2:3], v[78:79]
	v_pk_fma_f32 v[6:7], v[56:57], v[8:9], v[6:7]
	v_pk_fma_f32 v[2:3], v[22:23], v[42:43], v[2:3] op_sel_hi:[0,1,1]
	v_pk_mul_f32 v[4:5], v[4:5], v[18:19]
	s_waitcnt lgkmcnt(1)
	v_pk_fma_f32 v[2:3], v[58:59], v[2:3], v[6:7]
	v_pk_fma_f32 v[4:5], v[22:23], v[44:45], v[4:5] op_sel_hi:[0,1,1]
	v_pk_fma_f32 v[2:3], v[60:61], v[4:5], v[2:3]
	s_nop 0
	v_add_f32_e32 v2, v2, v3
	v_fma_mix_f32 v1, v1, v21, v2 op_sel:[0,1,0] op_sel_hi:[0,1,0]
	v_fma_mixlo_f16 v1, v1, v25, 0 op_sel:[0,1,0] op_sel_hi:[0,1,0]
	ds_write_b16 v68, v1 offset:36336
	v_lshlrev_b32_e32 v1, 9, v0
	v_and_b32_e32 v2, 0x38000, v1
	v_mov_b32_e32 v3, v67
	v_and_b32_e32 v1, 63, v0
	s_bfe_u32 s14, s2, 0x40003
	v_lshl_add_u64 v[2:3], s[18:19], 0, v[2:3]
	v_lshlrev_b32_e32 v58, 4, v1
	v_mov_b32_e32 v59, v67
	s_lshl_b32 s13, s14, 6
	v_lshl_add_u64 v[20:21], v[2:3], 0, v[58:59]
	s_lshl_b32 s26, s14, 10
	s_add_i32 s12, s13, 64
	v_lshl_add_u64 v[2:3], v[20:21], 0, s[26:27]
	s_and_b32 s15, s12, 0x3c0
	v_add_co_u32_e32 v4, vcc, s52, v2
	s_lshl_b32 s26, s15, 4
	s_lshl_b32 s12, s12, 4
	v_addc_co_u32_e32 v5, vcc, 0, v3, vcc
	global_load_dwordx4 v[28:31], v[2:3], off
	global_load_dwordx4 v[32:35], v[4:5], off
	v_lshl_add_u64 v[2:3], v[20:21], 0, s[26:27]
	s_or_b32 s26, s12, 0x4000
	s_add_i32 s12, s13, 0x80
	s_and_b32 s15, s12, 0x3c0
	v_lshl_add_u64 v[4:5], v[20:21], 0, s[26:27]
	s_lshl_b32 s26, s15, 4
	s_lshl_b32 s12, s12, 4
	global_load_dwordx4 v[36:39], v[2:3], off
	global_load_dwordx4 v[40:43], v[4:5], off
	v_lshl_add_u64 v[2:3], v[20:21], 0, s[26:27]
	s_or_b32 s26, s12, 0x4000
	s_add_i32 s12, s13, 0xc0
	s_and_b32 s15, s12, 0x3c0
	v_lshl_add_u64 v[4:5], v[20:21], 0, s[26:27]
	s_lshl_b32 s26, s15, 4
	s_lshl_b32 s12, s12, 4
	global_load_dwordx4 v[44:47], v[2:3], off
	global_load_dwordx4 v[48:51], v[4:5], off
	v_lshl_add_u64 v[2:3], v[20:21], 0, s[26:27]
	s_or_b32 s26, s12, 0x4000
	s_add_i32 s12, s13, 0x100
	s_and_b32 s15, s12, 0x3c0
	v_lshl_add_u64 v[4:5], v[20:21], 0, s[26:27]
	s_lshl_b32 s26, s15, 4
	s_lshl_b32 s12, s12, 4
	global_load_dwordx4 v[52:55], v[2:3], off
	global_load_dwordx4 v[60:63], v[4:5], off
	v_lshl_add_u64 v[2:3], v[20:21], 0, s[26:27]
	s_or_b32 s26, s12, 0x4000
	s_add_i32 s12, s13, 0x140
	s_and_b32 s15, s12, 0x3c0
	v_lshl_add_u64 v[4:5], v[20:21], 0, s[26:27]
	s_lshl_b32 s26, s15, 4
	s_lshl_b32 s12, s12, 4
	global_load_dwordx4 v[68:71], v[2:3], off
	global_load_dwordx4 v[72:75], v[4:5], off
	v_lshl_add_u64 v[2:3], v[20:21], 0, s[26:27]
	s_or_b32 s26, s12, 0x4000
	s_add_i32 s12, s13, 0x180
	s_and_b32 s15, s12, 0x3c0
	v_lshl_add_u64 v[4:5], v[20:21], 0, s[26:27]
	s_lshl_b32 s26, s15, 4
	s_lshl_b32 s12, s12, 4
	global_load_dwordx4 v[76:79], v[2:3], off
	global_load_dwordx4 v[82:85], v[4:5], off
	v_lshl_add_u64 v[2:3], v[20:21], 0, s[26:27]
	s_or_b32 s26, s12, 0x4000
	s_add_i32 s12, s13, 0x1c0
	s_and_b32 s15, s12, 0x3c0
	v_lshl_add_u64 v[4:5], v[20:21], 0, s[26:27]
	s_lshl_b32 s26, s15, 4
	s_lshl_b32 s12, s12, 4
	v_lshl_add_u64 v[18:19], v[20:21], 0, s[26:27]
	s_or_b32 s26, s12, 0x4000
	s_xor_b32 s15, s13, 0x200
	v_lshl_add_u64 v[22:23], v[20:21], 0, s[26:27]
	s_lshl_b32 s26, s15, 4
	global_load_dwordx4 v[14:17], v[2:3], off
	global_load_dwordx4 v[10:13], v[4:5], off
	global_load_dwordx4 v[6:9], v[18:19], off
	s_nop 0
	global_load_dwordx4 v[2:5], v[22:23], off
	v_lshl_add_u64 v[18:19], v[20:21], 0, s[26:27]
	v_add_co_u32_e32 v22, vcc, s52, v18
	s_waitcnt lgkmcnt(0)
	s_barrier
	v_addc_co_u32_e32 v23, vcc, 0, v19, vcc
	global_load_dwordx4 v[86:89], v[18:19], off
	global_load_dwordx4 v[90:93], v[22:23], off
	v_lshrrev_b32_e32 v118, 6, v0
	v_lshlrev_b32_e32 v22, 7, v118
	v_mov_b32_e32 v23, v67
	v_and_b32_e32 v81, 15, v0
	v_lshl_add_u64 v[24:25], s[4:5], 0, v[22:23]
	v_and_b32_e32 v18, 48, v0
	v_mov_b32_e32 v19, v67
	s_movk_i32 s12, 0x410
	v_lshl_add_u64 v[56:57], v[24:25], 0, v[18:19]
	v_mad_u32_u24 v19, v81, s12, v18
	v_add_u32_e32 v23, s13, v19
	ds_read_b128 v[94:97], v23 offset:4096
	ds_read_b128 v[98:101], v23 offset:20736
	v_or_b32_e32 v26, s28, v81
	v_mov_b32_e32 v27, v67
	v_lshlrev_b64 v[24:25], 10, v[26:27]
	v_or_b32_e32 v26, 16, v26
	v_lshlrev_b64 v[26:27], 10, v[26:27]
	v_lshrrev_b32_e32 v23, 1, v0
	v_lshl_add_u64 v[24:25], v[56:57], 0, v[24:25]
	v_lshl_add_u64 v[26:27], v[56:57], 0, v[26:27]
	v_and_b32_e32 v80, 24, v23
	s_lshl_b32 s14, s14, 5
	s_setprio 1
	s_waitcnt vmcnt(17) lgkmcnt(1)
	v_mfma_f32_16x16x32_f16 v[102:105], v[28:31], v[94:97], 0
	s_waitcnt lgkmcnt(0)
	v_mfma_f32_16x16x32_f16 v[28:31], v[28:31], v[98:101], 0
	s_waitcnt vmcnt(16)
	v_mfma_f32_16x16x32_f16 v[94:97], v[32:35], v[94:97], 0
	v_mfma_f32_16x16x32_f16 v[32:35], v[32:35], v[98:101], 0
	s_setprio 0
	s_add_i32 s16, s13, 0x240
	s_and_b32 s17, s16, 0x3c0
	s_lshl_b32 s26, s17, 4
	s_lshl_b32 s16, s16, 4
	v_lshl_add_u64 v[56:57], v[20:21], 0, s[26:27]
	s_or_b32 s26, s16, 0x4000
	v_lshl_add_u64 v[64:65], v[20:21], 0, s[26:27]
	global_load_dwordx4 v[98:101], v[56:57], off
	global_load_dwordx4 v[106:109], v[64:65], off
	s_add_i32 s16, s14, 32
	s_and_b32 s16, s16, 0x1e0
	v_lshl_add_u32 v23, s16, 1, v19
	ds_read_b128 v[110:113], v23 offset:4096
	ds_read_b128 v[114:117], v23 offset:20736
	s_setprio 1
	s_waitcnt vmcnt(17) lgkmcnt(1)
	v_mfma_f32_16x16x32_f16 v[102:105], v[36:39], v[110:113], v[102:105]
	s_waitcnt lgkmcnt(0)
	v_mfma_f32_16x16x32_f16 v[28:31], v[36:39], v[114:117], v[28:31]
	s_waitcnt vmcnt(16)
	v_mfma_f32_16x16x32_f16 v[36:39], v[40:43], v[110:113], v[94:97]
	v_mfma_f32_16x16x32_f16 v[32:35], v[40:43], v[114:117], v[32:35]
	s_setprio 0
	s_add_i32 s16, s13, 0x280
	s_and_b32 s17, s16, 0x3c0
	s_lshl_b32 s26, s17, 4
	s_lshl_b32 s16, s16, 4
	v_lshl_add_u64 v[56:57], v[20:21], 0, s[26:27]
	s_or_b32 s26, s16, 0x4000
	v_lshl_add_u64 v[64:65], v[20:21], 0, s[26:27]
	global_load_dwordx4 v[40:43], v[56:57], off
	global_load_dwordx4 v[94:97], v[64:65], off
	s_add_i32 s16, s14, 64
	s_and_b32 s16, s16, 0x1e0
	v_lshl_add_u32 v23, s16, 1, v19
	ds_read_b128 v[110:113], v23 offset:4096
	ds_read_b128 v[114:117], v23 offset:20736
	s_setprio 1
	s_waitcnt vmcnt(17) lgkmcnt(1)
	v_mfma_f32_16x16x32_f16 v[102:105], v[44:47], v[110:113], v[102:105]
	s_waitcnt lgkmcnt(0)
	v_mfma_f32_16x16x32_f16 v[28:31], v[44:47], v[114:117], v[28:31]
	s_waitcnt vmcnt(16)
	v_mfma_f32_16x16x32_f16 v[36:39], v[48:51], v[110:113], v[36:39]
	v_mfma_f32_16x16x32_f16 v[32:35], v[48:51], v[114:117], v[32:35]
	s_setprio 0
	s_add_i32 s16, s13, 0x2c0
	s_and_b32 s17, s16, 0x3c0
	s_lshl_b32 s26, s17, 4
	s_lshl_b32 s16, s16, 4
	v_lshl_add_u64 v[56:57], v[20:21], 0, s[26:27]
	s_or_b32 s26, s16, 0x4000
	v_lshl_add_u64 v[64:65], v[20:21], 0, s[26:27]
	global_load_dwordx4 v[44:47], v[56:57], off
	global_load_dwordx4 v[48:51], v[64:65], off
	s_add_i32 s16, s14, 0x60
	s_and_b32 s16, s16, 0x1e0
	v_lshl_add_u32 v23, s16, 1, v19
	ds_read_b128 v[110:113], v23 offset:4096
	ds_read_b128 v[114:117], v23 offset:20736
	s_setprio 1
	s_waitcnt vmcnt(17) lgkmcnt(1)
	v_mfma_f32_16x16x32_f16 v[102:105], v[52:55], v[110:113], v[102:105]
	s_waitcnt lgkmcnt(0)
	v_mfma_f32_16x16x32_f16 v[28:31], v[52:55], v[114:117], v[28:31]
	s_waitcnt vmcnt(16)
	v_mfma_f32_16x16x32_f16 v[36:39], v[60:63], v[110:113], v[36:39]
	v_mfma_f32_16x16x32_f16 v[32:35], v[60:63], v[114:117], v[32:35]
	s_setprio 0
	s_add_i32 s16, s13, 0x300
	s_and_b32 s17, s16, 0x3c0
	s_lshl_b32 s26, s17, 4
	s_lshl_b32 s16, s16, 4
	v_lshl_add_u64 v[56:57], v[20:21], 0, s[26:27]
	s_or_b32 s26, s16, 0x4000
	v_lshl_add_u64 v[64:65], v[20:21], 0, s[26:27]
	global_load_dwordx4 v[52:55], v[56:57], off
	global_load_dwordx4 v[60:63], v[64:65], off
	s_add_i32 s16, s14, 0x80
	s_and_b32 s16, s16, 0x1e0
	v_lshl_add_u32 v23, s16, 1, v19
	ds_read_b128 v[110:113], v23 offset:4096
	ds_read_b128 v[114:117], v23 offset:20736
	s_setprio 1
	s_waitcnt vmcnt(17) lgkmcnt(1)
	v_mfma_f32_16x16x32_f16 v[102:105], v[68:71], v[110:113], v[102:105]
	s_waitcnt lgkmcnt(0)
	v_mfma_f32_16x16x32_f16 v[28:31], v[68:71], v[114:117], v[28:31]
	s_waitcnt vmcnt(16)
	v_mfma_f32_16x16x32_f16 v[36:39], v[72:75], v[110:113], v[36:39]
	v_mfma_f32_16x16x32_f16 v[32:35], v[72:75], v[114:117], v[32:35]
	s_setprio 0
	s_add_i32 s16, s13, 0x340
	s_and_b32 s17, s16, 0x3c0
	s_lshl_b32 s26, s17, 4
	s_lshl_b32 s16, s16, 4
	v_lshl_add_u64 v[56:57], v[20:21], 0, s[26:27]
	s_or_b32 s26, s16, 0x4000
	v_lshl_add_u64 v[64:65], v[20:21], 0, s[26:27]
	global_load_dwordx4 v[68:71], v[56:57], off
	global_load_dwordx4 v[72:75], v[64:65], off
	s_add_i32 s16, s14, 0xa0
	s_and_b32 s16, s16, 0x1e0
	v_lshl_add_u32 v23, s16, 1, v19
	ds_read_b128 v[110:113], v23 offset:4096
	ds_read_b128 v[114:117], v23 offset:20736
	s_setprio 1
	s_waitcnt vmcnt(17) lgkmcnt(1)
	v_mfma_f32_16x16x32_f16 v[102:105], v[76:79], v[110:113], v[102:105]
	s_waitcnt lgkmcnt(0)
	v_mfma_f32_16x16x32_f16 v[28:31], v[76:79], v[114:117], v[28:31]
	s_waitcnt vmcnt(16)
	v_mfma_f32_16x16x32_f16 v[36:39], v[82:85], v[110:113], v[36:39]
	v_mfma_f32_16x16x32_f16 v[32:35], v[82:85], v[114:117], v[32:35]
	s_setprio 0
	s_add_i32 s16, s13, 0x380
	s_and_b32 s17, s16, 0x3c0
	s_lshl_b32 s26, s17, 4
	s_lshl_b32 s16, s16, 4
	v_lshl_add_u64 v[56:57], v[20:21], 0, s[26:27]
	s_or_b32 s26, s16, 0x4000
	v_lshl_add_u64 v[64:65], v[20:21], 0, s[26:27]
	global_load_dwordx4 v[76:79], v[56:57], off
	global_load_dwordx4 v[82:85], v[64:65], off
	s_add_i32 s16, s14, 0xc0
	s_and_b32 s16, s16, 0x1e0
	v_lshl_add_u32 v23, s16, 1, v19
	ds_read_b128 v[110:113], v23 offset:4096
	ds_read_b128 v[114:117], v23 offset:20736
	s_setprio 1
	s_waitcnt vmcnt(17) lgkmcnt(1)
	v_mfma_f32_16x16x32_f16 v[102:105], v[14:17], v[110:113], v[102:105]
	s_waitcnt lgkmcnt(0)
	v_mfma_f32_16x16x32_f16 v[14:17], v[14:17], v[114:117], v[28:31]
	s_waitcnt vmcnt(16)
	v_mfma_f32_16x16x32_f16 v[28:31], v[10:13], v[110:113], v[36:39]
	v_mfma_f32_16x16x32_f16 v[10:13], v[10:13], v[114:117], v[32:35]
	s_setprio 0
	s_addk_i32 s13, 0x3c0
	s_and_b32 s16, s13, 0x3c0
	s_lshl_b32 s26, s16, 4
	s_lshl_b32 s13, s13, 4
	v_lshl_add_u64 v[56:57], v[20:21], 0, s[26:27]
	s_or_b32 s26, s13, 0x4000
	v_lshl_add_u64 v[20:21], v[20:21], 0, s[26:27]
	global_load_dwordx4 v[32:35], v[56:57], off
	global_load_dwordx4 v[36:39], v[20:21], off
	s_add_i32 s13, s14, 0xe0
	s_and_b32 s13, s13, 0x1e0
	v_lshl_add_u32 v20, s13, 1, v19
	ds_read_b128 v[110:113], v20 offset:4096
	ds_read_b128 v[114:117], v20 offset:20736
	s_setprio 1
	s_waitcnt vmcnt(17) lgkmcnt(1)
	v_mfma_f32_16x16x32_f16 v[102:105], v[6:9], v[110:113], v[102:105]
	s_waitcnt lgkmcnt(0)
	v_mfma_f32_16x16x32_f16 v[6:9], v[6:9], v[114:117], v[14:17]
	s_waitcnt vmcnt(16)
	v_mfma_f32_16x16x32_f16 v[14:17], v[2:5], v[110:113], v[28:31]
	v_mfma_f32_16x16x32_f16 v[2:5], v[2:5], v[114:117], v[10:13]
	s_setprio 0
	v_add_u32_e32 v20, s15, v19
	s_nop 0
	ds_read_b128 v[10:13], v20 offset:4096
	ds_read_b128 v[28:31], v20 offset:20736
	s_setprio 1
	s_waitcnt vmcnt(15) lgkmcnt(1)
	v_mfma_f32_16x16x32_f16 v[102:105], v[86:89], v[10:13], v[102:105]
	s_waitcnt lgkmcnt(0)
	v_mfma_f32_16x16x32_f16 v[6:9], v[86:89], v[28:31], v[6:9]
	s_waitcnt vmcnt(14)
	v_mfma_f32_16x16x32_f16 v[10:13], v[90:93], v[10:13], v[14:17]
	v_mfma_f32_16x16x32_f16 v[2:5], v[90:93], v[28:31], v[2:5]
	s_setprio 0
	s_add_i32 s13, s14, 0x120
	s_and_b32 s13, s13, 0x1e0
	v_lshl_add_u32 v20, s13, 1, v19
	ds_read_b128 v[14:17], v20 offset:4096
	ds_read_b128 v[28:31], v20 offset:20736
	s_setprio 1
	s_waitcnt vmcnt(13) lgkmcnt(1)
	v_mfma_f32_16x16x32_f16 v[86:89], v[98:101], v[14:17], v[102:105]
	s_waitcnt lgkmcnt(0)
	v_mfma_f32_16x16x32_f16 v[6:9], v[98:101], v[28:31], v[6:9]
	s_waitcnt vmcnt(12)
	v_mfma_f32_16x16x32_f16 v[10:13], v[106:109], v[14:17], v[10:13]
	v_mfma_f32_16x16x32_f16 v[2:5], v[106:109], v[28:31], v[2:5]
	s_setprio 0
	s_add_i32 s13, s14, 0x140
	s_and_b32 s13, s13, 0x1e0
	v_lshl_add_u32 v20, s13, 1, v19
	ds_read_b128 v[14:17], v20 offset:4096
	ds_read_b128 v[28:31], v20 offset:20736
	s_setprio 1
	s_waitcnt vmcnt(11) lgkmcnt(1)
	v_mfma_f32_16x16x32_f16 v[86:89], v[40:43], v[14:17], v[86:89]
	s_waitcnt lgkmcnt(0)
	v_mfma_f32_16x16x32_f16 v[6:9], v[40:43], v[28:31], v[6:9]
	s_waitcnt vmcnt(10)
	v_mfma_f32_16x16x32_f16 v[10:13], v[94:97], v[14:17], v[10:13]
	v_mfma_f32_16x16x32_f16 v[2:5], v[94:97], v[28:31], v[2:5]
	s_setprio 0
	s_add_i32 s13, s14, 0x160
	s_and_b32 s13, s13, 0x1e0
	v_lshl_add_u32 v20, s13, 1, v19
	ds_read_b128 v[14:17], v20 offset:4096
	ds_read_b128 v[28:31], v20 offset:20736
	s_setprio 1
	s_waitcnt vmcnt(9) lgkmcnt(1)
	v_mfma_f32_16x16x32_f16 v[40:43], v[44:47], v[14:17], v[86:89]
	s_waitcnt lgkmcnt(0)
	v_mfma_f32_16x16x32_f16 v[6:9], v[44:47], v[28:31], v[6:9]
	s_waitcnt vmcnt(8)
	v_mfma_f32_16x16x32_f16 v[10:13], v[48:51], v[14:17], v[10:13]
	v_mfma_f32_16x16x32_f16 v[2:5], v[48:51], v[28:31], v[2:5]
	s_setprio 0
	s_add_i32 s13, s14, 0x180
	s_and_b32 s13, s13, 0x1e0
	v_lshl_add_u32 v20, s13, 1, v19
	ds_read_b128 v[14:17], v20 offset:4096
	ds_read_b128 v[28:31], v20 offset:20736
	s_setprio 1
	s_waitcnt vmcnt(7) lgkmcnt(1)
	v_mfma_f32_16x16x32_f16 v[40:43], v[52:55], v[14:17], v[40:43]
	s_waitcnt lgkmcnt(0)
	v_mfma_f32_16x16x32_f16 v[6:9], v[52:55], v[28:31], v[6:9]
	s_waitcnt vmcnt(6)
	v_mfma_f32_16x16x32_f16 v[10:13], v[60:63], v[14:17], v[10:13]
	v_mfma_f32_16x16x32_f16 v[2:5], v[60:63], v[28:31], v[2:5]
	s_setprio 0
	s_add_i32 s13, s14, 0x1a0
	s_and_b32 s13, s13, 0x1e0
	v_lshl_add_u32 v20, s13, 1, v19
	ds_read_b128 v[14:17], v20 offset:4096
	ds_read_b128 v[28:31], v20 offset:20736
	s_setprio 1
	s_waitcnt vmcnt(5) lgkmcnt(1)
	v_mfma_f32_16x16x32_f16 v[40:43], v[68:71], v[14:17], v[40:43]
	s_waitcnt lgkmcnt(0)
	v_mfma_f32_16x16x32_f16 v[6:9], v[68:71], v[28:31], v[6:9]
	s_waitcnt vmcnt(4)
	v_mfma_f32_16x16x32_f16 v[10:13], v[72:75], v[14:17], v[10:13]
	v_mfma_f32_16x16x32_f16 v[2:5], v[72:75], v[28:31], v[2:5]
	s_setprio 0
	s_add_i32 s13, s14, 0x1c0
	s_and_b32 s13, s13, 0x1e0
	v_lshl_add_u32 v20, s13, 1, v19
	ds_read_b128 v[14:17], v20 offset:4096
	ds_read_b128 v[28:31], v20 offset:20736
	s_setprio 1
	s_waitcnt vmcnt(3) lgkmcnt(1)
	v_mfma_f32_16x16x32_f16 v[40:43], v[76:79], v[14:17], v[40:43]
	s_waitcnt lgkmcnt(0)
	v_mfma_f32_16x16x32_f16 v[6:9], v[76:79], v[28:31], v[6:9]
	s_waitcnt vmcnt(2)
	v_mfma_f32_16x16x32_f16 v[10:13], v[82:85], v[14:17], v[10:13]
	v_mfma_f32_16x16x32_f16 v[2:5], v[82:85], v[28:31], v[2:5]
	s_setprio 0
	s_addk_i32 s14, 0x1e0
	s_and_b32 s13, s14, 0x1e0
	v_lshl_add_u32 v20, s13, 1, v19
	ds_read_b128 v[14:17], v20 offset:4096
	ds_read_b128 v[28:31], v20 offset:20736
	s_setprio 1
	s_waitcnt vmcnt(1) lgkmcnt(1)
	v_mfma_f32_16x16x32_f16 v[40:43], v[32:35], v[14:17], v[40:43]
	s_waitcnt lgkmcnt(0)
	v_mfma_f32_16x16x32_f16 v[6:9], v[32:35], v[28:31], v[6:9]
	s_waitcnt vmcnt(0)
	v_mfma_f32_16x16x32_f16 v[10:13], v[36:39], v[14:17], v[10:13]
	v_mfma_f32_16x16x32_f16 v[2:5], v[36:39], v[28:31], v[2:5]
	s_setprio 0
	v_add_u32_e32 v19, v19, v22
	v_lshlrev_b32_e32 v20, 15, v118
	v_mov_b32_e32 v21, v67
	s_bfe_u32 s22, s2, 0x30003
	v_lshl_add_u64 v[20:21], s[10:11], 0, v[20:21]
	s_lshl_b32 s26, s22, 10
	v_lshl_add_u64 v[64:65], v[20:21], 0, v[58:59]
	v_lshl_add_u64 v[52:53], v[64:65], 0, s[26:27]
	v_add_co_u32_e32 v76, vcc, s29, v52
	s_lshl_b32 s53, s22, 6
	s_nop 0
	v_addc_co_u32_e32 v77, vcc, 0, v53, vcc
	s_mov_b32 s14, 0x14000
	v_mov_b32_e32 v22, 0x14000
	v_mul_u32_u24_e32 v23, 0x210, v81
	s_add_i32 s38, s53, 64
	v_lshlrev_b32_e32 v83, 2, v118
	s_movk_i32 s16, 0x1040
	s_movk_i32 s18, 0x840
	v_lshl_or_b32 v1, v1, 3, v22
	v_add3_u32 v84, v23, v18, s14
	s_and_b32 s14, s38, 0x1c0
	s_movk_i32 s20, 0x210
	s_mov_b32 s19, s27
	v_mad_u32_u24 v56, v118, s16, v58
	v_or_b32_e32 v22, 1, v83
	v_mad_u32_u24 v98, v118, s18, v1
	s_lshl_b32 s18, s14, 4
	v_mad_u32_u24 v99, v22, s12, v58
	v_mad_u32_u24 v85, v22, s20, v1
	v_lshl_add_u64 v[54:55], v[64:65], 0, s[18:19]
	s_add_i32 s12, s53, 0xc0
	s_and_b32 s2, s3, 0x7ffffff
	s_lshl_b32 s3, s22, 5
	s_and_b32 s39, s12, 0x1c0
	s_lshl_b32 s14, s39, 4
	s_add_i32 s39, s3, 32
	s_and_b32 s39, s39, 0xe0
	v_lshl_add_u32 v82, s39, 1, v84
	s_add_i32 s11, s53, 0x80
	s_lshl_b32 s16, s38, 4
	s_mov_b32 s21, s27
	s_and_b32 s30, s11, 0x1c0
	s_lshl_b32 s11, s11, 4
	s_or_b32 s20, s16, 0x2000
	s_mov_b32 s23, s27
	s_mov_b32 s31, s27
	s_mov_b32 s35, s27
	s_or_b32 s22, s16, 0x6000
	s_lshl_b32 s30, s30, 4
	s_or_b32 s34, s11, 0x2000
	v_lshl_add_u64 v[26:27], v[64:65], 0, s[20:21]
	v_lshl_add_u64 v[28:29], v[64:65], 0, s[22:23]
	v_lshl_add_u64 v[30:31], v[64:65], 0, s[30:31]
	v_lshl_add_u64 v[32:33], v[64:65], 0, s[34:35]
	s_mov_b64 s[40:41], 0x40000
	v_lshl_add_u64 v[60:61], v[64:65], 0, s[40:41]
	s_mov_b32 s37, s27
	s_or_b32 s36, s11, 0x6000
	v_lshl_add_u64 v[74:75], v[64:65], 0, s[36:37]
	s_mov_b32 s15, s27
	s_lshl_b32 s12, s12, 4
	v_lshl_add_u64 v[70:71], v[64:65], 0, s[14:15]
	s_mov_b32 s17, s27
	s_or_b32 s16, s12, 0x2000
	s_mov_b32 s13, s27
	s_or_b32 s12, s12, 0x6000
	v_lshl_add_u64 v[72:73], v[64:65], 0, s[16:17]
	v_lshl_add_u64 v[68:69], v[64:65], 0, s[12:13]
	v_add_u32_e32 v1, s53, v84
	s_xor_b32 s10, s26, 0x1000
	s_mov_b32 s11, s27
	s_mov_b32 s49, s27
	s_mov_b32 s51, s27
	s_mov_b32 s47, s27
	v_pk_add_f32 v[14:15], v[180:181], v[40:41]
	v_pk_add_f32 v[16:17], v[182:183], v[42:43]
	v_pk_add_f32 v[10:11], v[184:185], v[10:11]
	v_pk_add_f32 v[12:13], v[186:187], v[12:13]
	v_pk_add_f32 v[6:7], v[188:189], v[6:7]
	v_pk_add_f32 v[8:9], v[190:191], v[8:9]
	v_pk_add_f32 v[2:3], v[192:193], v[2:3]
	v_pk_add_f32 v[4:5], v[194:195], v[4:5]
	ds_write_b128 v19, v[14:17] offset:37376
	ds_write_b128 v19, v[10:13] offset:37440
	ds_write_b128 v19, v[6:9] offset:54016
	ds_write_b128 v19, v[2:5] offset:54080
	v_mov_b64_e32 v[34:35], v[204:205]
	v_mov_b64_e32 v[36:37], v[206:207]
	v_mov_b64_e32 v[38:39], v[208:209]
	v_mov_b64_e32 v[40:41], v[210:211]
	v_add_co_u32_e32 v2, vcc, s52, v52
	s_waitcnt lgkmcnt(0)
	s_nop 0
	v_addc_co_u32_e32 v3, vcc, 0, v53, vcc
	v_add_co_u32_e32 v4, vcc, s33, v52
	s_barrier
	s_nop 0
	v_addc_co_u32_e32 v5, vcc, 0, v53, vcc
	global_load_dwordx4 v[14:17], v[2:3], off
	global_load_dwordx4 v[18:21], v[4:5], off
	global_load_dwordx4 v[22:25], v[52:53], off
	global_load_dwordx4 v[10:13], v[54:55], off
	ds_read_b128 v[2:5], v56 offset:37376
	ds_read_b128 v[6:9], v99 offset:37376
	v_add_co_u32_e32 v78, vcc, s52, v54
	s_mov_b32 s43, s27
	s_waitcnt lgkmcnt(1)
	v_add_f32_e32 v42, v2, v3
	v_add_f32_e32 v42, v42, v4
	v_add_f32_e32 v42, v42, v5
	v_addc_co_u32_e32 v79, vcc, 0, v55, vcc
	s_nop 0
	v_add_f32_dpp v42, v42, v42 quad_perm:[1,0,3,2] row_mask:0xf bank_mask:0xf bound_ctrl:1
	s_mov_b32 s45, s27
	s_mov_b32 s41, s27
	v_add_f32_dpp v42, v42, v42 quad_perm:[2,3,0,1] row_mask:0xf bank_mask:0xf bound_ctrl:1
	v_lshl_add_u64 v[62:63], v[64:65], 0, s[10:11]
	v_lshl_add_u64 v[58:59], s[4:5], 0, v[58:59]
	v_add_f32_dpp v42, v42, v42 row_half_mirror row_mask:0xf bank_mask:0xf bound_ctrl:1
	v_lshl_add_u64 v[152:153], v[60:61], 0, s[26:27]
	v_lshl_add_u64 v[154:155], v[60:61], 0, s[18:19]
	v_add_f32_dpp v42, v42, v42 row_mirror row_mask:0xf bank_mask:0xf bound_ctrl:1
	v_lshl_add_u64 v[156:157], v[60:61], 0, s[20:21]
	v_readlane_b32 s8, v42, 16
	v_readlane_b32 s9, v42, 48
	v_readlane_b32 s6, v42, 0
	v_readlane_b32 s7, v42, 32
	v_mov_b32_e32 v42, s8
	v_mov_b32_e32 v43, s9
	v_pk_add_f32 v[42:43], s[6:7], v[42:43]
	s_mov_b32 s6, 0x3b800000
	v_add_f32_e32 v42, v42, v43
	v_mul_f32_e32 v42, 0x3b800000, v42
	v_pk_add_f32 v[86:87], v[2:3], v[42:43] op_sel_hi:[1,0] neg_lo:[0,1] neg_hi:[0,1]
	v_pk_add_f32 v[88:89], v[4:5], v[42:43] op_sel_hi:[1,0] neg_lo:[0,1] neg_hi:[0,1]
	v_pk_mul_f32 v[42:43], v[86:87], v[86:87]
	v_pk_mul_f32 v[44:45], v[88:89], v[88:89]
	v_add_f32_e32 v42, v42, v43
	v_add_f32_e32 v42, v44, v42
	s_waitcnt lgkmcnt(0)
	v_add_f32_e32 v44, v6, v7
	v_add_f32_e32 v42, v45, v42
	v_add_f32_e32 v44, v44, v8
	v_add_f32_e32 v44, v44, v9
	v_add_f32_dpp v42, v42, v42 quad_perm:[1,0,3,2] row_mask:0xf bank_mask:0xf bound_ctrl:1
	v_lshl_add_u64 v[158:159], v[60:61], 0, s[22:23]
	v_add_f32_dpp v44, v44, v44 quad_perm:[1,0,3,2] row_mask:0xf bank_mask:0xf bound_ctrl:1
	v_add_f32_dpp v42, v42, v42 quad_perm:[2,3,0,1] row_mask:0xf bank_mask:0xf bound_ctrl:1
	v_lshl_add_u64 v[160:161], v[60:61], 0, s[30:31]
	v_add_f32_dpp v44, v44, v44 quad_perm:[2,3,0,1] row_mask:0xf bank_mask:0xf bound_ctrl:1
	v_add_f32_dpp v42, v42, v42 row_half_mirror row_mask:0xf bank_mask:0xf bound_ctrl:1
	v_lshl_add_u64 v[162:163], v[60:61], 0, s[34:35]
	v_add_f32_dpp v44, v44, v44 row_half_mirror row_mask:0xf bank_mask:0xf bound_ctrl:1
	v_add_f32_dpp v42, v42, v42 row_mirror row_mask:0xf bank_mask:0xf bound_ctrl:1
	v_lshl_add_u64 v[164:165], v[60:61], 0, s[36:37]
	v_readlane_b32 s7, v42, 16
	v_readlane_b32 s39, v42, 48
	v_add_f32_dpp v44, v44, v44 row_mirror row_mask:0xf bank_mask:0xf bound_ctrl:1
	v_readlane_b32 s8, v42, 0
	v_readlane_b32 s9, v42, 32
	v_mov_b32_e32 v42, s7
	v_mov_b32_e32 v43, s39
	v_readlane_b32 s7, v44, 16
	v_readlane_b32 s39, v44, 48
	v_pk_add_f32 v[42:43], s[8:9], v[42:43]
	v_readlane_b32 s8, v44, 0
	v_readlane_b32 s9, v44, 32
	v_mov_b32_e32 v44, s7
	v_mov_b32_e32 v45, s39
	v_pk_add_f32 v[44:45], s[8:9], v[44:45]
	s_nop 0
	v_add_f32_e32 v44, v44, v45
	v_mul_f32_e32 v44, 0x3b800000, v44
	v_pk_add_f32 v[90:91], v[6:7], v[44:45] op_sel_hi:[1,0] neg_lo:[0,1] neg_hi:[0,1]
	v_pk_add_f32 v[92:93], v[8:9], v[44:45] op_sel_hi:[1,0] neg_lo:[0,1] neg_hi:[0,1]
	v_pk_mul_f32 v[46:47], v[90:91], v[90:91]
	v_pk_mul_f32 v[44:45], v[92:93], v[92:93]
	v_add_f32_e32 v46, v46, v47
	v_add_f32_e32 v44, v44, v46
	v_add_f32_e32 v44, v45, v44
	v_mov_b32_e32 v47, v42
	s_nop 0
	v_add_f32_dpp v44, v44, v44 quad_perm:[1,0,3,2] row_mask:0xf bank_mask:0xf bound_ctrl:1
	s_nop 1
	v_add_f32_dpp v44, v44, v44 quad_perm:[2,3,0,1] row_mask:0xf bank_mask:0xf bound_ctrl:1
	s_nop 1
	v_add_f32_dpp v44, v44, v44 row_half_mirror row_mask:0xf bank_mask:0xf bound_ctrl:1
	s_nop 1
	v_add_f32_dpp v44, v44, v44 row_mirror row_mask:0xf bank_mask:0xf bound_ctrl:1
	s_nop 0
	v_readlane_b32 s7, v44, 16
	v_readlane_b32 s39, v44, 48
	v_readlane_b32 s8, v44, 0
	v_readlane_b32 s9, v44, 32
	v_mov_b32_e32 v44, s7
	v_mov_b32_e32 v45, s39
	v_pk_add_f32 v[44:45], s[8:9], v[44:45]
	s_mov_b32 s8, 0x3727c5ac
	v_mov_b32_e32 v46, v44
	v_mov_b32_e32 v42, v45
	v_pk_add_f32 v[42:43], v[46:47], v[42:43]
	v_mov_b64_e32 v[94:95], s[8:9]
	v_pk_fma_f32 v[96:97], v[42:43], s[6:7], v[94:95] op_sel_hi:[1,0,0]
	s_mov_b32 s7, 0x800000
	v_mul_f32_e32 v42, 0x4b800000, v97
	v_cmp_gt_f32_e32 vcc, s7, v97
	s_nop 1
	v_cndmask_b32_e32 v42, v97, v42, vcc
	v_rsq_f32_e32 v97, v42
	global_load_dwordx4 v[54:57], v[26:27], off
	global_load_dwordx4 v[50:53], v[28:29], off
	global_load_dwordx4 v[46:49], v[30:31], off
	global_load_dwordx4 v[42:45], v[32:33], off
	v_mul_f32_e32 v26, 0x45800000, v97
	v_cndmask_b32_e32 v26, v97, v26, vcc
	v_pk_mul_f32 v[28:29], v[86:87], v[26:27] op_sel_hi:[1,0]
	v_cmp_gt_f32_e32 vcc, s7, v96
	s_waitcnt vmcnt(8)
	v_pk_fma_f32 v[28:29], v[34:35], v[28:29], v[38:39]
	v_pk_mul_f32 v[26:27], v[88:89], v[26:27] op_sel_hi:[1,0]
	v_cvt_pk_f16_f32 v28, v28, v29
	v_mul_f32_e32 v29, 0x4b800000, v96
	v_cndmask_b32_e32 v29, v96, v29, vcc
	v_rsq_f32_e32 v32, v29
	v_pk_fma_f32 v[26:27], v[36:37], v[26:27], v[40:41]
	s_nop 0
	v_cvt_pk_f16_f32 v29, v26, v27
	v_mul_f32_e32 v26, 0x45800000, v32
	v_cndmask_b32_e32 v26, v32, v26, vcc
	ds_write_b64 v98, v[28:29]
	v_pk_mul_f32 v[28:29], v[90:91], v[26:27] op_sel_hi:[1,0]
	v_pk_mul_f32 v[26:27], v[92:93], v[26:27] op_sel_hi:[1,0]
	v_pk_fma_f32 v[28:29], v[34:35], v[28:29], v[38:39]
	v_pk_fma_f32 v[26:27], v[36:37], v[26:27], v[40:41]
	v_cvt_pk_f16_f32 v28, v28, v29
	v_cvt_pk_f16_f32 v29, v26, v27
	ds_write_b64 v85, v[28:29]
	ds_read_b128 v[26:29], v99 offset:38416
	v_add_co_u32_e32 v102, vcc, s52, v30
	s_nop 1
	v_addc_co_u32_e32 v103, vcc, 0, v31, vcc
	ds_read_b128 v[30:33], v99 offset:39456
	s_waitcnt lgkmcnt(1)
	v_add_f32_e32 v86, v26, v27
	v_add_f32_e32 v86, v86, v28
	v_add_f32_e32 v86, v86, v29
	s_nop 1
	v_add_f32_dpp v86, v86, v86 quad_perm:[1,0,3,2] row_mask:0xf bank_mask:0xf bound_ctrl:1
	s_nop 1
	v_add_f32_dpp v86, v86, v86 quad_perm:[2,3,0,1] row_mask:0xf bank_mask:0xf bound_ctrl:1
	s_nop 1
	v_add_f32_dpp v86, v86, v86 row_half_mirror row_mask:0xf bank_mask:0xf bound_ctrl:1
	s_nop 1
	v_add_f32_dpp v86, v86, v86 row_mirror row_mask:0xf bank_mask:0xf bound_ctrl:1
	s_nop 0
	v_readlane_b32 s39, v86, 16
	v_readlane_b32 s40, v86, 48
	v_readlane_b32 s8, v86, 0
	v_readlane_b32 s9, v86, 32
	v_mov_b32_e32 v86, s39
	v_mov_b32_e32 v87, s40
	v_pk_add_f32 v[86:87], s[8:9], v[86:87]
	s_nop 0
	v_add_f32_e32 v86, v86, v87
	v_mul_f32_e32 v86, 0x3b800000, v86
	v_pk_add_f32 v[104:105], v[26:27], v[86:87] op_sel_hi:[1,0] neg_lo:[0,1] neg_hi:[0,1]
	v_pk_add_f32 v[106:107], v[28:29], v[86:87] op_sel_hi:[1,0] neg_lo:[0,1] neg_hi:[0,1]
	v_pk_mul_f32 v[88:89], v[104:105], v[104:105]
	v_pk_mul_f32 v[86:87], v[106:107], v[106:107]
	v_add_f32_e32 v88, v88, v89
	v_add_f32_e32 v86, v86, v88
	s_waitcnt lgkmcnt(0)
	v_add_f32_e32 v88, v30, v31
	v_add_f32_e32 v86, v87, v86
	v_add_f32_e32 v88, v88, v32
	v_add_f32_e32 v88, v88, v33
	v_add_f32_dpp v86, v86, v86 quad_perm:[1,0,3,2] row_mask:0xf bank_mask:0xf bound_ctrl:1
	s_nop 0
	v_add_f32_dpp v88, v88, v88 quad_perm:[1,0,3,2] row_mask:0xf bank_mask:0xf bound_ctrl:1
	v_add_f32_dpp v86, v86, v86 quad_perm:[2,3,0,1] row_mask:0xf bank_mask:0xf bound_ctrl:1
	s_nop 0
	v_add_f32_dpp v88, v88, v88 quad_perm:[2,3,0,1] row_mask:0xf bank_mask:0xf bound_ctrl:1
	v_add_f32_dpp v86, v86, v86 row_half_mirror row_mask:0xf bank_mask:0xf bound_ctrl:1
	s_nop 0
	v_add_f32_dpp v88, v88, v88 row_half_mirror row_mask:0xf bank_mask:0xf bound_ctrl:1
	v_add_f32_dpp v86, v86, v86 row_mirror row_mask:0xf bank_mask:0xf bound_ctrl:1
	s_nop 0
	v_readlane_b32 s39, v86, 16
	v_readlane_b32 s40, v86, 48
	v_add_f32_dpp v88, v88, v88 row_mirror row_mask:0xf bank_mask:0xf bound_ctrl:1
	v_readlane_b32 s8, v86, 0
	v_readlane_b32 s9, v86, 32
	v_mov_b32_e32 v86, s39
	v_mov_b32_e32 v87, s40
	v_readlane_b32 s39, v88, 16
	v_readlane_b32 s40, v88, 48
	v_pk_add_f32 v[86:87], s[8:9], v[86:87]
	v_readlane_b32 s8, v88, 0
	v_readlane_b32 s9, v88, 32
	v_mov_b32_e32 v88, s39
	v_mov_b32_e32 v89, s40
	v_pk_add_f32 v[88:89], s[8:9], v[88:89]
	s_nop 0
	v_add_f32_e32 v88, v88, v89
	v_mul_f32_e32 v88, 0x3b800000, v88
	v_pk_add_f32 v[108:109], v[30:31], v[88:89] op_sel_hi:[1,0] neg_lo:[0,1] neg_hi:[0,1]
	v_pk_add_f32 v[110:111], v[32:33], v[88:89] op_sel_hi:[1,0] neg_lo:[0,1] neg_hi:[0,1]
	v_pk_mul_f32 v[90:91], v[108:109], v[108:109]
	v_pk_mul_f32 v[88:89], v[110:111], v[110:111]
	v_add_f32_e32 v90, v90, v91
	v_add_f32_e32 v88, v88, v90
	v_add_f32_e32 v88, v89, v88
	v_mov_b32_e32 v91, v86
	s_nop 0
	v_add_f32_dpp v88, v88, v88 quad_perm:[1,0,3,2] row_mask:0xf bank_mask:0xf bound_ctrl:1
	s_nop 1
	v_add_f32_dpp v88, v88, v88 quad_perm:[2,3,0,1] row_mask:0xf bank_mask:0xf bound_ctrl:1
	s_nop 1
	v_add_f32_dpp v88, v88, v88 row_half_mirror row_mask:0xf bank_mask:0xf bound_ctrl:1
	s_nop 1
	v_add_f32_dpp v88, v88, v88 row_mirror row_mask:0xf bank_mask:0xf bound_ctrl:1
	s_nop 0
	v_readlane_b32 s39, v88, 16
	v_readlane_b32 s40, v88, 48
	v_readlane_b32 s8, v88, 0
	v_readlane_b32 s9, v88, 32
	v_mov_b32_e32 v88, s39
	v_mov_b32_e32 v89, s40
	v_pk_add_f32 v[88:89], s[8:9], v[88:89]
	s_mov_b32 s9, s27
	v_mov_b32_e32 v90, v88
	v_mov_b32_e32 v86, v89
	v_pk_add_f32 v[86:87], v[90:91], v[86:87]
	s_mov_b32 s39, s27
	v_pk_fma_f32 v[112:113], v[86:87], s[6:7], v[94:95] op_sel_hi:[1,0,0]
	s_add_i32 s6, s53, 0x140
	v_mul_f32_e32 v86, 0x4b800000, v113
	v_cmp_gt_f32_e32 vcc, s7, v113
	s_nop 1
	v_cndmask_b32_e32 v86, v113, v86, vcc
	v_rsq_f32_e32 v113, v86
	global_load_dwordx4 v[86:89], v[78:79], off
	global_load_dwordx4 v[90:93], v[102:103], off
	global_load_dwordx4 v[94:97], v[76:77], off
	global_load_dwordx4 v[98:101], v[74:75], off
	v_mul_f32_e32 v74, 0x45800000, v113
	v_cndmask_b32_e32 v74, v113, v74, vcc
	v_pk_mul_f32 v[76:77], v[104:105], v[74:75] op_sel_hi:[1,0]
	v_mul_f32_e32 v75, 0x4b800000, v112
	v_cmp_gt_f32_e32 vcc, s7, v112
	v_pk_fma_f32 v[76:77], v[34:35], v[76:77], v[38:39]
	s_and_b32 s7, s6, 0x1c0
	v_cndmask_b32_e32 v75, v112, v75, vcc
	v_rsq_f32_e32 v78, v75
	v_pk_mul_f32 v[74:75], v[106:107], v[74:75] op_sel_hi:[1,0]
	v_cvt_pk_f16_f32 v76, v76, v77
	v_pk_fma_f32 v[74:75], v[36:37], v[74:75], v[40:41]
	s_lshl_b32 s6, s6, 4
	v_cvt_pk_f16_f32 v77, v74, v75
	v_mul_f32_e32 v74, 0x45800000, v78
	v_cndmask_b32_e32 v74, v78, v74, vcc
	v_pk_mul_f32 v[78:79], v[108:109], v[74:75] op_sel_hi:[1,0]
	s_or_b32 s50, s6, 0x2000
	v_pk_fma_f32 v[34:35], v[34:35], v[78:79], v[38:39]
	v_pk_mul_f32 v[38:39], v[110:111], v[74:75] op_sel_hi:[1,0]
	v_add_co_u32_e32 v78, vcc, s52, v70
	v_pk_fma_f32 v[36:37], v[36:37], v[38:39], v[40:41]
	v_cvt_pk_f16_f32 v34, v34, v35
	v_cvt_pk_f16_f32 v35, v36, v37
	v_addc_co_u32_e32 v79, vcc, 0, v71, vcc
	ds_write2_b64 v85, v[76:77], v[34:35] offset0:66 offset1:132
	s_waitcnt lgkmcnt(0)
	s_barrier
	global_load_dwordx4 v[34:37], v[70:71], off
	global_load_dwordx4 v[38:41], v[72:73], off
	s_nop 0
	global_load_dwordx4 v[70:73], v[78:79], off
	global_load_dwordx4 v[74:77], v[68:69], off
	s_or_b32 s46, s6, 0x6000
	s_sub_i32 s6, s38, s3
	s_and_b32 s6, s6, 0xe0
	v_lshl_add_u32 v172, s6, 1, v84
	s_add_i32 s6, s53, 0x180
	s_lshl_b32 s48, s7, 4
	s_and_b32 s7, s6, 0x1c0
	s_lshl_b32 s6, s6, 4
	s_or_b32 s44, s6, 0x2000
	s_or_b32 s40, s6, 0x6000
	s_add_i32 s6, s3, 0x60
	s_and_b32 s6, s6, 0xe0
	v_lshl_add_u32 v173, s6, 1, v84
	s_add_i32 s6, s53, 0x1c0
	s_xor_b32 s53, s53, 0x100
	v_add_u32_e32 v174, s53, v84
	s_add_i32 s53, s3, 0xa0
	s_lshl_b32 s42, s7, 4
	s_and_b32 s7, s6, 0x1c0
	s_lshl_b32 s6, s6, 4
	s_and_b32 s53, s53, 0xe0
	s_lshl_b32 s8, s7, 4
	s_or_b32 s38, s6, 0x2000
	s_or_b32 s6, s6, 0x6000
	s_mov_b32 s7, s27
	v_lshl_add_u32 v175, s53, 1, v84
	s_add_i32 s53, s3, 0xc0
	s_addk_i32 s3, 0xe0
	v_lshl_add_u64 v[68:69], v[64:65], 0, s[48:49]
	v_lshl_add_u64 v[78:79], v[64:65], 0, s[50:51]
	v_lshl_add_u64 v[138:139], v[64:65], 0, s[46:47]
	v_lshl_add_u64 v[140:141], v[64:65], 0, s[42:43]
	v_lshl_add_u64 v[142:143], v[64:65], 0, s[44:45]
	v_lshl_add_u64 v[144:145], v[64:65], 0, s[40:41]
	v_lshl_add_u64 v[146:147], v[64:65], 0, s[8:9]
	v_lshl_add_u64 v[148:149], v[64:65], 0, s[38:39]
	v_lshl_add_u64 v[150:151], v[64:65], 0, s[6:7]
	s_and_b32 s53, s53, 0xe0
	s_and_b32 s3, s3, 0xe0
	v_add_u32_e32 v64, s28, v83
	v_mov_b32_e32 v65, v67
	v_lshl_add_u32 v176, s53, 1, v84
	v_lshl_add_u32 v177, s3, 1, v84
	v_lshlrev_b64 v[84:85], 10, v[64:65]
	ds_read_b128 v[102:105], v1
	ds_read_b128 v[106:109], v1 offset:8448
	v_lshl_add_u64 v[166:167], v[58:59], 0, v[84:85]
	v_or_b32_e32 v84, 1, v64
	v_mov_b32_e32 v85, v67
	v_lshlrev_b64 v[84:85], 10, v[84:85]
	v_lshl_add_u64 v[168:169], v[58:59], 0, v[84:85]
	v_or_b32_e32 v84, 2, v64
	v_mov_b32_e32 v85, v67
	v_or_b32_e32 v64, 3, v64
	v_lshlrev_b64 v[84:85], 10, v[84:85]
	v_lshlrev_b64 v[64:65], 10, v[64:65]
	v_lshl_add_u64 v[170:171], v[58:59], 0, v[84:85]
	v_lshl_add_u64 v[58:59], v[58:59], 0, v[64:65]
	s_setprio 1
	s_waitcnt vmcnt(13) lgkmcnt(1)
	v_mfma_f32_16x16x32_f16 v[110:113], v[102:105], v[22:25], 0
	s_waitcnt lgkmcnt(0)
	v_mfma_f32_16x16x32_f16 v[22:25], v[106:109], v[22:25], 0
	s_waitcnt vmcnt(5)
	v_mfma_f32_16x16x32_f16 v[114:117], v[102:105], v[94:97], 0
	v_mfma_f32_16x16x32_f16 v[94:97], v[106:109], v[94:97], 0
	v_mfma_f32_16x16x32_f16 v[118:121], v[102:105], v[14:17], 0
	v_mfma_f32_16x16x32_f16 v[14:17], v[106:109], v[14:17], 0
	v_mfma_f32_16x16x32_f16 v[102:105], v[102:105], v[18:21], 0
	v_mfma_f32_16x16x32_f16 v[18:21], v[106:109], v[18:21], 0
	s_setprio 0
	v_add_co_u32_e32 v64, vcc, s29, v62
	global_load_dwordx4 v[106:109], v[62:63], off
	s_nop 0
	v_addc_co_u32_e32 v65, vcc, 0, v63, vcc
	v_add_co_u32_e32 v84, vcc, s52, v62
	s_nop 1
	v_addc_co_u32_e32 v85, vcc, 0, v63, vcc
	v_add_co_u32_e32 v62, vcc, s33, v62
	global_load_dwordx4 v[122:125], v[64:65], off
	global_load_dwordx4 v[126:129], v[84:85], off
	v_addc_co_u32_e32 v63, vcc, 0, v63, vcc
	global_load_dwordx4 v[62:65], v[62:63], off
	ds_read_b128 v[130:133], v82
	ds_read_b128 v[134:137], v82 offset:8448
	s_setprio 1
	s_waitcnt lgkmcnt(1)
	v_mfma_f32_16x16x32_f16 v[110:113], v[130:133], v[10:13], v[110:113]
	s_waitcnt lgkmcnt(0)
	v_mfma_f32_16x16x32_f16 v[10:13], v[134:137], v[10:13], v[22:25]
	v_mfma_f32_16x16x32_f16 v[22:25], v[130:133], v[54:57], v[114:117]
	v_mfma_f32_16x16x32_f16 v[54:57], v[134:137], v[54:57], v[94:97]
	v_mfma_f32_16x16x32_f16 v[94:97], v[130:133], v[86:89], v[118:121]
	v_mfma_f32_16x16x32_f16 v[14:17], v[134:137], v[86:89], v[14:17]
	v_mfma_f32_16x16x32_f16 v[84:87], v[130:133], v[50:53], v[102:105]
	v_mfma_f32_16x16x32_f16 v[18:21], v[134:137], v[50:53], v[18:21]
	s_setprio 0
	global_load_dwordx4 v[50:53], v[68:69], off
	global_load_dwordx4 v[102:105], v[78:79], off
	v_add_co_u32_e32 v68, vcc, s52, v68
	s_nop 1
	v_addc_co_u32_e32 v69, vcc, 0, v69, vcc
	global_load_dwordx4 v[114:117], v[68:69], off
	global_load_dwordx4 v[118:121], v[138:139], off
	ds_read_b128 v[130:133], v172
	ds_read_b128 v[134:137], v172 offset:8448
	s_setprio 1
	s_waitcnt lgkmcnt(1)
	v_mfma_f32_16x16x32_f16 v[110:113], v[130:133], v[46:49], v[110:113]
	s_waitcnt lgkmcnt(0)
	v_mfma_f32_16x16x32_f16 v[10:13], v[134:137], v[46:49], v[10:13]
	v_mfma_f32_16x16x32_f16 v[22:25], v[130:133], v[42:45], v[22:25]
	v_mfma_f32_16x16x32_f16 v[42:45], v[134:137], v[42:45], v[54:57]
	v_mfma_f32_16x16x32_f16 v[46:49], v[130:133], v[90:93], v[94:97]
	v_mfma_f32_16x16x32_f16 v[14:17], v[134:137], v[90:93], v[14:17]
	s_waitcnt vmcnt(12)
	v_mfma_f32_16x16x32_f16 v[54:57], v[130:133], v[98:101], v[84:87]
	v_mfma_f32_16x16x32_f16 v[18:21], v[134:137], v[98:101], v[18:21]
	s_setprio 0
	v_add_co_u32_e32 v68, vcc, s52, v140
	global_load_dwordx4 v[84:87], v[140:141], off
	global_load_dwordx4 v[88:91], v[142:143], off
	v_addc_co_u32_e32 v69, vcc, 0, v141, vcc
	global_load_dwordx4 v[92:95], v[68:69], off
	global_load_dwordx4 v[96:99], v[144:145], off
	ds_read_b128 v[130:133], v173
	ds_read_b128 v[134:137], v173 offset:8448
	s_setprio 1
	s_waitcnt vmcnt(15) lgkmcnt(1)
	v_mfma_f32_16x16x32_f16 v[110:113], v[130:133], v[34:37], v[110:113]
	s_waitcnt lgkmcnt(0)
	v_mfma_f32_16x16x32_f16 v[10:13], v[134:137], v[34:37], v[10:13]
	s_waitcnt vmcnt(14)
	v_mfma_f32_16x16x32_f16 v[22:25], v[130:133], v[38:41], v[22:25]
	v_mfma_f32_16x16x32_f16 v[34:37], v[134:137], v[38:41], v[42:45]
	s_waitcnt vmcnt(13)
	v_mfma_f32_16x16x32_f16 v[38:41], v[130:133], v[70:73], v[46:49]
	v_mfma_f32_16x16x32_f16 v[14:17], v[134:137], v[70:73], v[14:17]
	s_waitcnt vmcnt(12)
	v_mfma_f32_16x16x32_f16 v[42:45], v[130:133], v[74:77], v[54:57]
	v_mfma_f32_16x16x32_f16 v[18:21], v[134:137], v[74:77], v[18:21]
	s_setprio 0
	v_add_co_u32_e32 v68, vcc, s52, v146
	global_load_dwordx4 v[46:49], v[146:147], off
	global_load_dwordx4 v[54:57], v[148:149], off
	v_addc_co_u32_e32 v69, vcc, 0, v147, vcc
	global_load_dwordx4 v[68:71], v[68:69], off
	s_nop 0
	global_load_dwordx4 v[72:75], v[150:151], off
	ds_read_b128 v[76:79], v174
	ds_read_b128 v[130:133], v174 offset:8448
	s_setprio 1
	s_waitcnt vmcnt(15) lgkmcnt(1)
	v_mfma_f32_16x16x32_f16 v[110:113], v[76:79], v[106:109], v[110:113]
	s_waitcnt lgkmcnt(0)
	v_mfma_f32_16x16x32_f16 v[10:13], v[130:133], v[106:109], v[10:13]
	s_waitcnt vmcnt(14)
	v_mfma_f32_16x16x32_f16 v[22:25], v[76:79], v[122:125], v[22:25]
	v_mfma_f32_16x16x32_f16 v[34:37], v[130:133], v[122:125], v[34:37]
	s_waitcnt vmcnt(13)
	v_mfma_f32_16x16x32_f16 v[38:41], v[76:79], v[126:129], v[38:41]
	v_mfma_f32_16x16x32_f16 v[14:17], v[130:133], v[126:129], v[14:17]
	s_waitcnt vmcnt(12)
	v_mfma_f32_16x16x32_f16 v[42:45], v[76:79], v[62:65], v[42:45]
	v_mfma_f32_16x16x32_f16 v[18:21], v[130:133], v[62:65], v[18:21]
	s_setprio 0
	ds_read_b128 v[62:65], v175
	ds_read_b128 v[76:79], v175 offset:8448
	s_setprio 1
	s_waitcnt vmcnt(11) lgkmcnt(1)
	v_mfma_f32_16x16x32_f16 v[106:109], v[62:65], v[50:53], v[110:113]
	s_waitcnt lgkmcnt(0)
	v_mfma_f32_16x16x32_f16 v[10:13], v[76:79], v[50:53], v[10:13]
	s_waitcnt vmcnt(10)
	v_mfma_f32_16x16x32_f16 v[22:25], v[62:65], v[102:105], v[22:25]
	v_mfma_f32_16x16x32_f16 v[34:37], v[76:79], v[102:105], v[34:37]
	s_waitcnt vmcnt(9)
	v_mfma_f32_16x16x32_f16 v[38:41], v[62:65], v[114:117], v[38:41]
	v_mfma_f32_16x16x32_f16 v[14:17], v[76:79], v[114:117], v[14:17]
	s_waitcnt vmcnt(8)
	v_mfma_f32_16x16x32_f16 v[42:45], v[62:65], v[118:121], v[42:45]
	v_mfma_f32_16x16x32_f16 v[18:21], v[76:79], v[118:121], v[18:21]
	s_setprio 0
	ds_read_b128 v[50:53], v176
	ds_read_b128 v[62:65], v176 offset:8448
	s_setprio 1
	s_waitcnt vmcnt(7) lgkmcnt(1)
	v_mfma_f32_16x16x32_f16 v[76:79], v[50:53], v[84:87], v[106:109]
	s_waitcnt lgkmcnt(0)
	v_mfma_f32_16x16x32_f16 v[10:13], v[62:65], v[84:87], v[10:13]
	s_waitcnt vmcnt(6)
	v_mfma_f32_16x16x32_f16 v[22:25], v[50:53], v[88:91], v[22:25]
	v_mfma_f32_16x16x32_f16 v[34:37], v[62:65], v[88:91], v[34:37]
	s_waitcnt vmcnt(5)
	v_mfma_f32_16x16x32_f16 v[38:41], v[50:53], v[92:95], v[38:41]
	v_mfma_f32_16x16x32_f16 v[14:17], v[62:65], v[92:95], v[14:17]
	s_waitcnt vmcnt(4)
	v_mfma_f32_16x16x32_f16 v[42:45], v[50:53], v[96:99], v[42:45]
	v_mfma_f32_16x16x32_f16 v[18:21], v[62:65], v[96:99], v[18:21]
	s_setprio 0
	ds_read_b128 v[50:53], v177
	ds_read_b128 v[62:65], v177 offset:8448
	s_setprio 1
	s_waitcnt vmcnt(3) lgkmcnt(1)
	v_mfma_f32_16x16x32_f16 v[76:79], v[50:53], v[46:49], v[76:79]
	s_waitcnt lgkmcnt(0)
	v_mfma_f32_16x16x32_f16 v[10:13], v[62:65], v[46:49], v[10:13]
	s_waitcnt vmcnt(2)
	v_mfma_f32_16x16x32_f16 v[22:25], v[50:53], v[54:57], v[22:25]
	v_mfma_f32_16x16x32_f16 v[34:37], v[62:65], v[54:57], v[34:37]
	s_waitcnt vmcnt(1)
	v_mfma_f32_16x16x32_f16 v[38:41], v[50:53], v[68:71], v[38:41]
	v_mfma_f32_16x16x32_f16 v[14:17], v[62:65], v[68:71], v[14:17]
	s_waitcnt vmcnt(0)
	v_mfma_f32_16x16x32_f16 v[42:45], v[50:53], v[72:75], v[42:45]
	v_mfma_f32_16x16x32_f16 v[18:21], v[62:65], v[72:75], v[18:21]
	s_setprio 0
	v_add_co_u32_e32 v108, vcc, s29, v152
	v_and_b32_e32 v67, 0x1c0, v0
	s_nop 0
	v_addc_co_u32_e32 v109, vcc, 0, v153, vcc
	v_add_co_u32_e32 v46, vcc, s52, v152
	s_movk_i32 s4, 0x50
	s_nop 0
	v_addc_co_u32_e32 v47, vcc, 0, v153, vcc
	v_add_co_u32_e32 v68, vcc, s33, v152
	v_or_b32_e32 v116, 16, v67
	s_nop 0
	v_addc_co_u32_e32 v69, vcc, 0, v153, vcc
	v_add_co_u32_e32 v110, vcc, s52, v154
	global_load_dwordx4 v[46:49], v[46:47], off
	s_nop 0
	global_load_dwordx4 v[50:53], v[68:69], off
	global_load_dwordx4 v[54:57], v[152:153], off
	global_load_dwordx4 v[62:65], v[154:155], off
	v_addc_co_u32_e32 v111, vcc, 0, v155, vcc
	v_add_co_u32_e32 v112, vcc, s52, v160
	global_load_dwordx4 v[68:71], v[156:157], off
	global_load_dwordx4 v[72:75], v[158:159], off
	global_load_dwordx4 v[84:87], v[160:161], off
	global_load_dwordx4 v[88:91], v[162:163], off
	v_addc_co_u32_e32 v113, vcc, 0, v161, vcc
	global_load_dwordx4 v[92:95], v[110:111], off
	global_load_dwordx4 v[96:99], v[112:113], off
	global_load_dwordx4 v[100:103], v[108:109], off
	global_load_dwordx4 v[104:107], v[164:165], off
	s_nop 0
	global_store_dwordx4 v[166:167], v[2:5], off sc0 sc1
	global_store_dwordx4 v[168:169], v[6:9], off sc0 sc1
	global_store_dwordx4 v[170:171], v[26:29], off sc0 sc1
	global_store_dwordx4 v[58:59], v[30:33], off sc0 sc1
	v_and_b32_e32 v4, 0x1cf, v0
	v_cvt_pk_f16_f32 v3, v78, v79
	v_cvt_pk_f16_f32 v2, v76, v77
	v_mad_u32_u24 v4, v4, s4, v80
	v_or_b32_e32 v5, v116, v81
	v_or_b32_e32 v117, 32, v67
	ds_write_b64 v4, v[2:3]
	v_cvt_pk_f16_f32 v3, v24, v25
	v_cvt_pk_f16_f32 v2, v22, v23
	v_mad_u32_u24 v5, v5, s4, v80
	v_or_b32_e32 v6, v117, v81
	v_or_b32_e32 v118, 48, v67
	ds_write_b64 v5, v[2:3]
	v_cvt_pk_f16_f32 v3, v40, v41
	v_cvt_pk_f16_f32 v2, v38, v39
	v_mad_u32_u24 v6, v6, s4, v80
	v_or_b32_e32 v7, v118, v81
	ds_write_b64 v6, v[2:3]
	v_cvt_pk_f16_f32 v3, v44, v45
	v_cvt_pk_f16_f32 v2, v42, v43
	v_mad_u32_u24 v7, v7, s4, v80
	ds_write_b64 v7, v[2:3]
	v_cvt_pk_f16_f32 v3, v12, v13
	v_cvt_pk_f16_f32 v2, v10, v11
	ds_write_b64 v4, v[2:3] offset:32
	v_cvt_pk_f16_f32 v3, v36, v37
	v_cvt_pk_f16_f32 v2, v34, v35
	ds_write_b64 v5, v[2:3] offset:32
	v_cvt_pk_f16_f32 v3, v16, v17
	v_cvt_pk_f16_f32 v2, v14, v15
	v_lshl_add_u64 v[10:11], v[60:61], 0, s[14:15]
	ds_write_b64 v6, v[2:3] offset:32
	v_cvt_pk_f16_f32 v2, v18, v19
	v_add_co_u32_e32 v18, vcc, s52, v10
	v_cvt_pk_f16_f32 v3, v20, v21
	v_lshl_add_u64 v[12:13], v[60:61], 0, s[16:17]
	v_addc_co_u32_e32 v19, vcc, 0, v11, vcc
	ds_write_b64 v7, v[2:3] offset:32
	s_waitcnt lgkmcnt(0)
	s_barrier
	global_load_dwordx4 v[2:5], v[10:11], off
	global_load_dwordx4 v[6:9], v[12:13], off
	v_lshl_add_u64 v[20:21], v[60:61], 0, s[12:13]
	global_load_dwordx4 v[10:13], v[18:19], off
	global_load_dwordx4 v[14:17], v[20:21], off
	ds_read_b128 v[18:21], v1
	ds_read_b128 v[22:25], v1 offset:8448
	s_mov_b32 s3, s27
	s_setprio 1
	s_waitcnt vmcnt(17) lgkmcnt(1)
	v_mfma_f32_16x16x32_f16 v[26:29], v[18:21], v[54:57], 0
	s_waitcnt lgkmcnt(0)
	v_mfma_f32_16x16x32_f16 v[30:33], v[22:25], v[54:57], 0
	s_waitcnt vmcnt(9)
	v_mfma_f32_16x16x32_f16 v[34:37], v[18:21], v[100:103], 0
	v_mfma_f32_16x16x32_f16 v[38:41], v[22:25], v[100:103], 0
	v_mfma_f32_16x16x32_f16 v[42:45], v[18:21], v[46:49], 0
	v_mfma_f32_16x16x32_f16 v[46:49], v[22:25], v[46:49], 0
	v_mfma_f32_16x16x32_f16 v[18:21], v[18:21], v[50:53], 0
	v_mfma_f32_16x16x32_f16 v[22:25], v[22:25], v[50:53], 0
	s_setprio 0
	v_lshl_add_u64 v[58:59], v[60:61], 0, s[10:11]
	v_add_co_u32_e32 v76, vcc, s29, v58
	s_nop 1
	v_addc_co_u32_e32 v77, vcc, 0, v59, vcc
	v_add_co_u32_e32 v108, vcc, s52, v58
	global_load_dwordx4 v[50:53], v[58:59], off
	global_load_dwordx4 v[54:57], v[76:77], off
	v_addc_co_u32_e32 v109, vcc, 0, v59, vcc
	v_add_co_u32_e32 v58, vcc, s33, v58
	s_nop 1
	v_addc_co_u32_e32 v59, vcc, 0, v59, vcc
	global_load_dwordx4 v[76:79], v[108:109], off
	global_load_dwordx4 v[100:103], v[58:59], off
	ds_read_b128 v[108:111], v82
	ds_read_b128 v[112:115], v82 offset:8448
	s_setprio 1
	s_waitcnt lgkmcnt(1)
	v_mfma_f32_16x16x32_f16 v[26:29], v[108:111], v[62:65], v[26:29]
	s_waitcnt lgkmcnt(0)
	v_mfma_f32_16x16x32_f16 v[30:33], v[112:115], v[62:65], v[30:33]
	v_mfma_f32_16x16x32_f16 v[34:37], v[108:111], v[68:71], v[34:37]
	v_mfma_f32_16x16x32_f16 v[38:41], v[112:115], v[68:71], v[38:41]
	v_mfma_f32_16x16x32_f16 v[42:45], v[108:111], v[92:95], v[42:45]
	v_mfma_f32_16x16x32_f16 v[46:49], v[112:115], v[92:95], v[46:49]
	v_mfma_f32_16x16x32_f16 v[18:21], v[108:111], v[72:75], v[18:21]
	v_mfma_f32_16x16x32_f16 v[22:25], v[112:115], v[72:75], v[22:25]
	s_setprio 0
	v_lshl_add_u64 v[58:59], v[60:61], 0, s[48:49]
	v_lshl_add_u64 v[72:73], v[60:61], 0, s[50:51]
	global_load_dwordx4 v[62:65], v[58:59], off
	global_load_dwordx4 v[68:71], v[72:73], off
	v_add_co_u32_e32 v58, vcc, s52, v58
	v_lshl_add_u64 v[82:83], v[60:61], 0, s[46:47]
	s_nop 0
	v_addc_co_u32_e32 v59, vcc, 0, v59, vcc
	global_load_dwordx4 v[72:75], v[58:59], off
	global_load_dwordx4 v[92:95], v[82:83], off
	ds_read_b128 v[108:111], v172
	ds_read_b128 v[112:115], v172 offset:8448
	s_setprio 1
	s_waitcnt lgkmcnt(1)
	v_mfma_f32_16x16x32_f16 v[26:29], v[108:111], v[84:87], v[26:29]
	s_waitcnt lgkmcnt(0)
	v_mfma_f32_16x16x32_f16 v[30:33], v[112:115], v[84:87], v[30:33]
	v_mfma_f32_16x16x32_f16 v[34:37], v[108:111], v[88:91], v[34:37]
	v_mfma_f32_16x16x32_f16 v[38:41], v[112:115], v[88:91], v[38:41]
	v_mfma_f32_16x16x32_f16 v[42:45], v[108:111], v[96:99], v[42:45]
	v_mfma_f32_16x16x32_f16 v[46:49], v[112:115], v[96:99], v[46:49]
	s_waitcnt vmcnt(16)
	v_mfma_f32_16x16x32_f16 v[18:21], v[108:111], v[104:107], v[18:21]
	v_mfma_f32_16x16x32_f16 v[22:25], v[112:115], v[104:107], v[22:25]
	s_setprio 0
	v_lshl_add_u64 v[58:59], v[60:61], 0, s[42:43]
	v_lshl_add_u64 v[90:91], v[60:61], 0, s[44:45]
	global_load_dwordx4 v[82:85], v[58:59], off
	global_load_dwordx4 v[86:89], v[90:91], off
	v_add_co_u32_e32 v58, vcc, s52, v58
	v_lshl_add_u64 v[90:91], v[60:61], 0, s[40:41]
	s_nop 0
	v_addc_co_u32_e32 v59, vcc, 0, v59, vcc
	global_load_dwordx4 v[96:99], v[58:59], off
	global_load_dwordx4 v[104:107], v[90:91], off
	ds_read_b128 v[108:111], v173
	ds_read_b128 v[112:115], v173 offset:8448
	s_setprio 1
	s_waitcnt vmcnt(15) lgkmcnt(1)
	v_mfma_f32_16x16x32_f16 v[26:29], v[108:111], v[2:5], v[26:29]
	s_waitcnt lgkmcnt(0)
	v_mfma_f32_16x16x32_f16 v[2:5], v[112:115], v[2:5], v[30:33]
	s_waitcnt vmcnt(14)
	v_mfma_f32_16x16x32_f16 v[30:33], v[108:111], v[6:9], v[34:37]
	v_mfma_f32_16x16x32_f16 v[6:9], v[112:115], v[6:9], v[38:41]
	s_waitcnt vmcnt(13)
	v_mfma_f32_16x16x32_f16 v[34:37], v[108:111], v[10:13], v[42:45]
	v_mfma_f32_16x16x32_f16 v[10:13], v[112:115], v[10:13], v[46:49]
	s_waitcnt vmcnt(12)
	v_mfma_f32_16x16x32_f16 v[18:21], v[108:111], v[14:17], v[18:21]
	v_mfma_f32_16x16x32_f16 v[14:17], v[112:115], v[14:17], v[22:25]
	s_setprio 0
	v_lshl_add_u64 v[42:43], v[60:61], 0, s[8:9]
	v_add_co_u32_e32 v58, vcc, s52, v42
	v_lshl_add_u64 v[44:45], v[60:61], 0, s[38:39]
	s_nop 0
	v_addc_co_u32_e32 v59, vcc, 0, v43, vcc
	global_load_dwordx4 v[22:25], v[42:43], off
	global_load_dwordx4 v[38:41], v[44:45], off
	v_lshl_add_u64 v[60:61], v[60:61], 0, s[6:7]
	global_load_dwordx4 v[42:45], v[58:59], off
	global_load_dwordx4 v[46:49], v[60:61], off
	ds_read_b128 v[58:61], v174
	ds_read_b128 v[108:111], v174 offset:8448
	s_setprio 1
	s_waitcnt vmcnt(15) lgkmcnt(1)
	v_mfma_f32_16x16x32_f16 v[26:29], v[58:61], v[50:53], v[26:29]
	s_waitcnt lgkmcnt(0)
	v_mfma_f32_16x16x32_f16 v[2:5], v[108:111], v[50:53], v[2:5]
	s_waitcnt vmcnt(14)
	v_mfma_f32_16x16x32_f16 v[30:33], v[58:61], v[54:57], v[30:33]
	v_mfma_f32_16x16x32_f16 v[6:9], v[108:111], v[54:57], v[6:9]
	s_waitcnt vmcnt(13)
	v_mfma_f32_16x16x32_f16 v[34:37], v[58:61], v[76:79], v[34:37]
	v_mfma_f32_16x16x32_f16 v[10:13], v[108:111], v[76:79], v[10:13]
	s_waitcnt vmcnt(12)
	v_mfma_f32_16x16x32_f16 v[18:21], v[58:61], v[100:103], v[18:21]
	v_mfma_f32_16x16x32_f16 v[14:17], v[108:111], v[100:103], v[14:17]
	s_setprio 0
	ds_read_b128 v[50:53], v175
	ds_read_b128 v[54:57], v175 offset:8448
	s_setprio 1
	s_waitcnt vmcnt(11) lgkmcnt(1)
	v_mfma_f32_16x16x32_f16 v[26:29], v[50:53], v[62:65], v[26:29]
	s_waitcnt lgkmcnt(0)
	v_mfma_f32_16x16x32_f16 v[2:5], v[54:57], v[62:65], v[2:5]
	s_waitcnt vmcnt(10)
	v_mfma_f32_16x16x32_f16 v[30:33], v[50:53], v[68:71], v[30:33]
	v_mfma_f32_16x16x32_f16 v[6:9], v[54:57], v[68:71], v[6:9]
	s_waitcnt vmcnt(9)
	v_mfma_f32_16x16x32_f16 v[34:37], v[50:53], v[72:75], v[34:37]
	v_mfma_f32_16x16x32_f16 v[10:13], v[54:57], v[72:75], v[10:13]
	s_waitcnt vmcnt(8)
	v_mfma_f32_16x16x32_f16 v[18:21], v[50:53], v[92:95], v[18:21]
	v_mfma_f32_16x16x32_f16 v[14:17], v[54:57], v[92:95], v[14:17]
	s_setprio 0
	ds_read_b128 v[50:53], v176
	ds_read_b128 v[54:57], v176 offset:8448
	s_setprio 1
	s_waitcnt vmcnt(7) lgkmcnt(1)
	v_mfma_f32_16x16x32_f16 v[26:29], v[50:53], v[82:85], v[26:29]
	s_waitcnt lgkmcnt(0)
	v_mfma_f32_16x16x32_f16 v[2:5], v[54:57], v[82:85], v[2:5]
	s_waitcnt vmcnt(6)
	v_mfma_f32_16x16x32_f16 v[30:33], v[50:53], v[86:89], v[30:33]
	v_mfma_f32_16x16x32_f16 v[6:9], v[54:57], v[86:89], v[6:9]
	s_waitcnt vmcnt(5)
	v_mfma_f32_16x16x32_f16 v[34:37], v[50:53], v[96:99], v[34:37]
	v_mfma_f32_16x16x32_f16 v[58:61], v[54:57], v[96:99], v[10:13]
	s_waitcnt vmcnt(4)
	v_mfma_f32_16x16x32_f16 v[18:21], v[50:53], v[104:107], v[18:21]
	v_mfma_f32_16x16x32_f16 v[50:53], v[54:57], v[104:107], v[14:17]
	s_setprio 0
	ds_read_b128 v[54:57], v177
	ds_read_b128 v[62:65], v177 offset:8448
	s_setprio 1
	s_waitcnt vmcnt(3) lgkmcnt(1)
	v_mfma_f32_16x16x32_f16 v[26:29], v[54:57], v[22:25], v[26:29]
	s_waitcnt lgkmcnt(0)
	v_mfma_f32_16x16x32_f16 v[14:17], v[62:65], v[22:25], v[2:5]
	s_waitcnt vmcnt(2)
	v_mfma_f32_16x16x32_f16 v[22:25], v[54:57], v[38:41], v[30:33]
	v_mfma_f32_16x16x32_f16 v[10:13], v[62:65], v[38:41], v[6:9]
	s_waitcnt vmcnt(1)
	v_mfma_f32_16x16x32_f16 v[30:33], v[54:57], v[42:45], v[34:37]
	v_mfma_f32_16x16x32_f16 v[6:9], v[62:65], v[42:45], v[58:61]
	s_waitcnt vmcnt(0)
	v_mfma_f32_16x16x32_f16 v[34:37], v[54:57], v[46:49], v[18:21]
	v_mfma_f32_16x16x32_f16 v[2:5], v[62:65], v[46:49], v[50:53]
	s_setprio 0
	s_nop 1
	v_mul_u32_u24_e32 v52, 0x50, v0
	ds_read_b128 v[18:21], v52
	s_lshl_b64 s[2:3], s[2:3], 15
	v_or_b32_e32 v0, s2, v66
	v_mov_b32_e32 v1, s3
	v_lshl_add_u64 v[50:51], s[24:25], 0, v[0:1]
	ds_read_b128 v[38:41], v52 offset:16
	ds_read_b128 v[42:45], v52 offset:32
	ds_read_b128 v[46:49], v52 offset:48
	s_waitcnt lgkmcnt(3)
	global_store_dwordx4 v[50:51], v[18:21], off sc0 sc1
	s_nop 1
	v_add_co_u32_e32 v18, vcc, s29, v50
	s_nop 1
	v_addc_co_u32_e32 v19, vcc, 0, v51, vcc
	s_waitcnt lgkmcnt(2)
	global_store_dwordx4 v[18:19], v[38:41], off sc0 sc1
	v_or_b32_e32 v18, 0x4000, v0
	v_mov_b32_e32 v19, s3
	v_lshl_add_u64 v[20:21], s[24:25], 0, v[18:19]
	s_waitcnt lgkmcnt(1)
	global_store_dwordx4 v[20:21], v[42:45], off sc0 sc1
	v_mul_f32_e32 v20, 0xbfb8aa3b, v26
	v_exp_f32_e32 v38, v20
	v_add_co_u32_e32 v20, vcc, s33, v50
	v_or_b32_e32 v39, 0x200, v81
	s_nop 0
	v_addc_co_u32_e32 v21, vcc, 0, v51, vcc
	s_waitcnt lgkmcnt(0)
	global_store_dwordx4 v[20:21], v[46:49], off sc0 sc1
	v_add_f32_e32 v20, 1.0, v38
	v_rcp_f32_e32 v20, v20
	v_mul_f32_e32 v21, 0xbfb8aa3b, v27
	v_mul_f32_e32 v38, 0xbfb8aa3b, v28
	v_exp_f32_e32 v21, v21
	v_exp_f32_e32 v38, v38
	v_fma_mixlo_f16 v40, v26, v20, 0
	v_mul_f32_e32 v26, 0xbfb8aa3b, v29
	v_add_f32_e32 v20, 1.0, v21
	v_add_f32_e32 v21, 1.0, v38
	v_exp_f32_e32 v38, v26
	v_rcp_f32_e32 v20, v20
	v_rcp_f32_e32 v21, v21
	v_mov_b32_e32 v26, v27
	v_mov_b32_e32 v27, v28
	v_add_f32_e32 v28, 1.0, v38
	v_rcp_f32_e32 v28, v28
	v_pk_mul_f32 v[20:21], v[26:27], v[20:21]
	v_or_b32_e32 v27, v39, v67
	v_cvt_pk_f16_f32 v21, v20, v21
	v_fma_mixlo_f16 v26, v29, v28, 0
	v_pack_b32_f16 v20, v40, v21
	v_alignbit_b32 v21, v26, v21, 16
	v_mul_f32_e32 v26, 0xbfb8aa3b, v22
	v_exp_f32_e32 v26, v26
	v_mad_u32_u24 v27, v27, s4, v80
	ds_write_b64 v27, v[20:21]
	v_mul_f32_e32 v21, 0xbfb8aa3b, v23
	v_add_f32_e32 v20, 1.0, v26
	v_rcp_f32_e32 v20, v20
	v_mul_f32_e32 v26, 0xbfb8aa3b, v24
	v_exp_f32_e32 v21, v21
	v_exp_f32_e32 v26, v26
	v_fma_mixlo_f16 v28, v22, v20, 0
	v_mul_f32_e32 v22, 0xbfb8aa3b, v25
	v_add_f32_e32 v20, 1.0, v21
	v_add_f32_e32 v21, 1.0, v26
	v_exp_f32_e32 v26, v22
	v_rcp_f32_e32 v20, v20
	v_rcp_f32_e32 v21, v21
	v_mov_b32_e32 v22, v23
	v_mov_b32_e32 v23, v24
	v_add_f32_e32 v24, 1.0, v26
	v_rcp_f32_e32 v24, v24
	v_pk_mul_f32 v[20:21], v[22:23], v[20:21]
	v_or_b32_e32 v23, v116, v39
	v_cvt_pk_f16_f32 v21, v20, v21
	v_fma_mixlo_f16 v22, v25, v24, 0
	v_pack_b32_f16 v20, v28, v21
	v_alignbit_b32 v21, v22, v21, 16
	v_mul_f32_e32 v22, 0xbfb8aa3b, v30
	v_exp_f32_e32 v22, v22
	v_mad_u32_u24 v24, v23, s4, v80
	ds_write_b64 v24, v[20:21]
	v_mul_f32_e32 v21, 0xbfb8aa3b, v31
	v_add_f32_e32 v20, 1.0, v22
	v_mul_f32_e32 v22, 0xbfb8aa3b, v32
	v_rcp_f32_e32 v20, v20
	v_exp_f32_e32 v21, v21
	v_exp_f32_e32 v22, v22
	v_mov_b32_e32 v23, v32
	v_fma_mixlo_f16 v25, v30, v20, 0
	v_add_f32_e32 v20, 1.0, v21
	v_add_f32_e32 v21, 1.0, v22
	v_mul_f32_e32 v22, 0xbfb8aa3b, v33
	v_exp_f32_e32 v26, v22
	v_rcp_f32_e32 v20, v20
	v_rcp_f32_e32 v21, v21
	v_mov_b32_e32 v22, v31
	v_add_f32_e32 v26, 1.0, v26
	v_rcp_f32_e32 v26, v26
	v_pk_mul_f32 v[20:21], v[22:23], v[20:21]
	v_or_b32_e32 v23, v117, v39
	v_cvt_pk_f16_f32 v21, v20, v21
	v_fma_mixlo_f16 v22, v33, v26, 0
	v_pack_b32_f16 v20, v25, v21
	v_alignbit_b32 v21, v22, v21, 16
	v_mul_f32_e32 v22, 0xbfb8aa3b, v34
	v_exp_f32_e32 v22, v22
	v_mad_u32_u24 v25, v23, s4, v80
	ds_write_b64 v25, v[20:21]
	v_mul_f32_e32 v21, 0xbfb8aa3b, v35
	v_add_f32_e32 v20, 1.0, v22
	v_mul_f32_e32 v22, 0xbfb8aa3b, v36
	v_rcp_f32_e32 v20, v20
	v_exp_f32_e32 v21, v21
	v_exp_f32_e32 v22, v22
	v_mov_b32_e32 v23, v36
	v_fma_mixlo_f16 v26, v34, v20, 0
	v_add_f32_e32 v20, 1.0, v21
	v_add_f32_e32 v21, 1.0, v22
	v_mul_f32_e32 v22, 0xbfb8aa3b, v37
	v_exp_f32_e32 v28, v22
	v_rcp_f32_e32 v20, v20
	v_rcp_f32_e32 v21, v21
	v_mov_b32_e32 v22, v35
	v_add_f32_e32 v28, 1.0, v28
	v_rcp_f32_e32 v28, v28
	v_pk_mul_f32 v[20:21], v[22:23], v[20:21]
	v_or_b32_e32 v23, v118, v39
	v_cvt_pk_f16_f32 v21, v20, v21
	v_fma_mixlo_f16 v22, v37, v28, 0
	v_pack_b32_f16 v20, v26, v21
	v_alignbit_b32 v21, v22, v21, 16
	v_mul_f32_e32 v22, 0xbfb8aa3b, v14
	v_exp_f32_e32 v22, v22
	v_mad_u32_u24 v23, v23, s4, v80
	ds_write_b64 v23, v[20:21]
	v_mul_f32_e32 v21, 0xbfb8aa3b, v15
	v_add_f32_e32 v20, 1.0, v22
	v_rcp_f32_e32 v20, v20
	v_exp_f32_e32 v21, v21
	v_mul_f32_e32 v22, 0xbfb8aa3b, v16
	v_exp_f32_e32 v22, v22
	v_fma_mixlo_f16 v26, v14, v20, 0
	v_add_f32_e32 v14, 1.0, v21
	v_rcp_f32_e32 v20, v14
	v_add_f32_e32 v14, 1.0, v22
	v_rcp_f32_e32 v21, v14
	v_mov_b32_e32 v14, v15
	v_mul_f32_e32 v15, 0xbfb8aa3b, v17
	v_exp_f32_e32 v22, v15
	v_mov_b32_e32 v15, v16
	v_pk_mul_f32 v[14:15], v[14:15], v[20:21]
	v_mul_f32_e32 v20, 0xbfb8aa3b, v10
	v_cvt_pk_f16_f32 v15, v14, v15
	v_add_f32_e32 v14, 1.0, v22
	v_rcp_f32_e32 v16, v14
	v_exp_f32_e32 v20, v20
	v_pack_b32_f16 v14, v26, v15
	v_lshl_add_u64 v[0:1], s[0:1], 0, v[0:1]
	v_fma_mixlo_f16 v16, v17, v16, 0
	v_alignbit_b32 v15, v16, v15, 16
	ds_write_b64 v27, v[14:15] offset:32
	v_add_f32_e32 v14, 1.0, v20
	v_mul_f32_e32 v15, 0xbfb8aa3b, v11
	v_rcp_f32_e32 v14, v14
	v_exp_f32_e32 v15, v15
	v_mul_f32_e32 v16, 0xbfb8aa3b, v12
	v_exp_f32_e32 v16, v16
	v_fma_mixlo_f16 v17, v10, v14, 0
	v_add_f32_e32 v10, 1.0, v15
	v_rcp_f32_e32 v14, v10
	v_add_f32_e32 v10, 1.0, v16
	v_rcp_f32_e32 v15, v10
	v_mov_b32_e32 v10, v11
	v_mul_f32_e32 v11, 0xbfb8aa3b, v13
	v_exp_f32_e32 v16, v11
	v_mov_b32_e32 v11, v12
	v_pk_mul_f32 v[10:11], v[10:11], v[14:15]
	v_mul_f32_e32 v14, 0xbfb8aa3b, v6
	v_cvt_pk_f16_f32 v11, v10, v11
	v_add_f32_e32 v10, 1.0, v16
	v_rcp_f32_e32 v12, v10
	v_exp_f32_e32 v14, v14
	v_pack_b32_f16 v10, v17, v11
	v_fma_mixlo_f16 v12, v13, v12, 0
	v_alignbit_b32 v11, v12, v11, 16
	ds_write_b64 v24, v[10:11] offset:32
	v_add_f32_e32 v10, 1.0, v14
	v_mul_f32_e32 v11, 0xbfb8aa3b, v7
	v_rcp_f32_e32 v10, v10
	v_exp_f32_e32 v11, v11
	v_mul_f32_e32 v12, 0xbfb8aa3b, v8
	v_exp_f32_e32 v12, v12
	v_fma_mixlo_f16 v13, v6, v10, 0
	v_add_f32_e32 v6, 1.0, v11
	v_rcp_f32_e32 v10, v6
	v_add_f32_e32 v6, 1.0, v12
	v_rcp_f32_e32 v11, v6
	v_mov_b32_e32 v6, v7
	v_mul_f32_e32 v7, 0xbfb8aa3b, v9
	v_exp_f32_e32 v12, v7
	v_mov_b32_e32 v7, v8
	v_pk_mul_f32 v[6:7], v[6:7], v[10:11]
	v_mul_f32_e32 v10, 0xbfb8aa3b, v2
	v_cvt_pk_f16_f32 v7, v6, v7
	v_add_f32_e32 v6, 1.0, v12
	v_rcp_f32_e32 v8, v6
	v_exp_f32_e32 v10, v10
	v_pack_b32_f16 v6, v13, v7
	v_fma_mixlo_f16 v8, v9, v8, 0
	v_alignbit_b32 v7, v8, v7, 16
	ds_write_b64 v25, v[6:7] offset:32
	v_add_f32_e32 v6, 1.0, v10
	v_mul_f32_e32 v7, 0xbfb8aa3b, v3
	v_rcp_f32_e32 v6, v6
	v_exp_f32_e32 v7, v7
	v_mul_f32_e32 v8, 0xbfb8aa3b, v4
	v_exp_f32_e32 v8, v8
	v_fma_mixlo_f16 v9, v2, v6, 0
	v_add_f32_e32 v2, 1.0, v7
	v_mul_f32_e32 v7, 0xbfb8aa3b, v5
	v_rcp_f32_e32 v6, v2
	v_add_f32_e32 v2, 1.0, v8
	v_exp_f32_e32 v8, v7
	v_rcp_f32_e32 v7, v2
	v_mov_b32_e32 v2, v3
	v_mov_b32_e32 v3, v4
	v_add_f32_e32 v4, 1.0, v8
	v_rcp_f32_e32 v4, v4
	v_pk_mul_f32 v[2:3], v[2:3], v[6:7]
	v_fma_mixlo_f16 v4, v5, v4, 0
	v_cvt_pk_f16_f32 v3, v2, v3
	v_pack_b32_f16 v2, v9, v3
	v_alignbit_b32 v3, v4, v3, 16
	ds_write_b64 v23, v[2:3] offset:32
	s_waitcnt lgkmcnt(0)
	s_barrier
	ds_read_b128 v[2:5], v52 offset:40960
	ds_read_b128 v[6:9], v52 offset:40976
	ds_read_b128 v[10:13], v52 offset:40992
	ds_read_b128 v[14:17], v52 offset:41008
	s_waitcnt lgkmcnt(3)
	global_store_dwordx4 v[0:1], v[2:5], off sc0 sc1
	s_nop 1
	v_add_co_u32_e32 v2, vcc, 0x2000, v0
	s_nop 1
	v_addc_co_u32_e32 v3, vcc, 0, v1, vcc
	v_add_co_u32_e32 v0, vcc, 0x6000, v0
	s_waitcnt lgkmcnt(2)
	global_store_dwordx4 v[2:3], v[6:9], off sc0 sc1
	v_lshl_add_u64 v[2:3], s[0:1], 0, v[18:19]
	v_addc_co_u32_e32 v1, vcc, 0, v1, vcc
	s_waitcnt lgkmcnt(1)
	global_store_dwordx4 v[2:3], v[10:13], off sc0 sc1
	s_waitcnt lgkmcnt(0)
	global_store_dwordx4 v[0:1], v[14:17], off sc0 sc1
	s_endpgm
	.p2align	8

amdhsa.kernels:
  - .agpr_count:     0
    .args:
      - .actual_access:  read_only
        .address_space:  global
        .offset:         0
        .size:           8
        .value_kind:     global_buffer
      - .actual_access:  write_only
        .address_space:  global
        .offset:         8
        .size:           8
        .value_kind:     global_buffer
      - .offset:         16
        .size:           4
        .value_kind:     by_value
      - .offset:         20
        .size:           4
        .value_kind:     by_value
      - .actual_access:  read_only
        .address_space:  global
        .offset:         24
        .size:           8
        .value_kind:     global_buffer
      - .actual_access:  write_only
        .address_space:  global
        .offset:         32
        .size:           8
        .value_kind:     global_buffer
      - .offset:         40
        .size:           4
        .value_kind:     by_value
      - .offset:         44
        .size:           4
        .value_kind:     by_value
      - .actual_access:  read_only
        .address_space:  global
        .offset:         48
        .size:           8
        .value_kind:     global_buffer
      - .actual_access:  write_only
        .address_space:  global
        .offset:         56
        .size:           8
        .value_kind:     global_buffer
      - .offset:         64
        .size:           4
        .value_kind:     by_value
      - .offset:         68
        .size:           4
        .value_kind:     by_value
      - .actual_access:  read_only
        .address_space:  global
        .offset:         72
        .size:           8
        .value_kind:     global_buffer
      - .actual_access:  write_only
        .address_space:  global
        .offset:         80
        .size:           8
        .value_kind:     global_buffer
      - .offset:         88
        .size:           4
        .value_kind:     by_value
      - .actual_access:  read_only
        .address_space:  global
        .offset:         96
        .size:           8
        .value_kind:     global_buffer
      - .actual_access:  write_only
        .address_space:  global
        .offset:         104
        .size:           8
        .value_kind:     global_buffer
      - .offset:         112
        .size:           4
        .value_kind:     by_value
      - .offset:         120
        .size:           4
        .value_kind:     hidden_block_count_x
      - .offset:         124
        .size:           4
        .value_kind:     hidden_block_count_y
      - .offset:         128
        .size:           4
        .value_kind:     hidden_block_count_z
      - .offset:         132
        .size:           2
        .value_kind:     hidden_group_size_x
      - .offset:         134
        .size:           2
        .value_kind:     hidden_group_size_y
      - .offset:         136
        .size:           2
        .value_kind:     hidden_group_size_z
      - .offset:         138
        .size:           2
        .value_kind:     hidden_remainder_x
      - .offset:         140
        .size:           2
        .value_kind:     hidden_remainder_y
      - .offset:         142
        .size:           2
        .value_kind:     hidden_remainder_z
      - .offset:         160
        .size:           8
        .value_kind:     hidden_global_offset_x
      - .offset:         168
        .size:           8
        .value_kind:     hidden_global_offset_y
      - .offset:         176
        .size:           8
        .value_kind:     hidden_global_offset_z
      - .offset:         184
        .size:           2
        .value_kind:     hidden_grid_dims
    .group_segment_fixed_size: 0
    .kernarg_segment_align: 8
    .kernarg_segment_size: 376
    .language:       OpenCL C
    .language_version:
      - 2
      - 0
    .max_flat_workgroup_size: 1024
    .name:           _Z5k_swzPKfPDF16_iiS0_S1_iiS0_S1_iiS0_PfiS0_S1_i
    .private_segment_fixed_size: 0
    .sgpr_count:     32
    .sgpr_spill_count: 0
    .symbol:         _Z5k_swzPKfPDF16_iiS0_S1_iiS0_S1_iiS0_PfiS0_S1_i.kd
    .uniform_work_group_size: 1
    .uses_dynamic_stack: false
    .vgpr_count:     14
    .vgpr_spill_count: 0
    .wavefront_size: 64
  - .agpr_count:     0
    .args:
      - .actual_access:  read_only
        .address_space:  global
        .offset:         0
        .size:           8
        .value_kind:     global_buffer
      - .actual_access:  read_only
        .address_space:  global
        .offset:         8
        .size:           8
        .value_kind:     global_buffer
      - .actual_access:  write_only
        .address_space:  global
        .offset:         16
        .size:           8
        .value_kind:     global_buffer
      - .actual_access:  read_only
        .address_space:  global
        .offset:         24
        .size:           8
        .value_kind:     global_buffer
      - .actual_access:  read_only
        .address_space:  global
        .offset:         32
        .size:           8
        .value_kind:     global_buffer
      - .actual_access:  read_only
        .address_space:  global
        .offset:         40
        .size:           8
        .value_kind:     global_buffer
      - .actual_access:  write_only
        .address_space:  global
        .offset:         48
        .size:           8
        .value_kind:     global_buffer
    .group_segment_fixed_size: 98816
    .kernarg_segment_align: 8
    .kernarg_segment_size: 56
    .language:       OpenCL C
    .language_version:
      - 2
      - 0
    .max_flat_workgroup_size: 512
    .name:           _Z10k_ka_firstPKfPKiPfS0_S0_PKDF16_PDF16_
    .private_segment_fixed_size: 0
    .sgpr_count:     59
    .sgpr_spill_count: 0
    .symbol:         _Z10k_ka_firstPKfPKiPfS0_S0_PKDF16_PDF16_.kd
    .uniform_work_group_size: 1
    .uses_dynamic_stack: false
    .vgpr_count:     174
    .vgpr_spill_count: 0
    .wavefront_size: 64
  - .agpr_count:     0
    .args:
      - .actual_access:  read_only
        .address_space:  global
        .offset:         0
        .size:           8
        .value_kind:     global_buffer
      - .actual_access:  read_only
        .address_space:  global
        .offset:         8
        .size:           8
        .value_kind:     global_buffer
      - .actual_access:  read_only
        .address_space:  global
        .offset:         16
        .size:           8
        .value_kind:     global_buffer
      - .actual_access:  read_only
        .address_space:  global
        .offset:         24
        .size:           8
        .value_kind:     global_buffer
      - .actual_access:  read_only
        .address_space:  global
        .offset:         32
        .size:           8
        .value_kind:     global_buffer
      - .actual_access:  read_only
        .address_space:  global
        .offset:         40
        .size:           8
        .value_kind:     global_buffer
      - .actual_access:  write_only
        .address_space:  global
        .offset:         48
        .size:           8
        .value_kind:     global_buffer
      - .actual_access:  write_only
        .address_space:  global
        .offset:         56
        .size:           8
        .value_kind:     global_buffer
      - .actual_access:  write_only
        .address_space:  global
        .offset:         64
        .size:           8
        .value_kind:     global_buffer
      - .actual_access:  read_only
        .address_space:  global
        .offset:         72
        .size:           8
        .value_kind:     global_buffer
      - .actual_access:  write_only
        .address_space:  global
        .offset:         80
        .size:           8
        .value_kind:     global_buffer
      - .actual_access:  write_only
        .address_space:  global
        .offset:         88
        .size:           8
        .value_kind:     global_buffer
    .group_segment_fixed_size: 47616
    .kernarg_segment_align: 8
    .kernarg_segment_size: 96
    .language:       OpenCL C
    .language_version:
      - 2
      - 0
    .max_flat_workgroup_size: 512
    .name:           _Z12k_conv_xprojPKDF16_PKfS2_S0_S0_S2_PDF16_S3_PfS2_S3_S4_
    .private_segment_fixed_size: 0
    .sgpr_count:     32
    .sgpr_spill_count: 0
    .symbol:         _Z12k_conv_xprojPKDF16_PKfS2_S0_S0_S2_PDF16_S3_PfS2_S3_S4_.kd
    .uniform_work_group_size: 1
    .uses_dynamic_stack: false
    .vgpr_count:     160
    .vgpr_spill_count: 0
    .wavefront_size: 64
  - .agpr_count:     0
    .args:
      - .actual_access:  read_only
        .address_space:  global
        .offset:         0
        .size:           8
        .value_kind:     global_buffer
      - .actual_access:  read_only
        .address_space:  global
        .offset:         8
        .size:           8
        .value_kind:     global_buffer
      - .actual_access:  read_only
        .address_space:  global
        .offset:         16
        .size:           8
        .value_kind:     global_buffer
      - .actual_access:  write_only
        .address_space:  global
        .offset:         24
        .size:           8
        .value_kind:     global_buffer
    .group_segment_fixed_size: 16384
    .kernarg_segment_align: 8
    .kernarg_segment_size: 32
    .language:       OpenCL C
    .language_version:
      - 2
      - 0
    .max_flat_workgroup_size: 512
    .name:           _Z11k_scan_combPKDF16_PKfS2_PDF16_
    .private_segment_fixed_size: 0
    .sgpr_count:     18
    .sgpr_spill_count: 0
    .symbol:         _Z11k_scan_combPKDF16_PKfS2_PDF16_.kd
    .uniform_work_group_size: 1
    .uses_dynamic_stack: false
    .vgpr_count:     120
    .vgpr_spill_count: 0
    .wavefront_size: 64
  - .agpr_count:     0
    .args:
      - .actual_access:  read_only
        .address_space:  global
        .offset:         0
        .size:           8
        .value_kind:     global_buffer
      - .actual_access:  read_only
        .address_space:  global
        .offset:         8
        .size:           8
        .value_kind:     global_buffer
      - .actual_access:  read_only
        .address_space:  global
        .offset:         16
        .size:           8
        .value_kind:     global_buffer
      - .actual_access:  read_only
        .address_space:  global
        .offset:         24
        .size:           8
        .value_kind:     global_buffer
      - .actual_access:  write_only
        .address_space:  global
        .offset:         32
        .size:           8
        .value_kind:     global_buffer
    .group_segment_fixed_size: 32
    .kernarg_segment_align: 8
    .kernarg_segment_size: 40
    .language:       OpenCL C
    .language_version:
      - 2
      - 0
    .max_flat_workgroup_size: 256
    .name:           _Z6k_headPKfS0_S0_S0_Pf
    .private_segment_fixed_size: 0
    .sgpr_count:     86
    .sgpr_spill_count: 0
    .symbol:         _Z6k_headPKfS0_S0_S0_Pf.kd
    .uniform_work_group_size: 1
    .uses_dynamic_stack: false
    .vgpr_count:     92
    .vgpr_spill_count: 0
    .wavefront_size: 64
  - .agpr_count:     0
    .args:
      - .actual_access:  read_only
        .address_space:  global
        .offset:         0
        .size:           8
        .value_kind:     global_buffer
      - .actual_access:  read_only
        .address_space:  global
        .offset:         8
        .size:           8
        .value_kind:     global_buffer
      - .actual_access:  read_only
        .address_space:  global
        .offset:         16
        .size:           8
        .value_kind:     global_buffer
      - .actual_access:  read_only
        .address_space:  global
        .offset:         24
        .size:           8
        .value_kind:     global_buffer
      - .actual_access:  read_only
        .address_space:  global
        .offset:         32
        .size:           8
        .value_kind:     global_buffer
      - .actual_access:  read_only
        .address_space:  global
        .offset:         40
        .size:           8
        .value_kind:     global_buffer
      - .actual_access:  read_only
        .address_space:  global
        .offset:         48
        .size:           8
        .value_kind:     global_buffer
      - .address_space:  global
        .offset:         56
        .size:           8
        .value_kind:     global_buffer
      - .actual_access:  read_only
        .address_space:  global
        .offset:         64
        .size:           8
        .value_kind:     global_buffer
      - .actual_access:  read_only
        .address_space:  global
        .offset:         72
        .size:           8
        .value_kind:     global_buffer
      - .actual_access:  read_only
        .address_space:  global
        .offset:         80
        .size:           8
        .value_kind:     global_buffer
      - .address_space:  global
        .offset:         88
        .size:           8
        .value_kind:     global_buffer
      - .actual_access:  read_only
        .address_space:  global
        .offset:         96
        .size:           8
        .value_kind:     global_buffer
      - .actual_access:  read_only
        .address_space:  global
        .offset:         104
        .size:           8
        .value_kind:     global_buffer
      - .actual_access:  read_only
        .address_space:  global
        .offset:         112
        .size:           8
        .value_kind:     global_buffer
    .group_segment_fixed_size: 98816
    .kernarg_segment_align: 8
    .kernarg_segment_size: 120
    .language:       OpenCL C
    .language_version:
      - 2
      - 0
    .max_flat_workgroup_size: 512
    .name:           _Z4k_k2ILb0EEvPKDF16_S1_PKfS3_S3_S1_S1_PfS3_S3_S1_PDF16_PKiS4_S4_
    .private_segment_fixed_size: 0
    .sgpr_count:     64
    .sgpr_spill_count: 0
    .symbol:         _Z4k_k2ILb0EEvPKDF16_S1_PKfS3_S3_S1_S1_PfS3_S3_S1_PDF16_PKiS4_S4_.kd
    .uniform_work_group_size: 1
    .uses_dynamic_stack: false
    .vgpr_count:     212
    .vgpr_spill_count: 0
    .wavefront_size: 64
  - .agpr_count:     0
    .args:
      - .actual_access:  read_only
        .address_space:  global
        .offset:         0
        .size:           8
        .value_kind:     global_buffer
      - .actual_access:  read_only
        .address_space:  global
        .offset:         8
        .size:           8
        .value_kind:     global_buffer
      - .actual_access:  read_only
        .address_space:  global
        .offset:         16
        .size:           8
        .value_kind:     global_buffer
      - .actual_access:  read_only
        .address_space:  global
        .offset:         24
        .size:           8
        .value_kind:     global_buffer
      - .actual_access:  read_only
        .address_space:  global
        .offset:         32
        .size:           8
        .value_kind:     global_buffer
      - .actual_access:  read_only
        .address_space:  global
        .offset:         40
        .size:           8
        .value_kind:     global_buffer
      - .actual_access:  read_only
        .address_space:  global
        .offset:         48
        .size:           8
        .value_kind:     global_buffer
      - .actual_access:  read_only
        .address_space:  global
        .offset:         56
        .size:           8
        .value_kind:     global_buffer
      - .actual_access:  read_only
        .address_space:  global
        .offset:         64
        .size:           8
        .value_kind:     global_buffer
      - .actual_access:  read_only
        .address_space:  global
        .offset:         72
        .size:           8
        .value_kind:     global_buffer
      - .actual_access:  read_only
        .address_space:  global
        .offset:         80
        .size:           8
        .value_kind:     global_buffer
      - .actual_access:  read_only
        .address_space:  global
        .offset:         88
        .size:           8
        .value_kind:     global_buffer
      - .actual_access:  read_only
        .address_space:  global
        .offset:         96
        .size:           8
        .value_kind:     global_buffer
      - .actual_access:  write_only
        .address_space:  global
        .offset:         104
        .size:           8
        .value_kind:     global_buffer
      - .actual_access:  write_only
        .address_space:  global
        .offset:         112
        .size:           8
        .value_kind:     global_buffer
    .group_segment_fixed_size: 98816
    .kernarg_segment_align: 8
    .kernarg_segment_size: 120
    .language:       OpenCL C
    .language_version:
      - 2
      - 0
    .max_flat_workgroup_size: 512
    .name:           _Z4k_k2ILb1EEvPKDF16_S1_PKfS3_S3_S1_S1_PfS3_S3_S1_PDF16_PKiS4_S4_
    .private_segment_fixed_size: 0
    .sgpr_count:     44
    .sgpr_spill_count: 0
    .symbol:         _Z4k_k2ILb1EEvPKDF16_S1_PKfS3_S3_S1_S1_PfS3_S3_S1_PDF16_PKiS4_S4_.kd
    .uniform_work_group_size: 1
    .uses_dynamic_stack: false
    .vgpr_count:     160
    .vgpr_spill_count: 0
    .wavefront_size: 64
